# mid-MFMA-block s_setprio 0/1 flip pairs removed in all GEMM K-loops (priority stays raised through each 16/32-MFMA block)
# speedup vs baseline: 1.0026x; 1.0026x over previous
.LBB0_294:
	s_andn2_b64 vcc, exec, s[8:9]
	s_waitcnt lgkmcnt(0)
	s_cbranch_vccnz .Lzs_0
	s_add_i32 s14, s71, 0x80
	s_addk_i32 s70, 0x100
	s_mov_b32 s71, 0
	ds_read_b128 v[160:163], v144
	ds_read_b128 v[164:167], v145
	ds_read_b128 v[168:171], v140
	ds_read_b128 v[172:175], v141
	ds_read_b128 v[176:179], v146
	ds_read_b128 v[180:183], v147
	ds_read_b128 v[184:187], v148
	ds_read_b128 v[188:191], v149
	s_add_i32 s72, s14, 0x80
	s_cmp_eq_u32 s54, s71
	s_cselect_b32 s73, s13, s70
	s_cselect_b32 s72, s15, s72
	v_add_u32_e32 v159, s14, v157
	s_add_i32 m0, s22, 0xc000
	ds_read_b128 v[192:195], v158
	ds_read_b128 v[196:199], v158 offset:1024
	ds_read_b128 v[200:203], v158 offset:2048
	ds_read_b128 v[204:207], v158 offset:3072
	ds_read_b128 v[214:217], v158 offset:4096
	ds_read_b128 v[218:221], v158 offset:5120
	ds_read_b128 v[222:225], v158 offset:6144
	ds_read_b128 v[226:229], v158 offset:7168
	global_load_lds_dwordx4 v159, s[4:5]
	v_add_u32_e32 v159, s14, v156
	s_add_i32 m0, s22, 0xe000
	s_nop 0
	global_load_lds_dwordx4 v159, s[4:5]
	s_waitcnt vmcnt(8)
	s_waitcnt lgkmcnt(0)
	s_barrier
	s_setprio 1
	s_waitcnt lgkmcnt(0)
	v_mfma_f32_16x16x32_bf16 v[122:125], v[168:171], v[192:195], 0
	v_mfma_f32_16x16x32_bf16 v[126:129], v[164:167], v[192:195], 0
	v_mfma_f32_16x16x32_bf16 v[110:113], v[168:171], v[200:203], 0
	v_mfma_f32_16x16x32_bf16 v[106:109], v[164:167], v[200:203], 0
	v_mfma_f32_16x16x32_bf16 v[94:97], v[168:171], v[214:217], 0
	v_mfma_f32_16x16x32_bf16 v[90:93], v[164:167], v[214:217], 0
	v_mfma_f32_16x16x32_bf16 v[78:81], v[168:171], v[222:225], 0
	v_mfma_f32_16x16x32_bf16 v[74:77], v[164:167], v[222:225], 0
	v_mfma_f32_16x16x32_bf16 v[122:125], v[160:163], v[196:199], v[122:125]
	v_mfma_f32_16x16x32_bf16 v[126:129], v[176:179], v[196:199], v[126:129]
	v_mfma_f32_16x16x32_bf16 v[110:113], v[160:163], v[204:207], v[110:113]
	v_mfma_f32_16x16x32_bf16 v[106:109], v[176:179], v[204:207], v[106:109]
	v_mfma_f32_16x16x32_bf16 v[94:97], v[160:163], v[218:221], v[94:97]
	v_mfma_f32_16x16x32_bf16 v[90:93], v[176:179], v[218:221], v[90:93]
	v_mfma_f32_16x16x32_bf16 v[78:81], v[160:163], v[226:229], v[78:81]
	v_mfma_f32_16x16x32_bf16 v[74:77], v[176:179], v[226:229], v[74:77]
	v_mfma_f32_16x16x32_bf16 v[118:121], v[172:175], v[192:195], 0
	v_mfma_f32_16x16x32_bf16 v[114:117], v[184:187], v[192:195], 0
	v_mfma_f32_16x16x32_bf16 v[102:105], v[172:175], v[200:203], 0
	v_mfma_f32_16x16x32_bf16 v[98:101], v[184:187], v[200:203], 0
	v_mfma_f32_16x16x32_bf16 v[86:89], v[172:175], v[214:217], 0
	v_mfma_f32_16x16x32_bf16 v[82:85], v[184:187], v[214:217], 0
	v_mfma_f32_16x16x32_bf16 v[70:73], v[172:175], v[222:225], 0
	v_mfma_f32_16x16x32_bf16 v[66:69], v[184:187], v[222:225], 0
	v_mfma_f32_16x16x32_bf16 v[118:121], v[180:183], v[196:199], v[118:121]
	v_mfma_f32_16x16x32_bf16 v[114:117], v[188:191], v[196:199], v[114:117]
	v_mfma_f32_16x16x32_bf16 v[102:105], v[180:183], v[204:207], v[102:105]
	v_mfma_f32_16x16x32_bf16 v[98:101], v[188:191], v[204:207], v[98:101]
	v_mfma_f32_16x16x32_bf16 v[86:89], v[180:183], v[218:221], v[86:89]
	v_mfma_f32_16x16x32_bf16 v[82:85], v[188:191], v[218:221], v[82:85]
	v_mfma_f32_16x16x32_bf16 v[70:73], v[180:183], v[226:229], v[70:73]
	v_mfma_f32_16x16x32_bf16 v[66:69], v[188:191], v[226:229], v[66:69]
	s_setprio 0
	s_barrier
	s_mov_b32 m0, s23
	v_add_u32_e32 v159, s73, v134
	ds_read_b128 v[192:195], v158 offset:16384
	ds_read_b128 v[196:199], v158 offset:17408
	ds_read_b128 v[200:203], v158 offset:18432
	ds_read_b128 v[204:207], v158 offset:19456
	ds_read_b128 v[214:217], v158 offset:20480
	ds_read_b128 v[218:221], v158 offset:21504
	ds_read_b128 v[222:225], v158 offset:22528
	ds_read_b128 v[226:229], v158 offset:23552
	global_load_lds_dwordx4 v159, s[20:21]
	v_add_u32_e32 v159, s17, v159
	s_mov_b32 m0, s28
	s_nop 0
	global_load_lds_dwordx4 v159, s[20:21]
	v_add_u32_e32 v159, s73, v135
	s_mov_b32 m0, s29
	s_nop 0
	global_load_lds_dwordx4 v159, s[20:21]
	v_add_u32_e32 v159, s17, v159
	s_mov_b32 m0, s30
	s_nop 0
	global_load_lds_dwordx4 v159, s[20:21]
	v_add_u32_e32 v159, s72, v1
	s_mov_b32 m0, s22
	s_nop 0
	global_load_lds_dwordx4 v159, s[4:5]
	v_add_u32_e32 v159, s16, v159
	s_mov_b32 m0, s31
	s_nop 0
	global_load_lds_dwordx4 v159, s[4:5]
	s_waitcnt vmcnt(8)
	s_waitcnt lgkmcnt(0)
	s_barrier
	s_setprio 1
	s_waitcnt lgkmcnt(0)
	v_mfma_f32_16x16x32_bf16 v[62:65], v[168:171], v[192:195], 0
	v_mfma_f32_16x16x32_bf16 v[58:61], v[164:167], v[192:195], 0
	v_mfma_f32_16x16x32_bf16 v[46:49], v[168:171], v[200:203], 0
	v_mfma_f32_16x16x32_bf16 v[42:45], v[164:167], v[200:203], 0
	v_mfma_f32_16x16x32_bf16 v[30:33], v[168:171], v[214:217], 0
	v_mfma_f32_16x16x32_bf16 v[26:29], v[164:167], v[214:217], 0
	v_mfma_f32_16x16x32_bf16 v[14:17], v[168:171], v[222:225], 0
	v_mfma_f32_16x16x32_bf16 v[10:13], v[164:167], v[222:225], 0
	v_mfma_f32_16x16x32_bf16 v[62:65], v[160:163], v[196:199], v[62:65]
	v_mfma_f32_16x16x32_bf16 v[58:61], v[176:179], v[196:199], v[58:61]
	v_mfma_f32_16x16x32_bf16 v[46:49], v[160:163], v[204:207], v[46:49]
	v_mfma_f32_16x16x32_bf16 v[42:45], v[176:179], v[204:207], v[42:45]
	v_mfma_f32_16x16x32_bf16 v[30:33], v[160:163], v[218:221], v[30:33]
	v_mfma_f32_16x16x32_bf16 v[26:29], v[176:179], v[218:221], v[26:29]
	v_mfma_f32_16x16x32_bf16 v[14:17], v[160:163], v[226:229], v[14:17]
	v_mfma_f32_16x16x32_bf16 v[10:13], v[176:179], v[226:229], v[10:13]
	v_mfma_f32_16x16x32_bf16 v[54:57], v[172:175], v[192:195], 0
	v_mfma_f32_16x16x32_bf16 v[50:53], v[184:187], v[192:195], 0
	v_mfma_f32_16x16x32_bf16 v[38:41], v[172:175], v[200:203], 0
	v_mfma_f32_16x16x32_bf16 v[34:37], v[184:187], v[200:203], 0
	v_mfma_f32_16x16x32_bf16 v[22:25], v[172:175], v[214:217], 0
	v_mfma_f32_16x16x32_bf16 v[18:21], v[184:187], v[214:217], 0
	v_mfma_f32_16x16x32_bf16 v[6:9], v[172:175], v[222:225], 0
	v_mfma_f32_16x16x32_bf16 v[2:5], v[184:187], v[222:225], 0
	v_mfma_f32_16x16x32_bf16 v[54:57], v[180:183], v[196:199], v[54:57]
	v_mfma_f32_16x16x32_bf16 v[50:53], v[188:191], v[196:199], v[50:53]
	v_mfma_f32_16x16x32_bf16 v[38:41], v[180:183], v[204:207], v[38:41]
	v_mfma_f32_16x16x32_bf16 v[34:37], v[188:191], v[204:207], v[34:37]
	v_mfma_f32_16x16x32_bf16 v[22:25], v[180:183], v[218:221], v[22:25]
	v_mfma_f32_16x16x32_bf16 v[18:21], v[188:191], v[218:221], v[18:21]
	v_mfma_f32_16x16x32_bf16 v[6:9], v[180:183], v[226:229], v[6:9]
	v_mfma_f32_16x16x32_bf16 v[2:5], v[188:191], v[226:229], v[2:5]
	s_setprio 0
	s_barrier
	s_branch .Lmid_0
.LBB0_296:
	ds_read_b128 v[160:163], v144
	ds_read_b128 v[164:167], v145
	ds_read_b128 v[168:171], v140
	ds_read_b128 v[172:175], v141
	ds_read_b128 v[176:179], v146
	ds_read_b128 v[180:183], v147
	ds_read_b128 v[184:187], v148
	ds_read_b128 v[188:191], v149
	s_add_i32 s72, s14, 0x80
	s_cmp_eq_u32 s54, s71
	s_cselect_b32 s73, s13, s70
	s_cselect_b32 s72, s15, s72
	v_add_u32_e32 v159, s14, v157
	s_add_i32 m0, s22, 0xc000
	ds_read_b128 v[192:195], v158
	ds_read_b128 v[196:199], v158 offset:1024
	ds_read_b128 v[200:203], v158 offset:2048
	ds_read_b128 v[204:207], v158 offset:3072
	ds_read_b128 v[214:217], v158 offset:4096
	ds_read_b128 v[218:221], v158 offset:5120
	ds_read_b128 v[222:225], v158 offset:6144
	ds_read_b128 v[226:229], v158 offset:7168
	global_load_lds_dwordx4 v159, s[4:5]
	v_add_u32_e32 v159, s14, v156
	s_add_i32 m0, s22, 0xe000
	s_nop 0
	global_load_lds_dwordx4 v159, s[4:5]
	s_waitcnt vmcnt(8)
	s_waitcnt lgkmcnt(0)
	s_barrier
	s_setprio 1
	s_waitcnt lgkmcnt(0)
	v_mfma_f32_16x16x32_bf16 v[122:125], v[168:171], v[192:195], v[122:125]
	v_mfma_f32_16x16x32_bf16 v[126:129], v[164:167], v[192:195], v[126:129]
	v_mfma_f32_16x16x32_bf16 v[110:113], v[168:171], v[200:203], v[110:113]
	v_mfma_f32_16x16x32_bf16 v[106:109], v[164:167], v[200:203], v[106:109]
	v_mfma_f32_16x16x32_bf16 v[94:97], v[168:171], v[214:217], v[94:97]
	v_mfma_f32_16x16x32_bf16 v[90:93], v[164:167], v[214:217], v[90:93]
	v_mfma_f32_16x16x32_bf16 v[78:81], v[168:171], v[222:225], v[78:81]
	v_mfma_f32_16x16x32_bf16 v[74:77], v[164:167], v[222:225], v[74:77]
	v_mfma_f32_16x16x32_bf16 v[122:125], v[160:163], v[196:199], v[122:125]
	v_mfma_f32_16x16x32_bf16 v[126:129], v[176:179], v[196:199], v[126:129]
	v_mfma_f32_16x16x32_bf16 v[110:113], v[160:163], v[204:207], v[110:113]
	v_mfma_f32_16x16x32_bf16 v[106:109], v[176:179], v[204:207], v[106:109]
	v_mfma_f32_16x16x32_bf16 v[94:97], v[160:163], v[218:221], v[94:97]
	v_mfma_f32_16x16x32_bf16 v[90:93], v[176:179], v[218:221], v[90:93]
	v_mfma_f32_16x16x32_bf16 v[78:81], v[160:163], v[226:229], v[78:81]
	v_mfma_f32_16x16x32_bf16 v[74:77], v[176:179], v[226:229], v[74:77]
	v_mfma_f32_16x16x32_bf16 v[118:121], v[172:175], v[192:195], v[118:121]
	v_mfma_f32_16x16x32_bf16 v[114:117], v[184:187], v[192:195], v[114:117]
	v_mfma_f32_16x16x32_bf16 v[102:105], v[172:175], v[200:203], v[102:105]
	v_mfma_f32_16x16x32_bf16 v[98:101], v[184:187], v[200:203], v[98:101]
	v_mfma_f32_16x16x32_bf16 v[86:89], v[172:175], v[214:217], v[86:89]
	v_mfma_f32_16x16x32_bf16 v[82:85], v[184:187], v[214:217], v[82:85]
	v_mfma_f32_16x16x32_bf16 v[70:73], v[172:175], v[222:225], v[70:73]
	v_mfma_f32_16x16x32_bf16 v[66:69], v[184:187], v[222:225], v[66:69]
	v_mfma_f32_16x16x32_bf16 v[118:121], v[180:183], v[196:199], v[118:121]
	v_mfma_f32_16x16x32_bf16 v[114:117], v[188:191], v[196:199], v[114:117]
	v_mfma_f32_16x16x32_bf16 v[102:105], v[180:183], v[204:207], v[102:105]
	v_mfma_f32_16x16x32_bf16 v[98:101], v[188:191], v[204:207], v[98:101]
	v_mfma_f32_16x16x32_bf16 v[86:89], v[180:183], v[218:221], v[86:89]
	v_mfma_f32_16x16x32_bf16 v[82:85], v[188:191], v[218:221], v[82:85]
	v_mfma_f32_16x16x32_bf16 v[70:73], v[180:183], v[226:229], v[70:73]
	v_mfma_f32_16x16x32_bf16 v[66:69], v[188:191], v[226:229], v[66:69]
	s_setprio 0
	s_barrier
	s_mov_b32 m0, s23
	v_add_u32_e32 v159, s73, v134
	ds_read_b128 v[192:195], v158 offset:16384
	ds_read_b128 v[196:199], v158 offset:17408
	ds_read_b128 v[200:203], v158 offset:18432
	ds_read_b128 v[204:207], v158 offset:19456
	ds_read_b128 v[214:217], v158 offset:20480
	ds_read_b128 v[218:221], v158 offset:21504
	ds_read_b128 v[222:225], v158 offset:22528
	ds_read_b128 v[226:229], v158 offset:23552
	global_load_lds_dwordx4 v159, s[20:21]
	v_add_u32_e32 v159, s17, v159
	s_mov_b32 m0, s28
	s_nop 0
	global_load_lds_dwordx4 v159, s[20:21]
	v_add_u32_e32 v159, s73, v135
	s_mov_b32 m0, s29
	s_nop 0
	global_load_lds_dwordx4 v159, s[20:21]
	v_add_u32_e32 v159, s17, v159
	s_mov_b32 m0, s30
	s_nop 0
	global_load_lds_dwordx4 v159, s[20:21]
	v_add_u32_e32 v159, s72, v1
	s_mov_b32 m0, s22
	s_nop 0
	global_load_lds_dwordx4 v159, s[4:5]
	v_add_u32_e32 v159, s16, v159
	s_mov_b32 m0, s31
	s_nop 0
	global_load_lds_dwordx4 v159, s[4:5]
	s_waitcnt vmcnt(8)
	s_waitcnt lgkmcnt(0)
	s_barrier
	s_setprio 1
	s_waitcnt lgkmcnt(0)
	v_mfma_f32_16x16x32_bf16 v[62:65], v[168:171], v[192:195], v[62:65]
	v_mfma_f32_16x16x32_bf16 v[58:61], v[164:167], v[192:195], v[58:61]
	v_mfma_f32_16x16x32_bf16 v[46:49], v[168:171], v[200:203], v[46:49]
	v_mfma_f32_16x16x32_bf16 v[42:45], v[164:167], v[200:203], v[42:45]
	v_mfma_f32_16x16x32_bf16 v[30:33], v[168:171], v[214:217], v[30:33]
	v_mfma_f32_16x16x32_bf16 v[26:29], v[164:167], v[214:217], v[26:29]
	v_mfma_f32_16x16x32_bf16 v[14:17], v[168:171], v[222:225], v[14:17]
	v_mfma_f32_16x16x32_bf16 v[10:13], v[164:167], v[222:225], v[10:13]
	v_mfma_f32_16x16x32_bf16 v[62:65], v[160:163], v[196:199], v[62:65]
	v_mfma_f32_16x16x32_bf16 v[58:61], v[176:179], v[196:199], v[58:61]
	v_mfma_f32_16x16x32_bf16 v[46:49], v[160:163], v[204:207], v[46:49]
	v_mfma_f32_16x16x32_bf16 v[42:45], v[176:179], v[204:207], v[42:45]
	v_mfma_f32_16x16x32_bf16 v[30:33], v[160:163], v[218:221], v[30:33]
	v_mfma_f32_16x16x32_bf16 v[26:29], v[176:179], v[218:221], v[26:29]
	v_mfma_f32_16x16x32_bf16 v[14:17], v[160:163], v[226:229], v[14:17]
	v_mfma_f32_16x16x32_bf16 v[10:13], v[176:179], v[226:229], v[10:13]
	v_mfma_f32_16x16x32_bf16 v[54:57], v[172:175], v[192:195], v[54:57]
	v_mfma_f32_16x16x32_bf16 v[50:53], v[184:187], v[192:195], v[50:53]
	v_mfma_f32_16x16x32_bf16 v[38:41], v[172:175], v[200:203], v[38:41]
	v_mfma_f32_16x16x32_bf16 v[34:37], v[184:187], v[200:203], v[34:37]
	v_mfma_f32_16x16x32_bf16 v[22:25], v[172:175], v[214:217], v[22:25]
	v_mfma_f32_16x16x32_bf16 v[18:21], v[184:187], v[214:217], v[18:21]
	v_mfma_f32_16x16x32_bf16 v[6:9], v[172:175], v[222:225], v[6:9]
	v_mfma_f32_16x16x32_bf16 v[2:5], v[184:187], v[222:225], v[2:5]
	v_mfma_f32_16x16x32_bf16 v[54:57], v[180:183], v[196:199], v[54:57]
	v_mfma_f32_16x16x32_bf16 v[50:53], v[188:191], v[196:199], v[50:53]
	v_mfma_f32_16x16x32_bf16 v[38:41], v[180:183], v[204:207], v[38:41]
	v_mfma_f32_16x16x32_bf16 v[34:37], v[188:191], v[204:207], v[34:37]
	v_mfma_f32_16x16x32_bf16 v[22:25], v[180:183], v[218:221], v[22:25]
	v_mfma_f32_16x16x32_bf16 v[18:21], v[188:191], v[218:221], v[18:21]
	v_mfma_f32_16x16x32_bf16 v[6:9], v[180:183], v[226:229], v[6:9]
	v_mfma_f32_16x16x32_bf16 v[2:5], v[188:191], v[226:229], v[2:5]
	s_setprio 0
	s_barrier
.Lmid_0:
	ds_read_b128 v[160:163], v150
	ds_read_b128 v[164:167], v151
	ds_read_b128 v[168:171], v142
	ds_read_b128 v[172:175], v143
	ds_read_b128 v[176:179], v152
	ds_read_b128 v[180:183], v153
	ds_read_b128 v[184:187], v154
	ds_read_b128 v[188:191], v155
	s_mov_b32 m0, s35
	v_add_u32_e32 v159, s72, v136
	ds_read_b128 v[192:195], v158 offset:32768
	ds_read_b128 v[196:199], v158 offset:33792
	ds_read_b128 v[200:203], v158 offset:34816
	ds_read_b128 v[204:207], v158 offset:35840
	ds_read_b128 v[214:217], v158 offset:36864
	ds_read_b128 v[218:221], v158 offset:37888
	ds_read_b128 v[222:225], v158 offset:38912
	ds_read_b128 v[226:229], v158 offset:39936
	global_load_lds_dwordx4 v159, s[4:5]
	v_add_u32_e32 v159, s16, v159
	s_mov_b32 m0, s44
	s_nop 0
	global_load_lds_dwordx4 v159, s[4:5]
	s_waitcnt vmcnt(8)
	s_waitcnt lgkmcnt(0)
	s_barrier
	s_setprio 1
	s_waitcnt lgkmcnt(0)
	v_mfma_f32_16x16x32_bf16 v[122:125], v[168:171], v[192:195], v[122:125]
	v_mfma_f32_16x16x32_bf16 v[126:129], v[164:167], v[192:195], v[126:129]
	v_mfma_f32_16x16x32_bf16 v[110:113], v[168:171], v[200:203], v[110:113]
	v_mfma_f32_16x16x32_bf16 v[106:109], v[164:167], v[200:203], v[106:109]
	v_mfma_f32_16x16x32_bf16 v[94:97], v[168:171], v[214:217], v[94:97]
	v_mfma_f32_16x16x32_bf16 v[90:93], v[164:167], v[214:217], v[90:93]
	v_mfma_f32_16x16x32_bf16 v[78:81], v[168:171], v[222:225], v[78:81]
	v_mfma_f32_16x16x32_bf16 v[74:77], v[164:167], v[222:225], v[74:77]
	v_mfma_f32_16x16x32_bf16 v[122:125], v[160:163], v[196:199], v[122:125]
	v_mfma_f32_16x16x32_bf16 v[126:129], v[176:179], v[196:199], v[126:129]
	v_mfma_f32_16x16x32_bf16 v[110:113], v[160:163], v[204:207], v[110:113]
	v_mfma_f32_16x16x32_bf16 v[106:109], v[176:179], v[204:207], v[106:109]
	v_mfma_f32_16x16x32_bf16 v[94:97], v[160:163], v[218:221], v[94:97]
	v_mfma_f32_16x16x32_bf16 v[90:93], v[176:179], v[218:221], v[90:93]
	v_mfma_f32_16x16x32_bf16 v[78:81], v[160:163], v[226:229], v[78:81]
	v_mfma_f32_16x16x32_bf16 v[74:77], v[176:179], v[226:229], v[74:77]
	v_mfma_f32_16x16x32_bf16 v[118:121], v[172:175], v[192:195], v[118:121]
	v_mfma_f32_16x16x32_bf16 v[114:117], v[184:187], v[192:195], v[114:117]
	v_mfma_f32_16x16x32_bf16 v[102:105], v[172:175], v[200:203], v[102:105]
	v_mfma_f32_16x16x32_bf16 v[98:101], v[184:187], v[200:203], v[98:101]
	v_mfma_f32_16x16x32_bf16 v[86:89], v[172:175], v[214:217], v[86:89]
	v_mfma_f32_16x16x32_bf16 v[82:85], v[184:187], v[214:217], v[82:85]
	v_mfma_f32_16x16x32_bf16 v[70:73], v[172:175], v[222:225], v[70:73]
	v_mfma_f32_16x16x32_bf16 v[66:69], v[184:187], v[222:225], v[66:69]
	v_mfma_f32_16x16x32_bf16 v[118:121], v[180:183], v[196:199], v[118:121]
	v_mfma_f32_16x16x32_bf16 v[114:117], v[188:191], v[196:199], v[114:117]
	v_mfma_f32_16x16x32_bf16 v[102:105], v[180:183], v[204:207], v[102:105]
	v_mfma_f32_16x16x32_bf16 v[98:101], v[188:191], v[204:207], v[98:101]
	v_mfma_f32_16x16x32_bf16 v[86:89], v[180:183], v[218:221], v[86:89]
	v_mfma_f32_16x16x32_bf16 v[82:85], v[188:191], v[218:221], v[82:85]
	v_mfma_f32_16x16x32_bf16 v[70:73], v[180:183], v[226:229], v[70:73]
	v_mfma_f32_16x16x32_bf16 v[66:69], v[188:191], v[226:229], v[66:69]
	s_setprio 0
	s_barrier
	s_addk_i32 s73, 0x80
	s_mov_b32 m0, s46
	v_add_u32_e32 v159, s73, v134
	ds_read_b128 v[192:195], v158 offset:49152
	ds_read_b128 v[196:199], v158 offset:50176
	ds_read_b128 v[200:203], v158 offset:51200
	ds_read_b128 v[204:207], v158 offset:52224
	ds_read_b128 v[214:217], v158 offset:53248
	ds_read_b128 v[218:221], v158 offset:54272
	ds_read_b128 v[222:225], v158 offset:55296
	ds_read_b128 v[226:229], v158 offset:56320
	global_load_lds_dwordx4 v159, s[20:21]
	v_add_u32_e32 v159, s17, v159
	s_mov_b32 m0, s47
	s_nop 0
	global_load_lds_dwordx4 v159, s[20:21]
	v_add_u32_e32 v159, s73, v135
	s_mov_b32 m0, s50
	s_nop 0
	global_load_lds_dwordx4 v159, s[20:21]
	v_add_u32_e32 v159, s17, v159
	s_mov_b32 m0, s51
	s_nop 0
	global_load_lds_dwordx4 v159, s[20:21]
	v_add_u32_e32 v159, s72, v137
	s_mov_b32 m0, s48
	s_nop 0
	global_load_lds_dwordx4 v159, s[4:5]
	v_add_u32_e32 v159, s16, v159
	s_mov_b32 m0, s49
	s_nop 0
	global_load_lds_dwordx4 v159, s[4:5]
	s_waitcnt vmcnt(8)
	s_waitcnt lgkmcnt(0)
	s_barrier
	s_setprio 1
	s_waitcnt lgkmcnt(0)
	v_mfma_f32_16x16x32_bf16 v[62:65], v[168:171], v[192:195], v[62:65]
	v_mfma_f32_16x16x32_bf16 v[58:61], v[164:167], v[192:195], v[58:61]
	v_mfma_f32_16x16x32_bf16 v[46:49], v[168:171], v[200:203], v[46:49]
	v_mfma_f32_16x16x32_bf16 v[42:45], v[164:167], v[200:203], v[42:45]
	v_mfma_f32_16x16x32_bf16 v[30:33], v[168:171], v[214:217], v[30:33]
	v_mfma_f32_16x16x32_bf16 v[26:29], v[164:167], v[214:217], v[26:29]
	v_mfma_f32_16x16x32_bf16 v[14:17], v[168:171], v[222:225], v[14:17]
	v_mfma_f32_16x16x32_bf16 v[10:13], v[164:167], v[222:225], v[10:13]
	v_mfma_f32_16x16x32_bf16 v[62:65], v[160:163], v[196:199], v[62:65]
	v_mfma_f32_16x16x32_bf16 v[58:61], v[176:179], v[196:199], v[58:61]
	v_mfma_f32_16x16x32_bf16 v[46:49], v[160:163], v[204:207], v[46:49]
	v_mfma_f32_16x16x32_bf16 v[42:45], v[176:179], v[204:207], v[42:45]
	v_mfma_f32_16x16x32_bf16 v[30:33], v[160:163], v[218:221], v[30:33]
	v_mfma_f32_16x16x32_bf16 v[26:29], v[176:179], v[218:221], v[26:29]
	v_mfma_f32_16x16x32_bf16 v[14:17], v[160:163], v[226:229], v[14:17]
	v_mfma_f32_16x16x32_bf16 v[10:13], v[176:179], v[226:229], v[10:13]
	v_mfma_f32_16x16x32_bf16 v[54:57], v[172:175], v[192:195], v[54:57]
	v_mfma_f32_16x16x32_bf16 v[50:53], v[184:187], v[192:195], v[50:53]
	v_mfma_f32_16x16x32_bf16 v[38:41], v[172:175], v[200:203], v[38:41]
	v_mfma_f32_16x16x32_bf16 v[34:37], v[184:187], v[200:203], v[34:37]
	v_mfma_f32_16x16x32_bf16 v[22:25], v[172:175], v[214:217], v[22:25]
	v_mfma_f32_16x16x32_bf16 v[18:21], v[184:187], v[214:217], v[18:21]
	v_mfma_f32_16x16x32_bf16 v[6:9], v[172:175], v[222:225], v[6:9]
	v_mfma_f32_16x16x32_bf16 v[2:5], v[184:187], v[222:225], v[2:5]
	v_mfma_f32_16x16x32_bf16 v[54:57], v[180:183], v[196:199], v[54:57]
	v_mfma_f32_16x16x32_bf16 v[50:53], v[188:191], v[196:199], v[50:53]
	v_mfma_f32_16x16x32_bf16 v[38:41], v[180:183], v[204:207], v[38:41]
	v_mfma_f32_16x16x32_bf16 v[34:37], v[188:191], v[204:207], v[34:37]
	v_mfma_f32_16x16x32_bf16 v[22:25], v[180:183], v[218:221], v[22:25]
	v_mfma_f32_16x16x32_bf16 v[18:21], v[188:191], v[218:221], v[18:21]
	v_mfma_f32_16x16x32_bf16 v[6:9], v[180:183], v[226:229], v[6:9]
	v_mfma_f32_16x16x32_bf16 v[2:5], v[188:191], v[226:229], v[2:5]
	s_setprio 0
	s_barrier
	s_add_i32 s71, s71, 2
	s_addk_i32 s14, 0x100
	s_addk_i32 s70, 0x100
	s_cmp_ge_i32 s71, s52
	s_cbranch_scc0 .LBB0_296

.LBB0_584:
	ds_read_b128 v[54:57], v46
	ds_read_b128 v[58:61], v48
	s_add_i32 s67, s22, 0x80
	s_cmp_eq_u32 s58, s66
	s_cselect_b32 s68, s23, s65
	s_cselect_b32 s67, s21, s67
	v_add_u32_e32 v38, s22, v51
	s_add_i32 m0, s29, 0xc000
	ds_read_b128 v[62:65], v52
	ds_read_b128 v[66:69], v52 offset:1024
	ds_read_b128 v[70:73], v52 offset:2048
	ds_read_b128 v[74:77], v52 offset:3072
	ds_read_b128 v[78:81], v52 offset:4096
	ds_read_b128 v[82:85], v52 offset:5120
	ds_read_b128 v[86:89], v52 offset:6144
	ds_read_b128 v[90:93], v52 offset:7168
	global_load_lds_dwordx4 v38, s[4:5]
	v_add_u32_e32 v38, s22, v50
	s_add_i32 m0, s29, 0xe000
	s_nop 0
	global_load_lds_dwordx4 v38, s[4:5]
	s_waitcnt vmcnt(8)
	s_waitcnt lgkmcnt(0)
	s_barrier
	s_setprio 1
	s_waitcnt lgkmcnt(0)
	v_mfma_f32_16x16x32_bf16 v[26:29], v[54:57], v[62:65], v[26:29]
	v_mfma_f32_16x16x32_bf16 v[30:33], v[54:57], v[70:73], v[30:33]
	v_mfma_f32_16x16x32_bf16 v[22:25], v[54:57], v[78:81], v[22:25]
	v_mfma_f32_16x16x32_bf16 v[18:21], v[54:57], v[86:89], v[18:21]
	v_mfma_f32_16x16x32_bf16 v[26:29], v[58:61], v[66:69], v[26:29]
	v_mfma_f32_16x16x32_bf16 v[30:33], v[58:61], v[74:77], v[30:33]
	v_mfma_f32_16x16x32_bf16 v[22:25], v[58:61], v[82:85], v[22:25]
	v_mfma_f32_16x16x32_bf16 v[18:21], v[58:61], v[90:93], v[18:21]
	s_setprio 0
	s_barrier
	s_mov_b32 m0, s30
	v_add_u32_e32 v38, s68, v40
	ds_read_b128 v[62:65], v52 offset:16384
	ds_read_b128 v[66:69], v52 offset:17408
	ds_read_b128 v[70:73], v52 offset:18432
	ds_read_b128 v[74:77], v52 offset:19456
	ds_read_b128 v[78:81], v52 offset:20480
	ds_read_b128 v[82:85], v52 offset:21504
	ds_read_b128 v[86:89], v52 offset:22528
	ds_read_b128 v[90:93], v52 offset:23552
	global_load_lds_dwordx4 v38, s[6:7]
	v_add_u32_e32 v38, s28, v38
	s_mov_b32 m0, s31
	s_nop 0
	global_load_lds_dwordx4 v38, s[6:7]
	v_add_u32_e32 v38, s68, v41
	s_mov_b32 m0, s35
	s_nop 0
	global_load_lds_dwordx4 v38, s[6:7]
	v_add_u32_e32 v38, s28, v38
	s_mov_b32 m0, s44
	s_nop 0
	global_load_lds_dwordx4 v38, s[6:7]
	v_add_u32_e32 v38, s67, v1
	s_mov_b32 m0, s29
	s_nop 0
	global_load_lds_dwordx4 v38, s[4:5]
	v_add_u32_e32 v38, s25, v38
	s_mov_b32 m0, s45
	s_nop 0
	global_load_lds_dwordx4 v38, s[4:5]
	s_waitcnt vmcnt(8)
	s_waitcnt lgkmcnt(0)
	s_barrier
	s_setprio 1
	s_waitcnt lgkmcnt(0)
	v_mfma_f32_16x16x32_bf16 v[14:17], v[54:57], v[62:65], v[14:17]
	v_mfma_f32_16x16x32_bf16 v[10:13], v[54:57], v[70:73], v[10:13]
	v_mfma_f32_16x16x32_bf16 v[6:9], v[54:57], v[78:81], v[6:9]
	v_mfma_f32_16x16x32_bf16 v[2:5], v[54:57], v[86:89], v[2:5]
	v_mfma_f32_16x16x32_bf16 v[14:17], v[58:61], v[66:69], v[14:17]
	v_mfma_f32_16x16x32_bf16 v[10:13], v[58:61], v[74:77], v[10:13]
	v_mfma_f32_16x16x32_bf16 v[6:9], v[58:61], v[82:85], v[6:9]
	v_mfma_f32_16x16x32_bf16 v[2:5], v[58:61], v[90:93], v[2:5]
	s_setprio 0
	s_barrier
	ds_read_b128 v[54:57], v47
	ds_read_b128 v[58:61], v49
	s_mov_b32 m0, s46
	v_add_u32_e32 v38, s67, v42
	ds_read_b128 v[62:65], v52 offset:32768
	ds_read_b128 v[66:69], v52 offset:33792
	ds_read_b128 v[70:73], v52 offset:34816
	ds_read_b128 v[74:77], v52 offset:35840
	ds_read_b128 v[78:81], v52 offset:36864
	ds_read_b128 v[82:85], v52 offset:37888
	ds_read_b128 v[86:89], v52 offset:38912
	ds_read_b128 v[90:93], v52 offset:39936
	global_load_lds_dwordx4 v38, s[4:5]
	v_add_u32_e32 v38, s25, v38
	s_mov_b32 m0, s47
	s_nop 0
	global_load_lds_dwordx4 v38, s[4:5]
	s_waitcnt vmcnt(8)
	s_waitcnt lgkmcnt(0)
	s_barrier
	s_setprio 1
	s_waitcnt lgkmcnt(0)
	v_mfma_f32_16x16x32_bf16 v[26:29], v[54:57], v[62:65], v[26:29]
	v_mfma_f32_16x16x32_bf16 v[30:33], v[54:57], v[70:73], v[30:33]
	v_mfma_f32_16x16x32_bf16 v[22:25], v[54:57], v[78:81], v[22:25]
	v_mfma_f32_16x16x32_bf16 v[18:21], v[54:57], v[86:89], v[18:21]
	v_mfma_f32_16x16x32_bf16 v[26:29], v[58:61], v[66:69], v[26:29]
	v_mfma_f32_16x16x32_bf16 v[30:33], v[58:61], v[74:77], v[30:33]
	v_mfma_f32_16x16x32_bf16 v[22:25], v[58:61], v[82:85], v[22:25]
	v_mfma_f32_16x16x32_bf16 v[18:21], v[58:61], v[90:93], v[18:21]
	s_setprio 0
	s_barrier
	s_addk_i32 s68, 0x80
	s_mov_b32 m0, s50
	v_add_u32_e32 v38, s68, v40
	ds_read_b128 v[62:65], v52 offset:49152
	ds_read_b128 v[66:69], v52 offset:50176
	ds_read_b128 v[70:73], v52 offset:51200
	ds_read_b128 v[74:77], v52 offset:52224
	ds_read_b128 v[78:81], v52 offset:53248
	ds_read_b128 v[82:85], v52 offset:54272
	ds_read_b128 v[86:89], v52 offset:55296
	ds_read_b128 v[90:93], v52 offset:56320
	global_load_lds_dwordx4 v38, s[6:7]
	v_add_u32_e32 v38, s28, v38
	s_mov_b32 m0, s51
	s_nop 0
	global_load_lds_dwordx4 v38, s[6:7]
	v_add_u32_e32 v38, s68, v41
	s_mov_b32 m0, s54
	s_nop 0
	global_load_lds_dwordx4 v38, s[6:7]
	v_add_u32_e32 v38, s28, v38
	s_mov_b32 m0, s55
	s_nop 0
	global_load_lds_dwordx4 v38, s[6:7]
	v_add_u32_e32 v38, s67, v43
	s_mov_b32 m0, s52
	s_nop 0
	global_load_lds_dwordx4 v38, s[4:5]
	v_add_u32_e32 v38, s25, v38
	s_mov_b32 m0, s53
	s_nop 0
	global_load_lds_dwordx4 v38, s[4:5]
	s_waitcnt vmcnt(8)
	s_waitcnt lgkmcnt(0)
	s_barrier
	s_setprio 1
	s_waitcnt lgkmcnt(0)
	v_mfma_f32_16x16x32_bf16 v[14:17], v[54:57], v[62:65], v[14:17]
	v_mfma_f32_16x16x32_bf16 v[10:13], v[54:57], v[70:73], v[10:13]
	v_mfma_f32_16x16x32_bf16 v[6:9], v[54:57], v[78:81], v[6:9]
	v_mfma_f32_16x16x32_bf16 v[2:5], v[54:57], v[86:89], v[2:5]
	v_mfma_f32_16x16x32_bf16 v[14:17], v[58:61], v[66:69], v[14:17]
	v_mfma_f32_16x16x32_bf16 v[10:13], v[58:61], v[74:77], v[10:13]
	v_mfma_f32_16x16x32_bf16 v[6:9], v[58:61], v[82:85], v[6:9]
	v_mfma_f32_16x16x32_bf16 v[2:5], v[58:61], v[90:93], v[2:5]
	s_setprio 0
	s_barrier
	s_add_i32 s66, s66, 2
	s_addk_i32 s22, 0x100
	s_addk_i32 s65, 0x100
	s_cmp_ge_i32 s66, s56
	s_cbranch_scc0 .LBB0_584

.LBB0_601:
	s_andn2_b64 vcc, exec, s[10:11]
	s_cbranch_vccnz .Lzs_1
	s_add_i32 s16, s74, 0x80
	s_addk_i32 s73, 0x100
	s_mov_b32 s74, 0
	ds_read_b128 v[164:167], v147
	ds_read_b128 v[168:171], v148
	ds_read_b128 v[172:175], v143
	ds_read_b128 v[176:179], v144
	ds_read_b128 v[180:183], v149
	ds_read_b128 v[184:187], v150
	ds_read_b128 v[188:191], v151
	ds_read_b128 v[192:195], v152
	s_add_i32 s75, s16, 0x80
	s_cmp_eq_u32 s59, s74
	s_cselect_b32 s76, s17, s73
	s_cselect_b32 s75, s72, s75
	v_add_u32_e32 v134, s16, v160
	s_add_i32 m0, s28, 0xc000
	ds_read_b128 v[196:199], v161
	ds_read_b128 v[200:203], v161 offset:1024
	ds_read_b128 v[204:207], v161 offset:2048
	ds_read_b128 v[214:217], v161 offset:3072
	ds_read_b128 v[218:221], v161 offset:4096
	ds_read_b128 v[222:225], v161 offset:5120
	ds_read_b128 v[226:229], v161 offset:6144
	ds_read_b128 v[230:233], v161 offset:7168
	global_load_lds_dwordx4 v134, s[4:5]
	v_add_u32_e32 v134, s16, v159
	s_add_i32 m0, s28, 0xe000
	s_nop 0
	global_load_lds_dwordx4 v134, s[4:5]
	s_waitcnt vmcnt(8)
	s_waitcnt lgkmcnt(0)
	s_barrier
	s_setprio 1
	s_waitcnt lgkmcnt(0)
	v_mfma_f32_16x16x32_bf16 v[126:129], v[172:175], v[196:199], 0
	v_mfma_f32_16x16x32_bf16 v[122:125], v[168:171], v[196:199], 0
	v_mfma_f32_16x16x32_bf16 v[110:113], v[172:175], v[204:207], 0
	v_mfma_f32_16x16x32_bf16 v[106:109], v[168:171], v[204:207], 0
	v_mfma_f32_16x16x32_bf16 v[94:97], v[172:175], v[218:221], 0
	v_mfma_f32_16x16x32_bf16 v[90:93], v[168:171], v[218:221], 0
	v_mfma_f32_16x16x32_bf16 v[78:81], v[172:175], v[226:229], 0
	v_mfma_f32_16x16x32_bf16 v[74:77], v[168:171], v[226:229], 0
	v_mfma_f32_16x16x32_bf16 v[126:129], v[164:167], v[200:203], v[126:129]
	v_mfma_f32_16x16x32_bf16 v[122:125], v[180:183], v[200:203], v[122:125]
	v_mfma_f32_16x16x32_bf16 v[110:113], v[164:167], v[214:217], v[110:113]
	v_mfma_f32_16x16x32_bf16 v[106:109], v[180:183], v[214:217], v[106:109]
	v_mfma_f32_16x16x32_bf16 v[94:97], v[164:167], v[222:225], v[94:97]
	v_mfma_f32_16x16x32_bf16 v[90:93], v[180:183], v[222:225], v[90:93]
	v_mfma_f32_16x16x32_bf16 v[78:81], v[164:167], v[230:233], v[78:81]
	v_mfma_f32_16x16x32_bf16 v[74:77], v[180:183], v[230:233], v[74:77]
	v_mfma_f32_16x16x32_bf16 v[118:121], v[176:179], v[196:199], 0
	v_mfma_f32_16x16x32_bf16 v[114:117], v[188:191], v[196:199], 0
	v_mfma_f32_16x16x32_bf16 v[102:105], v[176:179], v[204:207], 0
	v_mfma_f32_16x16x32_bf16 v[98:101], v[188:191], v[204:207], 0
	v_mfma_f32_16x16x32_bf16 v[86:89], v[176:179], v[218:221], 0
	v_mfma_f32_16x16x32_bf16 v[82:85], v[188:191], v[218:221], 0
	v_mfma_f32_16x16x32_bf16 v[70:73], v[176:179], v[226:229], 0
	v_mfma_f32_16x16x32_bf16 v[66:69], v[188:191], v[226:229], 0
	v_mfma_f32_16x16x32_bf16 v[118:121], v[184:187], v[200:203], v[118:121]
	v_mfma_f32_16x16x32_bf16 v[114:117], v[192:195], v[200:203], v[114:117]
	v_mfma_f32_16x16x32_bf16 v[102:105], v[184:187], v[214:217], v[102:105]
	v_mfma_f32_16x16x32_bf16 v[98:101], v[192:195], v[214:217], v[98:101]
	v_mfma_f32_16x16x32_bf16 v[86:89], v[184:187], v[222:225], v[86:89]
	v_mfma_f32_16x16x32_bf16 v[82:85], v[192:195], v[222:225], v[82:85]
	v_mfma_f32_16x16x32_bf16 v[70:73], v[184:187], v[230:233], v[70:73]
	v_mfma_f32_16x16x32_bf16 v[66:69], v[192:195], v[230:233], v[66:69]
	s_setprio 0
	s_barrier
	s_mov_b32 m0, s29
	v_add_u32_e32 v134, s76, v135
	ds_read_b128 v[196:199], v161 offset:16384
	ds_read_b128 v[200:203], v161 offset:17408
	ds_read_b128 v[204:207], v161 offset:18432
	ds_read_b128 v[214:217], v161 offset:19456
	ds_read_b128 v[218:221], v161 offset:20480
	ds_read_b128 v[222:225], v161 offset:21504
	ds_read_b128 v[226:229], v161 offset:22528
	ds_read_b128 v[230:233], v161 offset:23552
	global_load_lds_dwordx4 v134, s[6:7]
	v_add_u32_e32 v134, s23, v134
	s_mov_b32 m0, s30
	s_nop 0
	global_load_lds_dwordx4 v134, s[6:7]
	v_add_u32_e32 v134, s76, v138
	s_mov_b32 m0, s31
	s_nop 0
	global_load_lds_dwordx4 v134, s[6:7]
	v_add_u32_e32 v134, s23, v134
	s_mov_b32 m0, s35
	s_nop 0
	global_load_lds_dwordx4 v134, s[6:7]
	v_add_u32_e32 v134, s75, v1
	s_mov_b32 m0, s28
	s_nop 0
	global_load_lds_dwordx4 v134, s[4:5]
	v_add_u32_e32 v134, s22, v134
	s_mov_b32 m0, s44
	s_nop 0
	global_load_lds_dwordx4 v134, s[4:5]
	s_waitcnt vmcnt(8)
	s_waitcnt lgkmcnt(0)
	s_barrier
	s_setprio 1
	s_waitcnt lgkmcnt(0)
	v_mfma_f32_16x16x32_bf16 v[62:65], v[172:175], v[196:199], 0
	v_mfma_f32_16x16x32_bf16 v[58:61], v[168:171], v[196:199], 0
	v_mfma_f32_16x16x32_bf16 v[46:49], v[172:175], v[204:207], 0
	v_mfma_f32_16x16x32_bf16 v[42:45], v[168:171], v[204:207], 0
	v_mfma_f32_16x16x32_bf16 v[30:33], v[172:175], v[218:221], 0
	v_mfma_f32_16x16x32_bf16 v[26:29], v[168:171], v[218:221], 0
	v_mfma_f32_16x16x32_bf16 v[14:17], v[172:175], v[226:229], 0
	v_mfma_f32_16x16x32_bf16 v[10:13], v[168:171], v[226:229], 0
	v_mfma_f32_16x16x32_bf16 v[62:65], v[164:167], v[200:203], v[62:65]
	v_mfma_f32_16x16x32_bf16 v[58:61], v[180:183], v[200:203], v[58:61]
	v_mfma_f32_16x16x32_bf16 v[46:49], v[164:167], v[214:217], v[46:49]
	v_mfma_f32_16x16x32_bf16 v[42:45], v[180:183], v[214:217], v[42:45]
	v_mfma_f32_16x16x32_bf16 v[30:33], v[164:167], v[222:225], v[30:33]
	v_mfma_f32_16x16x32_bf16 v[26:29], v[180:183], v[222:225], v[26:29]
	v_mfma_f32_16x16x32_bf16 v[14:17], v[164:167], v[230:233], v[14:17]
	v_mfma_f32_16x16x32_bf16 v[10:13], v[180:183], v[230:233], v[10:13]
	v_mfma_f32_16x16x32_bf16 v[54:57], v[176:179], v[196:199], 0
	v_mfma_f32_16x16x32_bf16 v[50:53], v[188:191], v[196:199], 0
	v_mfma_f32_16x16x32_bf16 v[38:41], v[176:179], v[204:207], 0
	v_mfma_f32_16x16x32_bf16 v[34:37], v[188:191], v[204:207], 0
	v_mfma_f32_16x16x32_bf16 v[22:25], v[176:179], v[218:221], 0
	v_mfma_f32_16x16x32_bf16 v[18:21], v[188:191], v[218:221], 0
	v_mfma_f32_16x16x32_bf16 v[6:9], v[176:179], v[226:229], 0
	v_mfma_f32_16x16x32_bf16 v[2:5], v[188:191], v[226:229], 0
	v_mfma_f32_16x16x32_bf16 v[54:57], v[184:187], v[200:203], v[54:57]
	v_mfma_f32_16x16x32_bf16 v[50:53], v[192:195], v[200:203], v[50:53]
	v_mfma_f32_16x16x32_bf16 v[38:41], v[184:187], v[214:217], v[38:41]
	v_mfma_f32_16x16x32_bf16 v[34:37], v[192:195], v[214:217], v[34:37]
	v_mfma_f32_16x16x32_bf16 v[22:25], v[184:187], v[222:225], v[22:25]
	v_mfma_f32_16x16x32_bf16 v[18:21], v[192:195], v[222:225], v[18:21]
	v_mfma_f32_16x16x32_bf16 v[6:9], v[184:187], v[230:233], v[6:9]
	v_mfma_f32_16x16x32_bf16 v[2:5], v[192:195], v[230:233], v[2:5]
	s_setprio 0
	s_barrier
	s_branch .Lmid_1
.LBB0_603:
	ds_read_b128 v[164:167], v147
	ds_read_b128 v[168:171], v148
	ds_read_b128 v[172:175], v143
	ds_read_b128 v[176:179], v144
	ds_read_b128 v[180:183], v149
	ds_read_b128 v[184:187], v150
	ds_read_b128 v[188:191], v151
	ds_read_b128 v[192:195], v152
	s_add_i32 s75, s16, 0x80
	s_cmp_eq_u32 s59, s74
	s_cselect_b32 s76, s17, s73
	s_cselect_b32 s75, s72, s75
	v_add_u32_e32 v134, s16, v160
	s_add_i32 m0, s28, 0xc000
	ds_read_b128 v[196:199], v161
	ds_read_b128 v[200:203], v161 offset:1024
	ds_read_b128 v[204:207], v161 offset:2048
	ds_read_b128 v[214:217], v161 offset:3072
	ds_read_b128 v[218:221], v161 offset:4096
	ds_read_b128 v[222:225], v161 offset:5120
	ds_read_b128 v[226:229], v161 offset:6144
	ds_read_b128 v[230:233], v161 offset:7168
	global_load_lds_dwordx4 v134, s[4:5]
	v_add_u32_e32 v134, s16, v159
	s_add_i32 m0, s28, 0xe000
	s_nop 0
	global_load_lds_dwordx4 v134, s[4:5]
	s_waitcnt vmcnt(8)
	s_waitcnt lgkmcnt(0)
	s_barrier
	s_setprio 1
	s_waitcnt lgkmcnt(0)
	v_mfma_f32_16x16x32_bf16 v[126:129], v[172:175], v[196:199], v[126:129]
	v_mfma_f32_16x16x32_bf16 v[122:125], v[168:171], v[196:199], v[122:125]
	v_mfma_f32_16x16x32_bf16 v[110:113], v[172:175], v[204:207], v[110:113]
	v_mfma_f32_16x16x32_bf16 v[106:109], v[168:171], v[204:207], v[106:109]
	v_mfma_f32_16x16x32_bf16 v[94:97], v[172:175], v[218:221], v[94:97]
	v_mfma_f32_16x16x32_bf16 v[90:93], v[168:171], v[218:221], v[90:93]
	v_mfma_f32_16x16x32_bf16 v[78:81], v[172:175], v[226:229], v[78:81]
	v_mfma_f32_16x16x32_bf16 v[74:77], v[168:171], v[226:229], v[74:77]
	v_mfma_f32_16x16x32_bf16 v[126:129], v[164:167], v[200:203], v[126:129]
	v_mfma_f32_16x16x32_bf16 v[122:125], v[180:183], v[200:203], v[122:125]
	v_mfma_f32_16x16x32_bf16 v[110:113], v[164:167], v[214:217], v[110:113]
	v_mfma_f32_16x16x32_bf16 v[106:109], v[180:183], v[214:217], v[106:109]
	v_mfma_f32_16x16x32_bf16 v[94:97], v[164:167], v[222:225], v[94:97]
	v_mfma_f32_16x16x32_bf16 v[90:93], v[180:183], v[222:225], v[90:93]
	v_mfma_f32_16x16x32_bf16 v[78:81], v[164:167], v[230:233], v[78:81]
	v_mfma_f32_16x16x32_bf16 v[74:77], v[180:183], v[230:233], v[74:77]
	v_mfma_f32_16x16x32_bf16 v[118:121], v[176:179], v[196:199], v[118:121]
	v_mfma_f32_16x16x32_bf16 v[114:117], v[188:191], v[196:199], v[114:117]
	v_mfma_f32_16x16x32_bf16 v[102:105], v[176:179], v[204:207], v[102:105]
	v_mfma_f32_16x16x32_bf16 v[98:101], v[188:191], v[204:207], v[98:101]
	v_mfma_f32_16x16x32_bf16 v[86:89], v[176:179], v[218:221], v[86:89]
	v_mfma_f32_16x16x32_bf16 v[82:85], v[188:191], v[218:221], v[82:85]
	v_mfma_f32_16x16x32_bf16 v[70:73], v[176:179], v[226:229], v[70:73]
	v_mfma_f32_16x16x32_bf16 v[66:69], v[188:191], v[226:229], v[66:69]
	v_mfma_f32_16x16x32_bf16 v[118:121], v[184:187], v[200:203], v[118:121]
	v_mfma_f32_16x16x32_bf16 v[114:117], v[192:195], v[200:203], v[114:117]
	v_mfma_f32_16x16x32_bf16 v[102:105], v[184:187], v[214:217], v[102:105]
	v_mfma_f32_16x16x32_bf16 v[98:101], v[192:195], v[214:217], v[98:101]
	v_mfma_f32_16x16x32_bf16 v[86:89], v[184:187], v[222:225], v[86:89]
	v_mfma_f32_16x16x32_bf16 v[82:85], v[192:195], v[222:225], v[82:85]
	v_mfma_f32_16x16x32_bf16 v[70:73], v[184:187], v[230:233], v[70:73]
	v_mfma_f32_16x16x32_bf16 v[66:69], v[192:195], v[230:233], v[66:69]
	s_setprio 0
	s_barrier
	s_mov_b32 m0, s29
	v_add_u32_e32 v134, s76, v135
	ds_read_b128 v[196:199], v161 offset:16384
	ds_read_b128 v[200:203], v161 offset:17408
	ds_read_b128 v[204:207], v161 offset:18432
	ds_read_b128 v[214:217], v161 offset:19456
	ds_read_b128 v[218:221], v161 offset:20480
	ds_read_b128 v[222:225], v161 offset:21504
	ds_read_b128 v[226:229], v161 offset:22528
	ds_read_b128 v[230:233], v161 offset:23552
	global_load_lds_dwordx4 v134, s[6:7]
	v_add_u32_e32 v134, s23, v134
	s_mov_b32 m0, s30
	s_nop 0
	global_load_lds_dwordx4 v134, s[6:7]
	v_add_u32_e32 v134, s76, v138
	s_mov_b32 m0, s31
	s_nop 0
	global_load_lds_dwordx4 v134, s[6:7]
	v_add_u32_e32 v134, s23, v134
	s_mov_b32 m0, s35
	s_nop 0
	global_load_lds_dwordx4 v134, s[6:7]
	v_add_u32_e32 v134, s75, v1
	s_mov_b32 m0, s28
	s_nop 0
	global_load_lds_dwordx4 v134, s[4:5]
	v_add_u32_e32 v134, s22, v134
	s_mov_b32 m0, s44
	s_nop 0
	global_load_lds_dwordx4 v134, s[4:5]
	s_waitcnt vmcnt(8)
	s_waitcnt lgkmcnt(0)
	s_barrier
	s_setprio 1
	s_waitcnt lgkmcnt(0)
	v_mfma_f32_16x16x32_bf16 v[62:65], v[172:175], v[196:199], v[62:65]
	v_mfma_f32_16x16x32_bf16 v[58:61], v[168:171], v[196:199], v[58:61]
	v_mfma_f32_16x16x32_bf16 v[46:49], v[172:175], v[204:207], v[46:49]
	v_mfma_f32_16x16x32_bf16 v[42:45], v[168:171], v[204:207], v[42:45]
	v_mfma_f32_16x16x32_bf16 v[30:33], v[172:175], v[218:221], v[30:33]
	v_mfma_f32_16x16x32_bf16 v[26:29], v[168:171], v[218:221], v[26:29]
	v_mfma_f32_16x16x32_bf16 v[14:17], v[172:175], v[226:229], v[14:17]
	v_mfma_f32_16x16x32_bf16 v[10:13], v[168:171], v[226:229], v[10:13]
	v_mfma_f32_16x16x32_bf16 v[62:65], v[164:167], v[200:203], v[62:65]
	v_mfma_f32_16x16x32_bf16 v[58:61], v[180:183], v[200:203], v[58:61]
	v_mfma_f32_16x16x32_bf16 v[46:49], v[164:167], v[214:217], v[46:49]
	v_mfma_f32_16x16x32_bf16 v[42:45], v[180:183], v[214:217], v[42:45]
	v_mfma_f32_16x16x32_bf16 v[30:33], v[164:167], v[222:225], v[30:33]
	v_mfma_f32_16x16x32_bf16 v[26:29], v[180:183], v[222:225], v[26:29]
	v_mfma_f32_16x16x32_bf16 v[14:17], v[164:167], v[230:233], v[14:17]
	v_mfma_f32_16x16x32_bf16 v[10:13], v[180:183], v[230:233], v[10:13]
	v_mfma_f32_16x16x32_bf16 v[54:57], v[176:179], v[196:199], v[54:57]
	v_mfma_f32_16x16x32_bf16 v[50:53], v[188:191], v[196:199], v[50:53]
	v_mfma_f32_16x16x32_bf16 v[38:41], v[176:179], v[204:207], v[38:41]
	v_mfma_f32_16x16x32_bf16 v[34:37], v[188:191], v[204:207], v[34:37]
	v_mfma_f32_16x16x32_bf16 v[22:25], v[176:179], v[218:221], v[22:25]
	v_mfma_f32_16x16x32_bf16 v[18:21], v[188:191], v[218:221], v[18:21]
	v_mfma_f32_16x16x32_bf16 v[6:9], v[176:179], v[226:229], v[6:9]
	v_mfma_f32_16x16x32_bf16 v[2:5], v[188:191], v[226:229], v[2:5]
	v_mfma_f32_16x16x32_bf16 v[54:57], v[184:187], v[200:203], v[54:57]
	v_mfma_f32_16x16x32_bf16 v[50:53], v[192:195], v[200:203], v[50:53]
	v_mfma_f32_16x16x32_bf16 v[38:41], v[184:187], v[214:217], v[38:41]
	v_mfma_f32_16x16x32_bf16 v[34:37], v[192:195], v[214:217], v[34:37]
	v_mfma_f32_16x16x32_bf16 v[22:25], v[184:187], v[222:225], v[22:25]
	v_mfma_f32_16x16x32_bf16 v[18:21], v[192:195], v[222:225], v[18:21]
	v_mfma_f32_16x16x32_bf16 v[6:9], v[184:187], v[230:233], v[6:9]
	v_mfma_f32_16x16x32_bf16 v[2:5], v[192:195], v[230:233], v[2:5]
	s_setprio 0
	s_barrier
.Lmid_1:
	ds_read_b128 v[164:167], v153
	ds_read_b128 v[168:171], v154
	ds_read_b128 v[172:175], v145
	ds_read_b128 v[176:179], v146
	ds_read_b128 v[180:183], v155
	ds_read_b128 v[184:187], v156
	ds_read_b128 v[188:191], v157
	ds_read_b128 v[192:195], v158
	s_mov_b32 m0, s45
	v_add_u32_e32 v134, s75, v139
	ds_read_b128 v[196:199], v161 offset:32768
	ds_read_b128 v[200:203], v161 offset:33792
	ds_read_b128 v[204:207], v161 offset:34816
	ds_read_b128 v[214:217], v161 offset:35840
	ds_read_b128 v[218:221], v161 offset:36864
	ds_read_b128 v[222:225], v161 offset:37888
	ds_read_b128 v[226:229], v161 offset:38912
	ds_read_b128 v[230:233], v161 offset:39936
	global_load_lds_dwordx4 v134, s[4:5]
	v_add_u32_e32 v134, s22, v134
	s_mov_b32 m0, s46
	s_nop 0
	global_load_lds_dwordx4 v134, s[4:5]
	s_waitcnt vmcnt(8)
	s_waitcnt lgkmcnt(0)
	s_barrier
	s_setprio 1
	s_waitcnt lgkmcnt(0)
	v_mfma_f32_16x16x32_bf16 v[126:129], v[172:175], v[196:199], v[126:129]
	v_mfma_f32_16x16x32_bf16 v[122:125], v[168:171], v[196:199], v[122:125]
	v_mfma_f32_16x16x32_bf16 v[110:113], v[172:175], v[204:207], v[110:113]
	v_mfma_f32_16x16x32_bf16 v[106:109], v[168:171], v[204:207], v[106:109]
	v_mfma_f32_16x16x32_bf16 v[94:97], v[172:175], v[218:221], v[94:97]
	v_mfma_f32_16x16x32_bf16 v[90:93], v[168:171], v[218:221], v[90:93]
	v_mfma_f32_16x16x32_bf16 v[78:81], v[172:175], v[226:229], v[78:81]
	v_mfma_f32_16x16x32_bf16 v[74:77], v[168:171], v[226:229], v[74:77]
	v_mfma_f32_16x16x32_bf16 v[126:129], v[164:167], v[200:203], v[126:129]
	v_mfma_f32_16x16x32_bf16 v[122:125], v[180:183], v[200:203], v[122:125]
	v_mfma_f32_16x16x32_bf16 v[110:113], v[164:167], v[214:217], v[110:113]
	v_mfma_f32_16x16x32_bf16 v[106:109], v[180:183], v[214:217], v[106:109]
	v_mfma_f32_16x16x32_bf16 v[94:97], v[164:167], v[222:225], v[94:97]
	v_mfma_f32_16x16x32_bf16 v[90:93], v[180:183], v[222:225], v[90:93]
	v_mfma_f32_16x16x32_bf16 v[78:81], v[164:167], v[230:233], v[78:81]
	v_mfma_f32_16x16x32_bf16 v[74:77], v[180:183], v[230:233], v[74:77]
	v_mfma_f32_16x16x32_bf16 v[118:121], v[176:179], v[196:199], v[118:121]
	v_mfma_f32_16x16x32_bf16 v[114:117], v[188:191], v[196:199], v[114:117]
	v_mfma_f32_16x16x32_bf16 v[102:105], v[176:179], v[204:207], v[102:105]
	v_mfma_f32_16x16x32_bf16 v[98:101], v[188:191], v[204:207], v[98:101]
	v_mfma_f32_16x16x32_bf16 v[86:89], v[176:179], v[218:221], v[86:89]
	v_mfma_f32_16x16x32_bf16 v[82:85], v[188:191], v[218:221], v[82:85]
	v_mfma_f32_16x16x32_bf16 v[70:73], v[176:179], v[226:229], v[70:73]
	v_mfma_f32_16x16x32_bf16 v[66:69], v[188:191], v[226:229], v[66:69]
	v_mfma_f32_16x16x32_bf16 v[118:121], v[184:187], v[200:203], v[118:121]
	v_mfma_f32_16x16x32_bf16 v[114:117], v[192:195], v[200:203], v[114:117]
	v_mfma_f32_16x16x32_bf16 v[102:105], v[184:187], v[214:217], v[102:105]
	v_mfma_f32_16x16x32_bf16 v[98:101], v[192:195], v[214:217], v[98:101]
	v_mfma_f32_16x16x32_bf16 v[86:89], v[184:187], v[222:225], v[86:89]
	v_mfma_f32_16x16x32_bf16 v[82:85], v[192:195], v[222:225], v[82:85]
	v_mfma_f32_16x16x32_bf16 v[70:73], v[184:187], v[230:233], v[70:73]
	v_mfma_f32_16x16x32_bf16 v[66:69], v[192:195], v[230:233], v[66:69]
	s_setprio 0
	s_barrier
	s_addk_i32 s76, 0x80
	s_mov_b32 m0, s48
	v_add_u32_e32 v134, s76, v135
	ds_read_b128 v[196:199], v161 offset:49152
	ds_read_b128 v[200:203], v161 offset:50176
	ds_read_b128 v[204:207], v161 offset:51200
	ds_read_b128 v[214:217], v161 offset:52224
	ds_read_b128 v[218:221], v161 offset:53248
	ds_read_b128 v[222:225], v161 offset:54272
	ds_read_b128 v[226:229], v161 offset:55296
	ds_read_b128 v[230:233], v161 offset:56320
	global_load_lds_dwordx4 v134, s[6:7]
	v_add_u32_e32 v134, s23, v134
	s_mov_b32 m0, s49
	s_nop 0
	global_load_lds_dwordx4 v134, s[6:7]
	v_add_u32_e32 v134, s76, v138
	s_mov_b32 m0, s52
	s_nop 0
	global_load_lds_dwordx4 v134, s[6:7]
	v_add_u32_e32 v134, s23, v134
	s_mov_b32 m0, s53
	s_nop 0
	global_load_lds_dwordx4 v134, s[6:7]
	v_add_u32_e32 v134, s75, v140
	s_mov_b32 m0, s50
	s_nop 0
	global_load_lds_dwordx4 v134, s[4:5]
	v_add_u32_e32 v134, s22, v134
	s_mov_b32 m0, s51
	s_nop 0
	global_load_lds_dwordx4 v134, s[4:5]
	s_waitcnt vmcnt(8)
	s_waitcnt lgkmcnt(0)
	s_barrier
	s_setprio 1
	s_waitcnt lgkmcnt(0)
	v_mfma_f32_16x16x32_bf16 v[62:65], v[172:175], v[196:199], v[62:65]
	v_mfma_f32_16x16x32_bf16 v[58:61], v[168:171], v[196:199], v[58:61]
	v_mfma_f32_16x16x32_bf16 v[46:49], v[172:175], v[204:207], v[46:49]
	v_mfma_f32_16x16x32_bf16 v[42:45], v[168:171], v[204:207], v[42:45]
	v_mfma_f32_16x16x32_bf16 v[30:33], v[172:175], v[218:221], v[30:33]
	v_mfma_f32_16x16x32_bf16 v[26:29], v[168:171], v[218:221], v[26:29]
	v_mfma_f32_16x16x32_bf16 v[14:17], v[172:175], v[226:229], v[14:17]
	v_mfma_f32_16x16x32_bf16 v[10:13], v[168:171], v[226:229], v[10:13]
	v_mfma_f32_16x16x32_bf16 v[62:65], v[164:167], v[200:203], v[62:65]
	v_mfma_f32_16x16x32_bf16 v[58:61], v[180:183], v[200:203], v[58:61]
	v_mfma_f32_16x16x32_bf16 v[46:49], v[164:167], v[214:217], v[46:49]
	v_mfma_f32_16x16x32_bf16 v[42:45], v[180:183], v[214:217], v[42:45]
	v_mfma_f32_16x16x32_bf16 v[30:33], v[164:167], v[222:225], v[30:33]
	v_mfma_f32_16x16x32_bf16 v[26:29], v[180:183], v[222:225], v[26:29]
	v_mfma_f32_16x16x32_bf16 v[14:17], v[164:167], v[230:233], v[14:17]
	v_mfma_f32_16x16x32_bf16 v[10:13], v[180:183], v[230:233], v[10:13]
	v_mfma_f32_16x16x32_bf16 v[54:57], v[176:179], v[196:199], v[54:57]
	v_mfma_f32_16x16x32_bf16 v[50:53], v[188:191], v[196:199], v[50:53]
	v_mfma_f32_16x16x32_bf16 v[38:41], v[176:179], v[204:207], v[38:41]
	v_mfma_f32_16x16x32_bf16 v[34:37], v[188:191], v[204:207], v[34:37]
	v_mfma_f32_16x16x32_bf16 v[22:25], v[176:179], v[218:221], v[22:25]
	v_mfma_f32_16x16x32_bf16 v[18:21], v[188:191], v[218:221], v[18:21]
	v_mfma_f32_16x16x32_bf16 v[6:9], v[176:179], v[226:229], v[6:9]
	v_mfma_f32_16x16x32_bf16 v[2:5], v[188:191], v[226:229], v[2:5]
	v_mfma_f32_16x16x32_bf16 v[54:57], v[184:187], v[200:203], v[54:57]
	v_mfma_f32_16x16x32_bf16 v[50:53], v[192:195], v[200:203], v[50:53]
	v_mfma_f32_16x16x32_bf16 v[38:41], v[184:187], v[214:217], v[38:41]
	v_mfma_f32_16x16x32_bf16 v[34:37], v[192:195], v[214:217], v[34:37]
	v_mfma_f32_16x16x32_bf16 v[22:25], v[184:187], v[222:225], v[22:25]
	v_mfma_f32_16x16x32_bf16 v[18:21], v[192:195], v[222:225], v[18:21]
	v_mfma_f32_16x16x32_bf16 v[6:9], v[184:187], v[230:233], v[6:9]
	v_mfma_f32_16x16x32_bf16 v[2:5], v[192:195], v[230:233], v[2:5]
	s_setprio 0
	s_barrier
	s_add_i32 s74, s74, 2
	s_addk_i32 s16, 0x100
	s_addk_i32 s73, 0x100
	s_cmp_ge_i32 s74, s54
	s_cbranch_scc0 .LBB0_603

.LBB0_618:
	s_andn2_b64 vcc, exec, s[10:11]
	s_cbranch_vccnz .Lzs_2
	s_add_i32 s16, s72, 0x80
	s_addk_i32 s71, 0x100
	s_mov_b32 s72, 0
	ds_read_b128 v[160:163], v144
	ds_read_b128 v[164:167], v145
	ds_read_b128 v[168:171], v140
	ds_read_b128 v[172:175], v141
	ds_read_b128 v[176:179], v146
	ds_read_b128 v[180:183], v147
	ds_read_b128 v[184:187], v148
	ds_read_b128 v[188:191], v149
	s_add_i32 s73, s16, 0x80
	s_cmp_eq_u32 s20, s72
	s_cselect_b32 s74, s15, s71
	s_cselect_b32 s73, s17, s73
	v_add_u32_e32 v159, s16, v157
	s_add_i32 m0, s28, 0xc000
	ds_read_b128 v[192:195], v158
	ds_read_b128 v[196:199], v158 offset:1024
	ds_read_b128 v[200:203], v158 offset:2048
	ds_read_b128 v[204:207], v158 offset:3072
	ds_read_b128 v[214:217], v158 offset:4096
	ds_read_b128 v[218:221], v158 offset:5120
	ds_read_b128 v[222:225], v158 offset:6144
	ds_read_b128 v[226:229], v158 offset:7168
	global_load_lds_dwordx4 v159, s[4:5]
	v_add_u32_e32 v159, s16, v156
	s_add_i32 m0, s28, 0xe000
	s_nop 0
	global_load_lds_dwordx4 v159, s[4:5]
	s_waitcnt vmcnt(8)
	s_waitcnt lgkmcnt(0)
	s_barrier
	s_setprio 1
	s_waitcnt lgkmcnt(0)
	v_mfma_f32_16x16x32_bf16 v[122:125], v[168:171], v[192:195], 0
	v_mfma_f32_16x16x32_bf16 v[126:129], v[164:167], v[192:195], 0
	v_mfma_f32_16x16x32_bf16 v[110:113], v[168:171], v[200:203], 0
	v_mfma_f32_16x16x32_bf16 v[106:109], v[164:167], v[200:203], 0
	v_mfma_f32_16x16x32_bf16 v[94:97], v[168:171], v[214:217], 0
	v_mfma_f32_16x16x32_bf16 v[90:93], v[164:167], v[214:217], 0
	v_mfma_f32_16x16x32_bf16 v[78:81], v[168:171], v[222:225], 0
	v_mfma_f32_16x16x32_bf16 v[74:77], v[164:167], v[222:225], 0
	v_mfma_f32_16x16x32_bf16 v[122:125], v[160:163], v[196:199], v[122:125]
	v_mfma_f32_16x16x32_bf16 v[126:129], v[176:179], v[196:199], v[126:129]
	v_mfma_f32_16x16x32_bf16 v[110:113], v[160:163], v[204:207], v[110:113]
	v_mfma_f32_16x16x32_bf16 v[106:109], v[176:179], v[204:207], v[106:109]
	v_mfma_f32_16x16x32_bf16 v[94:97], v[160:163], v[218:221], v[94:97]
	v_mfma_f32_16x16x32_bf16 v[90:93], v[176:179], v[218:221], v[90:93]
	v_mfma_f32_16x16x32_bf16 v[78:81], v[160:163], v[226:229], v[78:81]
	v_mfma_f32_16x16x32_bf16 v[74:77], v[176:179], v[226:229], v[74:77]
	v_mfma_f32_16x16x32_bf16 v[118:121], v[172:175], v[192:195], 0
	v_mfma_f32_16x16x32_bf16 v[114:117], v[184:187], v[192:195], 0
	v_mfma_f32_16x16x32_bf16 v[102:105], v[172:175], v[200:203], 0
	v_mfma_f32_16x16x32_bf16 v[98:101], v[184:187], v[200:203], 0
	v_mfma_f32_16x16x32_bf16 v[86:89], v[172:175], v[214:217], 0
	v_mfma_f32_16x16x32_bf16 v[82:85], v[184:187], v[214:217], 0
	v_mfma_f32_16x16x32_bf16 v[70:73], v[172:175], v[222:225], 0
	v_mfma_f32_16x16x32_bf16 v[66:69], v[184:187], v[222:225], 0
	v_mfma_f32_16x16x32_bf16 v[118:121], v[180:183], v[196:199], v[118:121]
	v_mfma_f32_16x16x32_bf16 v[114:117], v[188:191], v[196:199], v[114:117]
	v_mfma_f32_16x16x32_bf16 v[102:105], v[180:183], v[204:207], v[102:105]
	v_mfma_f32_16x16x32_bf16 v[98:101], v[188:191], v[204:207], v[98:101]
	v_mfma_f32_16x16x32_bf16 v[86:89], v[180:183], v[218:221], v[86:89]
	v_mfma_f32_16x16x32_bf16 v[82:85], v[188:191], v[218:221], v[82:85]
	v_mfma_f32_16x16x32_bf16 v[70:73], v[180:183], v[226:229], v[70:73]
	v_mfma_f32_16x16x32_bf16 v[66:69], v[188:191], v[226:229], v[66:69]
	s_setprio 0
	s_barrier
	s_mov_b32 m0, s29
	v_add_u32_e32 v159, s74, v134
	ds_read_b128 v[192:195], v158 offset:16384
	ds_read_b128 v[196:199], v158 offset:17408
	ds_read_b128 v[200:203], v158 offset:18432
	ds_read_b128 v[204:207], v158 offset:19456
	ds_read_b128 v[214:217], v158 offset:20480
	ds_read_b128 v[218:221], v158 offset:21504
	ds_read_b128 v[222:225], v158 offset:22528
	ds_read_b128 v[226:229], v158 offset:23552
	global_load_lds_dwordx4 v159, s[6:7]
	v_add_u32_e32 v159, s23, v159
	s_mov_b32 m0, s30
	s_nop 0
	global_load_lds_dwordx4 v159, s[6:7]
	v_add_u32_e32 v159, s74, v135
	s_mov_b32 m0, s31
	s_nop 0
	global_load_lds_dwordx4 v159, s[6:7]
	v_add_u32_e32 v159, s23, v159
	s_mov_b32 m0, s35
	s_nop 0
	global_load_lds_dwordx4 v159, s[6:7]
	v_add_u32_e32 v159, s73, v1
	s_mov_b32 m0, s28
	s_nop 0
	global_load_lds_dwordx4 v159, s[4:5]
	v_add_u32_e32 v159, s22, v159
	s_mov_b32 m0, s44
	s_nop 0
	global_load_lds_dwordx4 v159, s[4:5]
	s_waitcnt vmcnt(8)
	s_waitcnt lgkmcnt(0)
	s_barrier
	s_setprio 1
	s_waitcnt lgkmcnt(0)
	v_mfma_f32_16x16x32_bf16 v[62:65], v[168:171], v[192:195], 0
	v_mfma_f32_16x16x32_bf16 v[58:61], v[164:167], v[192:195], 0
	v_mfma_f32_16x16x32_bf16 v[46:49], v[168:171], v[200:203], 0
	v_mfma_f32_16x16x32_bf16 v[42:45], v[164:167], v[200:203], 0
	v_mfma_f32_16x16x32_bf16 v[30:33], v[168:171], v[214:217], 0
	v_mfma_f32_16x16x32_bf16 v[26:29], v[164:167], v[214:217], 0
	v_mfma_f32_16x16x32_bf16 v[14:17], v[168:171], v[222:225], 0
	v_mfma_f32_16x16x32_bf16 v[10:13], v[164:167], v[222:225], 0
	v_mfma_f32_16x16x32_bf16 v[62:65], v[160:163], v[196:199], v[62:65]
	v_mfma_f32_16x16x32_bf16 v[58:61], v[176:179], v[196:199], v[58:61]
	v_mfma_f32_16x16x32_bf16 v[46:49], v[160:163], v[204:207], v[46:49]
	v_mfma_f32_16x16x32_bf16 v[42:45], v[176:179], v[204:207], v[42:45]
	v_mfma_f32_16x16x32_bf16 v[30:33], v[160:163], v[218:221], v[30:33]
	v_mfma_f32_16x16x32_bf16 v[26:29], v[176:179], v[218:221], v[26:29]
	v_mfma_f32_16x16x32_bf16 v[14:17], v[160:163], v[226:229], v[14:17]
	v_mfma_f32_16x16x32_bf16 v[10:13], v[176:179], v[226:229], v[10:13]
	v_mfma_f32_16x16x32_bf16 v[54:57], v[172:175], v[192:195], 0
	v_mfma_f32_16x16x32_bf16 v[50:53], v[184:187], v[192:195], 0
	v_mfma_f32_16x16x32_bf16 v[38:41], v[172:175], v[200:203], 0
	v_mfma_f32_16x16x32_bf16 v[34:37], v[184:187], v[200:203], 0
	v_mfma_f32_16x16x32_bf16 v[22:25], v[172:175], v[214:217], 0
	v_mfma_f32_16x16x32_bf16 v[18:21], v[184:187], v[214:217], 0
	v_mfma_f32_16x16x32_bf16 v[6:9], v[172:175], v[222:225], 0
	v_mfma_f32_16x16x32_bf16 v[2:5], v[184:187], v[222:225], 0
	v_mfma_f32_16x16x32_bf16 v[54:57], v[180:183], v[196:199], v[54:57]
	v_mfma_f32_16x16x32_bf16 v[50:53], v[188:191], v[196:199], v[50:53]
	v_mfma_f32_16x16x32_bf16 v[38:41], v[180:183], v[204:207], v[38:41]
	v_mfma_f32_16x16x32_bf16 v[34:37], v[188:191], v[204:207], v[34:37]
	v_mfma_f32_16x16x32_bf16 v[22:25], v[180:183], v[218:221], v[22:25]
	v_mfma_f32_16x16x32_bf16 v[18:21], v[188:191], v[218:221], v[18:21]
	v_mfma_f32_16x16x32_bf16 v[6:9], v[180:183], v[226:229], v[6:9]
	v_mfma_f32_16x16x32_bf16 v[2:5], v[188:191], v[226:229], v[2:5]
	s_setprio 0
	s_barrier
	s_branch .Lmid_2
.LBB0_620:
	ds_read_b128 v[160:163], v144
	ds_read_b128 v[164:167], v145
	ds_read_b128 v[168:171], v140
	ds_read_b128 v[172:175], v141
	ds_read_b128 v[176:179], v146
	ds_read_b128 v[180:183], v147
	ds_read_b128 v[184:187], v148
	ds_read_b128 v[188:191], v149
	s_add_i32 s73, s16, 0x80
	s_cmp_eq_u32 s20, s72
	s_cselect_b32 s74, s15, s71
	s_cselect_b32 s73, s17, s73
	v_add_u32_e32 v159, s16, v157
	s_add_i32 m0, s28, 0xc000
	ds_read_b128 v[192:195], v158
	ds_read_b128 v[196:199], v158 offset:1024
	ds_read_b128 v[200:203], v158 offset:2048
	ds_read_b128 v[204:207], v158 offset:3072
	ds_read_b128 v[214:217], v158 offset:4096
	ds_read_b128 v[218:221], v158 offset:5120
	ds_read_b128 v[222:225], v158 offset:6144
	ds_read_b128 v[226:229], v158 offset:7168
	global_load_lds_dwordx4 v159, s[4:5]
	v_add_u32_e32 v159, s16, v156
	s_add_i32 m0, s28, 0xe000
	s_nop 0
	global_load_lds_dwordx4 v159, s[4:5]
	s_waitcnt vmcnt(8)
	s_waitcnt lgkmcnt(0)
	s_barrier
	s_setprio 1
	s_waitcnt lgkmcnt(0)
	v_mfma_f32_16x16x32_bf16 v[122:125], v[168:171], v[192:195], v[122:125]
	v_mfma_f32_16x16x32_bf16 v[126:129], v[164:167], v[192:195], v[126:129]
	v_mfma_f32_16x16x32_bf16 v[110:113], v[168:171], v[200:203], v[110:113]
	v_mfma_f32_16x16x32_bf16 v[106:109], v[164:167], v[200:203], v[106:109]
	v_mfma_f32_16x16x32_bf16 v[94:97], v[168:171], v[214:217], v[94:97]
	v_mfma_f32_16x16x32_bf16 v[90:93], v[164:167], v[214:217], v[90:93]
	v_mfma_f32_16x16x32_bf16 v[78:81], v[168:171], v[222:225], v[78:81]
	v_mfma_f32_16x16x32_bf16 v[74:77], v[164:167], v[222:225], v[74:77]
	v_mfma_f32_16x16x32_bf16 v[122:125], v[160:163], v[196:199], v[122:125]
	v_mfma_f32_16x16x32_bf16 v[126:129], v[176:179], v[196:199], v[126:129]
	v_mfma_f32_16x16x32_bf16 v[110:113], v[160:163], v[204:207], v[110:113]
	v_mfma_f32_16x16x32_bf16 v[106:109], v[176:179], v[204:207], v[106:109]
	v_mfma_f32_16x16x32_bf16 v[94:97], v[160:163], v[218:221], v[94:97]
	v_mfma_f32_16x16x32_bf16 v[90:93], v[176:179], v[218:221], v[90:93]
	v_mfma_f32_16x16x32_bf16 v[78:81], v[160:163], v[226:229], v[78:81]
	v_mfma_f32_16x16x32_bf16 v[74:77], v[176:179], v[226:229], v[74:77]
	v_mfma_f32_16x16x32_bf16 v[118:121], v[172:175], v[192:195], v[118:121]
	v_mfma_f32_16x16x32_bf16 v[114:117], v[184:187], v[192:195], v[114:117]
	v_mfma_f32_16x16x32_bf16 v[102:105], v[172:175], v[200:203], v[102:105]
	v_mfma_f32_16x16x32_bf16 v[98:101], v[184:187], v[200:203], v[98:101]
	v_mfma_f32_16x16x32_bf16 v[86:89], v[172:175], v[214:217], v[86:89]
	v_mfma_f32_16x16x32_bf16 v[82:85], v[184:187], v[214:217], v[82:85]
	v_mfma_f32_16x16x32_bf16 v[70:73], v[172:175], v[222:225], v[70:73]
	v_mfma_f32_16x16x32_bf16 v[66:69], v[184:187], v[222:225], v[66:69]
	v_mfma_f32_16x16x32_bf16 v[118:121], v[180:183], v[196:199], v[118:121]
	v_mfma_f32_16x16x32_bf16 v[114:117], v[188:191], v[196:199], v[114:117]
	v_mfma_f32_16x16x32_bf16 v[102:105], v[180:183], v[204:207], v[102:105]
	v_mfma_f32_16x16x32_bf16 v[98:101], v[188:191], v[204:207], v[98:101]
	v_mfma_f32_16x16x32_bf16 v[86:89], v[180:183], v[218:221], v[86:89]
	v_mfma_f32_16x16x32_bf16 v[82:85], v[188:191], v[218:221], v[82:85]
	v_mfma_f32_16x16x32_bf16 v[70:73], v[180:183], v[226:229], v[70:73]
	v_mfma_f32_16x16x32_bf16 v[66:69], v[188:191], v[226:229], v[66:69]
	s_setprio 0
	s_barrier
	s_mov_b32 m0, s29
	v_add_u32_e32 v159, s74, v134
	ds_read_b128 v[192:195], v158 offset:16384
	ds_read_b128 v[196:199], v158 offset:17408
	ds_read_b128 v[200:203], v158 offset:18432
	ds_read_b128 v[204:207], v158 offset:19456
	ds_read_b128 v[214:217], v158 offset:20480
	ds_read_b128 v[218:221], v158 offset:21504
	ds_read_b128 v[222:225], v158 offset:22528
	ds_read_b128 v[226:229], v158 offset:23552
	global_load_lds_dwordx4 v159, s[6:7]
	v_add_u32_e32 v159, s23, v159
	s_mov_b32 m0, s30
	s_nop 0
	global_load_lds_dwordx4 v159, s[6:7]
	v_add_u32_e32 v159, s74, v135
	s_mov_b32 m0, s31
	s_nop 0
	global_load_lds_dwordx4 v159, s[6:7]
	v_add_u32_e32 v159, s23, v159
	s_mov_b32 m0, s35
	s_nop 0
	global_load_lds_dwordx4 v159, s[6:7]
	v_add_u32_e32 v159, s73, v1
	s_mov_b32 m0, s28
	s_nop 0
	global_load_lds_dwordx4 v159, s[4:5]
	v_add_u32_e32 v159, s22, v159
	s_mov_b32 m0, s44
	s_nop 0
	global_load_lds_dwordx4 v159, s[4:5]
	s_waitcnt vmcnt(8)
	s_waitcnt lgkmcnt(0)
	s_barrier
	s_setprio 1
	s_waitcnt lgkmcnt(0)
	v_mfma_f32_16x16x32_bf16 v[62:65], v[168:171], v[192:195], v[62:65]
	v_mfma_f32_16x16x32_bf16 v[58:61], v[164:167], v[192:195], v[58:61]
	v_mfma_f32_16x16x32_bf16 v[46:49], v[168:171], v[200:203], v[46:49]
	v_mfma_f32_16x16x32_bf16 v[42:45], v[164:167], v[200:203], v[42:45]
	v_mfma_f32_16x16x32_bf16 v[30:33], v[168:171], v[214:217], v[30:33]
	v_mfma_f32_16x16x32_bf16 v[26:29], v[164:167], v[214:217], v[26:29]
	v_mfma_f32_16x16x32_bf16 v[14:17], v[168:171], v[222:225], v[14:17]
	v_mfma_f32_16x16x32_bf16 v[10:13], v[164:167], v[222:225], v[10:13]
	v_mfma_f32_16x16x32_bf16 v[62:65], v[160:163], v[196:199], v[62:65]
	v_mfma_f32_16x16x32_bf16 v[58:61], v[176:179], v[196:199], v[58:61]
	v_mfma_f32_16x16x32_bf16 v[46:49], v[160:163], v[204:207], v[46:49]
	v_mfma_f32_16x16x32_bf16 v[42:45], v[176:179], v[204:207], v[42:45]
	v_mfma_f32_16x16x32_bf16 v[30:33], v[160:163], v[218:221], v[30:33]
	v_mfma_f32_16x16x32_bf16 v[26:29], v[176:179], v[218:221], v[26:29]
	v_mfma_f32_16x16x32_bf16 v[14:17], v[160:163], v[226:229], v[14:17]
	v_mfma_f32_16x16x32_bf16 v[10:13], v[176:179], v[226:229], v[10:13]
	v_mfma_f32_16x16x32_bf16 v[54:57], v[172:175], v[192:195], v[54:57]
	v_mfma_f32_16x16x32_bf16 v[50:53], v[184:187], v[192:195], v[50:53]
	v_mfma_f32_16x16x32_bf16 v[38:41], v[172:175], v[200:203], v[38:41]
	v_mfma_f32_16x16x32_bf16 v[34:37], v[184:187], v[200:203], v[34:37]
	v_mfma_f32_16x16x32_bf16 v[22:25], v[172:175], v[214:217], v[22:25]
	v_mfma_f32_16x16x32_bf16 v[18:21], v[184:187], v[214:217], v[18:21]
	v_mfma_f32_16x16x32_bf16 v[6:9], v[172:175], v[222:225], v[6:9]
	v_mfma_f32_16x16x32_bf16 v[2:5], v[184:187], v[222:225], v[2:5]
	v_mfma_f32_16x16x32_bf16 v[54:57], v[180:183], v[196:199], v[54:57]
	v_mfma_f32_16x16x32_bf16 v[50:53], v[188:191], v[196:199], v[50:53]
	v_mfma_f32_16x16x32_bf16 v[38:41], v[180:183], v[204:207], v[38:41]
	v_mfma_f32_16x16x32_bf16 v[34:37], v[188:191], v[204:207], v[34:37]
	v_mfma_f32_16x16x32_bf16 v[22:25], v[180:183], v[218:221], v[22:25]
	v_mfma_f32_16x16x32_bf16 v[18:21], v[188:191], v[218:221], v[18:21]
	v_mfma_f32_16x16x32_bf16 v[6:9], v[180:183], v[226:229], v[6:9]
	v_mfma_f32_16x16x32_bf16 v[2:5], v[188:191], v[226:229], v[2:5]
	s_setprio 0
	s_barrier
.Lmid_2:
	ds_read_b128 v[160:163], v150
	ds_read_b128 v[164:167], v151
	ds_read_b128 v[168:171], v142
	ds_read_b128 v[172:175], v143
	ds_read_b128 v[176:179], v152
	ds_read_b128 v[180:183], v153
	ds_read_b128 v[184:187], v154
	ds_read_b128 v[188:191], v155
	s_mov_b32 m0, s45
	v_add_u32_e32 v159, s73, v136
	ds_read_b128 v[192:195], v158 offset:32768
	ds_read_b128 v[196:199], v158 offset:33792
	ds_read_b128 v[200:203], v158 offset:34816
	ds_read_b128 v[204:207], v158 offset:35840
	ds_read_b128 v[214:217], v158 offset:36864
	ds_read_b128 v[218:221], v158 offset:37888
	ds_read_b128 v[222:225], v158 offset:38912
	ds_read_b128 v[226:229], v158 offset:39936
	global_load_lds_dwordx4 v159, s[4:5]
	v_add_u32_e32 v159, s22, v159
	s_mov_b32 m0, s46
	s_nop 0
	global_load_lds_dwordx4 v159, s[4:5]
	s_waitcnt vmcnt(8)
	s_waitcnt lgkmcnt(0)
	s_barrier
	s_setprio 1
	s_waitcnt lgkmcnt(0)
	v_mfma_f32_16x16x32_bf16 v[122:125], v[168:171], v[192:195], v[122:125]
	v_mfma_f32_16x16x32_bf16 v[126:129], v[164:167], v[192:195], v[126:129]
	v_mfma_f32_16x16x32_bf16 v[110:113], v[168:171], v[200:203], v[110:113]
	v_mfma_f32_16x16x32_bf16 v[106:109], v[164:167], v[200:203], v[106:109]
	v_mfma_f32_16x16x32_bf16 v[94:97], v[168:171], v[214:217], v[94:97]
	v_mfma_f32_16x16x32_bf16 v[90:93], v[164:167], v[214:217], v[90:93]
	v_mfma_f32_16x16x32_bf16 v[78:81], v[168:171], v[222:225], v[78:81]
	v_mfma_f32_16x16x32_bf16 v[74:77], v[164:167], v[222:225], v[74:77]
	v_mfma_f32_16x16x32_bf16 v[122:125], v[160:163], v[196:199], v[122:125]
	v_mfma_f32_16x16x32_bf16 v[126:129], v[176:179], v[196:199], v[126:129]
	v_mfma_f32_16x16x32_bf16 v[110:113], v[160:163], v[204:207], v[110:113]
	v_mfma_f32_16x16x32_bf16 v[106:109], v[176:179], v[204:207], v[106:109]
	v_mfma_f32_16x16x32_bf16 v[94:97], v[160:163], v[218:221], v[94:97]
	v_mfma_f32_16x16x32_bf16 v[90:93], v[176:179], v[218:221], v[90:93]
	v_mfma_f32_16x16x32_bf16 v[78:81], v[160:163], v[226:229], v[78:81]
	v_mfma_f32_16x16x32_bf16 v[74:77], v[176:179], v[226:229], v[74:77]
	v_mfma_f32_16x16x32_bf16 v[118:121], v[172:175], v[192:195], v[118:121]
	v_mfma_f32_16x16x32_bf16 v[114:117], v[184:187], v[192:195], v[114:117]
	v_mfma_f32_16x16x32_bf16 v[102:105], v[172:175], v[200:203], v[102:105]
	v_mfma_f32_16x16x32_bf16 v[98:101], v[184:187], v[200:203], v[98:101]
	v_mfma_f32_16x16x32_bf16 v[86:89], v[172:175], v[214:217], v[86:89]
	v_mfma_f32_16x16x32_bf16 v[82:85], v[184:187], v[214:217], v[82:85]
	v_mfma_f32_16x16x32_bf16 v[70:73], v[172:175], v[222:225], v[70:73]
	v_mfma_f32_16x16x32_bf16 v[66:69], v[184:187], v[222:225], v[66:69]
	v_mfma_f32_16x16x32_bf16 v[118:121], v[180:183], v[196:199], v[118:121]
	v_mfma_f32_16x16x32_bf16 v[114:117], v[188:191], v[196:199], v[114:117]
	v_mfma_f32_16x16x32_bf16 v[102:105], v[180:183], v[204:207], v[102:105]
	v_mfma_f32_16x16x32_bf16 v[98:101], v[188:191], v[204:207], v[98:101]
	v_mfma_f32_16x16x32_bf16 v[86:89], v[180:183], v[218:221], v[86:89]
	v_mfma_f32_16x16x32_bf16 v[82:85], v[188:191], v[218:221], v[82:85]
	v_mfma_f32_16x16x32_bf16 v[70:73], v[180:183], v[226:229], v[70:73]
	v_mfma_f32_16x16x32_bf16 v[66:69], v[188:191], v[226:229], v[66:69]
	s_setprio 0
	s_barrier
	s_addk_i32 s74, 0x80
	s_mov_b32 m0, s49
	v_add_u32_e32 v159, s74, v134
	ds_read_b128 v[192:195], v158 offset:49152
	ds_read_b128 v[196:199], v158 offset:50176
	ds_read_b128 v[200:203], v158 offset:51200
	ds_read_b128 v[204:207], v158 offset:52224
	ds_read_b128 v[214:217], v158 offset:53248
	ds_read_b128 v[218:221], v158 offset:54272
	ds_read_b128 v[222:225], v158 offset:55296
	ds_read_b128 v[226:229], v158 offset:56320
	global_load_lds_dwordx4 v159, s[6:7]
	v_add_u32_e32 v159, s23, v159
	s_mov_b32 m0, s50
	s_nop 0
	global_load_lds_dwordx4 v159, s[6:7]
	v_add_u32_e32 v159, s74, v135
	s_mov_b32 m0, s53
	s_nop 0
	global_load_lds_dwordx4 v159, s[6:7]
	v_add_u32_e32 v159, s23, v159
	s_mov_b32 m0, s54
	s_nop 0
	global_load_lds_dwordx4 v159, s[6:7]
	v_add_u32_e32 v159, s73, v137
	s_mov_b32 m0, s51
	s_nop 0
	global_load_lds_dwordx4 v159, s[4:5]
	v_add_u32_e32 v159, s22, v159
	s_mov_b32 m0, s52
	s_nop 0
	global_load_lds_dwordx4 v159, s[4:5]
	s_waitcnt vmcnt(8)
	s_waitcnt lgkmcnt(0)
	s_barrier
	s_setprio 1
	s_waitcnt lgkmcnt(0)
	v_mfma_f32_16x16x32_bf16 v[62:65], v[168:171], v[192:195], v[62:65]
	v_mfma_f32_16x16x32_bf16 v[58:61], v[164:167], v[192:195], v[58:61]
	v_mfma_f32_16x16x32_bf16 v[46:49], v[168:171], v[200:203], v[46:49]
	v_mfma_f32_16x16x32_bf16 v[42:45], v[164:167], v[200:203], v[42:45]
	v_mfma_f32_16x16x32_bf16 v[30:33], v[168:171], v[214:217], v[30:33]
	v_mfma_f32_16x16x32_bf16 v[26:29], v[164:167], v[214:217], v[26:29]
	v_mfma_f32_16x16x32_bf16 v[14:17], v[168:171], v[222:225], v[14:17]
	v_mfma_f32_16x16x32_bf16 v[10:13], v[164:167], v[222:225], v[10:13]
	v_mfma_f32_16x16x32_bf16 v[62:65], v[160:163], v[196:199], v[62:65]
	v_mfma_f32_16x16x32_bf16 v[58:61], v[176:179], v[196:199], v[58:61]
	v_mfma_f32_16x16x32_bf16 v[46:49], v[160:163], v[204:207], v[46:49]
	v_mfma_f32_16x16x32_bf16 v[42:45], v[176:179], v[204:207], v[42:45]
	v_mfma_f32_16x16x32_bf16 v[30:33], v[160:163], v[218:221], v[30:33]
	v_mfma_f32_16x16x32_bf16 v[26:29], v[176:179], v[218:221], v[26:29]
	v_mfma_f32_16x16x32_bf16 v[14:17], v[160:163], v[226:229], v[14:17]
	v_mfma_f32_16x16x32_bf16 v[10:13], v[176:179], v[226:229], v[10:13]
	v_mfma_f32_16x16x32_bf16 v[54:57], v[172:175], v[192:195], v[54:57]
	v_mfma_f32_16x16x32_bf16 v[50:53], v[184:187], v[192:195], v[50:53]
	v_mfma_f32_16x16x32_bf16 v[38:41], v[172:175], v[200:203], v[38:41]
	v_mfma_f32_16x16x32_bf16 v[34:37], v[184:187], v[200:203], v[34:37]
	v_mfma_f32_16x16x32_bf16 v[22:25], v[172:175], v[214:217], v[22:25]
	v_mfma_f32_16x16x32_bf16 v[18:21], v[184:187], v[214:217], v[18:21]
	v_mfma_f32_16x16x32_bf16 v[6:9], v[172:175], v[222:225], v[6:9]
	v_mfma_f32_16x16x32_bf16 v[2:5], v[184:187], v[222:225], v[2:5]
	v_mfma_f32_16x16x32_bf16 v[54:57], v[180:183], v[196:199], v[54:57]
	v_mfma_f32_16x16x32_bf16 v[50:53], v[188:191], v[196:199], v[50:53]
	v_mfma_f32_16x16x32_bf16 v[38:41], v[180:183], v[204:207], v[38:41]
	v_mfma_f32_16x16x32_bf16 v[34:37], v[188:191], v[204:207], v[34:37]
	v_mfma_f32_16x16x32_bf16 v[22:25], v[180:183], v[218:221], v[22:25]
	v_mfma_f32_16x16x32_bf16 v[18:21], v[188:191], v[218:221], v[18:21]
	v_mfma_f32_16x16x32_bf16 v[6:9], v[180:183], v[226:229], v[6:9]
	v_mfma_f32_16x16x32_bf16 v[2:5], v[188:191], v[226:229], v[2:5]
	s_setprio 0
	s_barrier
	s_add_i32 s72, s72, 2
	s_addk_i32 s16, 0x100
	s_addk_i32 s71, 0x100
	s_cmp_ge_i32 s72, s55
	s_cbranch_scc0 .LBB0_620

.LBB0_635:
	s_andn2_b64 vcc, exec, s[20:21]
	s_cbranch_vccnz .Lzs_3
	s_add_i32 s28, s79, 0x80
	s_add_i32 s79, s75, 0x100
	s_mov_b32 s80, 0
	ds_read_b128 v[130:133], v188
	ds_read_b128 v[134:137], v189
	ds_read_b128 v[138:141], v184
	ds_read_b128 v[142:145], v185
	ds_read_b128 v[146:149], v190
	ds_read_b128 v[150:153], v191
	ds_read_b128 v[154:157], v192
	ds_read_b128 v[158:161], v193
	s_add_i32 s75, s28, 0x80
	s_cmp_eq_u32 s66, s80
	s_cselect_b32 s81, s25, s79
	s_cselect_b32 s75, s29, s75
	v_add_u32_e32 v203, s28, v201
	s_add_i32 m0, s46, 0xc000
	ds_read_b128 v[162:165], v202
	ds_read_b128 v[166:169], v202 offset:1024
	ds_read_b128 v[170:173], v202 offset:2048
	ds_read_b128 v[204:207], v202 offset:3072
	ds_read_b128 v[214:217], v202 offset:4096
	ds_read_b128 v[218:221], v202 offset:5120
	ds_read_b128 v[222:225], v202 offset:6144
	ds_read_b128 v[226:229], v202 offset:7168
	global_load_lds_dwordx4 v203, s[4:5]
	v_add_u32_e32 v203, s28, v200
	s_add_i32 m0, s46, 0xe000
	s_nop 0
	global_load_lds_dwordx4 v203, s[4:5]
	s_waitcnt vmcnt(8)
	s_waitcnt lgkmcnt(0)
	s_barrier
	s_setprio 1
	s_waitcnt lgkmcnt(0)
	v_mfma_f32_16x16x32_bf16 v[126:129], v[138:141], v[162:165], 0
	v_mfma_f32_16x16x32_bf16 v[118:121], v[134:137], v[162:165], 0
	v_mfma_f32_16x16x32_bf16 v[110:113], v[138:141], v[170:173], 0
	v_mfma_f32_16x16x32_bf16 v[102:105], v[134:137], v[170:173], 0
	v_mfma_f32_16x16x32_bf16 v[94:97], v[138:141], v[214:217], 0
	v_mfma_f32_16x16x32_bf16 v[86:89], v[134:137], v[214:217], 0
	v_mfma_f32_16x16x32_bf16 v[78:81], v[138:141], v[222:225], 0
	v_mfma_f32_16x16x32_bf16 v[70:73], v[134:137], v[222:225], 0
	v_mfma_f32_16x16x32_bf16 v[126:129], v[130:133], v[166:169], v[126:129]
	v_mfma_f32_16x16x32_bf16 v[118:121], v[146:149], v[166:169], v[118:121]
	v_mfma_f32_16x16x32_bf16 v[110:113], v[130:133], v[204:207], v[110:113]
	v_mfma_f32_16x16x32_bf16 v[102:105], v[146:149], v[204:207], v[102:105]
	v_mfma_f32_16x16x32_bf16 v[94:97], v[130:133], v[218:221], v[94:97]
	v_mfma_f32_16x16x32_bf16 v[86:89], v[146:149], v[218:221], v[86:89]
	v_mfma_f32_16x16x32_bf16 v[78:81], v[130:133], v[226:229], v[78:81]
	v_mfma_f32_16x16x32_bf16 v[70:73], v[146:149], v[226:229], v[70:73]
	v_mfma_f32_16x16x32_bf16 v[122:125], v[142:145], v[162:165], 0
	v_mfma_f32_16x16x32_bf16 v[114:117], v[154:157], v[162:165], 0
	v_mfma_f32_16x16x32_bf16 v[106:109], v[142:145], v[170:173], 0
	v_mfma_f32_16x16x32_bf16 v[98:101], v[154:157], v[170:173], 0
	v_mfma_f32_16x16x32_bf16 v[90:93], v[142:145], v[214:217], 0
	v_mfma_f32_16x16x32_bf16 v[82:85], v[154:157], v[214:217], 0
	v_mfma_f32_16x16x32_bf16 v[74:77], v[142:145], v[222:225], 0
	v_mfma_f32_16x16x32_bf16 v[66:69], v[154:157], v[222:225], 0
	v_mfma_f32_16x16x32_bf16 v[122:125], v[150:153], v[166:169], v[122:125]
	v_mfma_f32_16x16x32_bf16 v[114:117], v[158:161], v[166:169], v[114:117]
	v_mfma_f32_16x16x32_bf16 v[106:109], v[150:153], v[204:207], v[106:109]
	v_mfma_f32_16x16x32_bf16 v[98:101], v[158:161], v[204:207], v[98:101]
	v_mfma_f32_16x16x32_bf16 v[90:93], v[150:153], v[218:221], v[90:93]
	v_mfma_f32_16x16x32_bf16 v[82:85], v[158:161], v[218:221], v[82:85]
	v_mfma_f32_16x16x32_bf16 v[74:77], v[150:153], v[226:229], v[74:77]
	v_mfma_f32_16x16x32_bf16 v[66:69], v[158:161], v[226:229], v[66:69]
	s_setprio 0
	s_barrier
	s_mov_b32 m0, s47
	v_add_u32_e32 v203, s81, v178
	ds_read_b128 v[162:165], v202 offset:16384
	ds_read_b128 v[166:169], v202 offset:17408
	ds_read_b128 v[170:173], v202 offset:18432
	ds_read_b128 v[204:207], v202 offset:19456
	ds_read_b128 v[214:217], v202 offset:20480
	ds_read_b128 v[218:221], v202 offset:21504
	ds_read_b128 v[222:225], v202 offset:22528
	ds_read_b128 v[226:229], v202 offset:23552
	global_load_lds_dwordx4 v203, s[6:7]
	v_add_u32_e32 v203, s35, v203
	s_mov_b32 m0, s48
	s_nop 0
	global_load_lds_dwordx4 v203, s[6:7]
	v_add_u32_e32 v203, s81, v179
	s_mov_b32 m0, s49
	s_nop 0
	global_load_lds_dwordx4 v203, s[6:7]
	v_add_u32_e32 v203, s35, v203
	s_mov_b32 m0, s50
	s_nop 0
	global_load_lds_dwordx4 v203, s[6:7]
	v_add_u32_e32 v203, s75, v1
	s_mov_b32 m0, s46
	s_nop 0
	global_load_lds_dwordx4 v203, s[4:5]
	v_add_u32_e32 v203, s31, v203
	s_mov_b32 m0, s51
	s_nop 0
	global_load_lds_dwordx4 v203, s[4:5]
	s_waitcnt vmcnt(8)
	s_waitcnt lgkmcnt(0)
	s_barrier
	s_setprio 1
	s_waitcnt lgkmcnt(0)
	v_mfma_f32_16x16x32_bf16 v[62:65], v[138:141], v[162:165], 0
	v_mfma_f32_16x16x32_bf16 v[54:57], v[134:137], v[162:165], 0
	v_mfma_f32_16x16x32_bf16 v[46:49], v[138:141], v[170:173], 0
	v_mfma_f32_16x16x32_bf16 v[38:41], v[134:137], v[170:173], 0
	v_mfma_f32_16x16x32_bf16 v[30:33], v[138:141], v[214:217], 0
	v_mfma_f32_16x16x32_bf16 v[22:25], v[134:137], v[214:217], 0
	v_mfma_f32_16x16x32_bf16 v[14:17], v[138:141], v[222:225], 0
	v_mfma_f32_16x16x32_bf16 v[6:9], v[134:137], v[222:225], 0
	v_mfma_f32_16x16x32_bf16 v[62:65], v[130:133], v[166:169], v[62:65]
	v_mfma_f32_16x16x32_bf16 v[54:57], v[146:149], v[166:169], v[54:57]
	v_mfma_f32_16x16x32_bf16 v[46:49], v[130:133], v[204:207], v[46:49]
	v_mfma_f32_16x16x32_bf16 v[38:41], v[146:149], v[204:207], v[38:41]
	v_mfma_f32_16x16x32_bf16 v[30:33], v[130:133], v[218:221], v[30:33]
	v_mfma_f32_16x16x32_bf16 v[22:25], v[146:149], v[218:221], v[22:25]
	v_mfma_f32_16x16x32_bf16 v[14:17], v[130:133], v[226:229], v[14:17]
	v_mfma_f32_16x16x32_bf16 v[6:9], v[146:149], v[226:229], v[6:9]
	v_mfma_f32_16x16x32_bf16 v[58:61], v[142:145], v[162:165], 0
	v_mfma_f32_16x16x32_bf16 v[50:53], v[154:157], v[162:165], 0
	v_mfma_f32_16x16x32_bf16 v[42:45], v[142:145], v[170:173], 0
	v_mfma_f32_16x16x32_bf16 v[34:37], v[154:157], v[170:173], 0
	v_mfma_f32_16x16x32_bf16 v[26:29], v[142:145], v[214:217], 0
	v_mfma_f32_16x16x32_bf16 v[18:21], v[154:157], v[214:217], 0
	v_mfma_f32_16x16x32_bf16 v[10:13], v[142:145], v[222:225], 0
	v_mfma_f32_16x16x32_bf16 v[2:5], v[154:157], v[222:225], 0
	v_mfma_f32_16x16x32_bf16 v[58:61], v[150:153], v[166:169], v[58:61]
	v_mfma_f32_16x16x32_bf16 v[50:53], v[158:161], v[166:169], v[50:53]
	v_mfma_f32_16x16x32_bf16 v[42:45], v[150:153], v[204:207], v[42:45]
	v_mfma_f32_16x16x32_bf16 v[34:37], v[158:161], v[204:207], v[34:37]
	v_mfma_f32_16x16x32_bf16 v[26:29], v[150:153], v[218:221], v[26:29]
	v_mfma_f32_16x16x32_bf16 v[18:21], v[158:161], v[218:221], v[18:21]
	v_mfma_f32_16x16x32_bf16 v[10:13], v[150:153], v[226:229], v[10:13]
	v_mfma_f32_16x16x32_bf16 v[2:5], v[158:161], v[226:229], v[2:5]
	s_setprio 0
	s_barrier
	s_branch .Lmid_3
.LBB0_637:
	ds_read_b128 v[130:133], v188
	ds_read_b128 v[134:137], v189
	ds_read_b128 v[138:141], v184
	ds_read_b128 v[142:145], v185
	ds_read_b128 v[146:149], v190
	ds_read_b128 v[150:153], v191
	ds_read_b128 v[154:157], v192
	ds_read_b128 v[158:161], v193
	s_add_i32 s75, s28, 0x80
	s_cmp_eq_u32 s66, s80
	s_cselect_b32 s81, s25, s79
	s_cselect_b32 s75, s29, s75
	v_add_u32_e32 v203, s28, v201
	s_add_i32 m0, s46, 0xc000
	ds_read_b128 v[162:165], v202
	ds_read_b128 v[166:169], v202 offset:1024
	ds_read_b128 v[170:173], v202 offset:2048
	ds_read_b128 v[204:207], v202 offset:3072
	ds_read_b128 v[214:217], v202 offset:4096
	ds_read_b128 v[218:221], v202 offset:5120
	ds_read_b128 v[222:225], v202 offset:6144
	ds_read_b128 v[226:229], v202 offset:7168
	global_load_lds_dwordx4 v203, s[4:5]
	v_add_u32_e32 v203, s28, v200
	s_add_i32 m0, s46, 0xe000
	s_nop 0
	global_load_lds_dwordx4 v203, s[4:5]
	s_waitcnt vmcnt(8)
	s_waitcnt lgkmcnt(0)
	s_barrier
	s_setprio 1
	s_waitcnt lgkmcnt(0)
	v_mfma_f32_16x16x32_bf16 v[126:129], v[138:141], v[162:165], v[126:129]
	v_mfma_f32_16x16x32_bf16 v[118:121], v[134:137], v[162:165], v[118:121]
	v_mfma_f32_16x16x32_bf16 v[110:113], v[138:141], v[170:173], v[110:113]
	v_mfma_f32_16x16x32_bf16 v[102:105], v[134:137], v[170:173], v[102:105]
	v_mfma_f32_16x16x32_bf16 v[94:97], v[138:141], v[214:217], v[94:97]
	v_mfma_f32_16x16x32_bf16 v[86:89], v[134:137], v[214:217], v[86:89]
	v_mfma_f32_16x16x32_bf16 v[78:81], v[138:141], v[222:225], v[78:81]
	v_mfma_f32_16x16x32_bf16 v[70:73], v[134:137], v[222:225], v[70:73]
	v_mfma_f32_16x16x32_bf16 v[126:129], v[130:133], v[166:169], v[126:129]
	v_mfma_f32_16x16x32_bf16 v[118:121], v[146:149], v[166:169], v[118:121]
	v_mfma_f32_16x16x32_bf16 v[110:113], v[130:133], v[204:207], v[110:113]
	v_mfma_f32_16x16x32_bf16 v[102:105], v[146:149], v[204:207], v[102:105]
	v_mfma_f32_16x16x32_bf16 v[94:97], v[130:133], v[218:221], v[94:97]
	v_mfma_f32_16x16x32_bf16 v[86:89], v[146:149], v[218:221], v[86:89]
	v_mfma_f32_16x16x32_bf16 v[78:81], v[130:133], v[226:229], v[78:81]
	v_mfma_f32_16x16x32_bf16 v[70:73], v[146:149], v[226:229], v[70:73]
	v_mfma_f32_16x16x32_bf16 v[122:125], v[142:145], v[162:165], v[122:125]
	v_mfma_f32_16x16x32_bf16 v[114:117], v[154:157], v[162:165], v[114:117]
	v_mfma_f32_16x16x32_bf16 v[106:109], v[142:145], v[170:173], v[106:109]
	v_mfma_f32_16x16x32_bf16 v[98:101], v[154:157], v[170:173], v[98:101]
	v_mfma_f32_16x16x32_bf16 v[90:93], v[142:145], v[214:217], v[90:93]
	v_mfma_f32_16x16x32_bf16 v[82:85], v[154:157], v[214:217], v[82:85]
	v_mfma_f32_16x16x32_bf16 v[74:77], v[142:145], v[222:225], v[74:77]
	v_mfma_f32_16x16x32_bf16 v[66:69], v[154:157], v[222:225], v[66:69]
	v_mfma_f32_16x16x32_bf16 v[122:125], v[150:153], v[166:169], v[122:125]
	v_mfma_f32_16x16x32_bf16 v[114:117], v[158:161], v[166:169], v[114:117]
	v_mfma_f32_16x16x32_bf16 v[106:109], v[150:153], v[204:207], v[106:109]
	v_mfma_f32_16x16x32_bf16 v[98:101], v[158:161], v[204:207], v[98:101]
	v_mfma_f32_16x16x32_bf16 v[90:93], v[150:153], v[218:221], v[90:93]
	v_mfma_f32_16x16x32_bf16 v[82:85], v[158:161], v[218:221], v[82:85]
	v_mfma_f32_16x16x32_bf16 v[74:77], v[150:153], v[226:229], v[74:77]
	v_mfma_f32_16x16x32_bf16 v[66:69], v[158:161], v[226:229], v[66:69]
	s_setprio 0
	s_barrier
	s_mov_b32 m0, s47
	v_add_u32_e32 v203, s81, v178
	ds_read_b128 v[162:165], v202 offset:16384
	ds_read_b128 v[166:169], v202 offset:17408
	ds_read_b128 v[170:173], v202 offset:18432
	ds_read_b128 v[204:207], v202 offset:19456
	ds_read_b128 v[214:217], v202 offset:20480
	ds_read_b128 v[218:221], v202 offset:21504
	ds_read_b128 v[222:225], v202 offset:22528
	ds_read_b128 v[226:229], v202 offset:23552
	global_load_lds_dwordx4 v203, s[6:7]
	v_add_u32_e32 v203, s35, v203
	s_mov_b32 m0, s48
	s_nop 0
	global_load_lds_dwordx4 v203, s[6:7]
	v_add_u32_e32 v203, s81, v179
	s_mov_b32 m0, s49
	s_nop 0
	global_load_lds_dwordx4 v203, s[6:7]
	v_add_u32_e32 v203, s35, v203
	s_mov_b32 m0, s50
	s_nop 0
	global_load_lds_dwordx4 v203, s[6:7]
	v_add_u32_e32 v203, s75, v1
	s_mov_b32 m0, s46
	s_nop 0
	global_load_lds_dwordx4 v203, s[4:5]
	v_add_u32_e32 v203, s31, v203
	s_mov_b32 m0, s51
	s_nop 0
	global_load_lds_dwordx4 v203, s[4:5]
	s_waitcnt vmcnt(8)
	s_waitcnt lgkmcnt(0)
	s_barrier
	s_setprio 1
	s_waitcnt lgkmcnt(0)
	v_mfma_f32_16x16x32_bf16 v[62:65], v[138:141], v[162:165], v[62:65]
	v_mfma_f32_16x16x32_bf16 v[54:57], v[134:137], v[162:165], v[54:57]
	v_mfma_f32_16x16x32_bf16 v[46:49], v[138:141], v[170:173], v[46:49]
	v_mfma_f32_16x16x32_bf16 v[38:41], v[134:137], v[170:173], v[38:41]
	v_mfma_f32_16x16x32_bf16 v[30:33], v[138:141], v[214:217], v[30:33]
	v_mfma_f32_16x16x32_bf16 v[22:25], v[134:137], v[214:217], v[22:25]
	v_mfma_f32_16x16x32_bf16 v[14:17], v[138:141], v[222:225], v[14:17]
	v_mfma_f32_16x16x32_bf16 v[6:9], v[134:137], v[222:225], v[6:9]
	v_mfma_f32_16x16x32_bf16 v[62:65], v[130:133], v[166:169], v[62:65]
	v_mfma_f32_16x16x32_bf16 v[54:57], v[146:149], v[166:169], v[54:57]
	v_mfma_f32_16x16x32_bf16 v[46:49], v[130:133], v[204:207], v[46:49]
	v_mfma_f32_16x16x32_bf16 v[38:41], v[146:149], v[204:207], v[38:41]
	v_mfma_f32_16x16x32_bf16 v[30:33], v[130:133], v[218:221], v[30:33]
	v_mfma_f32_16x16x32_bf16 v[22:25], v[146:149], v[218:221], v[22:25]
	v_mfma_f32_16x16x32_bf16 v[14:17], v[130:133], v[226:229], v[14:17]
	v_mfma_f32_16x16x32_bf16 v[6:9], v[146:149], v[226:229], v[6:9]
	v_mfma_f32_16x16x32_bf16 v[58:61], v[142:145], v[162:165], v[58:61]
	v_mfma_f32_16x16x32_bf16 v[50:53], v[154:157], v[162:165], v[50:53]
	v_mfma_f32_16x16x32_bf16 v[42:45], v[142:145], v[170:173], v[42:45]
	v_mfma_f32_16x16x32_bf16 v[34:37], v[154:157], v[170:173], v[34:37]
	v_mfma_f32_16x16x32_bf16 v[26:29], v[142:145], v[214:217], v[26:29]
	v_mfma_f32_16x16x32_bf16 v[18:21], v[154:157], v[214:217], v[18:21]
	v_mfma_f32_16x16x32_bf16 v[10:13], v[142:145], v[222:225], v[10:13]
	v_mfma_f32_16x16x32_bf16 v[2:5], v[154:157], v[222:225], v[2:5]
	v_mfma_f32_16x16x32_bf16 v[58:61], v[150:153], v[166:169], v[58:61]
	v_mfma_f32_16x16x32_bf16 v[50:53], v[158:161], v[166:169], v[50:53]
	v_mfma_f32_16x16x32_bf16 v[42:45], v[150:153], v[204:207], v[42:45]
	v_mfma_f32_16x16x32_bf16 v[34:37], v[158:161], v[204:207], v[34:37]
	v_mfma_f32_16x16x32_bf16 v[26:29], v[150:153], v[218:221], v[26:29]
	v_mfma_f32_16x16x32_bf16 v[18:21], v[158:161], v[218:221], v[18:21]
	v_mfma_f32_16x16x32_bf16 v[10:13], v[150:153], v[226:229], v[10:13]
	v_mfma_f32_16x16x32_bf16 v[2:5], v[158:161], v[226:229], v[2:5]
	s_setprio 0
	s_barrier
.Lmid_3:
	ds_read_b128 v[130:133], v194
	ds_read_b128 v[134:137], v195
	ds_read_b128 v[138:141], v186
	ds_read_b128 v[142:145], v187
	ds_read_b128 v[146:149], v196
	ds_read_b128 v[150:153], v197
	ds_read_b128 v[154:157], v198
	ds_read_b128 v[158:161], v199
	s_mov_b32 m0, s52
	v_add_u32_e32 v203, s75, v180
	ds_read_b128 v[162:165], v202 offset:32768
	ds_read_b128 v[166:169], v202 offset:33792
	ds_read_b128 v[170:173], v202 offset:34816
	ds_read_b128 v[204:207], v202 offset:35840
	ds_read_b128 v[214:217], v202 offset:36864
	ds_read_b128 v[218:221], v202 offset:37888
	ds_read_b128 v[222:225], v202 offset:38912
	ds_read_b128 v[226:229], v202 offset:39936
	global_load_lds_dwordx4 v203, s[4:5]
	v_add_u32_e32 v203, s31, v203
	s_mov_b32 m0, s53
	s_nop 0
	global_load_lds_dwordx4 v203, s[4:5]
	s_waitcnt vmcnt(8)
	s_waitcnt lgkmcnt(0)
	s_barrier
	s_setprio 1
	s_waitcnt lgkmcnt(0)
	v_mfma_f32_16x16x32_bf16 v[126:129], v[138:141], v[162:165], v[126:129]
	v_mfma_f32_16x16x32_bf16 v[118:121], v[134:137], v[162:165], v[118:121]
	v_mfma_f32_16x16x32_bf16 v[110:113], v[138:141], v[170:173], v[110:113]
	v_mfma_f32_16x16x32_bf16 v[102:105], v[134:137], v[170:173], v[102:105]
	v_mfma_f32_16x16x32_bf16 v[94:97], v[138:141], v[214:217], v[94:97]
	v_mfma_f32_16x16x32_bf16 v[86:89], v[134:137], v[214:217], v[86:89]
	v_mfma_f32_16x16x32_bf16 v[78:81], v[138:141], v[222:225], v[78:81]
	v_mfma_f32_16x16x32_bf16 v[70:73], v[134:137], v[222:225], v[70:73]
	v_mfma_f32_16x16x32_bf16 v[126:129], v[130:133], v[166:169], v[126:129]
	v_mfma_f32_16x16x32_bf16 v[118:121], v[146:149], v[166:169], v[118:121]
	v_mfma_f32_16x16x32_bf16 v[110:113], v[130:133], v[204:207], v[110:113]
	v_mfma_f32_16x16x32_bf16 v[102:105], v[146:149], v[204:207], v[102:105]
	v_mfma_f32_16x16x32_bf16 v[94:97], v[130:133], v[218:221], v[94:97]
	v_mfma_f32_16x16x32_bf16 v[86:89], v[146:149], v[218:221], v[86:89]
	v_mfma_f32_16x16x32_bf16 v[78:81], v[130:133], v[226:229], v[78:81]
	v_mfma_f32_16x16x32_bf16 v[70:73], v[146:149], v[226:229], v[70:73]
	v_mfma_f32_16x16x32_bf16 v[122:125], v[142:145], v[162:165], v[122:125]
	v_mfma_f32_16x16x32_bf16 v[114:117], v[154:157], v[162:165], v[114:117]
	v_mfma_f32_16x16x32_bf16 v[106:109], v[142:145], v[170:173], v[106:109]
	v_mfma_f32_16x16x32_bf16 v[98:101], v[154:157], v[170:173], v[98:101]
	v_mfma_f32_16x16x32_bf16 v[90:93], v[142:145], v[214:217], v[90:93]
	v_mfma_f32_16x16x32_bf16 v[82:85], v[154:157], v[214:217], v[82:85]
	v_mfma_f32_16x16x32_bf16 v[74:77], v[142:145], v[222:225], v[74:77]
	v_mfma_f32_16x16x32_bf16 v[66:69], v[154:157], v[222:225], v[66:69]
	v_mfma_f32_16x16x32_bf16 v[122:125], v[150:153], v[166:169], v[122:125]
	v_mfma_f32_16x16x32_bf16 v[114:117], v[158:161], v[166:169], v[114:117]
	v_mfma_f32_16x16x32_bf16 v[106:109], v[150:153], v[204:207], v[106:109]
	v_mfma_f32_16x16x32_bf16 v[98:101], v[158:161], v[204:207], v[98:101]
	v_mfma_f32_16x16x32_bf16 v[90:93], v[150:153], v[218:221], v[90:93]
	v_mfma_f32_16x16x32_bf16 v[82:85], v[158:161], v[218:221], v[82:85]
	v_mfma_f32_16x16x32_bf16 v[74:77], v[150:153], v[226:229], v[74:77]
	v_mfma_f32_16x16x32_bf16 v[66:69], v[158:161], v[226:229], v[66:69]
	s_setprio 0
	s_barrier
	s_addk_i32 s81, 0x80
	s_mov_b32 m0, s55
	v_add_u32_e32 v203, s81, v178
	ds_read_b128 v[162:165], v202 offset:49152
	ds_read_b128 v[166:169], v202 offset:50176
	ds_read_b128 v[170:173], v202 offset:51200
	ds_read_b128 v[204:207], v202 offset:52224
	ds_read_b128 v[214:217], v202 offset:53248
	ds_read_b128 v[218:221], v202 offset:54272
	ds_read_b128 v[222:225], v202 offset:55296
	ds_read_b128 v[226:229], v202 offset:56320
	global_load_lds_dwordx4 v203, s[6:7]
	v_add_u32_e32 v203, s35, v203
	s_mov_b32 m0, s56
	s_nop 0
	global_load_lds_dwordx4 v203, s[6:7]
	v_add_u32_e32 v203, s81, v179
	s_mov_b32 m0, s59
	s_nop 0
	global_load_lds_dwordx4 v203, s[6:7]
	v_add_u32_e32 v203, s35, v203
	s_mov_b32 m0, s60
	s_nop 0
	global_load_lds_dwordx4 v203, s[6:7]
	v_add_u32_e32 v203, s75, v181
	s_mov_b32 m0, s57
	s_nop 0
	global_load_lds_dwordx4 v203, s[4:5]
	v_add_u32_e32 v203, s31, v203
	s_mov_b32 m0, s58
	s_nop 0
	global_load_lds_dwordx4 v203, s[4:5]
	s_waitcnt vmcnt(8)
	s_waitcnt lgkmcnt(0)
	s_barrier
	s_setprio 1
	s_waitcnt lgkmcnt(0)
	v_mfma_f32_16x16x32_bf16 v[62:65], v[138:141], v[162:165], v[62:65]
	v_mfma_f32_16x16x32_bf16 v[54:57], v[134:137], v[162:165], v[54:57]
	v_mfma_f32_16x16x32_bf16 v[46:49], v[138:141], v[170:173], v[46:49]
	v_mfma_f32_16x16x32_bf16 v[38:41], v[134:137], v[170:173], v[38:41]
	v_mfma_f32_16x16x32_bf16 v[30:33], v[138:141], v[214:217], v[30:33]
	v_mfma_f32_16x16x32_bf16 v[22:25], v[134:137], v[214:217], v[22:25]
	v_mfma_f32_16x16x32_bf16 v[14:17], v[138:141], v[222:225], v[14:17]
	v_mfma_f32_16x16x32_bf16 v[6:9], v[134:137], v[222:225], v[6:9]
	v_mfma_f32_16x16x32_bf16 v[62:65], v[130:133], v[166:169], v[62:65]
	v_mfma_f32_16x16x32_bf16 v[54:57], v[146:149], v[166:169], v[54:57]
	v_mfma_f32_16x16x32_bf16 v[46:49], v[130:133], v[204:207], v[46:49]
	v_mfma_f32_16x16x32_bf16 v[38:41], v[146:149], v[204:207], v[38:41]
	v_mfma_f32_16x16x32_bf16 v[30:33], v[130:133], v[218:221], v[30:33]
	v_mfma_f32_16x16x32_bf16 v[22:25], v[146:149], v[218:221], v[22:25]
	v_mfma_f32_16x16x32_bf16 v[14:17], v[130:133], v[226:229], v[14:17]
	v_mfma_f32_16x16x32_bf16 v[6:9], v[146:149], v[226:229], v[6:9]
	v_mfma_f32_16x16x32_bf16 v[58:61], v[142:145], v[162:165], v[58:61]
	v_mfma_f32_16x16x32_bf16 v[50:53], v[154:157], v[162:165], v[50:53]
	v_mfma_f32_16x16x32_bf16 v[42:45], v[142:145], v[170:173], v[42:45]
	v_mfma_f32_16x16x32_bf16 v[34:37], v[154:157], v[170:173], v[34:37]
	v_mfma_f32_16x16x32_bf16 v[26:29], v[142:145], v[214:217], v[26:29]
	v_mfma_f32_16x16x32_bf16 v[18:21], v[154:157], v[214:217], v[18:21]
	v_mfma_f32_16x16x32_bf16 v[10:13], v[142:145], v[222:225], v[10:13]
	v_mfma_f32_16x16x32_bf16 v[2:5], v[154:157], v[222:225], v[2:5]
	v_mfma_f32_16x16x32_bf16 v[58:61], v[150:153], v[166:169], v[58:61]
	v_mfma_f32_16x16x32_bf16 v[50:53], v[158:161], v[166:169], v[50:53]
	v_mfma_f32_16x16x32_bf16 v[42:45], v[150:153], v[204:207], v[42:45]
	v_mfma_f32_16x16x32_bf16 v[34:37], v[158:161], v[204:207], v[34:37]
	v_mfma_f32_16x16x32_bf16 v[26:29], v[150:153], v[218:221], v[26:29]
	v_mfma_f32_16x16x32_bf16 v[18:21], v[158:161], v[218:221], v[18:21]
	v_mfma_f32_16x16x32_bf16 v[10:13], v[150:153], v[226:229], v[10:13]
	v_mfma_f32_16x16x32_bf16 v[2:5], v[158:161], v[226:229], v[2:5]
	s_setprio 0
	s_barrier
	s_add_i32 s80, s80, 2
	s_addk_i32 s28, 0x100
	s_addk_i32 s79, 0x100
	s_cmp_ge_i32 s80, s61
	s_cbranch_scc0 .LBB0_637

.LBB0_1181:
	s_andn2_b64 vcc, exec, s[16:17]
	s_waitcnt lgkmcnt(0)
	s_cbranch_vccnz .Lzs_4
	s_add_i32 s6, s58, 0x80
	s_add_i32 s58, s59, 0x100
	s_mov_b32 s59, 0
	ds_read_b128 v[114:117], v206
	ds_read_b128 v[118:121], v207
	ds_read_b128 v[122:125], v202
	ds_read_b128 v[126:129], v203
	ds_read_b128 v[146:149], v208
	ds_read_b128 v[150:153], v209
	ds_read_b128 v[154:157], v211
	ds_read_b128 v[158:161], v213
	s_add_i32 s60, s6, 0x80
	s_cmp_eq_u32 s90, s59
	s_cselect_b32 s61, s5, s58
	s_cselect_b32 s60, s7, s60
	v_add_u32_e32 v194, s6, v221
	s_add_i32 m0, s70, 0xc000
	ds_read_b128 v[162:165], v222
	ds_read_b128 v[170:173], v222 offset:1024
	ds_read_b128 v[174:177], v222 offset:2048
	ds_read_b128 v[178:181], v222 offset:3072
	ds_read_b128 v[182:185], v222 offset:4096
	ds_read_b128 v[186:189], v222 offset:5120
	ds_read_b128 v[190:193], v222 offset:6144
	ds_read_b128 v[226:229], v222 offset:7168
	global_load_lds_dwordx4 v194, s[8:9]
	v_add_u32_e32 v194, s6, v220
	s_add_i32 m0, s70, 0xe000
	s_nop 0
	global_load_lds_dwordx4 v194, s[8:9]
	s_waitcnt vmcnt(8)
	s_waitcnt lgkmcnt(0)
	s_barrier
	s_setprio 1
	s_waitcnt lgkmcnt(0)
	v_mfma_f32_16x16x32_bf16 v[142:145], v[122:125], v[162:165], 0
	v_mfma_f32_16x16x32_bf16 v[138:141], v[118:121], v[162:165], 0
	v_mfma_f32_16x16x32_bf16 v[110:113], v[122:125], v[174:177], 0
	v_mfma_f32_16x16x32_bf16 v[106:109], v[118:121], v[174:177], 0
	v_mfma_f32_16x16x32_bf16 v[94:97], v[122:125], v[182:185], 0
	v_mfma_f32_16x16x32_bf16 v[90:93], v[118:121], v[182:185], 0
	v_mfma_f32_16x16x32_bf16 v[78:81], v[122:125], v[190:193], 0
	v_mfma_f32_16x16x32_bf16 v[74:77], v[118:121], v[190:193], 0
	v_mfma_f32_16x16x32_bf16 v[142:145], v[114:117], v[170:173], v[142:145]
	v_mfma_f32_16x16x32_bf16 v[138:141], v[146:149], v[170:173], v[138:141]
	v_mfma_f32_16x16x32_bf16 v[110:113], v[114:117], v[178:181], v[110:113]
	v_mfma_f32_16x16x32_bf16 v[106:109], v[146:149], v[178:181], v[106:109]
	v_mfma_f32_16x16x32_bf16 v[94:97], v[114:117], v[186:189], v[94:97]
	v_mfma_f32_16x16x32_bf16 v[90:93], v[146:149], v[186:189], v[90:93]
	v_mfma_f32_16x16x32_bf16 v[78:81], v[114:117], v[226:229], v[78:81]
	v_mfma_f32_16x16x32_bf16 v[74:77], v[146:149], v[226:229], v[74:77]
	v_mfma_f32_16x16x32_bf16 v[134:137], v[126:129], v[162:165], 0
	v_mfma_f32_16x16x32_bf16 v[130:133], v[154:157], v[162:165], 0
	v_mfma_f32_16x16x32_bf16 v[102:105], v[126:129], v[174:177], 0
	v_mfma_f32_16x16x32_bf16 v[98:101], v[154:157], v[174:177], 0
	v_mfma_f32_16x16x32_bf16 v[86:89], v[126:129], v[182:185], 0
	v_mfma_f32_16x16x32_bf16 v[82:85], v[154:157], v[182:185], 0
	v_mfma_f32_16x16x32_bf16 v[70:73], v[126:129], v[190:193], 0
	v_mfma_f32_16x16x32_bf16 v[66:69], v[154:157], v[190:193], 0
	v_mfma_f32_16x16x32_bf16 v[134:137], v[150:153], v[170:173], v[134:137]
	v_mfma_f32_16x16x32_bf16 v[130:133], v[158:161], v[170:173], v[130:133]
	v_mfma_f32_16x16x32_bf16 v[102:105], v[150:153], v[178:181], v[102:105]
	v_mfma_f32_16x16x32_bf16 v[98:101], v[158:161], v[178:181], v[98:101]
	v_mfma_f32_16x16x32_bf16 v[86:89], v[150:153], v[186:189], v[86:89]
	v_mfma_f32_16x16x32_bf16 v[82:85], v[158:161], v[186:189], v[82:85]
	v_mfma_f32_16x16x32_bf16 v[70:73], v[150:153], v[226:229], v[70:73]
	v_mfma_f32_16x16x32_bf16 v[66:69], v[158:161], v[226:229], v[66:69]
	s_setprio 0
	s_barrier
	s_mov_b32 m0, s71
	v_add_u32_e32 v194, s61, v196
	ds_read_b128 v[162:165], v222 offset:16384
	ds_read_b128 v[170:173], v222 offset:17408
	ds_read_b128 v[174:177], v222 offset:18432
	ds_read_b128 v[178:181], v222 offset:19456
	ds_read_b128 v[182:185], v222 offset:20480
	ds_read_b128 v[186:189], v222 offset:21504
	ds_read_b128 v[190:193], v222 offset:22528
	ds_read_b128 v[226:229], v222 offset:23552
	global_load_lds_dwordx4 v194, s[20:21]
	v_add_u32_e32 v194, s35, v194
	s_mov_b32 m0, s72
	s_nop 0
	global_load_lds_dwordx4 v194, s[20:21]
	v_add_u32_e32 v194, s61, v197
	s_mov_b32 m0, s73
	s_nop 0
	global_load_lds_dwordx4 v194, s[20:21]
	v_add_u32_e32 v194, s35, v194
	s_mov_b32 m0, s76
	s_nop 0
	global_load_lds_dwordx4 v194, s[20:21]
	v_add_u32_e32 v194, s60, v1
	s_mov_b32 m0, s70
	s_nop 0
	global_load_lds_dwordx4 v194, s[8:9]
	v_add_u32_e32 v194, s29, v194
	s_mov_b32 m0, s77
	s_nop 0
	global_load_lds_dwordx4 v194, s[8:9]
	s_waitcnt vmcnt(8)
	s_waitcnt lgkmcnt(0)
	s_barrier
	s_setprio 1
	s_waitcnt lgkmcnt(0)
	v_mfma_f32_16x16x32_bf16 v[62:65], v[122:125], v[162:165], 0
	v_mfma_f32_16x16x32_bf16 v[58:61], v[118:121], v[162:165], 0
	v_mfma_f32_16x16x32_bf16 v[46:49], v[122:125], v[174:177], 0
	v_mfma_f32_16x16x32_bf16 v[42:45], v[118:121], v[174:177], 0
	v_mfma_f32_16x16x32_bf16 v[30:33], v[122:125], v[182:185], 0
	v_mfma_f32_16x16x32_bf16 v[26:29], v[118:121], v[182:185], 0
	v_mfma_f32_16x16x32_bf16 v[14:17], v[122:125], v[190:193], 0
	v_mfma_f32_16x16x32_bf16 v[10:13], v[118:121], v[190:193], 0
	v_mfma_f32_16x16x32_bf16 v[62:65], v[114:117], v[170:173], v[62:65]
	v_mfma_f32_16x16x32_bf16 v[58:61], v[146:149], v[170:173], v[58:61]
	v_mfma_f32_16x16x32_bf16 v[46:49], v[114:117], v[178:181], v[46:49]
	v_mfma_f32_16x16x32_bf16 v[42:45], v[146:149], v[178:181], v[42:45]
	v_mfma_f32_16x16x32_bf16 v[30:33], v[114:117], v[186:189], v[30:33]
	v_mfma_f32_16x16x32_bf16 v[26:29], v[146:149], v[186:189], v[26:29]
	v_mfma_f32_16x16x32_bf16 v[14:17], v[114:117], v[226:229], v[14:17]
	v_mfma_f32_16x16x32_bf16 v[10:13], v[146:149], v[226:229], v[10:13]
	v_mfma_f32_16x16x32_bf16 v[54:57], v[126:129], v[162:165], 0
	v_mfma_f32_16x16x32_bf16 v[50:53], v[154:157], v[162:165], 0
	v_mfma_f32_16x16x32_bf16 v[38:41], v[126:129], v[174:177], 0
	v_mfma_f32_16x16x32_bf16 v[34:37], v[154:157], v[174:177], 0
	v_mfma_f32_16x16x32_bf16 v[22:25], v[126:129], v[182:185], 0
	v_mfma_f32_16x16x32_bf16 v[18:21], v[154:157], v[182:185], 0
	v_mfma_f32_16x16x32_bf16 v[6:9], v[126:129], v[190:193], 0
	v_mfma_f32_16x16x32_bf16 v[2:5], v[154:157], v[190:193], 0
	v_mfma_f32_16x16x32_bf16 v[54:57], v[150:153], v[170:173], v[54:57]
	v_mfma_f32_16x16x32_bf16 v[50:53], v[158:161], v[170:173], v[50:53]
	v_mfma_f32_16x16x32_bf16 v[38:41], v[150:153], v[178:181], v[38:41]
	v_mfma_f32_16x16x32_bf16 v[34:37], v[158:161], v[178:181], v[34:37]
	v_mfma_f32_16x16x32_bf16 v[22:25], v[150:153], v[186:189], v[22:25]
	v_mfma_f32_16x16x32_bf16 v[18:21], v[158:161], v[186:189], v[18:21]
	v_mfma_f32_16x16x32_bf16 v[6:9], v[150:153], v[226:229], v[6:9]
	v_mfma_f32_16x16x32_bf16 v[2:5], v[158:161], v[226:229], v[2:5]
	s_setprio 0
	s_barrier
	s_branch .Lmid_4
.LBB0_1183:
	ds_read_b128 v[114:117], v206
	ds_read_b128 v[118:121], v207
	ds_read_b128 v[122:125], v202
	ds_read_b128 v[126:129], v203
	ds_read_b128 v[146:149], v208
	ds_read_b128 v[150:153], v209
	ds_read_b128 v[154:157], v211
	ds_read_b128 v[158:161], v213
	s_add_i32 s60, s6, 0x80
	s_cmp_eq_u32 s90, s59
	s_cselect_b32 s61, s5, s58
	s_cselect_b32 s60, s7, s60
	v_add_u32_e32 v194, s6, v221
	s_add_i32 m0, s70, 0xc000
	ds_read_b128 v[162:165], v222
	ds_read_b128 v[170:173], v222 offset:1024
	ds_read_b128 v[174:177], v222 offset:2048
	ds_read_b128 v[178:181], v222 offset:3072
	ds_read_b128 v[182:185], v222 offset:4096
	ds_read_b128 v[186:189], v222 offset:5120
	ds_read_b128 v[190:193], v222 offset:6144
	ds_read_b128 v[226:229], v222 offset:7168
	global_load_lds_dwordx4 v194, s[8:9]
	v_add_u32_e32 v194, s6, v220
	s_add_i32 m0, s70, 0xe000
	s_nop 0
	global_load_lds_dwordx4 v194, s[8:9]
	s_waitcnt vmcnt(8)
	s_waitcnt lgkmcnt(0)
	s_barrier
	s_setprio 1
	s_waitcnt lgkmcnt(0)
	v_mfma_f32_16x16x32_bf16 v[142:145], v[122:125], v[162:165], v[142:145]
	v_mfma_f32_16x16x32_bf16 v[138:141], v[118:121], v[162:165], v[138:141]
	v_mfma_f32_16x16x32_bf16 v[110:113], v[122:125], v[174:177], v[110:113]
	v_mfma_f32_16x16x32_bf16 v[106:109], v[118:121], v[174:177], v[106:109]
	v_mfma_f32_16x16x32_bf16 v[94:97], v[122:125], v[182:185], v[94:97]
	v_mfma_f32_16x16x32_bf16 v[90:93], v[118:121], v[182:185], v[90:93]
	v_mfma_f32_16x16x32_bf16 v[78:81], v[122:125], v[190:193], v[78:81]
	v_mfma_f32_16x16x32_bf16 v[74:77], v[118:121], v[190:193], v[74:77]
	v_mfma_f32_16x16x32_bf16 v[142:145], v[114:117], v[170:173], v[142:145]
	v_mfma_f32_16x16x32_bf16 v[138:141], v[146:149], v[170:173], v[138:141]
	v_mfma_f32_16x16x32_bf16 v[110:113], v[114:117], v[178:181], v[110:113]
	v_mfma_f32_16x16x32_bf16 v[106:109], v[146:149], v[178:181], v[106:109]
	v_mfma_f32_16x16x32_bf16 v[94:97], v[114:117], v[186:189], v[94:97]
	v_mfma_f32_16x16x32_bf16 v[90:93], v[146:149], v[186:189], v[90:93]
	v_mfma_f32_16x16x32_bf16 v[78:81], v[114:117], v[226:229], v[78:81]
	v_mfma_f32_16x16x32_bf16 v[74:77], v[146:149], v[226:229], v[74:77]
	v_mfma_f32_16x16x32_bf16 v[134:137], v[126:129], v[162:165], v[134:137]
	v_mfma_f32_16x16x32_bf16 v[130:133], v[154:157], v[162:165], v[130:133]
	v_mfma_f32_16x16x32_bf16 v[102:105], v[126:129], v[174:177], v[102:105]
	v_mfma_f32_16x16x32_bf16 v[98:101], v[154:157], v[174:177], v[98:101]
	v_mfma_f32_16x16x32_bf16 v[86:89], v[126:129], v[182:185], v[86:89]
	v_mfma_f32_16x16x32_bf16 v[82:85], v[154:157], v[182:185], v[82:85]
	v_mfma_f32_16x16x32_bf16 v[70:73], v[126:129], v[190:193], v[70:73]
	v_mfma_f32_16x16x32_bf16 v[66:69], v[154:157], v[190:193], v[66:69]
	v_mfma_f32_16x16x32_bf16 v[134:137], v[150:153], v[170:173], v[134:137]
	v_mfma_f32_16x16x32_bf16 v[130:133], v[158:161], v[170:173], v[130:133]
	v_mfma_f32_16x16x32_bf16 v[102:105], v[150:153], v[178:181], v[102:105]
	v_mfma_f32_16x16x32_bf16 v[98:101], v[158:161], v[178:181], v[98:101]
	v_mfma_f32_16x16x32_bf16 v[86:89], v[150:153], v[186:189], v[86:89]
	v_mfma_f32_16x16x32_bf16 v[82:85], v[158:161], v[186:189], v[82:85]
	v_mfma_f32_16x16x32_bf16 v[70:73], v[150:153], v[226:229], v[70:73]
	v_mfma_f32_16x16x32_bf16 v[66:69], v[158:161], v[226:229], v[66:69]
	s_setprio 0
	s_barrier
	s_mov_b32 m0, s71
	v_add_u32_e32 v194, s61, v196
	ds_read_b128 v[162:165], v222 offset:16384
	ds_read_b128 v[170:173], v222 offset:17408
	ds_read_b128 v[174:177], v222 offset:18432
	ds_read_b128 v[178:181], v222 offset:19456
	ds_read_b128 v[182:185], v222 offset:20480
	ds_read_b128 v[186:189], v222 offset:21504
	ds_read_b128 v[190:193], v222 offset:22528
	ds_read_b128 v[226:229], v222 offset:23552
	global_load_lds_dwordx4 v194, s[20:21]
	v_add_u32_e32 v194, s35, v194
	s_mov_b32 m0, s72
	s_nop 0
	global_load_lds_dwordx4 v194, s[20:21]
	v_add_u32_e32 v194, s61, v197
	s_mov_b32 m0, s73
	s_nop 0
	global_load_lds_dwordx4 v194, s[20:21]
	v_add_u32_e32 v194, s35, v194
	s_mov_b32 m0, s76
	s_nop 0
	global_load_lds_dwordx4 v194, s[20:21]
	v_add_u32_e32 v194, s60, v1
	s_mov_b32 m0, s70
	s_nop 0
	global_load_lds_dwordx4 v194, s[8:9]
	v_add_u32_e32 v194, s29, v194
	s_mov_b32 m0, s77
	s_nop 0
	global_load_lds_dwordx4 v194, s[8:9]
	s_waitcnt vmcnt(8)
	s_waitcnt lgkmcnt(0)
	s_barrier
	s_setprio 1
	s_waitcnt lgkmcnt(0)
	v_mfma_f32_16x16x32_bf16 v[62:65], v[122:125], v[162:165], v[62:65]
	v_mfma_f32_16x16x32_bf16 v[58:61], v[118:121], v[162:165], v[58:61]
	v_mfma_f32_16x16x32_bf16 v[46:49], v[122:125], v[174:177], v[46:49]
	v_mfma_f32_16x16x32_bf16 v[42:45], v[118:121], v[174:177], v[42:45]
	v_mfma_f32_16x16x32_bf16 v[30:33], v[122:125], v[182:185], v[30:33]
	v_mfma_f32_16x16x32_bf16 v[26:29], v[118:121], v[182:185], v[26:29]
	v_mfma_f32_16x16x32_bf16 v[14:17], v[122:125], v[190:193], v[14:17]
	v_mfma_f32_16x16x32_bf16 v[10:13], v[118:121], v[190:193], v[10:13]
	v_mfma_f32_16x16x32_bf16 v[62:65], v[114:117], v[170:173], v[62:65]
	v_mfma_f32_16x16x32_bf16 v[58:61], v[146:149], v[170:173], v[58:61]
	v_mfma_f32_16x16x32_bf16 v[46:49], v[114:117], v[178:181], v[46:49]
	v_mfma_f32_16x16x32_bf16 v[42:45], v[146:149], v[178:181], v[42:45]
	v_mfma_f32_16x16x32_bf16 v[30:33], v[114:117], v[186:189], v[30:33]
	v_mfma_f32_16x16x32_bf16 v[26:29], v[146:149], v[186:189], v[26:29]
	v_mfma_f32_16x16x32_bf16 v[14:17], v[114:117], v[226:229], v[14:17]
	v_mfma_f32_16x16x32_bf16 v[10:13], v[146:149], v[226:229], v[10:13]
	v_mfma_f32_16x16x32_bf16 v[54:57], v[126:129], v[162:165], v[54:57]
	v_mfma_f32_16x16x32_bf16 v[50:53], v[154:157], v[162:165], v[50:53]
	v_mfma_f32_16x16x32_bf16 v[38:41], v[126:129], v[174:177], v[38:41]
	v_mfma_f32_16x16x32_bf16 v[34:37], v[154:157], v[174:177], v[34:37]
	v_mfma_f32_16x16x32_bf16 v[22:25], v[126:129], v[182:185], v[22:25]
	v_mfma_f32_16x16x32_bf16 v[18:21], v[154:157], v[182:185], v[18:21]
	v_mfma_f32_16x16x32_bf16 v[6:9], v[126:129], v[190:193], v[6:9]
	v_mfma_f32_16x16x32_bf16 v[2:5], v[154:157], v[190:193], v[2:5]
	v_mfma_f32_16x16x32_bf16 v[54:57], v[150:153], v[170:173], v[54:57]
	v_mfma_f32_16x16x32_bf16 v[50:53], v[158:161], v[170:173], v[50:53]
	v_mfma_f32_16x16x32_bf16 v[38:41], v[150:153], v[178:181], v[38:41]
	v_mfma_f32_16x16x32_bf16 v[34:37], v[158:161], v[178:181], v[34:37]
	v_mfma_f32_16x16x32_bf16 v[22:25], v[150:153], v[186:189], v[22:25]
	v_mfma_f32_16x16x32_bf16 v[18:21], v[158:161], v[186:189], v[18:21]
	v_mfma_f32_16x16x32_bf16 v[6:9], v[150:153], v[226:229], v[6:9]
	v_mfma_f32_16x16x32_bf16 v[2:5], v[158:161], v[226:229], v[2:5]
	s_setprio 0
	s_barrier
.Lmid_4:
	ds_read_b128 v[114:117], v214
	ds_read_b128 v[118:121], v215
	ds_read_b128 v[122:125], v204
	ds_read_b128 v[126:129], v205
	ds_read_b128 v[146:149], v216
	ds_read_b128 v[150:153], v217
	ds_read_b128 v[154:157], v218
	ds_read_b128 v[158:161], v219
	s_mov_b32 m0, s78
	v_add_u32_e32 v194, s60, v198
	ds_read_b128 v[162:165], v222 offset:32768
	ds_read_b128 v[170:173], v222 offset:33792
	ds_read_b128 v[174:177], v222 offset:34816
	ds_read_b128 v[178:181], v222 offset:35840
	ds_read_b128 v[182:185], v222 offset:36864
	ds_read_b128 v[186:189], v222 offset:37888
	ds_read_b128 v[190:193], v222 offset:38912
	ds_read_b128 v[226:229], v222 offset:39936
	global_load_lds_dwordx4 v194, s[8:9]
	v_add_u32_e32 v194, s29, v194
	s_mov_b32 m0, s79
	s_nop 0
	global_load_lds_dwordx4 v194, s[8:9]
	s_waitcnt vmcnt(8)
	s_waitcnt lgkmcnt(0)
	s_barrier
	s_setprio 1
	s_waitcnt lgkmcnt(0)
	v_mfma_f32_16x16x32_bf16 v[142:145], v[122:125], v[162:165], v[142:145]
	v_mfma_f32_16x16x32_bf16 v[138:141], v[118:121], v[162:165], v[138:141]
	v_mfma_f32_16x16x32_bf16 v[110:113], v[122:125], v[174:177], v[110:113]
	v_mfma_f32_16x16x32_bf16 v[106:109], v[118:121], v[174:177], v[106:109]
	v_mfma_f32_16x16x32_bf16 v[94:97], v[122:125], v[182:185], v[94:97]
	v_mfma_f32_16x16x32_bf16 v[90:93], v[118:121], v[182:185], v[90:93]
	v_mfma_f32_16x16x32_bf16 v[78:81], v[122:125], v[190:193], v[78:81]
	v_mfma_f32_16x16x32_bf16 v[74:77], v[118:121], v[190:193], v[74:77]
	v_mfma_f32_16x16x32_bf16 v[142:145], v[114:117], v[170:173], v[142:145]
	v_mfma_f32_16x16x32_bf16 v[138:141], v[146:149], v[170:173], v[138:141]
	v_mfma_f32_16x16x32_bf16 v[110:113], v[114:117], v[178:181], v[110:113]
	v_mfma_f32_16x16x32_bf16 v[106:109], v[146:149], v[178:181], v[106:109]
	v_mfma_f32_16x16x32_bf16 v[94:97], v[114:117], v[186:189], v[94:97]
	v_mfma_f32_16x16x32_bf16 v[90:93], v[146:149], v[186:189], v[90:93]
	v_mfma_f32_16x16x32_bf16 v[78:81], v[114:117], v[226:229], v[78:81]
	v_mfma_f32_16x16x32_bf16 v[74:77], v[146:149], v[226:229], v[74:77]
	v_mfma_f32_16x16x32_bf16 v[134:137], v[126:129], v[162:165], v[134:137]
	v_mfma_f32_16x16x32_bf16 v[130:133], v[154:157], v[162:165], v[130:133]
	v_mfma_f32_16x16x32_bf16 v[102:105], v[126:129], v[174:177], v[102:105]
	v_mfma_f32_16x16x32_bf16 v[98:101], v[154:157], v[174:177], v[98:101]
	v_mfma_f32_16x16x32_bf16 v[86:89], v[126:129], v[182:185], v[86:89]
	v_mfma_f32_16x16x32_bf16 v[82:85], v[154:157], v[182:185], v[82:85]
	v_mfma_f32_16x16x32_bf16 v[70:73], v[126:129], v[190:193], v[70:73]
	v_mfma_f32_16x16x32_bf16 v[66:69], v[154:157], v[190:193], v[66:69]
	v_mfma_f32_16x16x32_bf16 v[134:137], v[150:153], v[170:173], v[134:137]
	v_mfma_f32_16x16x32_bf16 v[130:133], v[158:161], v[170:173], v[130:133]
	v_mfma_f32_16x16x32_bf16 v[102:105], v[150:153], v[178:181], v[102:105]
	v_mfma_f32_16x16x32_bf16 v[98:101], v[158:161], v[178:181], v[98:101]
	v_mfma_f32_16x16x32_bf16 v[86:89], v[150:153], v[186:189], v[86:89]
	v_mfma_f32_16x16x32_bf16 v[82:85], v[158:161], v[186:189], v[82:85]
	v_mfma_f32_16x16x32_bf16 v[70:73], v[150:153], v[226:229], v[70:73]
	v_mfma_f32_16x16x32_bf16 v[66:69], v[158:161], v[226:229], v[66:69]
	s_setprio 0
	s_barrier
	s_addk_i32 s61, 0x80
	s_mov_b32 m0, s81
	v_add_u32_e32 v194, s61, v196
	ds_read_b128 v[162:165], v222 offset:49152
	ds_read_b128 v[170:173], v222 offset:50176
	ds_read_b128 v[174:177], v222 offset:51200
	ds_read_b128 v[178:181], v222 offset:52224
	ds_read_b128 v[182:185], v222 offset:53248
	ds_read_b128 v[186:189], v222 offset:54272
	ds_read_b128 v[190:193], v222 offset:55296
	ds_read_b128 v[226:229], v222 offset:56320
	global_load_lds_dwordx4 v194, s[20:21]
	v_add_u32_e32 v194, s35, v194
	s_mov_b32 m0, s82
	s_nop 0
	global_load_lds_dwordx4 v194, s[20:21]
	v_add_u32_e32 v194, s61, v197
	s_mov_b32 m0, s85
	s_nop 0
	global_load_lds_dwordx4 v194, s[20:21]
	v_add_u32_e32 v194, s35, v194
	s_mov_b32 m0, s86
	s_nop 0
	global_load_lds_dwordx4 v194, s[20:21]
	v_add_u32_e32 v194, s60, v201
	s_mov_b32 m0, s83
	s_nop 0
	global_load_lds_dwordx4 v194, s[8:9]
	v_add_u32_e32 v194, s29, v194
	s_mov_b32 m0, s84
	s_nop 0
	global_load_lds_dwordx4 v194, s[8:9]
	s_waitcnt vmcnt(8)
	s_waitcnt lgkmcnt(0)
	s_barrier
	s_setprio 1
	s_waitcnt lgkmcnt(0)
	v_mfma_f32_16x16x32_bf16 v[62:65], v[122:125], v[162:165], v[62:65]
	v_mfma_f32_16x16x32_bf16 v[58:61], v[118:121], v[162:165], v[58:61]
	v_mfma_f32_16x16x32_bf16 v[46:49], v[122:125], v[174:177], v[46:49]
	v_mfma_f32_16x16x32_bf16 v[42:45], v[118:121], v[174:177], v[42:45]
	v_mfma_f32_16x16x32_bf16 v[30:33], v[122:125], v[182:185], v[30:33]
	v_mfma_f32_16x16x32_bf16 v[26:29], v[118:121], v[182:185], v[26:29]
	v_mfma_f32_16x16x32_bf16 v[14:17], v[122:125], v[190:193], v[14:17]
	v_mfma_f32_16x16x32_bf16 v[10:13], v[118:121], v[190:193], v[10:13]
	v_mfma_f32_16x16x32_bf16 v[62:65], v[114:117], v[170:173], v[62:65]
	v_mfma_f32_16x16x32_bf16 v[58:61], v[146:149], v[170:173], v[58:61]
	v_mfma_f32_16x16x32_bf16 v[46:49], v[114:117], v[178:181], v[46:49]
	v_mfma_f32_16x16x32_bf16 v[42:45], v[146:149], v[178:181], v[42:45]
	v_mfma_f32_16x16x32_bf16 v[30:33], v[114:117], v[186:189], v[30:33]
	v_mfma_f32_16x16x32_bf16 v[26:29], v[146:149], v[186:189], v[26:29]
	v_mfma_f32_16x16x32_bf16 v[14:17], v[114:117], v[226:229], v[14:17]
	v_mfma_f32_16x16x32_bf16 v[10:13], v[146:149], v[226:229], v[10:13]
	v_mfma_f32_16x16x32_bf16 v[54:57], v[126:129], v[162:165], v[54:57]
	v_mfma_f32_16x16x32_bf16 v[50:53], v[154:157], v[162:165], v[50:53]
	v_mfma_f32_16x16x32_bf16 v[38:41], v[126:129], v[174:177], v[38:41]
	v_mfma_f32_16x16x32_bf16 v[34:37], v[154:157], v[174:177], v[34:37]
	v_mfma_f32_16x16x32_bf16 v[22:25], v[126:129], v[182:185], v[22:25]
	v_mfma_f32_16x16x32_bf16 v[18:21], v[154:157], v[182:185], v[18:21]
	v_mfma_f32_16x16x32_bf16 v[6:9], v[126:129], v[190:193], v[6:9]
	v_mfma_f32_16x16x32_bf16 v[2:5], v[154:157], v[190:193], v[2:5]
	v_mfma_f32_16x16x32_bf16 v[54:57], v[150:153], v[170:173], v[54:57]
	v_mfma_f32_16x16x32_bf16 v[50:53], v[158:161], v[170:173], v[50:53]
	v_mfma_f32_16x16x32_bf16 v[38:41], v[150:153], v[178:181], v[38:41]
	v_mfma_f32_16x16x32_bf16 v[34:37], v[158:161], v[178:181], v[34:37]
	v_mfma_f32_16x16x32_bf16 v[22:25], v[150:153], v[186:189], v[22:25]
	v_mfma_f32_16x16x32_bf16 v[18:21], v[158:161], v[186:189], v[18:21]
	v_mfma_f32_16x16x32_bf16 v[6:9], v[150:153], v[226:229], v[6:9]
	v_mfma_f32_16x16x32_bf16 v[2:5], v[158:161], v[226:229], v[2:5]
	s_setprio 0
	s_barrier
	s_add_i32 s59, s59, 2
	s_addk_i32 s6, 0x100
	s_addk_i32 s58, 0x100
	s_cmp_ge_i32 s59, s87
	s_cbranch_scc0 .LBB0_1183

.Lphr_0:
	ds_read_b128 v[18:21], v177
	ds_read_b128 v[22:25], v178
	ds_read_b128 v[26:29], v185
	ds_read_b128 v[30:33], v186
	ds_read_b128 v[2:5], v179
	ds_read_b128 v[6:9], v180
	ds_read_b128 v[10:13], v187
	ds_read_b128 v[14:17], v188
	s_add_i32 s75, s92, 0x80
	s_and_b64 s[30:31], s[30:31], exec
	s_cselect_b32 s75, s75, s91
	s_cselect_b32 s96, s93, s29
	s_add_i32 s30, s75, 0x80
	s_add_i32 s31, s96, 0x80
	v_mov_b32_e32 v162, v1
	ds_read_b128 v[198:201], v193
	ds_read_b128 v[202:205], v193 offset:1024
	ds_read_b128 v[214:217], v193 offset:2048
	ds_read_b128 v[218:221], v193 offset:3072
	ds_read_b128 v[222:225], v193 offset:4096
	ds_read_b128 v[226:229], v193 offset:5120
	ds_read_b128 v[230:233], v193 offset:6144
	ds_read_b128 v[234:237], v193 offset:7168
	s_add_i32 s97, s92, s65
	v_add_u32_e32 v162, s97, v162
	s_add_i32 m0, s47, 0xc000
	s_add_i32 s97, s92, s74
	global_load_lds_dwordx4 v162, s[10:11]
	v_mov_b32_e32 v162, v1
	s_add_i32 m0, s47, 0xe000
	v_add_u32_e32 v162, s97, v162
	global_load_lds_dwordx4 v162, s[10:11]
	s_waitcnt vmcnt(8)
	s_waitcnt lgkmcnt(0)
	s_barrier
	s_setprio 1
	s_waitcnt lgkmcnt(0)
	v_mfma_f32_16x16x128_f8f6f4 v[158:161], v[18:25], v[198:205], 0
	v_mfma_f32_16x16x128_f8f6f4 v[150:153], v[26:33], v[198:205], 0
	v_mfma_f32_16x16x128_f8f6f4 v[142:145], v[18:25], v[214:221], 0
	v_mfma_f32_16x16x128_f8f6f4 v[134:137], v[26:33], v[214:221], 0
	v_mfma_f32_16x16x128_f8f6f4 v[126:129], v[18:25], v[222:229], 0
	v_mfma_f32_16x16x128_f8f6f4 v[118:121], v[26:33], v[222:229], 0
	v_mfma_f32_16x16x128_f8f6f4 v[110:113], v[18:25], v[230:237], 0
	v_mfma_f32_16x16x128_f8f6f4 v[102:105], v[26:33], v[230:237], 0
	v_mfma_f32_16x16x128_f8f6f4 v[154:157], v[2:9], v[198:205], 0
	v_mfma_f32_16x16x128_f8f6f4 v[146:149], v[10:17], v[198:205], 0
	v_mfma_f32_16x16x128_f8f6f4 v[138:141], v[2:9], v[214:221], 0
	v_mfma_f32_16x16x128_f8f6f4 v[130:133], v[10:17], v[214:221], 0
	v_mfma_f32_16x16x128_f8f6f4 v[122:125], v[2:9], v[222:229], 0
	v_mfma_f32_16x16x128_f8f6f4 v[114:117], v[10:17], v[222:229], 0
	v_mfma_f32_16x16x128_f8f6f4 v[106:109], v[2:9], v[230:237], 0
	v_mfma_f32_16x16x128_f8f6f4 v[98:101], v[10:17], v[230:237], 0
	s_setprio 0
	s_barrier
	v_mov_b32_e32 v162, v174
	ds_read_b128 v[198:201], v193 offset:16384
	ds_read_b128 v[202:205], v193 offset:17408
	ds_read_b128 v[214:217], v193 offset:18432
	ds_read_b128 v[218:221], v193 offset:19456
	ds_read_b128 v[222:225], v193 offset:20480
	ds_read_b128 v[226:229], v193 offset:21504
	ds_read_b128 v[230:233], v193 offset:22528
	ds_read_b128 v[234:237], v193 offset:23552
	s_mov_b32 m0, s48
	v_add_u32_e32 v162, s96, v162
	global_load_lds_dwordx4 v162, s[20:21]
	v_mov_b32_e32 v162, v174
	s_add_i32 s96, s96, s46
	v_add_u32_e32 v162, s96, v162
	s_mov_b32 m0, s49
	s_add_i32 s96, s96, s46
	global_load_lds_dwordx4 v162, s[20:21]
	v_mov_b32_e32 v162, v174
	s_mov_b32 m0, s50
	v_add_u32_e32 v162, s96, v162
	global_load_lds_dwordx4 v162, s[20:21]
	v_mov_b32_e32 v162, v174
	s_add_i32 s96, s96, s46
	v_add_u32_e32 v162, s96, v162
	s_mov_b32 m0, s51
	s_nop 0
	global_load_lds_dwordx4 v162, s[20:21]
	v_mov_b32_e32 v162, v1
	s_mov_b32 m0, s47
	v_add_u32_e32 v162, s75, v162
	global_load_lds_dwordx4 v162, s[10:11]
	v_mov_b32_e32 v162, v1
	s_add_i32 s75, s75, s45
	v_add_u32_e32 v162, s75, v162
	s_mov_b32 m0, s52
	s_nop 0
	global_load_lds_dwordx4 v162, s[10:11]
	s_waitcnt vmcnt(8)
	s_waitcnt lgkmcnt(0)
	s_barrier
	s_setprio 1
	s_waitcnt lgkmcnt(0)
	v_mfma_f32_16x16x128_f8f6f4 v[94:97], v[18:25], v[198:205], 0
	v_mfma_f32_16x16x128_f8f6f4 v[86:89], v[26:33], v[198:205], 0
	v_mfma_f32_16x16x128_f8f6f4 v[78:81], v[18:25], v[214:221], 0
	v_mfma_f32_16x16x128_f8f6f4 v[70:73], v[26:33], v[214:221], 0
	v_mfma_f32_16x16x128_f8f6f4 v[62:65], v[18:25], v[222:229], 0
	v_mfma_f32_16x16x128_f8f6f4 v[54:57], v[26:33], v[222:229], 0
	v_mfma_f32_16x16x128_f8f6f4 v[46:49], v[18:25], v[230:237], 0
	v_mfma_f32_16x16x128_f8f6f4 v[38:41], v[26:33], v[230:237], 0
	v_mfma_f32_16x16x128_f8f6f4 v[90:93], v[2:9], v[198:205], 0
	v_mfma_f32_16x16x128_f8f6f4 v[82:85], v[10:17], v[198:205], 0
	v_mfma_f32_16x16x128_f8f6f4 v[74:77], v[2:9], v[214:221], 0
	v_mfma_f32_16x16x128_f8f6f4 v[66:69], v[10:17], v[214:221], 0
	v_mfma_f32_16x16x128_f8f6f4 v[58:61], v[2:9], v[222:229], 0
	v_mfma_f32_16x16x128_f8f6f4 v[50:53], v[10:17], v[222:229], 0
	v_mfma_f32_16x16x128_f8f6f4 v[42:45], v[2:9], v[230:237], 0
	v_mfma_f32_16x16x128_f8f6f4 v[34:37], v[10:17], v[230:237], 0
	s_setprio 0
	s_barrier
	s_branch .Lmidr_0
.LBB0_1397:
	ds_read_b128 v[18:21], v177
	ds_read_b128 v[22:25], v178
	ds_read_b128 v[26:29], v185
	ds_read_b128 v[30:33], v186
	ds_read_b128 v[2:5], v179
	ds_read_b128 v[6:9], v180
	ds_read_b128 v[10:13], v187
	ds_read_b128 v[14:17], v188
	s_add_i32 s75, s92, 0x80
	s_and_b64 s[30:31], s[30:31], exec
	s_cselect_b32 s75, s75, s91
	s_cselect_b32 s96, s93, s29
	s_add_i32 s30, s75, 0x80
	s_add_i32 s31, s96, 0x80
	v_mov_b32_e32 v162, v1
	ds_read_b128 v[198:201], v193
	ds_read_b128 v[202:205], v193 offset:1024
	ds_read_b128 v[214:217], v193 offset:2048
	ds_read_b128 v[218:221], v193 offset:3072
	ds_read_b128 v[222:225], v193 offset:4096
	ds_read_b128 v[226:229], v193 offset:5120
	ds_read_b128 v[230:233], v193 offset:6144
	ds_read_b128 v[234:237], v193 offset:7168
	s_add_i32 s97, s92, s65
	v_add_u32_e32 v162, s97, v162
	s_add_i32 m0, s47, 0xc000
	s_add_i32 s97, s92, s74
	global_load_lds_dwordx4 v162, s[10:11]
	v_mov_b32_e32 v162, v1
	s_add_i32 m0, s47, 0xe000
	v_add_u32_e32 v162, s97, v162
	global_load_lds_dwordx4 v162, s[10:11]
	s_waitcnt vmcnt(8)
	s_waitcnt lgkmcnt(0)
	s_barrier
	s_setprio 1
	s_waitcnt lgkmcnt(0)
	v_mfma_f32_16x16x128_f8f6f4 v[158:161], v[18:25], v[198:205], v[158:161]
	v_mfma_f32_16x16x128_f8f6f4 v[150:153], v[26:33], v[198:205], v[150:153]
	v_mfma_f32_16x16x128_f8f6f4 v[142:145], v[18:25], v[214:221], v[142:145]
	v_mfma_f32_16x16x128_f8f6f4 v[134:137], v[26:33], v[214:221], v[134:137]
	v_mfma_f32_16x16x128_f8f6f4 v[126:129], v[18:25], v[222:229], v[126:129]
	v_mfma_f32_16x16x128_f8f6f4 v[118:121], v[26:33], v[222:229], v[118:121]
	v_mfma_f32_16x16x128_f8f6f4 v[110:113], v[18:25], v[230:237], v[110:113]
	v_mfma_f32_16x16x128_f8f6f4 v[102:105], v[26:33], v[230:237], v[102:105]
	v_mfma_f32_16x16x128_f8f6f4 v[154:157], v[2:9], v[198:205], v[154:157]
	v_mfma_f32_16x16x128_f8f6f4 v[146:149], v[10:17], v[198:205], v[146:149]
	v_mfma_f32_16x16x128_f8f6f4 v[138:141], v[2:9], v[214:221], v[138:141]
	v_mfma_f32_16x16x128_f8f6f4 v[130:133], v[10:17], v[214:221], v[130:133]
	v_mfma_f32_16x16x128_f8f6f4 v[122:125], v[2:9], v[222:229], v[122:125]
	v_mfma_f32_16x16x128_f8f6f4 v[114:117], v[10:17], v[222:229], v[114:117]
	v_mfma_f32_16x16x128_f8f6f4 v[106:109], v[2:9], v[230:237], v[106:109]
	v_mfma_f32_16x16x128_f8f6f4 v[98:101], v[10:17], v[230:237], v[98:101]
	s_setprio 0
	s_barrier
	v_mov_b32_e32 v162, v174
	ds_read_b128 v[198:201], v193 offset:16384
	ds_read_b128 v[202:205], v193 offset:17408
	ds_read_b128 v[214:217], v193 offset:18432
	ds_read_b128 v[218:221], v193 offset:19456
	ds_read_b128 v[222:225], v193 offset:20480
	ds_read_b128 v[226:229], v193 offset:21504
	ds_read_b128 v[230:233], v193 offset:22528
	ds_read_b128 v[234:237], v193 offset:23552
	s_mov_b32 m0, s48
	v_add_u32_e32 v162, s96, v162
	global_load_lds_dwordx4 v162, s[20:21]
	v_mov_b32_e32 v162, v174
	s_add_i32 s96, s96, s46
	v_add_u32_e32 v162, s96, v162
	s_mov_b32 m0, s49
	s_add_i32 s96, s96, s46
	global_load_lds_dwordx4 v162, s[20:21]
	v_mov_b32_e32 v162, v174
	s_mov_b32 m0, s50
	v_add_u32_e32 v162, s96, v162
	global_load_lds_dwordx4 v162, s[20:21]
	v_mov_b32_e32 v162, v174
	s_add_i32 s96, s96, s46
	v_add_u32_e32 v162, s96, v162
	s_mov_b32 m0, s51
	s_nop 0
	global_load_lds_dwordx4 v162, s[20:21]
	v_mov_b32_e32 v162, v1
	s_mov_b32 m0, s47
	v_add_u32_e32 v162, s75, v162
	global_load_lds_dwordx4 v162, s[10:11]
	v_mov_b32_e32 v162, v1
	s_add_i32 s75, s75, s45
	v_add_u32_e32 v162, s75, v162
	s_mov_b32 m0, s52
	s_nop 0
	global_load_lds_dwordx4 v162, s[10:11]
	s_waitcnt vmcnt(8)
	s_waitcnt lgkmcnt(0)
	s_barrier
	s_setprio 1
	s_waitcnt lgkmcnt(0)
	v_mfma_f32_16x16x128_f8f6f4 v[94:97], v[18:25], v[198:205], v[94:97]
	v_mfma_f32_16x16x128_f8f6f4 v[86:89], v[26:33], v[198:205], v[86:89]
	v_mfma_f32_16x16x128_f8f6f4 v[78:81], v[18:25], v[214:221], v[78:81]
	v_mfma_f32_16x16x128_f8f6f4 v[70:73], v[26:33], v[214:221], v[70:73]
	v_mfma_f32_16x16x128_f8f6f4 v[62:65], v[18:25], v[222:229], v[62:65]
	v_mfma_f32_16x16x128_f8f6f4 v[54:57], v[26:33], v[222:229], v[54:57]
	v_mfma_f32_16x16x128_f8f6f4 v[46:49], v[18:25], v[230:237], v[46:49]
	v_mfma_f32_16x16x128_f8f6f4 v[38:41], v[26:33], v[230:237], v[38:41]
	v_mfma_f32_16x16x128_f8f6f4 v[90:93], v[2:9], v[198:205], v[90:93]
	v_mfma_f32_16x16x128_f8f6f4 v[82:85], v[10:17], v[198:205], v[82:85]
	v_mfma_f32_16x16x128_f8f6f4 v[74:77], v[2:9], v[214:221], v[74:77]
	v_mfma_f32_16x16x128_f8f6f4 v[66:69], v[10:17], v[214:221], v[66:69]
	v_mfma_f32_16x16x128_f8f6f4 v[58:61], v[2:9], v[222:229], v[58:61]
	v_mfma_f32_16x16x128_f8f6f4 v[50:53], v[10:17], v[222:229], v[50:53]
	v_mfma_f32_16x16x128_f8f6f4 v[42:45], v[2:9], v[230:237], v[42:45]
	v_mfma_f32_16x16x128_f8f6f4 v[34:37], v[10:17], v[230:237], v[34:37]
	s_setprio 0
	s_barrier
.Lmidr_0:
	ds_read_b128 v[2:5], v181
	ds_read_b128 v[6:9], v182
	ds_read_b128 v[10:13], v189
	ds_read_b128 v[14:17], v190
	ds_read_b128 v[18:21], v183
	ds_read_b128 v[22:25], v184
	ds_read_b128 v[26:29], v191
	ds_read_b128 v[30:33], v192
	v_mov_b32_e32 v162, v1
	ds_read_b128 v[198:201], v193 offset:32768
	ds_read_b128 v[202:205], v193 offset:33792
	ds_read_b128 v[214:217], v193 offset:34816
	ds_read_b128 v[218:221], v193 offset:35840
	ds_read_b128 v[222:225], v193 offset:36864
	ds_read_b128 v[226:229], v193 offset:37888
	ds_read_b128 v[230:233], v193 offset:38912
	ds_read_b128 v[234:237], v193 offset:39936
	s_add_i32 s75, s75, s45
	s_mov_b32 m0, s53
	v_add_u32_e32 v162, s75, v162
	global_load_lds_dwordx4 v162, s[10:11]
	v_mov_b32_e32 v162, v1
	s_add_i32 s75, s75, s45
	v_add_u32_e32 v162, s75, v162
	s_mov_b32 m0, s54
	s_nop 0
	global_load_lds_dwordx4 v162, s[10:11]
	s_waitcnt vmcnt(8)
	s_waitcnt lgkmcnt(0)
	s_barrier
	s_setprio 1
	s_waitcnt lgkmcnt(0)
	v_mfma_f32_16x16x128_f8f6f4 v[158:161], v[2:9], v[198:205], v[158:161]
	v_mfma_f32_16x16x128_f8f6f4 v[150:153], v[10:17], v[198:205], v[150:153]
	v_mfma_f32_16x16x128_f8f6f4 v[142:145], v[2:9], v[214:221], v[142:145]
	v_mfma_f32_16x16x128_f8f6f4 v[134:137], v[10:17], v[214:221], v[134:137]
	v_mfma_f32_16x16x128_f8f6f4 v[126:129], v[2:9], v[222:229], v[126:129]
	v_mfma_f32_16x16x128_f8f6f4 v[118:121], v[10:17], v[222:229], v[118:121]
	v_mfma_f32_16x16x128_f8f6f4 v[110:113], v[2:9], v[230:237], v[110:113]
	v_mfma_f32_16x16x128_f8f6f4 v[102:105], v[10:17], v[230:237], v[102:105]
	v_mfma_f32_16x16x128_f8f6f4 v[154:157], v[18:25], v[198:205], v[154:157]
	v_mfma_f32_16x16x128_f8f6f4 v[146:149], v[26:33], v[198:205], v[146:149]
	v_mfma_f32_16x16x128_f8f6f4 v[138:141], v[18:25], v[214:221], v[138:141]
	v_mfma_f32_16x16x128_f8f6f4 v[130:133], v[26:33], v[214:221], v[130:133]
	v_mfma_f32_16x16x128_f8f6f4 v[122:125], v[18:25], v[222:229], v[122:125]
	v_mfma_f32_16x16x128_f8f6f4 v[114:117], v[26:33], v[222:229], v[114:117]
	v_mfma_f32_16x16x128_f8f6f4 v[106:109], v[18:25], v[230:237], v[106:109]
	v_mfma_f32_16x16x128_f8f6f4 v[98:101], v[26:33], v[230:237], v[98:101]
	s_setprio 0
	s_barrier
	v_mov_b32_e32 v162, v174
	ds_read_b128 v[198:201], v193 offset:49152
	ds_read_b128 v[202:205], v193 offset:50176
	ds_read_b128 v[214:217], v193 offset:51200
	ds_read_b128 v[218:221], v193 offset:52224
	ds_read_b128 v[222:225], v193 offset:53248
	ds_read_b128 v[226:229], v193 offset:54272
	ds_read_b128 v[230:233], v193 offset:55296
	ds_read_b128 v[234:237], v193 offset:56320
	s_mov_b32 m0, s58
	v_add_u32_e32 v162, s31, v162
	global_load_lds_dwordx4 v162, s[20:21]
	v_mov_b32_e32 v162, v174
	s_add_i32 s31, s31, s46
	v_add_u32_e32 v162, s31, v162
	s_mov_b32 m0, s59
	s_add_i32 s31, s31, s46
	global_load_lds_dwordx4 v162, s[20:21]
	v_mov_b32_e32 v162, v174
	s_mov_b32 m0, s62
	v_add_u32_e32 v162, s31, v162
	global_load_lds_dwordx4 v162, s[20:21]
	v_mov_b32_e32 v162, v174
	s_add_i32 s31, s31, s46
	v_add_u32_e32 v162, s31, v162
	s_mov_b32 m0, s63
	s_nop 0
	global_load_lds_dwordx4 v162, s[20:21]
	v_mov_b32_e32 v162, v1
	s_mov_b32 m0, s60
	v_add_u32_e32 v162, s30, v162
	global_load_lds_dwordx4 v162, s[10:11]
	v_mov_b32_e32 v162, v1
	s_add_i32 s30, s30, s45
	v_add_u32_e32 v162, s30, v162
	s_mov_b32 m0, s61
	s_nop 0
	global_load_lds_dwordx4 v162, s[10:11]
	s_waitcnt vmcnt(8)
	s_waitcnt lgkmcnt(0)
	s_barrier
	s_setprio 1
	s_waitcnt lgkmcnt(0)
	v_mfma_f32_16x16x128_f8f6f4 v[94:97], v[2:9], v[198:205], v[94:97]
	v_mfma_f32_16x16x128_f8f6f4 v[86:89], v[10:17], v[198:205], v[86:89]
	v_mfma_f32_16x16x128_f8f6f4 v[78:81], v[2:9], v[214:221], v[78:81]
	v_mfma_f32_16x16x128_f8f6f4 v[70:73], v[10:17], v[214:221], v[70:73]
	v_mfma_f32_16x16x128_f8f6f4 v[62:65], v[2:9], v[222:229], v[62:65]
	v_mfma_f32_16x16x128_f8f6f4 v[54:57], v[10:17], v[222:229], v[54:57]
	v_mfma_f32_16x16x128_f8f6f4 v[46:49], v[2:9], v[230:237], v[46:49]
	v_mfma_f32_16x16x128_f8f6f4 v[38:41], v[10:17], v[230:237], v[38:41]
	v_mfma_f32_16x16x128_f8f6f4 v[90:93], v[18:25], v[198:205], v[90:93]
	v_mfma_f32_16x16x128_f8f6f4 v[82:85], v[26:33], v[198:205], v[82:85]
	v_mfma_f32_16x16x128_f8f6f4 v[74:77], v[18:25], v[214:221], v[74:77]
	v_mfma_f32_16x16x128_f8f6f4 v[66:69], v[26:33], v[214:221], v[66:69]
	v_mfma_f32_16x16x128_f8f6f4 v[58:61], v[18:25], v[222:229], v[58:61]
	v_mfma_f32_16x16x128_f8f6f4 v[50:53], v[26:33], v[222:229], v[50:53]
	v_mfma_f32_16x16x128_f8f6f4 v[42:45], v[18:25], v[230:237], v[42:45]
	v_mfma_f32_16x16x128_f8f6f4 v[34:37], v[26:33], v[230:237], v[34:37]
	s_setprio 0
	s_barrier
	s_add_i32 s94, s94, 2
	s_addk_i32 s92, 0x100
	s_addk_i32 s93, 0x100
	s_cmp_ge_i32 s94, s64
	s_cbranch_scc1 .LBB0_1400

.LBB0_1601:
	s_andn2_b64 vcc, exec, s[12:13]
	s_cbranch_vccnz .Lzs_6
	s_add_i32 s6, s61, 0x80
	s_add_i32 s61, s62, 0x100
	s_mov_b32 s62, 0
	ds_read_b128 v[18:21], v235
	ds_read_b128 v[22:25], v236
	ds_read_b128 v[26:29], v243
	ds_read_b128 v[30:33], v244
	s_waitcnt lgkmcnt(0)
	ds_read_b128 v[2:5], v237
	ds_read_b128 v[6:9], v238
	ds_read_b128 v[10:13], v245
	ds_read_b128 v[14:17], v246
	s_add_i32 s63, s6, 0x80
	s_cmp_eq_u32 s89, s62
	s_cselect_b32 s65, s7, s63
	s_cselect_b32 s64, s5, s61
	s_add_i32 s63, s65, 0x80
	v_mov_b32_e32 v194, v1
	ds_read_b128 v[162:165], v251
	ds_read_b128 v[166:169], v251 offset:1024
	ds_read_b128 v[170:173], v251 offset:2048
	ds_read_b128 v[174:177], v251 offset:3072
	ds_read_b128 v[178:181], v251 offset:4096
	ds_read_b128 v[182:185], v251 offset:5120
	ds_read_b128 v[186:189], v251 offset:6144
	ds_read_b128 v[190:193], v251 offset:7168
	s_add_i32 s66, s6, s86
	v_add_u32_e32 v194, s66, v194
	s_add_i32 m0, s70, 0xc000
	s_add_i32 s66, s6, s93
	global_load_lds_dwordx4 v194, s[8:9]
	v_mov_b32_e32 v194, v1
	s_add_i32 m0, s70, 0xe000
	v_add_u32_e32 v194, s66, v194
	global_load_lds_dwordx4 v194, s[8:9]
	s_waitcnt vmcnt(8)
	s_waitcnt lgkmcnt(0)
	s_barrier
	s_setprio 1
	s_waitcnt lgkmcnt(0)
	v_mfma_f32_16x16x128_f8f6f4 v[158:161], v[18:25], v[162:169], 0
	v_mfma_f32_16x16x128_f8f6f4 v[154:157], v[26:33], v[162:169], 0
	v_mfma_f32_16x16x128_f8f6f4 v[142:145], v[18:25], v[170:177], 0
	v_mfma_f32_16x16x128_f8f6f4 v[138:141], v[26:33], v[170:177], 0
	v_mfma_f32_16x16x128_f8f6f4 v[126:129], v[18:25], v[178:185], 0
	v_mfma_f32_16x16x128_f8f6f4 v[122:125], v[26:33], v[178:185], 0
	v_mfma_f32_16x16x128_f8f6f4 v[110:113], v[18:25], v[186:193], 0
	v_mfma_f32_16x16x128_f8f6f4 v[106:109], v[26:33], v[186:193], 0
	v_mfma_f32_16x16x128_f8f6f4 v[150:153], v[2:9], v[162:169], 0
	v_mfma_f32_16x16x128_f8f6f4 v[146:149], v[10:17], v[162:169], 0
	v_mfma_f32_16x16x128_f8f6f4 v[134:137], v[2:9], v[170:177], 0
	v_mfma_f32_16x16x128_f8f6f4 v[130:133], v[10:17], v[170:177], 0
	v_mfma_f32_16x16x128_f8f6f4 v[118:121], v[2:9], v[178:185], 0
	v_mfma_f32_16x16x128_f8f6f4 v[114:117], v[10:17], v[178:185], 0
	v_mfma_f32_16x16x128_f8f6f4 v[102:105], v[2:9], v[186:193], 0
	v_mfma_f32_16x16x128_f8f6f4 v[98:101], v[10:17], v[186:193], 0
	s_setprio 0
	s_barrier
	v_mov_b32_e32 v194, v211
	ds_read_b128 v[162:165], v251 offset:16384
	ds_read_b128 v[166:169], v251 offset:17408
	ds_read_b128 v[170:173], v251 offset:18432
	ds_read_b128 v[174:177], v251 offset:19456
	ds_read_b128 v[178:181], v251 offset:20480
	ds_read_b128 v[182:185], v251 offset:21504
	ds_read_b128 v[186:189], v251 offset:22528
	ds_read_b128 v[190:193], v251 offset:23552
	s_mov_b32 m0, s71
	v_add_u32_e32 v194, s64, v194
	global_load_lds_dwordx4 v194, s[20:21]
	v_mov_b32_e32 v194, v211
	s_add_i32 s66, s64, s35
	v_add_u32_e32 v194, s66, v194
	s_mov_b32 m0, s72
	s_add_i32 s66, s66, s35
	global_load_lds_dwordx4 v194, s[20:21]
	v_mov_b32_e32 v194, v211
	s_mov_b32 m0, s73
	v_add_u32_e32 v194, s66, v194
	global_load_lds_dwordx4 v194, s[20:21]
	v_mov_b32_e32 v194, v211
	s_add_i32 s66, s66, s35
	v_add_u32_e32 v194, s66, v194
	s_mov_b32 m0, s76
	s_nop 0
	global_load_lds_dwordx4 v194, s[20:21]
	v_mov_b32_e32 v194, v1
	s_mov_b32 m0, s70
	v_add_u32_e32 v194, s65, v194
	global_load_lds_dwordx4 v194, s[8:9]
	v_mov_b32_e32 v194, v1
	s_add_i32 s65, s65, s23
	v_add_u32_e32 v194, s65, v194
	s_mov_b32 m0, s77
	s_nop 0
	global_load_lds_dwordx4 v194, s[8:9]
	s_waitcnt vmcnt(8)
	s_waitcnt lgkmcnt(0)
	s_barrier
	s_setprio 1
	s_waitcnt lgkmcnt(0)
	v_mfma_f32_16x16x128_f8f6f4 v[94:97], v[18:25], v[162:169], 0
	v_mfma_f32_16x16x128_f8f6f4 v[90:93], v[26:33], v[162:169], 0
	v_mfma_f32_16x16x128_f8f6f4 v[78:81], v[18:25], v[170:177], 0
	v_mfma_f32_16x16x128_f8f6f4 v[74:77], v[26:33], v[170:177], 0
	v_mfma_f32_16x16x128_f8f6f4 v[62:65], v[18:25], v[178:185], 0
	v_mfma_f32_16x16x128_f8f6f4 v[58:61], v[26:33], v[178:185], 0
	v_mfma_f32_16x16x128_f8f6f4 v[46:49], v[18:25], v[186:193], 0
	v_mfma_f32_16x16x128_f8f6f4 v[42:45], v[26:33], v[186:193], 0
	v_mfma_f32_16x16x128_f8f6f4 v[86:89], v[2:9], v[162:169], 0
	v_mfma_f32_16x16x128_f8f6f4 v[82:85], v[10:17], v[162:169], 0
	v_mfma_f32_16x16x128_f8f6f4 v[70:73], v[2:9], v[170:177], 0
	v_mfma_f32_16x16x128_f8f6f4 v[66:69], v[10:17], v[170:177], 0
	v_mfma_f32_16x16x128_f8f6f4 v[54:57], v[2:9], v[178:185], 0
	v_mfma_f32_16x16x128_f8f6f4 v[50:53], v[10:17], v[178:185], 0
	v_mfma_f32_16x16x128_f8f6f4 v[38:41], v[2:9], v[186:193], 0
	v_mfma_f32_16x16x128_f8f6f4 v[34:37], v[10:17], v[186:193], 0
	s_setprio 0
	s_barrier
	s_branch .Lmid_5
.LBB0_1603:
	ds_read_b128 v[18:21], v235
	ds_read_b128 v[22:25], v236
	ds_read_b128 v[26:29], v243
	ds_read_b128 v[30:33], v244
	s_waitcnt lgkmcnt(0)
	ds_read_b128 v[2:5], v237
	ds_read_b128 v[6:9], v238
	ds_read_b128 v[10:13], v245
	ds_read_b128 v[14:17], v246
	s_add_i32 s63, s6, 0x80
	s_cmp_eq_u32 s89, s62
	s_cselect_b32 s65, s7, s63
	s_cselect_b32 s64, s5, s61
	s_add_i32 s63, s65, 0x80
	v_mov_b32_e32 v194, v1
	ds_read_b128 v[162:165], v251
	ds_read_b128 v[166:169], v251 offset:1024
	ds_read_b128 v[170:173], v251 offset:2048
	ds_read_b128 v[174:177], v251 offset:3072
	ds_read_b128 v[178:181], v251 offset:4096
	ds_read_b128 v[182:185], v251 offset:5120
	ds_read_b128 v[186:189], v251 offset:6144
	ds_read_b128 v[190:193], v251 offset:7168
	s_add_i32 s66, s6, s86
	v_add_u32_e32 v194, s66, v194
	s_add_i32 m0, s70, 0xc000
	s_add_i32 s66, s6, s93
	global_load_lds_dwordx4 v194, s[8:9]
	v_mov_b32_e32 v194, v1
	s_add_i32 m0, s70, 0xe000
	v_add_u32_e32 v194, s66, v194
	global_load_lds_dwordx4 v194, s[8:9]
	s_waitcnt vmcnt(8)
	s_waitcnt lgkmcnt(0)
	s_barrier
	s_setprio 1
	s_waitcnt lgkmcnt(0)
	v_mfma_f32_16x16x128_f8f6f4 v[158:161], v[18:25], v[162:169], v[158:161]
	v_mfma_f32_16x16x128_f8f6f4 v[154:157], v[26:33], v[162:169], v[154:157]
	v_mfma_f32_16x16x128_f8f6f4 v[142:145], v[18:25], v[170:177], v[142:145]
	v_mfma_f32_16x16x128_f8f6f4 v[138:141], v[26:33], v[170:177], v[138:141]
	v_mfma_f32_16x16x128_f8f6f4 v[126:129], v[18:25], v[178:185], v[126:129]
	v_mfma_f32_16x16x128_f8f6f4 v[122:125], v[26:33], v[178:185], v[122:125]
	v_mfma_f32_16x16x128_f8f6f4 v[110:113], v[18:25], v[186:193], v[110:113]
	v_mfma_f32_16x16x128_f8f6f4 v[106:109], v[26:33], v[186:193], v[106:109]
	v_mfma_f32_16x16x128_f8f6f4 v[150:153], v[2:9], v[162:169], v[150:153]
	v_mfma_f32_16x16x128_f8f6f4 v[146:149], v[10:17], v[162:169], v[146:149]
	v_mfma_f32_16x16x128_f8f6f4 v[134:137], v[2:9], v[170:177], v[134:137]
	v_mfma_f32_16x16x128_f8f6f4 v[130:133], v[10:17], v[170:177], v[130:133]
	v_mfma_f32_16x16x128_f8f6f4 v[118:121], v[2:9], v[178:185], v[118:121]
	v_mfma_f32_16x16x128_f8f6f4 v[114:117], v[10:17], v[178:185], v[114:117]
	v_mfma_f32_16x16x128_f8f6f4 v[102:105], v[2:9], v[186:193], v[102:105]
	v_mfma_f32_16x16x128_f8f6f4 v[98:101], v[10:17], v[186:193], v[98:101]
	s_setprio 0
	s_barrier
	v_mov_b32_e32 v194, v211
	ds_read_b128 v[162:165], v251 offset:16384
	ds_read_b128 v[166:169], v251 offset:17408
	ds_read_b128 v[170:173], v251 offset:18432
	ds_read_b128 v[174:177], v251 offset:19456
	ds_read_b128 v[178:181], v251 offset:20480
	ds_read_b128 v[182:185], v251 offset:21504
	ds_read_b128 v[186:189], v251 offset:22528
	ds_read_b128 v[190:193], v251 offset:23552
	s_mov_b32 m0, s71
	v_add_u32_e32 v194, s64, v194
	global_load_lds_dwordx4 v194, s[20:21]
	v_mov_b32_e32 v194, v211
	s_add_i32 s66, s64, s35
	v_add_u32_e32 v194, s66, v194
	s_mov_b32 m0, s72
	s_add_i32 s66, s66, s35
	global_load_lds_dwordx4 v194, s[20:21]
	v_mov_b32_e32 v194, v211
	s_mov_b32 m0, s73
	v_add_u32_e32 v194, s66, v194
	global_load_lds_dwordx4 v194, s[20:21]
	v_mov_b32_e32 v194, v211
	s_add_i32 s66, s66, s35
	v_add_u32_e32 v194, s66, v194
	s_mov_b32 m0, s76
	s_nop 0
	global_load_lds_dwordx4 v194, s[20:21]
	v_mov_b32_e32 v194, v1
	s_mov_b32 m0, s70
	v_add_u32_e32 v194, s65, v194
	global_load_lds_dwordx4 v194, s[8:9]
	v_mov_b32_e32 v194, v1
	s_add_i32 s65, s65, s23
	v_add_u32_e32 v194, s65, v194
	s_mov_b32 m0, s77
	s_nop 0
	global_load_lds_dwordx4 v194, s[8:9]
	s_waitcnt vmcnt(8)
	s_waitcnt lgkmcnt(0)
	s_barrier
	s_setprio 1
	s_waitcnt lgkmcnt(0)
	v_mfma_f32_16x16x128_f8f6f4 v[94:97], v[18:25], v[162:169], v[94:97]
	v_mfma_f32_16x16x128_f8f6f4 v[90:93], v[26:33], v[162:169], v[90:93]
	v_mfma_f32_16x16x128_f8f6f4 v[78:81], v[18:25], v[170:177], v[78:81]
	v_mfma_f32_16x16x128_f8f6f4 v[74:77], v[26:33], v[170:177], v[74:77]
	v_mfma_f32_16x16x128_f8f6f4 v[62:65], v[18:25], v[178:185], v[62:65]
	v_mfma_f32_16x16x128_f8f6f4 v[58:61], v[26:33], v[178:185], v[58:61]
	v_mfma_f32_16x16x128_f8f6f4 v[46:49], v[18:25], v[186:193], v[46:49]
	v_mfma_f32_16x16x128_f8f6f4 v[42:45], v[26:33], v[186:193], v[42:45]
	v_mfma_f32_16x16x128_f8f6f4 v[86:89], v[2:9], v[162:169], v[86:89]
	v_mfma_f32_16x16x128_f8f6f4 v[82:85], v[10:17], v[162:169], v[82:85]
	v_mfma_f32_16x16x128_f8f6f4 v[70:73], v[2:9], v[170:177], v[70:73]
	v_mfma_f32_16x16x128_f8f6f4 v[66:69], v[10:17], v[170:177], v[66:69]
	v_mfma_f32_16x16x128_f8f6f4 v[54:57], v[2:9], v[178:185], v[54:57]
	v_mfma_f32_16x16x128_f8f6f4 v[50:53], v[10:17], v[178:185], v[50:53]
	v_mfma_f32_16x16x128_f8f6f4 v[38:41], v[2:9], v[186:193], v[38:41]
	v_mfma_f32_16x16x128_f8f6f4 v[34:37], v[10:17], v[186:193], v[34:37]
	s_setprio 0
	s_barrier
.Lmid_5:
	ds_read_b128 v[2:5], v239
	ds_read_b128 v[6:9], v240
	ds_read_b128 v[10:13], v247
	ds_read_b128 v[14:17], v248
	ds_read_b128 v[18:21], v241
	ds_read_b128 v[22:25], v242
	ds_read_b128 v[26:29], v249
	ds_read_b128 v[30:33], v250
	v_mov_b32_e32 v194, v1
	ds_read_b128 v[162:165], v251 offset:32768
	ds_read_b128 v[166:169], v251 offset:33792
	ds_read_b128 v[170:173], v251 offset:34816
	ds_read_b128 v[174:177], v251 offset:35840
	ds_read_b128 v[178:181], v251 offset:36864
	ds_read_b128 v[182:185], v251 offset:37888
	ds_read_b128 v[186:189], v251 offset:38912
	ds_read_b128 v[190:193], v251 offset:39936
	s_add_i32 s65, s65, s23
	s_mov_b32 m0, s78
	v_add_u32_e32 v194, s65, v194
	global_load_lds_dwordx4 v194, s[8:9]
	v_mov_b32_e32 v194, v1
	s_add_i32 s65, s65, s23
	v_add_u32_e32 v194, s65, v194
	s_mov_b32 m0, s44
	s_nop 0
	global_load_lds_dwordx4 v194, s[8:9]
	s_waitcnt vmcnt(8)
	s_waitcnt lgkmcnt(0)
	s_barrier
	s_setprio 1
	s_waitcnt lgkmcnt(0)
	v_mfma_f32_16x16x128_f8f6f4 v[158:161], v[2:9], v[162:169], v[158:161]
	v_mfma_f32_16x16x128_f8f6f4 v[154:157], v[10:17], v[162:169], v[154:157]
	v_mfma_f32_16x16x128_f8f6f4 v[142:145], v[2:9], v[170:177], v[142:145]
	v_mfma_f32_16x16x128_f8f6f4 v[138:141], v[10:17], v[170:177], v[138:141]
	v_mfma_f32_16x16x128_f8f6f4 v[126:129], v[2:9], v[178:185], v[126:129]
	v_mfma_f32_16x16x128_f8f6f4 v[122:125], v[10:17], v[178:185], v[122:125]
	v_mfma_f32_16x16x128_f8f6f4 v[110:113], v[2:9], v[186:193], v[110:113]
	v_mfma_f32_16x16x128_f8f6f4 v[106:109], v[10:17], v[186:193], v[106:109]
	v_mfma_f32_16x16x128_f8f6f4 v[150:153], v[18:25], v[162:169], v[150:153]
	v_mfma_f32_16x16x128_f8f6f4 v[146:149], v[26:33], v[162:169], v[146:149]
	v_mfma_f32_16x16x128_f8f6f4 v[134:137], v[18:25], v[170:177], v[134:137]
	v_mfma_f32_16x16x128_f8f6f4 v[130:133], v[26:33], v[170:177], v[130:133]
	v_mfma_f32_16x16x128_f8f6f4 v[118:121], v[18:25], v[178:185], v[118:121]
	v_mfma_f32_16x16x128_f8f6f4 v[114:117], v[26:33], v[178:185], v[114:117]
	v_mfma_f32_16x16x128_f8f6f4 v[102:105], v[18:25], v[186:193], v[102:105]
	v_mfma_f32_16x16x128_f8f6f4 v[98:101], v[26:33], v[186:193], v[98:101]
	s_setprio 0
	s_barrier
	v_mov_b32_e32 v194, v211
	ds_read_b128 v[162:165], v251 offset:49152
	ds_read_b128 v[166:169], v251 offset:50176
	ds_read_b128 v[170:173], v251 offset:51200
	ds_read_b128 v[174:177], v251 offset:52224
	ds_read_b128 v[178:181], v251 offset:53248
	ds_read_b128 v[182:185], v251 offset:54272
	ds_read_b128 v[186:189], v251 offset:55296
	ds_read_b128 v[190:193], v251 offset:56320
	s_addk_i32 s64, 0x80
	s_mov_b32 m0, s79
	v_add_u32_e32 v194, s64, v194
	global_load_lds_dwordx4 v194, s[20:21]
	v_mov_b32_e32 v194, v211
	s_add_i32 s64, s64, s35
	v_add_u32_e32 v194, s64, v194
	s_mov_b32 m0, s80
	s_add_i32 s64, s64, s35
	global_load_lds_dwordx4 v194, s[20:21]
	v_mov_b32_e32 v194, v211
	s_mov_b32 m0, s83
	v_add_u32_e32 v194, s64, v194
	global_load_lds_dwordx4 v194, s[20:21]
	v_mov_b32_e32 v194, v211
	s_add_i32 s64, s64, s35
	v_add_u32_e32 v194, s64, v194
	s_mov_b32 m0, s84
	s_nop 0
	global_load_lds_dwordx4 v194, s[20:21]
	v_mov_b32_e32 v194, v1
	s_mov_b32 m0, s81
	v_add_u32_e32 v194, s63, v194
	global_load_lds_dwordx4 v194, s[8:9]
	v_mov_b32_e32 v194, v1
	s_add_i32 s63, s63, s23
	v_add_u32_e32 v194, s63, v194
	s_mov_b32 m0, s82
	s_nop 0
	global_load_lds_dwordx4 v194, s[8:9]
	s_waitcnt vmcnt(8)
	s_waitcnt lgkmcnt(0)
	s_barrier
	s_setprio 1
	s_waitcnt lgkmcnt(0)
	v_mfma_f32_16x16x128_f8f6f4 v[94:97], v[2:9], v[162:169], v[94:97]
	v_mfma_f32_16x16x128_f8f6f4 v[90:93], v[10:17], v[162:169], v[90:93]
	v_mfma_f32_16x16x128_f8f6f4 v[78:81], v[2:9], v[170:177], v[78:81]
	v_mfma_f32_16x16x128_f8f6f4 v[74:77], v[10:17], v[170:177], v[74:77]
	v_mfma_f32_16x16x128_f8f6f4 v[62:65], v[2:9], v[178:185], v[62:65]
	v_mfma_f32_16x16x128_f8f6f4 v[58:61], v[10:17], v[178:185], v[58:61]
	v_mfma_f32_16x16x128_f8f6f4 v[46:49], v[2:9], v[186:193], v[46:49]
	v_mfma_f32_16x16x128_f8f6f4 v[42:45], v[10:17], v[186:193], v[42:45]
	v_mfma_f32_16x16x128_f8f6f4 v[86:89], v[18:25], v[162:169], v[86:89]
	v_mfma_f32_16x16x128_f8f6f4 v[82:85], v[26:33], v[162:169], v[82:85]
	v_mfma_f32_16x16x128_f8f6f4 v[70:73], v[18:25], v[170:177], v[70:73]
	v_mfma_f32_16x16x128_f8f6f4 v[66:69], v[26:33], v[170:177], v[66:69]
	v_mfma_f32_16x16x128_f8f6f4 v[54:57], v[18:25], v[178:185], v[54:57]
	v_mfma_f32_16x16x128_f8f6f4 v[50:53], v[26:33], v[178:185], v[50:53]
	v_mfma_f32_16x16x128_f8f6f4 v[38:41], v[18:25], v[186:193], v[38:41]
	v_mfma_f32_16x16x128_f8f6f4 v[34:37], v[26:33], v[186:193], v[34:37]
	s_setprio 0
	s_barrier
	s_add_i32 s62, s62, 2
	s_addk_i32 s6, 0x100
	s_addk_i32 s61, 0x100
	s_cmp_ge_i32 s62, s85
	s_cbranch_scc0 .LBB0_1603

.Lphr_1:
	ds_read_b128 v[132:135], v170
	ds_read_b128 v[136:139], v171
	ds_read_b128 v[140:143], v166
	ds_read_b128 v[154:157], v167
	ds_read_b128 v[188:191], v172
	ds_read_b128 v[192:195], v173
	ds_read_b128 v[196:199], v174
	ds_read_b128 v[200:203], v175
	s_add_i32 s75, s94, 0x80
	s_and_b64 s[50:51], s[50:51], exec
	s_cselect_b32 s50, s75, s49
	s_cselect_b32 s75, s95, s93
	s_add_i32 s51, s75, 0x80
	v_add_u32_e32 v144, s94, v183
	s_add_i32 m0, s52, 0xc000
	ds_read_b128 v[204:207], v184
	ds_read_b128 v[214:217], v184 offset:1024
	ds_read_b128 v[218:221], v184 offset:2048
	ds_read_b128 v[222:225], v184 offset:3072
	ds_read_b128 v[226:229], v184 offset:4096
	ds_read_b128 v[230:233], v184 offset:5120
	ds_read_b128 v[234:237], v184 offset:6144
	ds_read_b128 v[238:241], v184 offset:7168
	global_load_lds_dwordx4 v144, s[8:9]
	v_add_u32_e32 v144, s94, v182
	s_add_i32 m0, s52, 0xe000
	s_nop 0
	global_load_lds_dwordx4 v144, s[8:9]
	s_waitcnt vmcnt(8)
	s_waitcnt lgkmcnt(0)
	s_barrier
	s_setprio 1
	s_waitcnt lgkmcnt(0)
	v_mfma_f32_16x16x32_bf16 v[126:129], v[140:143], v[204:207], 0
	v_mfma_f32_16x16x32_bf16 v[122:125], v[136:139], v[204:207], 0
	v_mfma_f32_16x16x32_bf16 v[110:113], v[140:143], v[218:221], 0
	v_mfma_f32_16x16x32_bf16 v[106:109], v[136:139], v[218:221], 0
	v_mfma_f32_16x16x32_bf16 v[94:97], v[140:143], v[226:229], 0
	v_mfma_f32_16x16x32_bf16 v[90:93], v[136:139], v[226:229], 0
	v_mfma_f32_16x16x32_bf16 v[78:81], v[140:143], v[234:237], 0
	v_mfma_f32_16x16x32_bf16 v[74:77], v[136:139], v[234:237], 0
	v_mfma_f32_16x16x32_bf16 v[126:129], v[132:135], v[214:217], v[126:129]
	v_mfma_f32_16x16x32_bf16 v[122:125], v[188:191], v[214:217], v[122:125]
	v_mfma_f32_16x16x32_bf16 v[110:113], v[132:135], v[222:225], v[110:113]
	v_mfma_f32_16x16x32_bf16 v[106:109], v[188:191], v[222:225], v[106:109]
	v_mfma_f32_16x16x32_bf16 v[94:97], v[132:135], v[230:233], v[94:97]
	v_mfma_f32_16x16x32_bf16 v[90:93], v[188:191], v[230:233], v[90:93]
	v_mfma_f32_16x16x32_bf16 v[78:81], v[132:135], v[238:241], v[78:81]
	v_mfma_f32_16x16x32_bf16 v[74:77], v[188:191], v[238:241], v[74:77]
	v_mfma_f32_16x16x32_bf16 v[118:121], v[154:157], v[204:207], 0
	v_mfma_f32_16x16x32_bf16 v[114:117], v[196:199], v[204:207], 0
	v_mfma_f32_16x16x32_bf16 v[102:105], v[154:157], v[218:221], 0
	v_mfma_f32_16x16x32_bf16 v[98:101], v[196:199], v[218:221], 0
	v_mfma_f32_16x16x32_bf16 v[86:89], v[154:157], v[226:229], 0
	v_mfma_f32_16x16x32_bf16 v[82:85], v[196:199], v[226:229], 0
	v_mfma_f32_16x16x32_bf16 v[70:73], v[154:157], v[234:237], 0
	v_mfma_f32_16x16x32_bf16 v[66:69], v[196:199], v[234:237], 0
	v_mfma_f32_16x16x32_bf16 v[118:121], v[192:195], v[214:217], v[118:121]
	v_mfma_f32_16x16x32_bf16 v[114:117], v[200:203], v[214:217], v[114:117]
	v_mfma_f32_16x16x32_bf16 v[102:105], v[192:195], v[222:225], v[102:105]
	v_mfma_f32_16x16x32_bf16 v[98:101], v[200:203], v[222:225], v[98:101]
	v_mfma_f32_16x16x32_bf16 v[86:89], v[192:195], v[230:233], v[86:89]
	v_mfma_f32_16x16x32_bf16 v[82:85], v[200:203], v[230:233], v[82:85]
	v_mfma_f32_16x16x32_bf16 v[70:73], v[192:195], v[238:241], v[70:73]
	v_mfma_f32_16x16x32_bf16 v[66:69], v[200:203], v[238:241], v[66:69]
	s_setprio 0
	s_barrier
	s_mov_b32 m0, s53
	v_add_u32_e32 v144, s75, v160
	ds_read_b128 v[204:207], v184 offset:16384
	ds_read_b128 v[214:217], v184 offset:17408
	ds_read_b128 v[218:221], v184 offset:18432
	ds_read_b128 v[222:225], v184 offset:19456
	ds_read_b128 v[226:229], v184 offset:20480
	ds_read_b128 v[230:233], v184 offset:21504
	ds_read_b128 v[234:237], v184 offset:22528
	ds_read_b128 v[238:241], v184 offset:23552
	global_load_lds_dwordx4 v144, s[20:21]
	v_add_u32_e32 v144, s45, v144
	s_mov_b32 m0, s54
	s_nop 0
	global_load_lds_dwordx4 v144, s[20:21]
	v_add_u32_e32 v144, s75, v161
	s_mov_b32 m0, s55
	s_nop 0
	global_load_lds_dwordx4 v144, s[20:21]
	v_add_u32_e32 v144, s45, v144
	s_mov_b32 m0, s56
	s_nop 0
	global_load_lds_dwordx4 v144, s[20:21]
	v_add_u32_e32 v144, s50, v1
	s_mov_b32 m0, s52
	s_nop 0
	global_load_lds_dwordx4 v144, s[8:9]
	v_add_u32_e32 v144, s44, v144
	s_mov_b32 m0, s57
	s_nop 0
	global_load_lds_dwordx4 v144, s[8:9]
	s_waitcnt vmcnt(8)
	s_waitcnt lgkmcnt(0)
	s_barrier
	s_setprio 1
	s_waitcnt lgkmcnt(0)
	v_mfma_f32_16x16x32_bf16 v[62:65], v[140:143], v[204:207], 0
	v_mfma_f32_16x16x32_bf16 v[58:61], v[136:139], v[204:207], 0
	v_mfma_f32_16x16x32_bf16 v[46:49], v[140:143], v[218:221], 0
	v_mfma_f32_16x16x32_bf16 v[42:45], v[136:139], v[218:221], 0
	v_mfma_f32_16x16x32_bf16 v[30:33], v[140:143], v[226:229], 0
	v_mfma_f32_16x16x32_bf16 v[26:29], v[136:139], v[226:229], 0
	v_mfma_f32_16x16x32_bf16 v[14:17], v[140:143], v[234:237], 0
	v_mfma_f32_16x16x32_bf16 v[10:13], v[136:139], v[234:237], 0
	v_mfma_f32_16x16x32_bf16 v[62:65], v[132:135], v[214:217], v[62:65]
	v_mfma_f32_16x16x32_bf16 v[58:61], v[188:191], v[214:217], v[58:61]
	v_mfma_f32_16x16x32_bf16 v[46:49], v[132:135], v[222:225], v[46:49]
	v_mfma_f32_16x16x32_bf16 v[42:45], v[188:191], v[222:225], v[42:45]
	v_mfma_f32_16x16x32_bf16 v[30:33], v[132:135], v[230:233], v[30:33]
	v_mfma_f32_16x16x32_bf16 v[26:29], v[188:191], v[230:233], v[26:29]
	v_mfma_f32_16x16x32_bf16 v[14:17], v[132:135], v[238:241], v[14:17]
	v_mfma_f32_16x16x32_bf16 v[10:13], v[188:191], v[238:241], v[10:13]
	v_mfma_f32_16x16x32_bf16 v[54:57], v[154:157], v[204:207], 0
	v_mfma_f32_16x16x32_bf16 v[50:53], v[196:199], v[204:207], 0
	v_mfma_f32_16x16x32_bf16 v[38:41], v[154:157], v[218:221], 0
	v_mfma_f32_16x16x32_bf16 v[34:37], v[196:199], v[218:221], 0
	v_mfma_f32_16x16x32_bf16 v[22:25], v[154:157], v[226:229], 0
	v_mfma_f32_16x16x32_bf16 v[18:21], v[196:199], v[226:229], 0
	v_mfma_f32_16x16x32_bf16 v[6:9], v[154:157], v[234:237], 0
	v_mfma_f32_16x16x32_bf16 v[2:5], v[196:199], v[234:237], 0
	v_mfma_f32_16x16x32_bf16 v[54:57], v[192:195], v[214:217], v[54:57]
	v_mfma_f32_16x16x32_bf16 v[50:53], v[200:203], v[214:217], v[50:53]
	v_mfma_f32_16x16x32_bf16 v[38:41], v[192:195], v[222:225], v[38:41]
	v_mfma_f32_16x16x32_bf16 v[34:37], v[200:203], v[222:225], v[34:37]
	v_mfma_f32_16x16x32_bf16 v[22:25], v[192:195], v[230:233], v[22:25]
	v_mfma_f32_16x16x32_bf16 v[18:21], v[200:203], v[230:233], v[18:21]
	v_mfma_f32_16x16x32_bf16 v[6:9], v[192:195], v[238:241], v[6:9]
	v_mfma_f32_16x16x32_bf16 v[2:5], v[200:203], v[238:241], v[2:5]
	s_setprio 0
	s_barrier
	s_branch .Lmidr_1
.LBB0_1841:
	ds_read_b128 v[132:135], v170
	ds_read_b128 v[136:139], v171
	ds_read_b128 v[140:143], v166
	ds_read_b128 v[154:157], v167
	ds_read_b128 v[188:191], v172
	ds_read_b128 v[192:195], v173
	ds_read_b128 v[196:199], v174
	ds_read_b128 v[200:203], v175
	s_add_i32 s75, s94, 0x80
	s_and_b64 s[50:51], s[50:51], exec
	s_cselect_b32 s50, s75, s49
	s_cselect_b32 s75, s95, s93
	s_add_i32 s51, s75, 0x80
	v_add_u32_e32 v144, s94, v183
	s_add_i32 m0, s52, 0xc000
	ds_read_b128 v[204:207], v184
	ds_read_b128 v[214:217], v184 offset:1024
	ds_read_b128 v[218:221], v184 offset:2048
	ds_read_b128 v[222:225], v184 offset:3072
	ds_read_b128 v[226:229], v184 offset:4096
	ds_read_b128 v[230:233], v184 offset:5120
	ds_read_b128 v[234:237], v184 offset:6144
	ds_read_b128 v[238:241], v184 offset:7168
	global_load_lds_dwordx4 v144, s[8:9]
	v_add_u32_e32 v144, s94, v182
	s_add_i32 m0, s52, 0xe000
	s_nop 0
	global_load_lds_dwordx4 v144, s[8:9]
	s_waitcnt vmcnt(8)
	s_waitcnt lgkmcnt(0)
	s_barrier
	s_setprio 1
	s_waitcnt lgkmcnt(0)
	v_mfma_f32_16x16x32_bf16 v[126:129], v[140:143], v[204:207], v[126:129]
	v_mfma_f32_16x16x32_bf16 v[122:125], v[136:139], v[204:207], v[122:125]
	v_mfma_f32_16x16x32_bf16 v[110:113], v[140:143], v[218:221], v[110:113]
	v_mfma_f32_16x16x32_bf16 v[106:109], v[136:139], v[218:221], v[106:109]
	v_mfma_f32_16x16x32_bf16 v[94:97], v[140:143], v[226:229], v[94:97]
	v_mfma_f32_16x16x32_bf16 v[90:93], v[136:139], v[226:229], v[90:93]
	v_mfma_f32_16x16x32_bf16 v[78:81], v[140:143], v[234:237], v[78:81]
	v_mfma_f32_16x16x32_bf16 v[74:77], v[136:139], v[234:237], v[74:77]
	v_mfma_f32_16x16x32_bf16 v[126:129], v[132:135], v[214:217], v[126:129]
	v_mfma_f32_16x16x32_bf16 v[122:125], v[188:191], v[214:217], v[122:125]
	v_mfma_f32_16x16x32_bf16 v[110:113], v[132:135], v[222:225], v[110:113]
	v_mfma_f32_16x16x32_bf16 v[106:109], v[188:191], v[222:225], v[106:109]
	v_mfma_f32_16x16x32_bf16 v[94:97], v[132:135], v[230:233], v[94:97]
	v_mfma_f32_16x16x32_bf16 v[90:93], v[188:191], v[230:233], v[90:93]
	v_mfma_f32_16x16x32_bf16 v[78:81], v[132:135], v[238:241], v[78:81]
	v_mfma_f32_16x16x32_bf16 v[74:77], v[188:191], v[238:241], v[74:77]
	v_mfma_f32_16x16x32_bf16 v[118:121], v[154:157], v[204:207], v[118:121]
	v_mfma_f32_16x16x32_bf16 v[114:117], v[196:199], v[204:207], v[114:117]
	v_mfma_f32_16x16x32_bf16 v[102:105], v[154:157], v[218:221], v[102:105]
	v_mfma_f32_16x16x32_bf16 v[98:101], v[196:199], v[218:221], v[98:101]
	v_mfma_f32_16x16x32_bf16 v[86:89], v[154:157], v[226:229], v[86:89]
	v_mfma_f32_16x16x32_bf16 v[82:85], v[196:199], v[226:229], v[82:85]
	v_mfma_f32_16x16x32_bf16 v[70:73], v[154:157], v[234:237], v[70:73]
	v_mfma_f32_16x16x32_bf16 v[66:69], v[196:199], v[234:237], v[66:69]
	v_mfma_f32_16x16x32_bf16 v[118:121], v[192:195], v[214:217], v[118:121]
	v_mfma_f32_16x16x32_bf16 v[114:117], v[200:203], v[214:217], v[114:117]
	v_mfma_f32_16x16x32_bf16 v[102:105], v[192:195], v[222:225], v[102:105]
	v_mfma_f32_16x16x32_bf16 v[98:101], v[200:203], v[222:225], v[98:101]
	v_mfma_f32_16x16x32_bf16 v[86:89], v[192:195], v[230:233], v[86:89]
	v_mfma_f32_16x16x32_bf16 v[82:85], v[200:203], v[230:233], v[82:85]
	v_mfma_f32_16x16x32_bf16 v[70:73], v[192:195], v[238:241], v[70:73]
	v_mfma_f32_16x16x32_bf16 v[66:69], v[200:203], v[238:241], v[66:69]
	s_setprio 0
	s_barrier
	s_mov_b32 m0, s53
	v_add_u32_e32 v144, s75, v160
	ds_read_b128 v[204:207], v184 offset:16384
	ds_read_b128 v[214:217], v184 offset:17408
	ds_read_b128 v[218:221], v184 offset:18432
	ds_read_b128 v[222:225], v184 offset:19456
	ds_read_b128 v[226:229], v184 offset:20480
	ds_read_b128 v[230:233], v184 offset:21504
	ds_read_b128 v[234:237], v184 offset:22528
	ds_read_b128 v[238:241], v184 offset:23552
	global_load_lds_dwordx4 v144, s[20:21]
	v_add_u32_e32 v144, s45, v144
	s_mov_b32 m0, s54
	s_nop 0
	global_load_lds_dwordx4 v144, s[20:21]
	v_add_u32_e32 v144, s75, v161
	s_mov_b32 m0, s55
	s_nop 0
	global_load_lds_dwordx4 v144, s[20:21]
	v_add_u32_e32 v144, s45, v144
	s_mov_b32 m0, s56
	s_nop 0
	global_load_lds_dwordx4 v144, s[20:21]
	v_add_u32_e32 v144, s50, v1
	s_mov_b32 m0, s52
	s_nop 0
	global_load_lds_dwordx4 v144, s[8:9]
	v_add_u32_e32 v144, s44, v144
	s_mov_b32 m0, s57
	s_nop 0
	global_load_lds_dwordx4 v144, s[8:9]
	s_waitcnt vmcnt(8)
	s_waitcnt lgkmcnt(0)
	s_barrier
	s_setprio 1
	s_waitcnt lgkmcnt(0)
	v_mfma_f32_16x16x32_bf16 v[62:65], v[140:143], v[204:207], v[62:65]
	v_mfma_f32_16x16x32_bf16 v[58:61], v[136:139], v[204:207], v[58:61]
	v_mfma_f32_16x16x32_bf16 v[46:49], v[140:143], v[218:221], v[46:49]
	v_mfma_f32_16x16x32_bf16 v[42:45], v[136:139], v[218:221], v[42:45]
	v_mfma_f32_16x16x32_bf16 v[30:33], v[140:143], v[226:229], v[30:33]
	v_mfma_f32_16x16x32_bf16 v[26:29], v[136:139], v[226:229], v[26:29]
	v_mfma_f32_16x16x32_bf16 v[14:17], v[140:143], v[234:237], v[14:17]
	v_mfma_f32_16x16x32_bf16 v[10:13], v[136:139], v[234:237], v[10:13]
	v_mfma_f32_16x16x32_bf16 v[62:65], v[132:135], v[214:217], v[62:65]
	v_mfma_f32_16x16x32_bf16 v[58:61], v[188:191], v[214:217], v[58:61]
	v_mfma_f32_16x16x32_bf16 v[46:49], v[132:135], v[222:225], v[46:49]
	v_mfma_f32_16x16x32_bf16 v[42:45], v[188:191], v[222:225], v[42:45]
	v_mfma_f32_16x16x32_bf16 v[30:33], v[132:135], v[230:233], v[30:33]
	v_mfma_f32_16x16x32_bf16 v[26:29], v[188:191], v[230:233], v[26:29]
	v_mfma_f32_16x16x32_bf16 v[14:17], v[132:135], v[238:241], v[14:17]
	v_mfma_f32_16x16x32_bf16 v[10:13], v[188:191], v[238:241], v[10:13]
	v_mfma_f32_16x16x32_bf16 v[54:57], v[154:157], v[204:207], v[54:57]
	v_mfma_f32_16x16x32_bf16 v[50:53], v[196:199], v[204:207], v[50:53]
	v_mfma_f32_16x16x32_bf16 v[38:41], v[154:157], v[218:221], v[38:41]
	v_mfma_f32_16x16x32_bf16 v[34:37], v[196:199], v[218:221], v[34:37]
	v_mfma_f32_16x16x32_bf16 v[22:25], v[154:157], v[226:229], v[22:25]
	v_mfma_f32_16x16x32_bf16 v[18:21], v[196:199], v[226:229], v[18:21]
	v_mfma_f32_16x16x32_bf16 v[6:9], v[154:157], v[234:237], v[6:9]
	v_mfma_f32_16x16x32_bf16 v[2:5], v[196:199], v[234:237], v[2:5]
	v_mfma_f32_16x16x32_bf16 v[54:57], v[192:195], v[214:217], v[54:57]
	v_mfma_f32_16x16x32_bf16 v[50:53], v[200:203], v[214:217], v[50:53]
	v_mfma_f32_16x16x32_bf16 v[38:41], v[192:195], v[222:225], v[38:41]
	v_mfma_f32_16x16x32_bf16 v[34:37], v[200:203], v[222:225], v[34:37]
	v_mfma_f32_16x16x32_bf16 v[22:25], v[192:195], v[230:233], v[22:25]
	v_mfma_f32_16x16x32_bf16 v[18:21], v[200:203], v[230:233], v[18:21]
	v_mfma_f32_16x16x32_bf16 v[6:9], v[192:195], v[238:241], v[6:9]
	v_mfma_f32_16x16x32_bf16 v[2:5], v[200:203], v[238:241], v[2:5]
	s_setprio 0
	s_barrier
.Lmidr_1:
	ds_read_b128 v[132:135], v176
	ds_read_b128 v[136:139], v177
	ds_read_b128 v[140:143], v168
	ds_read_b128 v[154:157], v169
	ds_read_b128 v[188:191], v178
	ds_read_b128 v[192:195], v179
	ds_read_b128 v[196:199], v180
	ds_read_b128 v[200:203], v181
	s_mov_b32 m0, s58
	v_add_u32_e32 v144, s50, v162
	ds_read_b128 v[204:207], v184 offset:32768
	ds_read_b128 v[214:217], v184 offset:33792
	ds_read_b128 v[218:221], v184 offset:34816
	ds_read_b128 v[222:225], v184 offset:35840
	ds_read_b128 v[226:229], v184 offset:36864
	ds_read_b128 v[230:233], v184 offset:37888
	ds_read_b128 v[234:237], v184 offset:38912
	ds_read_b128 v[238:241], v184 offset:39936
	global_load_lds_dwordx4 v144, s[8:9]
	v_add_u32_e32 v144, s44, v144
	s_mov_b32 m0, s59
	s_nop 0
	global_load_lds_dwordx4 v144, s[8:9]
	s_waitcnt vmcnt(8)
	s_waitcnt lgkmcnt(0)
	s_barrier
	s_setprio 1
	s_waitcnt lgkmcnt(0)
	v_mfma_f32_16x16x32_bf16 v[126:129], v[140:143], v[204:207], v[126:129]
	v_mfma_f32_16x16x32_bf16 v[122:125], v[136:139], v[204:207], v[122:125]
	v_mfma_f32_16x16x32_bf16 v[110:113], v[140:143], v[218:221], v[110:113]
	v_mfma_f32_16x16x32_bf16 v[106:109], v[136:139], v[218:221], v[106:109]
	v_mfma_f32_16x16x32_bf16 v[94:97], v[140:143], v[226:229], v[94:97]
	v_mfma_f32_16x16x32_bf16 v[90:93], v[136:139], v[226:229], v[90:93]
	v_mfma_f32_16x16x32_bf16 v[78:81], v[140:143], v[234:237], v[78:81]
	v_mfma_f32_16x16x32_bf16 v[74:77], v[136:139], v[234:237], v[74:77]
	v_mfma_f32_16x16x32_bf16 v[126:129], v[132:135], v[214:217], v[126:129]
	v_mfma_f32_16x16x32_bf16 v[122:125], v[188:191], v[214:217], v[122:125]
	v_mfma_f32_16x16x32_bf16 v[110:113], v[132:135], v[222:225], v[110:113]
	v_mfma_f32_16x16x32_bf16 v[106:109], v[188:191], v[222:225], v[106:109]
	v_mfma_f32_16x16x32_bf16 v[94:97], v[132:135], v[230:233], v[94:97]
	v_mfma_f32_16x16x32_bf16 v[90:93], v[188:191], v[230:233], v[90:93]
	v_mfma_f32_16x16x32_bf16 v[78:81], v[132:135], v[238:241], v[78:81]
	v_mfma_f32_16x16x32_bf16 v[74:77], v[188:191], v[238:241], v[74:77]
	v_mfma_f32_16x16x32_bf16 v[118:121], v[154:157], v[204:207], v[118:121]
	v_mfma_f32_16x16x32_bf16 v[114:117], v[196:199], v[204:207], v[114:117]
	v_mfma_f32_16x16x32_bf16 v[102:105], v[154:157], v[218:221], v[102:105]
	v_mfma_f32_16x16x32_bf16 v[98:101], v[196:199], v[218:221], v[98:101]
	v_mfma_f32_16x16x32_bf16 v[86:89], v[154:157], v[226:229], v[86:89]
	v_mfma_f32_16x16x32_bf16 v[82:85], v[196:199], v[226:229], v[82:85]
	v_mfma_f32_16x16x32_bf16 v[70:73], v[154:157], v[234:237], v[70:73]
	v_mfma_f32_16x16x32_bf16 v[66:69], v[196:199], v[234:237], v[66:69]
	v_mfma_f32_16x16x32_bf16 v[118:121], v[192:195], v[214:217], v[118:121]
	v_mfma_f32_16x16x32_bf16 v[114:117], v[200:203], v[214:217], v[114:117]
	v_mfma_f32_16x16x32_bf16 v[102:105], v[192:195], v[222:225], v[102:105]
	v_mfma_f32_16x16x32_bf16 v[98:101], v[200:203], v[222:225], v[98:101]
	v_mfma_f32_16x16x32_bf16 v[86:89], v[192:195], v[230:233], v[86:89]
	v_mfma_f32_16x16x32_bf16 v[82:85], v[200:203], v[230:233], v[82:85]
	v_mfma_f32_16x16x32_bf16 v[70:73], v[192:195], v[238:241], v[70:73]
	v_mfma_f32_16x16x32_bf16 v[66:69], v[200:203], v[238:241], v[66:69]
	s_setprio 0
	s_barrier
	s_mov_b32 m0, s64
	v_add_u32_e32 v144, s51, v160
	ds_read_b128 v[204:207], v184 offset:49152
	ds_read_b128 v[214:217], v184 offset:50176
	ds_read_b128 v[218:221], v184 offset:51200
	ds_read_b128 v[222:225], v184 offset:52224
	ds_read_b128 v[226:229], v184 offset:53248
	ds_read_b128 v[230:233], v184 offset:54272
	ds_read_b128 v[234:237], v184 offset:55296
	ds_read_b128 v[238:241], v184 offset:56320
	global_load_lds_dwordx4 v144, s[20:21]
	v_add_u32_e32 v144, s45, v144
	s_mov_b32 m0, s65
	s_nop 0
	global_load_lds_dwordx4 v144, s[20:21]
	v_add_u32_e32 v144, s51, v161
	s_mov_b32 m0, s68
	s_nop 0
	global_load_lds_dwordx4 v144, s[20:21]
	v_add_u32_e32 v144, s45, v144
	s_mov_b32 m0, s69
	s_nop 0
	global_load_lds_dwordx4 v144, s[20:21]
	v_add_u32_e32 v144, s50, v165
	s_mov_b32 m0, s66
	s_nop 0
	global_load_lds_dwordx4 v144, s[8:9]
	v_add_u32_e32 v144, s44, v144
	s_mov_b32 m0, s67
	s_nop 0
	global_load_lds_dwordx4 v144, s[8:9]
	s_waitcnt vmcnt(8)
	s_waitcnt lgkmcnt(0)
	s_barrier
	s_setprio 1
	s_waitcnt lgkmcnt(0)
	v_mfma_f32_16x16x32_bf16 v[62:65], v[140:143], v[204:207], v[62:65]
	v_mfma_f32_16x16x32_bf16 v[58:61], v[136:139], v[204:207], v[58:61]
	v_mfma_f32_16x16x32_bf16 v[46:49], v[140:143], v[218:221], v[46:49]
	v_mfma_f32_16x16x32_bf16 v[42:45], v[136:139], v[218:221], v[42:45]
	v_mfma_f32_16x16x32_bf16 v[30:33], v[140:143], v[226:229], v[30:33]
	v_mfma_f32_16x16x32_bf16 v[26:29], v[136:139], v[226:229], v[26:29]
	v_mfma_f32_16x16x32_bf16 v[14:17], v[140:143], v[234:237], v[14:17]
	v_mfma_f32_16x16x32_bf16 v[10:13], v[136:139], v[234:237], v[10:13]
	v_mfma_f32_16x16x32_bf16 v[62:65], v[132:135], v[214:217], v[62:65]
	v_mfma_f32_16x16x32_bf16 v[58:61], v[188:191], v[214:217], v[58:61]
	v_mfma_f32_16x16x32_bf16 v[46:49], v[132:135], v[222:225], v[46:49]
	v_mfma_f32_16x16x32_bf16 v[42:45], v[188:191], v[222:225], v[42:45]
	v_mfma_f32_16x16x32_bf16 v[30:33], v[132:135], v[230:233], v[30:33]
	v_mfma_f32_16x16x32_bf16 v[26:29], v[188:191], v[230:233], v[26:29]
	v_mfma_f32_16x16x32_bf16 v[14:17], v[132:135], v[238:241], v[14:17]
	v_mfma_f32_16x16x32_bf16 v[10:13], v[188:191], v[238:241], v[10:13]
	v_mfma_f32_16x16x32_bf16 v[54:57], v[154:157], v[204:207], v[54:57]
	v_mfma_f32_16x16x32_bf16 v[50:53], v[196:199], v[204:207], v[50:53]
	v_mfma_f32_16x16x32_bf16 v[38:41], v[154:157], v[218:221], v[38:41]
	v_mfma_f32_16x16x32_bf16 v[34:37], v[196:199], v[218:221], v[34:37]
	v_mfma_f32_16x16x32_bf16 v[22:25], v[154:157], v[226:229], v[22:25]
	v_mfma_f32_16x16x32_bf16 v[18:21], v[196:199], v[226:229], v[18:21]
	v_mfma_f32_16x16x32_bf16 v[6:9], v[154:157], v[234:237], v[6:9]
	v_mfma_f32_16x16x32_bf16 v[2:5], v[196:199], v[234:237], v[2:5]
	v_mfma_f32_16x16x32_bf16 v[54:57], v[192:195], v[214:217], v[54:57]
	v_mfma_f32_16x16x32_bf16 v[50:53], v[200:203], v[214:217], v[50:53]
	v_mfma_f32_16x16x32_bf16 v[38:41], v[192:195], v[222:225], v[38:41]
	v_mfma_f32_16x16x32_bf16 v[34:37], v[200:203], v[222:225], v[34:37]
	v_mfma_f32_16x16x32_bf16 v[22:25], v[192:195], v[230:233], v[22:25]
	v_mfma_f32_16x16x32_bf16 v[18:21], v[200:203], v[230:233], v[18:21]
	v_mfma_f32_16x16x32_bf16 v[6:9], v[192:195], v[238:241], v[6:9]
	v_mfma_f32_16x16x32_bf16 v[2:5], v[200:203], v[238:241], v[2:5]
	s_setprio 0
	s_barrier
	s_add_i32 s96, s96, 2
	s_addk_i32 s94, 0x100
	s_addk_i32 s95, 0x100
	s_cmp_ge_i32 s96, s62
	s_cbranch_scc1 .LBB0_1844

.LBB0_2045:
	s_andn2_b64 vcc, exec, s[16:17]
	s_cbranch_vccnz .Lzs_8
	s_add_i32 s30, s48, 0x100
	s_mov_b32 s48, 0
	ds_read_b128 v[138:141], v156
	ds_read_b128 v[142:145], v157
	ds_read_b128 v[168:171], v152
	ds_read_b128 v[172:175], v153
	ds_read_b128 v[176:179], v158
	ds_read_b128 v[180:183], v159
	ds_read_b128 v[184:187], v160
	ds_read_b128 v[188:191], v161
	s_add_i32 s49, s48, 2
	s_add_i32 s50, s73, s46
	s_cmp_eq_u32 s71, s48
	s_cselect_b32 s48, s47, s50
	s_cselect_b32 s51, s31, s30
	v_add_u32_e32 v133, s46, v132
	s_add_i32 m0, s52, 0xc000
	ds_read_b128 v[192:195], v131
	ds_read_b128 v[196:199], v131 offset:1024
	ds_read_b128 v[200:203], v131 offset:2048
	ds_read_b128 v[204:207], v131 offset:3072
	ds_read_b128 v[214:217], v131 offset:4096
	ds_read_b128 v[218:221], v131 offset:5120
	ds_read_b128 v[222:225], v131 offset:6144
	ds_read_b128 v[226:229], v131 offset:7168
	global_load_lds_dwordx4 v133, s[6:7]
	v_add_u32_e32 v133, s46, v130
	s_add_i32 m0, s52, 0xe000
	s_nop 0
	global_load_lds_dwordx4 v133, s[6:7]
	s_waitcnt vmcnt(8)
	s_waitcnt lgkmcnt(0)
	s_barrier
	s_setprio 1
	s_waitcnt lgkmcnt(0)
	v_mfma_f32_16x16x32_bf16 v[122:125], v[168:171], v[192:195], 0
	v_mfma_f32_16x16x32_bf16 v[126:129], v[142:145], v[192:195], 0
	v_mfma_f32_16x16x32_bf16 v[110:113], v[168:171], v[200:203], 0
	v_mfma_f32_16x16x32_bf16 v[106:109], v[142:145], v[200:203], 0
	v_mfma_f32_16x16x32_bf16 v[94:97], v[168:171], v[214:217], 0
	v_mfma_f32_16x16x32_bf16 v[90:93], v[142:145], v[214:217], 0
	v_mfma_f32_16x16x32_bf16 v[78:81], v[168:171], v[222:225], 0
	v_mfma_f32_16x16x32_bf16 v[74:77], v[142:145], v[222:225], 0
	v_mfma_f32_16x16x32_bf16 v[122:125], v[138:141], v[196:199], v[122:125]
	v_mfma_f32_16x16x32_bf16 v[126:129], v[176:179], v[196:199], v[126:129]
	v_mfma_f32_16x16x32_bf16 v[110:113], v[138:141], v[204:207], v[110:113]
	v_mfma_f32_16x16x32_bf16 v[106:109], v[176:179], v[204:207], v[106:109]
	v_mfma_f32_16x16x32_bf16 v[94:97], v[138:141], v[218:221], v[94:97]
	v_mfma_f32_16x16x32_bf16 v[90:93], v[176:179], v[218:221], v[90:93]
	v_mfma_f32_16x16x32_bf16 v[78:81], v[138:141], v[226:229], v[78:81]
	v_mfma_f32_16x16x32_bf16 v[74:77], v[176:179], v[226:229], v[74:77]
	v_mfma_f32_16x16x32_bf16 v[118:121], v[172:175], v[192:195], 0
	v_mfma_f32_16x16x32_bf16 v[114:117], v[184:187], v[192:195], 0
	v_mfma_f32_16x16x32_bf16 v[102:105], v[172:175], v[200:203], 0
	v_mfma_f32_16x16x32_bf16 v[98:101], v[184:187], v[200:203], 0
	v_mfma_f32_16x16x32_bf16 v[86:89], v[172:175], v[214:217], 0
	v_mfma_f32_16x16x32_bf16 v[82:85], v[184:187], v[214:217], 0
	v_mfma_f32_16x16x32_bf16 v[70:73], v[172:175], v[222:225], 0
	v_mfma_f32_16x16x32_bf16 v[66:69], v[184:187], v[222:225], 0
	v_mfma_f32_16x16x32_bf16 v[118:121], v[180:183], v[196:199], v[118:121]
	v_mfma_f32_16x16x32_bf16 v[114:117], v[188:191], v[196:199], v[114:117]
	v_mfma_f32_16x16x32_bf16 v[102:105], v[180:183], v[204:207], v[102:105]
	v_mfma_f32_16x16x32_bf16 v[98:101], v[188:191], v[204:207], v[98:101]
	v_mfma_f32_16x16x32_bf16 v[86:89], v[180:183], v[218:221], v[86:89]
	v_mfma_f32_16x16x32_bf16 v[82:85], v[188:191], v[218:221], v[82:85]
	v_mfma_f32_16x16x32_bf16 v[70:73], v[180:183], v[226:229], v[70:73]
	v_mfma_f32_16x16x32_bf16 v[66:69], v[188:191], v[226:229], v[66:69]
	s_setprio 0
	s_barrier
	s_mov_b32 m0, s53
	v_add_u32_e32 v133, s51, v146
	ds_read_b128 v[192:195], v131 offset:16384
	ds_read_b128 v[196:199], v131 offset:17408
	ds_read_b128 v[200:203], v131 offset:18432
	ds_read_b128 v[204:207], v131 offset:19456
	ds_read_b128 v[214:217], v131 offset:20480
	ds_read_b128 v[218:221], v131 offset:21504
	ds_read_b128 v[222:225], v131 offset:22528
	ds_read_b128 v[226:229], v131 offset:23552
	global_load_lds_dwordx4 v133, s[8:9]
	v_add_u32_e32 v133, s45, v133
	s_mov_b32 m0, s54
	s_nop 0
	global_load_lds_dwordx4 v133, s[8:9]
	v_add_u32_e32 v133, s51, v147
	s_mov_b32 m0, s55
	s_nop 0
	global_load_lds_dwordx4 v133, s[8:9]
	v_add_u32_e32 v133, s45, v133
	s_mov_b32 m0, s56
	s_nop 0
	global_load_lds_dwordx4 v133, s[8:9]
	v_add_u32_e32 v133, s48, v1
	s_mov_b32 m0, s52
	s_nop 0
	global_load_lds_dwordx4 v133, s[6:7]
	v_add_u32_e32 v133, s44, v133
	s_mov_b32 m0, s57
	s_nop 0
	global_load_lds_dwordx4 v133, s[6:7]
	s_waitcnt vmcnt(8)
	s_waitcnt lgkmcnt(0)
	s_barrier
	s_setprio 1
	s_waitcnt lgkmcnt(0)
	v_mfma_f32_16x16x32_bf16 v[62:65], v[168:171], v[192:195], 0
	v_mfma_f32_16x16x32_bf16 v[58:61], v[142:145], v[192:195], 0
	v_mfma_f32_16x16x32_bf16 v[46:49], v[168:171], v[200:203], 0
	v_mfma_f32_16x16x32_bf16 v[42:45], v[142:145], v[200:203], 0
	v_mfma_f32_16x16x32_bf16 v[30:33], v[168:171], v[214:217], 0
	v_mfma_f32_16x16x32_bf16 v[26:29], v[142:145], v[214:217], 0
	v_mfma_f32_16x16x32_bf16 v[14:17], v[168:171], v[222:225], 0
	v_mfma_f32_16x16x32_bf16 v[10:13], v[142:145], v[222:225], 0
	v_mfma_f32_16x16x32_bf16 v[62:65], v[138:141], v[196:199], v[62:65]
	v_mfma_f32_16x16x32_bf16 v[58:61], v[176:179], v[196:199], v[58:61]
	v_mfma_f32_16x16x32_bf16 v[46:49], v[138:141], v[204:207], v[46:49]
	v_mfma_f32_16x16x32_bf16 v[42:45], v[176:179], v[204:207], v[42:45]
	v_mfma_f32_16x16x32_bf16 v[30:33], v[138:141], v[218:221], v[30:33]
	v_mfma_f32_16x16x32_bf16 v[26:29], v[176:179], v[218:221], v[26:29]
	v_mfma_f32_16x16x32_bf16 v[14:17], v[138:141], v[226:229], v[14:17]
	v_mfma_f32_16x16x32_bf16 v[10:13], v[176:179], v[226:229], v[10:13]
	v_mfma_f32_16x16x32_bf16 v[54:57], v[172:175], v[192:195], 0
	v_mfma_f32_16x16x32_bf16 v[50:53], v[184:187], v[192:195], 0
	v_mfma_f32_16x16x32_bf16 v[38:41], v[172:175], v[200:203], 0
	v_mfma_f32_16x16x32_bf16 v[34:37], v[184:187], v[200:203], 0
	v_mfma_f32_16x16x32_bf16 v[22:25], v[172:175], v[214:217], 0
	v_mfma_f32_16x16x32_bf16 v[18:21], v[184:187], v[214:217], 0
	v_mfma_f32_16x16x32_bf16 v[6:9], v[172:175], v[222:225], 0
	v_mfma_f32_16x16x32_bf16 v[2:5], v[184:187], v[222:225], 0
	v_mfma_f32_16x16x32_bf16 v[54:57], v[180:183], v[196:199], v[54:57]
	v_mfma_f32_16x16x32_bf16 v[50:53], v[188:191], v[196:199], v[50:53]
	v_mfma_f32_16x16x32_bf16 v[38:41], v[180:183], v[204:207], v[38:41]
	v_mfma_f32_16x16x32_bf16 v[34:37], v[188:191], v[204:207], v[34:37]
	v_mfma_f32_16x16x32_bf16 v[22:25], v[180:183], v[218:221], v[22:25]
	v_mfma_f32_16x16x32_bf16 v[18:21], v[188:191], v[218:221], v[18:21]
	v_mfma_f32_16x16x32_bf16 v[6:9], v[180:183], v[226:229], v[6:9]
	v_mfma_f32_16x16x32_bf16 v[2:5], v[188:191], v[226:229], v[2:5]
	s_setprio 0
	s_barrier
	s_branch .Lmid_6
.LBB0_2047:
	ds_read_b128 v[138:141], v156
	ds_read_b128 v[142:145], v157
	ds_read_b128 v[168:171], v152
	ds_read_b128 v[172:175], v153
	ds_read_b128 v[176:179], v158
	ds_read_b128 v[180:183], v159
	ds_read_b128 v[184:187], v160
	ds_read_b128 v[188:191], v161
	s_add_i32 s49, s48, 2
	s_add_i32 s50, s73, s46
	s_cmp_eq_u32 s71, s48
	s_cselect_b32 s48, s47, s50
	s_cselect_b32 s51, s31, s30
	v_add_u32_e32 v133, s46, v132
	s_add_i32 m0, s52, 0xc000
	ds_read_b128 v[192:195], v131
	ds_read_b128 v[196:199], v131 offset:1024
	ds_read_b128 v[200:203], v131 offset:2048
	ds_read_b128 v[204:207], v131 offset:3072
	ds_read_b128 v[214:217], v131 offset:4096
	ds_read_b128 v[218:221], v131 offset:5120
	ds_read_b128 v[222:225], v131 offset:6144
	ds_read_b128 v[226:229], v131 offset:7168
	global_load_lds_dwordx4 v133, s[6:7]
	v_add_u32_e32 v133, s46, v130
	s_add_i32 m0, s52, 0xe000
	s_nop 0
	global_load_lds_dwordx4 v133, s[6:7]
	s_waitcnt vmcnt(8)
	s_waitcnt lgkmcnt(0)
	s_barrier
	s_setprio 1
	s_waitcnt lgkmcnt(0)
	v_mfma_f32_16x16x32_bf16 v[122:125], v[168:171], v[192:195], v[122:125]
	v_mfma_f32_16x16x32_bf16 v[126:129], v[142:145], v[192:195], v[126:129]
	v_mfma_f32_16x16x32_bf16 v[110:113], v[168:171], v[200:203], v[110:113]
	v_mfma_f32_16x16x32_bf16 v[106:109], v[142:145], v[200:203], v[106:109]
	v_mfma_f32_16x16x32_bf16 v[94:97], v[168:171], v[214:217], v[94:97]
	v_mfma_f32_16x16x32_bf16 v[90:93], v[142:145], v[214:217], v[90:93]
	v_mfma_f32_16x16x32_bf16 v[78:81], v[168:171], v[222:225], v[78:81]
	v_mfma_f32_16x16x32_bf16 v[74:77], v[142:145], v[222:225], v[74:77]
	v_mfma_f32_16x16x32_bf16 v[122:125], v[138:141], v[196:199], v[122:125]
	v_mfma_f32_16x16x32_bf16 v[126:129], v[176:179], v[196:199], v[126:129]
	v_mfma_f32_16x16x32_bf16 v[110:113], v[138:141], v[204:207], v[110:113]
	v_mfma_f32_16x16x32_bf16 v[106:109], v[176:179], v[204:207], v[106:109]
	v_mfma_f32_16x16x32_bf16 v[94:97], v[138:141], v[218:221], v[94:97]
	v_mfma_f32_16x16x32_bf16 v[90:93], v[176:179], v[218:221], v[90:93]
	v_mfma_f32_16x16x32_bf16 v[78:81], v[138:141], v[226:229], v[78:81]
	v_mfma_f32_16x16x32_bf16 v[74:77], v[176:179], v[226:229], v[74:77]
	v_mfma_f32_16x16x32_bf16 v[118:121], v[172:175], v[192:195], v[118:121]
	v_mfma_f32_16x16x32_bf16 v[114:117], v[184:187], v[192:195], v[114:117]
	v_mfma_f32_16x16x32_bf16 v[102:105], v[172:175], v[200:203], v[102:105]
	v_mfma_f32_16x16x32_bf16 v[98:101], v[184:187], v[200:203], v[98:101]
	v_mfma_f32_16x16x32_bf16 v[86:89], v[172:175], v[214:217], v[86:89]
	v_mfma_f32_16x16x32_bf16 v[82:85], v[184:187], v[214:217], v[82:85]
	v_mfma_f32_16x16x32_bf16 v[70:73], v[172:175], v[222:225], v[70:73]
	v_mfma_f32_16x16x32_bf16 v[66:69], v[184:187], v[222:225], v[66:69]
	v_mfma_f32_16x16x32_bf16 v[118:121], v[180:183], v[196:199], v[118:121]
	v_mfma_f32_16x16x32_bf16 v[114:117], v[188:191], v[196:199], v[114:117]
	v_mfma_f32_16x16x32_bf16 v[102:105], v[180:183], v[204:207], v[102:105]
	v_mfma_f32_16x16x32_bf16 v[98:101], v[188:191], v[204:207], v[98:101]
	v_mfma_f32_16x16x32_bf16 v[86:89], v[180:183], v[218:221], v[86:89]
	v_mfma_f32_16x16x32_bf16 v[82:85], v[188:191], v[218:221], v[82:85]
	v_mfma_f32_16x16x32_bf16 v[70:73], v[180:183], v[226:229], v[70:73]
	v_mfma_f32_16x16x32_bf16 v[66:69], v[188:191], v[226:229], v[66:69]
	s_setprio 0
	s_barrier
	s_mov_b32 m0, s53
	v_add_u32_e32 v133, s51, v146
	ds_read_b128 v[192:195], v131 offset:16384
	ds_read_b128 v[196:199], v131 offset:17408
	ds_read_b128 v[200:203], v131 offset:18432
	ds_read_b128 v[204:207], v131 offset:19456
	ds_read_b128 v[214:217], v131 offset:20480
	ds_read_b128 v[218:221], v131 offset:21504
	ds_read_b128 v[222:225], v131 offset:22528
	ds_read_b128 v[226:229], v131 offset:23552
	global_load_lds_dwordx4 v133, s[8:9]
	v_add_u32_e32 v133, s45, v133
	s_mov_b32 m0, s54
	s_nop 0
	global_load_lds_dwordx4 v133, s[8:9]
	v_add_u32_e32 v133, s51, v147
	s_mov_b32 m0, s55
	s_nop 0
	global_load_lds_dwordx4 v133, s[8:9]
	v_add_u32_e32 v133, s45, v133
	s_mov_b32 m0, s56
	s_nop 0
	global_load_lds_dwordx4 v133, s[8:9]
	v_add_u32_e32 v133, s48, v1
	s_mov_b32 m0, s52
	s_nop 0
	global_load_lds_dwordx4 v133, s[6:7]
	v_add_u32_e32 v133, s44, v133
	s_mov_b32 m0, s57
	s_nop 0
	global_load_lds_dwordx4 v133, s[6:7]
	s_waitcnt vmcnt(8)
	s_waitcnt lgkmcnt(0)
	s_barrier
	s_setprio 1
	s_waitcnt lgkmcnt(0)
	v_mfma_f32_16x16x32_bf16 v[62:65], v[168:171], v[192:195], v[62:65]
	v_mfma_f32_16x16x32_bf16 v[58:61], v[142:145], v[192:195], v[58:61]
	v_mfma_f32_16x16x32_bf16 v[46:49], v[168:171], v[200:203], v[46:49]
	v_mfma_f32_16x16x32_bf16 v[42:45], v[142:145], v[200:203], v[42:45]
	v_mfma_f32_16x16x32_bf16 v[30:33], v[168:171], v[214:217], v[30:33]
	v_mfma_f32_16x16x32_bf16 v[26:29], v[142:145], v[214:217], v[26:29]
	v_mfma_f32_16x16x32_bf16 v[14:17], v[168:171], v[222:225], v[14:17]
	v_mfma_f32_16x16x32_bf16 v[10:13], v[142:145], v[222:225], v[10:13]
	v_mfma_f32_16x16x32_bf16 v[62:65], v[138:141], v[196:199], v[62:65]
	v_mfma_f32_16x16x32_bf16 v[58:61], v[176:179], v[196:199], v[58:61]
	v_mfma_f32_16x16x32_bf16 v[46:49], v[138:141], v[204:207], v[46:49]
	v_mfma_f32_16x16x32_bf16 v[42:45], v[176:179], v[204:207], v[42:45]
	v_mfma_f32_16x16x32_bf16 v[30:33], v[138:141], v[218:221], v[30:33]
	v_mfma_f32_16x16x32_bf16 v[26:29], v[176:179], v[218:221], v[26:29]
	v_mfma_f32_16x16x32_bf16 v[14:17], v[138:141], v[226:229], v[14:17]
	v_mfma_f32_16x16x32_bf16 v[10:13], v[176:179], v[226:229], v[10:13]
	v_mfma_f32_16x16x32_bf16 v[54:57], v[172:175], v[192:195], v[54:57]
	v_mfma_f32_16x16x32_bf16 v[50:53], v[184:187], v[192:195], v[50:53]
	v_mfma_f32_16x16x32_bf16 v[38:41], v[172:175], v[200:203], v[38:41]
	v_mfma_f32_16x16x32_bf16 v[34:37], v[184:187], v[200:203], v[34:37]
	v_mfma_f32_16x16x32_bf16 v[22:25], v[172:175], v[214:217], v[22:25]
	v_mfma_f32_16x16x32_bf16 v[18:21], v[184:187], v[214:217], v[18:21]
	v_mfma_f32_16x16x32_bf16 v[6:9], v[172:175], v[222:225], v[6:9]
	v_mfma_f32_16x16x32_bf16 v[2:5], v[184:187], v[222:225], v[2:5]
	v_mfma_f32_16x16x32_bf16 v[54:57], v[180:183], v[196:199], v[54:57]
	v_mfma_f32_16x16x32_bf16 v[50:53], v[188:191], v[196:199], v[50:53]
	v_mfma_f32_16x16x32_bf16 v[38:41], v[180:183], v[204:207], v[38:41]
	v_mfma_f32_16x16x32_bf16 v[34:37], v[188:191], v[204:207], v[34:37]
	v_mfma_f32_16x16x32_bf16 v[22:25], v[180:183], v[218:221], v[22:25]
	v_mfma_f32_16x16x32_bf16 v[18:21], v[188:191], v[218:221], v[18:21]
	v_mfma_f32_16x16x32_bf16 v[6:9], v[180:183], v[226:229], v[6:9]
	v_mfma_f32_16x16x32_bf16 v[2:5], v[188:191], v[226:229], v[2:5]
	s_setprio 0
	s_barrier
.Lmid_6:
	ds_read_b128 v[138:141], v162
	ds_read_b128 v[142:145], v163
	ds_read_b128 v[168:171], v154
	ds_read_b128 v[172:175], v155
	ds_read_b128 v[176:179], v164
	ds_read_b128 v[180:183], v165
	ds_read_b128 v[184:187], v166
	ds_read_b128 v[188:191], v167
	s_mov_b32 m0, s58
	v_add_u32_e32 v133, s48, v148
	ds_read_b128 v[192:195], v131 offset:32768
	ds_read_b128 v[196:199], v131 offset:33792
	ds_read_b128 v[200:203], v131 offset:34816
	ds_read_b128 v[204:207], v131 offset:35840
	ds_read_b128 v[214:217], v131 offset:36864
	ds_read_b128 v[218:221], v131 offset:37888
	ds_read_b128 v[222:225], v131 offset:38912
	ds_read_b128 v[226:229], v131 offset:39936
	global_load_lds_dwordx4 v133, s[6:7]
	v_add_u32_e32 v133, s44, v133
	s_mov_b32 m0, s59
	s_nop 0
	global_load_lds_dwordx4 v133, s[6:7]
	s_waitcnt vmcnt(8)
	s_waitcnt lgkmcnt(0)
	s_barrier
	s_setprio 1
	s_waitcnt lgkmcnt(0)
	v_mfma_f32_16x16x32_bf16 v[122:125], v[168:171], v[192:195], v[122:125]
	v_mfma_f32_16x16x32_bf16 v[126:129], v[142:145], v[192:195], v[126:129]
	v_mfma_f32_16x16x32_bf16 v[110:113], v[168:171], v[200:203], v[110:113]
	v_mfma_f32_16x16x32_bf16 v[106:109], v[142:145], v[200:203], v[106:109]
	v_mfma_f32_16x16x32_bf16 v[94:97], v[168:171], v[214:217], v[94:97]
	v_mfma_f32_16x16x32_bf16 v[90:93], v[142:145], v[214:217], v[90:93]
	v_mfma_f32_16x16x32_bf16 v[78:81], v[168:171], v[222:225], v[78:81]
	v_mfma_f32_16x16x32_bf16 v[74:77], v[142:145], v[222:225], v[74:77]
	v_mfma_f32_16x16x32_bf16 v[122:125], v[138:141], v[196:199], v[122:125]
	v_mfma_f32_16x16x32_bf16 v[126:129], v[176:179], v[196:199], v[126:129]
	v_mfma_f32_16x16x32_bf16 v[110:113], v[138:141], v[204:207], v[110:113]
	v_mfma_f32_16x16x32_bf16 v[106:109], v[176:179], v[204:207], v[106:109]
	v_mfma_f32_16x16x32_bf16 v[94:97], v[138:141], v[218:221], v[94:97]
	v_mfma_f32_16x16x32_bf16 v[90:93], v[176:179], v[218:221], v[90:93]
	v_mfma_f32_16x16x32_bf16 v[78:81], v[138:141], v[226:229], v[78:81]
	v_mfma_f32_16x16x32_bf16 v[74:77], v[176:179], v[226:229], v[74:77]
	v_mfma_f32_16x16x32_bf16 v[118:121], v[172:175], v[192:195], v[118:121]
	v_mfma_f32_16x16x32_bf16 v[114:117], v[184:187], v[192:195], v[114:117]
	v_mfma_f32_16x16x32_bf16 v[102:105], v[172:175], v[200:203], v[102:105]
	v_mfma_f32_16x16x32_bf16 v[98:101], v[184:187], v[200:203], v[98:101]
	v_mfma_f32_16x16x32_bf16 v[86:89], v[172:175], v[214:217], v[86:89]
	v_mfma_f32_16x16x32_bf16 v[82:85], v[184:187], v[214:217], v[82:85]
	v_mfma_f32_16x16x32_bf16 v[70:73], v[172:175], v[222:225], v[70:73]
	v_mfma_f32_16x16x32_bf16 v[66:69], v[184:187], v[222:225], v[66:69]
	v_mfma_f32_16x16x32_bf16 v[118:121], v[180:183], v[196:199], v[118:121]
	v_mfma_f32_16x16x32_bf16 v[114:117], v[188:191], v[196:199], v[114:117]
	v_mfma_f32_16x16x32_bf16 v[102:105], v[180:183], v[204:207], v[102:105]
	v_mfma_f32_16x16x32_bf16 v[98:101], v[188:191], v[204:207], v[98:101]
	v_mfma_f32_16x16x32_bf16 v[86:89], v[180:183], v[218:221], v[86:89]
	v_mfma_f32_16x16x32_bf16 v[82:85], v[188:191], v[218:221], v[82:85]
	v_mfma_f32_16x16x32_bf16 v[70:73], v[180:183], v[226:229], v[70:73]
	v_mfma_f32_16x16x32_bf16 v[66:69], v[188:191], v[226:229], v[66:69]
	s_setprio 0
	s_barrier
	s_addk_i32 s51, 0x80
	s_mov_b32 m0, s61
	v_add_u32_e32 v133, s51, v146
	ds_read_b128 v[192:195], v131 offset:49152
	ds_read_b128 v[196:199], v131 offset:50176
	ds_read_b128 v[200:203], v131 offset:51200
	ds_read_b128 v[204:207], v131 offset:52224
	ds_read_b128 v[214:217], v131 offset:53248
	ds_read_b128 v[218:221], v131 offset:54272
	ds_read_b128 v[222:225], v131 offset:55296
	ds_read_b128 v[226:229], v131 offset:56320
	global_load_lds_dwordx4 v133, s[8:9]
	v_add_u32_e32 v133, s45, v133
	s_mov_b32 m0, s62
	s_nop 0
	global_load_lds_dwordx4 v133, s[8:9]
	v_add_u32_e32 v133, s51, v147
	s_mov_b32 m0, s65
	s_nop 0
	global_load_lds_dwordx4 v133, s[8:9]
	v_add_u32_e32 v133, s45, v133
	s_mov_b32 m0, s66
	s_nop 0
	global_load_lds_dwordx4 v133, s[8:9]
	v_add_u32_e32 v133, s48, v149
	s_mov_b32 m0, s63
	s_nop 0
	global_load_lds_dwordx4 v133, s[6:7]
	v_add_u32_e32 v133, s44, v133
	s_mov_b32 m0, s64
	s_nop 0
	global_load_lds_dwordx4 v133, s[6:7]
	s_waitcnt vmcnt(8)
	s_waitcnt lgkmcnt(0)
	s_barrier
	s_setprio 1
	s_waitcnt lgkmcnt(0)
	v_mfma_f32_16x16x32_bf16 v[62:65], v[168:171], v[192:195], v[62:65]
	v_mfma_f32_16x16x32_bf16 v[58:61], v[142:145], v[192:195], v[58:61]
	v_mfma_f32_16x16x32_bf16 v[46:49], v[168:171], v[200:203], v[46:49]
	v_mfma_f32_16x16x32_bf16 v[42:45], v[142:145], v[200:203], v[42:45]
	v_mfma_f32_16x16x32_bf16 v[30:33], v[168:171], v[214:217], v[30:33]
	v_mfma_f32_16x16x32_bf16 v[26:29], v[142:145], v[214:217], v[26:29]
	v_mfma_f32_16x16x32_bf16 v[14:17], v[168:171], v[222:225], v[14:17]
	v_mfma_f32_16x16x32_bf16 v[10:13], v[142:145], v[222:225], v[10:13]
	v_mfma_f32_16x16x32_bf16 v[62:65], v[138:141], v[196:199], v[62:65]
	v_mfma_f32_16x16x32_bf16 v[58:61], v[176:179], v[196:199], v[58:61]
	v_mfma_f32_16x16x32_bf16 v[46:49], v[138:141], v[204:207], v[46:49]
	v_mfma_f32_16x16x32_bf16 v[42:45], v[176:179], v[204:207], v[42:45]
	v_mfma_f32_16x16x32_bf16 v[30:33], v[138:141], v[218:221], v[30:33]
	v_mfma_f32_16x16x32_bf16 v[26:29], v[176:179], v[218:221], v[26:29]
	v_mfma_f32_16x16x32_bf16 v[14:17], v[138:141], v[226:229], v[14:17]
	v_mfma_f32_16x16x32_bf16 v[10:13], v[176:179], v[226:229], v[10:13]
	v_mfma_f32_16x16x32_bf16 v[54:57], v[172:175], v[192:195], v[54:57]
	v_mfma_f32_16x16x32_bf16 v[50:53], v[184:187], v[192:195], v[50:53]
	v_mfma_f32_16x16x32_bf16 v[38:41], v[172:175], v[200:203], v[38:41]
	v_mfma_f32_16x16x32_bf16 v[34:37], v[184:187], v[200:203], v[34:37]
	v_mfma_f32_16x16x32_bf16 v[22:25], v[172:175], v[214:217], v[22:25]
	v_mfma_f32_16x16x32_bf16 v[18:21], v[184:187], v[214:217], v[18:21]
	v_mfma_f32_16x16x32_bf16 v[6:9], v[172:175], v[222:225], v[6:9]
	v_mfma_f32_16x16x32_bf16 v[2:5], v[184:187], v[222:225], v[2:5]
	v_mfma_f32_16x16x32_bf16 v[54:57], v[180:183], v[196:199], v[54:57]
	v_mfma_f32_16x16x32_bf16 v[50:53], v[188:191], v[196:199], v[50:53]
	v_mfma_f32_16x16x32_bf16 v[38:41], v[180:183], v[204:207], v[38:41]
	v_mfma_f32_16x16x32_bf16 v[34:37], v[188:191], v[204:207], v[34:37]
	v_mfma_f32_16x16x32_bf16 v[22:25], v[180:183], v[218:221], v[22:25]
	v_mfma_f32_16x16x32_bf16 v[18:21], v[188:191], v[218:221], v[18:21]
	v_mfma_f32_16x16x32_bf16 v[6:9], v[180:183], v[226:229], v[6:9]
	v_mfma_f32_16x16x32_bf16 v[2:5], v[188:191], v[226:229], v[2:5]
	s_setprio 0
	s_barrier
	s_addk_i32 s30, 0x100
	s_cmp_ge_i32 s49, s67
	s_mov_b32 s46, s50
	s_mov_b32 s48, s49
	s_cbranch_scc0 .LBB0_2047

.LBB0_2335:
	s_andn2_b64 vcc, exec, s[14:15]
	s_cbranch_vccnz .Lzs_9
	s_add_i32 s50, s87, 0x80
	s_add_i32 s87, s75, 0x100
	s_mov_b32 s88, 0
	ds_read_b128 v[130:133], v194
	ds_read_b128 v[134:137], v195
	ds_read_b128 v[138:141], v190
	ds_read_b128 v[142:145], v191
	ds_read_b128 v[146:149], v196
	ds_read_b128 v[150:153], v197
	ds_read_b128 v[154:157], v198
	ds_read_b128 v[158:161], v199
	s_add_i32 s75, s50, 0x80
	s_cmp_eq_u32 s70, s88
	s_cselect_b32 s89, s51, s87
	s_cselect_b32 s75, s49, s75
	v_add_u32_e32 v178, s50, v207
	s_add_i32 m0, s53, 0xc000
	ds_read_b128 v[162:165], v208
	ds_read_b128 v[166:169], v208 offset:1024
	ds_read_b128 v[170:173], v208 offset:2048
	ds_read_b128 v[180:183], v208 offset:3072
	ds_read_b128 v[214:217], v208 offset:4096
	ds_read_b128 v[218:221], v208 offset:5120
	ds_read_b128 v[222:225], v208 offset:6144
	ds_read_b128 v[226:229], v208 offset:7168
	global_load_lds_dwordx4 v178, s[4:5]
	v_add_u32_e32 v178, s50, v206
	s_add_i32 m0, s53, 0xe000
	s_nop 0
	global_load_lds_dwordx4 v178, s[4:5]
	s_waitcnt vmcnt(8)
	s_waitcnt lgkmcnt(0)
	s_barrier
	s_setprio 1
	s_waitcnt lgkmcnt(0)
	v_mfma_f32_16x16x32_bf16 v[126:129], v[138:141], v[162:165], 0
	v_mfma_f32_16x16x32_bf16 v[122:125], v[134:137], v[162:165], 0
	v_mfma_f32_16x16x32_bf16 v[110:113], v[138:141], v[170:173], 0
	v_mfma_f32_16x16x32_bf16 v[106:109], v[134:137], v[170:173], 0
	v_mfma_f32_16x16x32_bf16 v[94:97], v[138:141], v[214:217], 0
	v_mfma_f32_16x16x32_bf16 v[90:93], v[134:137], v[214:217], 0
	v_mfma_f32_16x16x32_bf16 v[78:81], v[138:141], v[222:225], 0
	v_mfma_f32_16x16x32_bf16 v[74:77], v[134:137], v[222:225], 0
	v_mfma_f32_16x16x32_bf16 v[126:129], v[130:133], v[166:169], v[126:129]
	v_mfma_f32_16x16x32_bf16 v[122:125], v[146:149], v[166:169], v[122:125]
	v_mfma_f32_16x16x32_bf16 v[110:113], v[130:133], v[180:183], v[110:113]
	v_mfma_f32_16x16x32_bf16 v[106:109], v[146:149], v[180:183], v[106:109]
	v_mfma_f32_16x16x32_bf16 v[94:97], v[130:133], v[218:221], v[94:97]
	v_mfma_f32_16x16x32_bf16 v[90:93], v[146:149], v[218:221], v[90:93]
	v_mfma_f32_16x16x32_bf16 v[78:81], v[130:133], v[226:229], v[78:81]
	v_mfma_f32_16x16x32_bf16 v[74:77], v[146:149], v[226:229], v[74:77]
	v_mfma_f32_16x16x32_bf16 v[118:121], v[142:145], v[162:165], 0
	v_mfma_f32_16x16x32_bf16 v[114:117], v[154:157], v[162:165], 0
	v_mfma_f32_16x16x32_bf16 v[102:105], v[142:145], v[170:173], 0
	v_mfma_f32_16x16x32_bf16 v[98:101], v[154:157], v[170:173], 0
	v_mfma_f32_16x16x32_bf16 v[86:89], v[142:145], v[214:217], 0
	v_mfma_f32_16x16x32_bf16 v[82:85], v[154:157], v[214:217], 0
	v_mfma_f32_16x16x32_bf16 v[70:73], v[142:145], v[222:225], 0
	v_mfma_f32_16x16x32_bf16 v[66:69], v[154:157], v[222:225], 0
	v_mfma_f32_16x16x32_bf16 v[118:121], v[150:153], v[166:169], v[118:121]
	v_mfma_f32_16x16x32_bf16 v[114:117], v[158:161], v[166:169], v[114:117]
	v_mfma_f32_16x16x32_bf16 v[102:105], v[150:153], v[180:183], v[102:105]
	v_mfma_f32_16x16x32_bf16 v[98:101], v[158:161], v[180:183], v[98:101]
	v_mfma_f32_16x16x32_bf16 v[86:89], v[150:153], v[218:221], v[86:89]
	v_mfma_f32_16x16x32_bf16 v[82:85], v[158:161], v[218:221], v[82:85]
	v_mfma_f32_16x16x32_bf16 v[70:73], v[150:153], v[226:229], v[70:73]
	v_mfma_f32_16x16x32_bf16 v[66:69], v[158:161], v[226:229], v[66:69]
	s_setprio 0
	s_barrier
	s_mov_b32 m0, s54
	v_add_u32_e32 v178, s89, v184
	ds_read_b128 v[162:165], v208 offset:16384
	ds_read_b128 v[166:169], v208 offset:17408
	ds_read_b128 v[170:173], v208 offset:18432
	ds_read_b128 v[180:183], v208 offset:19456
	ds_read_b128 v[214:217], v208 offset:20480
	ds_read_b128 v[218:221], v208 offset:21504
	ds_read_b128 v[222:225], v208 offset:22528
	ds_read_b128 v[226:229], v208 offset:23552
	global_load_lds_dwordx4 v178, s[6:7]
	v_add_u32_e32 v178, s52, v178
	s_mov_b32 m0, s55
	s_nop 0
	global_load_lds_dwordx4 v178, s[6:7]
	v_add_u32_e32 v178, s89, v185
	s_mov_b32 m0, s56
	s_nop 0
	global_load_lds_dwordx4 v178, s[6:7]
	v_add_u32_e32 v178, s52, v178
	s_mov_b32 m0, s57
	s_nop 0
	global_load_lds_dwordx4 v178, s[6:7]
	v_add_u32_e32 v178, s75, v1
	s_mov_b32 m0, s53
	s_nop 0
	global_load_lds_dwordx4 v178, s[4:5]
	v_add_u32_e32 v178, s45, v178
	s_mov_b32 m0, s58
	s_nop 0
	global_load_lds_dwordx4 v178, s[4:5]
	s_waitcnt vmcnt(8)
	s_waitcnt lgkmcnt(0)
	s_barrier
	s_setprio 1
	s_waitcnt lgkmcnt(0)
	v_mfma_f32_16x16x32_bf16 v[62:65], v[138:141], v[162:165], 0
	v_mfma_f32_16x16x32_bf16 v[58:61], v[134:137], v[162:165], 0
	v_mfma_f32_16x16x32_bf16 v[46:49], v[138:141], v[170:173], 0
	v_mfma_f32_16x16x32_bf16 v[42:45], v[134:137], v[170:173], 0
	v_mfma_f32_16x16x32_bf16 v[30:33], v[138:141], v[214:217], 0
	v_mfma_f32_16x16x32_bf16 v[26:29], v[134:137], v[214:217], 0
	v_mfma_f32_16x16x32_bf16 v[14:17], v[138:141], v[222:225], 0
	v_mfma_f32_16x16x32_bf16 v[10:13], v[134:137], v[222:225], 0
	v_mfma_f32_16x16x32_bf16 v[62:65], v[130:133], v[166:169], v[62:65]
	v_mfma_f32_16x16x32_bf16 v[58:61], v[146:149], v[166:169], v[58:61]
	v_mfma_f32_16x16x32_bf16 v[46:49], v[130:133], v[180:183], v[46:49]
	v_mfma_f32_16x16x32_bf16 v[42:45], v[146:149], v[180:183], v[42:45]
	v_mfma_f32_16x16x32_bf16 v[30:33], v[130:133], v[218:221], v[30:33]
	v_mfma_f32_16x16x32_bf16 v[26:29], v[146:149], v[218:221], v[26:29]
	v_mfma_f32_16x16x32_bf16 v[14:17], v[130:133], v[226:229], v[14:17]
	v_mfma_f32_16x16x32_bf16 v[10:13], v[146:149], v[226:229], v[10:13]
	v_mfma_f32_16x16x32_bf16 v[54:57], v[142:145], v[162:165], 0
	v_mfma_f32_16x16x32_bf16 v[50:53], v[154:157], v[162:165], 0
	v_mfma_f32_16x16x32_bf16 v[38:41], v[142:145], v[170:173], 0
	v_mfma_f32_16x16x32_bf16 v[34:37], v[154:157], v[170:173], 0
	v_mfma_f32_16x16x32_bf16 v[22:25], v[142:145], v[214:217], 0
	v_mfma_f32_16x16x32_bf16 v[18:21], v[154:157], v[214:217], 0
	v_mfma_f32_16x16x32_bf16 v[6:9], v[142:145], v[222:225], 0
	v_mfma_f32_16x16x32_bf16 v[2:5], v[154:157], v[222:225], 0
	v_mfma_f32_16x16x32_bf16 v[54:57], v[150:153], v[166:169], v[54:57]
	v_mfma_f32_16x16x32_bf16 v[50:53], v[158:161], v[166:169], v[50:53]
	v_mfma_f32_16x16x32_bf16 v[38:41], v[150:153], v[180:183], v[38:41]
	v_mfma_f32_16x16x32_bf16 v[34:37], v[158:161], v[180:183], v[34:37]
	v_mfma_f32_16x16x32_bf16 v[22:25], v[150:153], v[218:221], v[22:25]
	v_mfma_f32_16x16x32_bf16 v[18:21], v[158:161], v[218:221], v[18:21]
	v_mfma_f32_16x16x32_bf16 v[6:9], v[150:153], v[226:229], v[6:9]
	v_mfma_f32_16x16x32_bf16 v[2:5], v[158:161], v[226:229], v[2:5]
	s_setprio 0
	s_barrier
	s_branch .Lmid_7
.LBB0_2337:
	ds_read_b128 v[130:133], v194
	ds_read_b128 v[134:137], v195
	ds_read_b128 v[138:141], v190
	ds_read_b128 v[142:145], v191
	ds_read_b128 v[146:149], v196
	ds_read_b128 v[150:153], v197
	ds_read_b128 v[154:157], v198
	ds_read_b128 v[158:161], v199
	s_add_i32 s75, s50, 0x80
	s_cmp_eq_u32 s70, s88
	s_cselect_b32 s89, s51, s87
	s_cselect_b32 s75, s49, s75
	v_add_u32_e32 v178, s50, v207
	s_add_i32 m0, s53, 0xc000
	ds_read_b128 v[162:165], v208
	ds_read_b128 v[166:169], v208 offset:1024
	ds_read_b128 v[170:173], v208 offset:2048
	ds_read_b128 v[180:183], v208 offset:3072
	ds_read_b128 v[214:217], v208 offset:4096
	ds_read_b128 v[218:221], v208 offset:5120
	ds_read_b128 v[222:225], v208 offset:6144
	ds_read_b128 v[226:229], v208 offset:7168
	global_load_lds_dwordx4 v178, s[4:5]
	v_add_u32_e32 v178, s50, v206
	s_add_i32 m0, s53, 0xe000
	s_nop 0
	global_load_lds_dwordx4 v178, s[4:5]
	s_waitcnt vmcnt(8)
	s_waitcnt lgkmcnt(0)
	s_barrier
	s_setprio 1
	s_waitcnt lgkmcnt(0)
	v_mfma_f32_16x16x32_bf16 v[126:129], v[138:141], v[162:165], v[126:129]
	v_mfma_f32_16x16x32_bf16 v[122:125], v[134:137], v[162:165], v[122:125]
	v_mfma_f32_16x16x32_bf16 v[110:113], v[138:141], v[170:173], v[110:113]
	v_mfma_f32_16x16x32_bf16 v[106:109], v[134:137], v[170:173], v[106:109]
	v_mfma_f32_16x16x32_bf16 v[94:97], v[138:141], v[214:217], v[94:97]
	v_mfma_f32_16x16x32_bf16 v[90:93], v[134:137], v[214:217], v[90:93]
	v_mfma_f32_16x16x32_bf16 v[78:81], v[138:141], v[222:225], v[78:81]
	v_mfma_f32_16x16x32_bf16 v[74:77], v[134:137], v[222:225], v[74:77]
	v_mfma_f32_16x16x32_bf16 v[126:129], v[130:133], v[166:169], v[126:129]
	v_mfma_f32_16x16x32_bf16 v[122:125], v[146:149], v[166:169], v[122:125]
	v_mfma_f32_16x16x32_bf16 v[110:113], v[130:133], v[180:183], v[110:113]
	v_mfma_f32_16x16x32_bf16 v[106:109], v[146:149], v[180:183], v[106:109]
	v_mfma_f32_16x16x32_bf16 v[94:97], v[130:133], v[218:221], v[94:97]
	v_mfma_f32_16x16x32_bf16 v[90:93], v[146:149], v[218:221], v[90:93]
	v_mfma_f32_16x16x32_bf16 v[78:81], v[130:133], v[226:229], v[78:81]
	v_mfma_f32_16x16x32_bf16 v[74:77], v[146:149], v[226:229], v[74:77]
	v_mfma_f32_16x16x32_bf16 v[118:121], v[142:145], v[162:165], v[118:121]
	v_mfma_f32_16x16x32_bf16 v[114:117], v[154:157], v[162:165], v[114:117]
	v_mfma_f32_16x16x32_bf16 v[102:105], v[142:145], v[170:173], v[102:105]
	v_mfma_f32_16x16x32_bf16 v[98:101], v[154:157], v[170:173], v[98:101]
	v_mfma_f32_16x16x32_bf16 v[86:89], v[142:145], v[214:217], v[86:89]
	v_mfma_f32_16x16x32_bf16 v[82:85], v[154:157], v[214:217], v[82:85]
	v_mfma_f32_16x16x32_bf16 v[70:73], v[142:145], v[222:225], v[70:73]
	v_mfma_f32_16x16x32_bf16 v[66:69], v[154:157], v[222:225], v[66:69]
	v_mfma_f32_16x16x32_bf16 v[118:121], v[150:153], v[166:169], v[118:121]
	v_mfma_f32_16x16x32_bf16 v[114:117], v[158:161], v[166:169], v[114:117]
	v_mfma_f32_16x16x32_bf16 v[102:105], v[150:153], v[180:183], v[102:105]
	v_mfma_f32_16x16x32_bf16 v[98:101], v[158:161], v[180:183], v[98:101]
	v_mfma_f32_16x16x32_bf16 v[86:89], v[150:153], v[218:221], v[86:89]
	v_mfma_f32_16x16x32_bf16 v[82:85], v[158:161], v[218:221], v[82:85]
	v_mfma_f32_16x16x32_bf16 v[70:73], v[150:153], v[226:229], v[70:73]
	v_mfma_f32_16x16x32_bf16 v[66:69], v[158:161], v[226:229], v[66:69]
	s_setprio 0
	s_barrier
	s_mov_b32 m0, s54
	v_add_u32_e32 v178, s89, v184
	ds_read_b128 v[162:165], v208 offset:16384
	ds_read_b128 v[166:169], v208 offset:17408
	ds_read_b128 v[170:173], v208 offset:18432
	ds_read_b128 v[180:183], v208 offset:19456
	ds_read_b128 v[214:217], v208 offset:20480
	ds_read_b128 v[218:221], v208 offset:21504
	ds_read_b128 v[222:225], v208 offset:22528
	ds_read_b128 v[226:229], v208 offset:23552
	global_load_lds_dwordx4 v178, s[6:7]
	v_add_u32_e32 v178, s52, v178
	s_mov_b32 m0, s55
	s_nop 0
	global_load_lds_dwordx4 v178, s[6:7]
	v_add_u32_e32 v178, s89, v185
	s_mov_b32 m0, s56
	s_nop 0
	global_load_lds_dwordx4 v178, s[6:7]
	v_add_u32_e32 v178, s52, v178
	s_mov_b32 m0, s57
	s_nop 0
	global_load_lds_dwordx4 v178, s[6:7]
	v_add_u32_e32 v178, s75, v1
	s_mov_b32 m0, s53
	s_nop 0
	global_load_lds_dwordx4 v178, s[4:5]
	v_add_u32_e32 v178, s45, v178
	s_mov_b32 m0, s58
	s_nop 0
	global_load_lds_dwordx4 v178, s[4:5]
	s_waitcnt vmcnt(8)
	s_waitcnt lgkmcnt(0)
	s_barrier
	s_setprio 1
	s_waitcnt lgkmcnt(0)
	v_mfma_f32_16x16x32_bf16 v[62:65], v[138:141], v[162:165], v[62:65]
	v_mfma_f32_16x16x32_bf16 v[58:61], v[134:137], v[162:165], v[58:61]
	v_mfma_f32_16x16x32_bf16 v[46:49], v[138:141], v[170:173], v[46:49]
	v_mfma_f32_16x16x32_bf16 v[42:45], v[134:137], v[170:173], v[42:45]
	v_mfma_f32_16x16x32_bf16 v[30:33], v[138:141], v[214:217], v[30:33]
	v_mfma_f32_16x16x32_bf16 v[26:29], v[134:137], v[214:217], v[26:29]
	v_mfma_f32_16x16x32_bf16 v[14:17], v[138:141], v[222:225], v[14:17]
	v_mfma_f32_16x16x32_bf16 v[10:13], v[134:137], v[222:225], v[10:13]
	v_mfma_f32_16x16x32_bf16 v[62:65], v[130:133], v[166:169], v[62:65]
	v_mfma_f32_16x16x32_bf16 v[58:61], v[146:149], v[166:169], v[58:61]
	v_mfma_f32_16x16x32_bf16 v[46:49], v[130:133], v[180:183], v[46:49]
	v_mfma_f32_16x16x32_bf16 v[42:45], v[146:149], v[180:183], v[42:45]
	v_mfma_f32_16x16x32_bf16 v[30:33], v[130:133], v[218:221], v[30:33]
	v_mfma_f32_16x16x32_bf16 v[26:29], v[146:149], v[218:221], v[26:29]
	v_mfma_f32_16x16x32_bf16 v[14:17], v[130:133], v[226:229], v[14:17]
	v_mfma_f32_16x16x32_bf16 v[10:13], v[146:149], v[226:229], v[10:13]
	v_mfma_f32_16x16x32_bf16 v[54:57], v[142:145], v[162:165], v[54:57]
	v_mfma_f32_16x16x32_bf16 v[50:53], v[154:157], v[162:165], v[50:53]
	v_mfma_f32_16x16x32_bf16 v[38:41], v[142:145], v[170:173], v[38:41]
	v_mfma_f32_16x16x32_bf16 v[34:37], v[154:157], v[170:173], v[34:37]
	v_mfma_f32_16x16x32_bf16 v[22:25], v[142:145], v[214:217], v[22:25]
	v_mfma_f32_16x16x32_bf16 v[18:21], v[154:157], v[214:217], v[18:21]
	v_mfma_f32_16x16x32_bf16 v[6:9], v[142:145], v[222:225], v[6:9]
	v_mfma_f32_16x16x32_bf16 v[2:5], v[154:157], v[222:225], v[2:5]
	v_mfma_f32_16x16x32_bf16 v[54:57], v[150:153], v[166:169], v[54:57]
	v_mfma_f32_16x16x32_bf16 v[50:53], v[158:161], v[166:169], v[50:53]
	v_mfma_f32_16x16x32_bf16 v[38:41], v[150:153], v[180:183], v[38:41]
	v_mfma_f32_16x16x32_bf16 v[34:37], v[158:161], v[180:183], v[34:37]
	v_mfma_f32_16x16x32_bf16 v[22:25], v[150:153], v[218:221], v[22:25]
	v_mfma_f32_16x16x32_bf16 v[18:21], v[158:161], v[218:221], v[18:21]
	v_mfma_f32_16x16x32_bf16 v[6:9], v[150:153], v[226:229], v[6:9]
	v_mfma_f32_16x16x32_bf16 v[2:5], v[158:161], v[226:229], v[2:5]
	s_setprio 0
	s_barrier
.Lmid_7:
	ds_read_b128 v[130:133], v200
	ds_read_b128 v[134:137], v201
	ds_read_b128 v[138:141], v192
	ds_read_b128 v[142:145], v193
	ds_read_b128 v[146:149], v202
	ds_read_b128 v[150:153], v203
	ds_read_b128 v[154:157], v204
	ds_read_b128 v[158:161], v205
	s_mov_b32 m0, s59
	v_add_u32_e32 v178, s75, v186
	ds_read_b128 v[162:165], v208 offset:32768
	ds_read_b128 v[166:169], v208 offset:33792
	ds_read_b128 v[170:173], v208 offset:34816
	ds_read_b128 v[180:183], v208 offset:35840
	ds_read_b128 v[214:217], v208 offset:36864
	ds_read_b128 v[218:221], v208 offset:37888
	ds_read_b128 v[222:225], v208 offset:38912
	ds_read_b128 v[226:229], v208 offset:39936
	global_load_lds_dwordx4 v178, s[4:5]
	v_add_u32_e32 v178, s45, v178
	s_mov_b32 m0, s60
	s_nop 0
	global_load_lds_dwordx4 v178, s[4:5]
	s_waitcnt vmcnt(8)
	s_waitcnt lgkmcnt(0)
	s_barrier
	s_setprio 1
	s_waitcnt lgkmcnt(0)
	v_mfma_f32_16x16x32_bf16 v[126:129], v[138:141], v[162:165], v[126:129]
	v_mfma_f32_16x16x32_bf16 v[122:125], v[134:137], v[162:165], v[122:125]
	v_mfma_f32_16x16x32_bf16 v[110:113], v[138:141], v[170:173], v[110:113]
	v_mfma_f32_16x16x32_bf16 v[106:109], v[134:137], v[170:173], v[106:109]
	v_mfma_f32_16x16x32_bf16 v[94:97], v[138:141], v[214:217], v[94:97]
	v_mfma_f32_16x16x32_bf16 v[90:93], v[134:137], v[214:217], v[90:93]
	v_mfma_f32_16x16x32_bf16 v[78:81], v[138:141], v[222:225], v[78:81]
	v_mfma_f32_16x16x32_bf16 v[74:77], v[134:137], v[222:225], v[74:77]
	v_mfma_f32_16x16x32_bf16 v[126:129], v[130:133], v[166:169], v[126:129]
	v_mfma_f32_16x16x32_bf16 v[122:125], v[146:149], v[166:169], v[122:125]
	v_mfma_f32_16x16x32_bf16 v[110:113], v[130:133], v[180:183], v[110:113]
	v_mfma_f32_16x16x32_bf16 v[106:109], v[146:149], v[180:183], v[106:109]
	v_mfma_f32_16x16x32_bf16 v[94:97], v[130:133], v[218:221], v[94:97]
	v_mfma_f32_16x16x32_bf16 v[90:93], v[146:149], v[218:221], v[90:93]
	v_mfma_f32_16x16x32_bf16 v[78:81], v[130:133], v[226:229], v[78:81]
	v_mfma_f32_16x16x32_bf16 v[74:77], v[146:149], v[226:229], v[74:77]
	v_mfma_f32_16x16x32_bf16 v[118:121], v[142:145], v[162:165], v[118:121]
	v_mfma_f32_16x16x32_bf16 v[114:117], v[154:157], v[162:165], v[114:117]
	v_mfma_f32_16x16x32_bf16 v[102:105], v[142:145], v[170:173], v[102:105]
	v_mfma_f32_16x16x32_bf16 v[98:101], v[154:157], v[170:173], v[98:101]
	v_mfma_f32_16x16x32_bf16 v[86:89], v[142:145], v[214:217], v[86:89]
	v_mfma_f32_16x16x32_bf16 v[82:85], v[154:157], v[214:217], v[82:85]
	v_mfma_f32_16x16x32_bf16 v[70:73], v[142:145], v[222:225], v[70:73]
	v_mfma_f32_16x16x32_bf16 v[66:69], v[154:157], v[222:225], v[66:69]
	v_mfma_f32_16x16x32_bf16 v[118:121], v[150:153], v[166:169], v[118:121]
	v_mfma_f32_16x16x32_bf16 v[114:117], v[158:161], v[166:169], v[114:117]
	v_mfma_f32_16x16x32_bf16 v[102:105], v[150:153], v[180:183], v[102:105]
	v_mfma_f32_16x16x32_bf16 v[98:101], v[158:161], v[180:183], v[98:101]
	v_mfma_f32_16x16x32_bf16 v[86:89], v[150:153], v[218:221], v[86:89]
	v_mfma_f32_16x16x32_bf16 v[82:85], v[158:161], v[218:221], v[82:85]
	v_mfma_f32_16x16x32_bf16 v[70:73], v[150:153], v[226:229], v[70:73]
	v_mfma_f32_16x16x32_bf16 v[66:69], v[158:161], v[226:229], v[66:69]
	s_setprio 0
	s_barrier
	s_addk_i32 s89, 0x80
	s_mov_b32 m0, s63
	v_add_u32_e32 v178, s89, v184
	ds_read_b128 v[162:165], v208 offset:49152
	ds_read_b128 v[166:169], v208 offset:50176
	ds_read_b128 v[170:173], v208 offset:51200
	ds_read_b128 v[180:183], v208 offset:52224
	ds_read_b128 v[214:217], v208 offset:53248
	ds_read_b128 v[218:221], v208 offset:54272
	ds_read_b128 v[222:225], v208 offset:55296
	ds_read_b128 v[226:229], v208 offset:56320
	global_load_lds_dwordx4 v178, s[6:7]
	v_add_u32_e32 v178, s52, v178
	s_mov_b32 m0, s64
	s_nop 0
	global_load_lds_dwordx4 v178, s[6:7]
	v_add_u32_e32 v178, s89, v185
	s_mov_b32 m0, s67
	s_nop 0
	global_load_lds_dwordx4 v178, s[6:7]
	v_add_u32_e32 v178, s52, v178
	s_mov_b32 m0, s68
	s_nop 0
	global_load_lds_dwordx4 v178, s[6:7]
	v_add_u32_e32 v178, s75, v189
	s_mov_b32 m0, s65
	s_nop 0
	global_load_lds_dwordx4 v178, s[4:5]
	v_add_u32_e32 v178, s45, v178
	s_mov_b32 m0, s66
	s_nop 0
	global_load_lds_dwordx4 v178, s[4:5]
	s_waitcnt vmcnt(8)
	s_waitcnt lgkmcnt(0)
	s_barrier
	s_setprio 1
	s_waitcnt lgkmcnt(0)
	v_mfma_f32_16x16x32_bf16 v[62:65], v[138:141], v[162:165], v[62:65]
	v_mfma_f32_16x16x32_bf16 v[58:61], v[134:137], v[162:165], v[58:61]
	v_mfma_f32_16x16x32_bf16 v[46:49], v[138:141], v[170:173], v[46:49]
	v_mfma_f32_16x16x32_bf16 v[42:45], v[134:137], v[170:173], v[42:45]
	v_mfma_f32_16x16x32_bf16 v[30:33], v[138:141], v[214:217], v[30:33]
	v_mfma_f32_16x16x32_bf16 v[26:29], v[134:137], v[214:217], v[26:29]
	v_mfma_f32_16x16x32_bf16 v[14:17], v[138:141], v[222:225], v[14:17]
	v_mfma_f32_16x16x32_bf16 v[10:13], v[134:137], v[222:225], v[10:13]
	v_mfma_f32_16x16x32_bf16 v[62:65], v[130:133], v[166:169], v[62:65]
	v_mfma_f32_16x16x32_bf16 v[58:61], v[146:149], v[166:169], v[58:61]
	v_mfma_f32_16x16x32_bf16 v[46:49], v[130:133], v[180:183], v[46:49]
	v_mfma_f32_16x16x32_bf16 v[42:45], v[146:149], v[180:183], v[42:45]
	v_mfma_f32_16x16x32_bf16 v[30:33], v[130:133], v[218:221], v[30:33]
	v_mfma_f32_16x16x32_bf16 v[26:29], v[146:149], v[218:221], v[26:29]
	v_mfma_f32_16x16x32_bf16 v[14:17], v[130:133], v[226:229], v[14:17]
	v_mfma_f32_16x16x32_bf16 v[10:13], v[146:149], v[226:229], v[10:13]
	v_mfma_f32_16x16x32_bf16 v[54:57], v[142:145], v[162:165], v[54:57]
	v_mfma_f32_16x16x32_bf16 v[50:53], v[154:157], v[162:165], v[50:53]
	v_mfma_f32_16x16x32_bf16 v[38:41], v[142:145], v[170:173], v[38:41]
	v_mfma_f32_16x16x32_bf16 v[34:37], v[154:157], v[170:173], v[34:37]
	v_mfma_f32_16x16x32_bf16 v[22:25], v[142:145], v[214:217], v[22:25]
	v_mfma_f32_16x16x32_bf16 v[18:21], v[154:157], v[214:217], v[18:21]
	v_mfma_f32_16x16x32_bf16 v[6:9], v[142:145], v[222:225], v[6:9]
	v_mfma_f32_16x16x32_bf16 v[2:5], v[154:157], v[222:225], v[2:5]
	v_mfma_f32_16x16x32_bf16 v[54:57], v[150:153], v[166:169], v[54:57]
	v_mfma_f32_16x16x32_bf16 v[50:53], v[158:161], v[166:169], v[50:53]
	v_mfma_f32_16x16x32_bf16 v[38:41], v[150:153], v[180:183], v[38:41]
	v_mfma_f32_16x16x32_bf16 v[34:37], v[158:161], v[180:183], v[34:37]
	v_mfma_f32_16x16x32_bf16 v[22:25], v[150:153], v[218:221], v[22:25]
	v_mfma_f32_16x16x32_bf16 v[18:21], v[158:161], v[218:221], v[18:21]
	v_mfma_f32_16x16x32_bf16 v[6:9], v[150:153], v[226:229], v[6:9]
	v_mfma_f32_16x16x32_bf16 v[2:5], v[158:161], v[226:229], v[2:5]
	s_setprio 0
	s_barrier
	s_add_i32 s88, s88, 2
	s_addk_i32 s50, 0x100
	s_addk_i32 s87, 0x100
	s_cmp_ge_i32 s88, s61
	s_cbranch_scc0 .LBB0_2337

.LBB0_2519:
	s_andn2_b64 vcc, exec, s[14:15]
	s_cbranch_vccnz .Lzs_10
	s_add_i32 s56, s96, 0x80
	s_add_i32 s57, s74, 0x100
	s_mov_b32 s74, 0
	ds_read_b128 v[90:93], v160
	ds_read_b128 v[94:97], v161
	ds_read_b128 v[142:145], v156
	ds_read_b128 v[146:149], v157
	ds_read_b128 v[176:179], v162
	ds_read_b128 v[180:183], v163
	ds_read_b128 v[184:187], v164
	ds_read_b128 v[188:191], v165
	s_add_i32 s96, s56, 0x80
	s_cmp_eq_u32 s81, s74
	s_cselect_b32 vcc_lo, s55, s57
	s_cselect_b32 s96, s45, s96
	v_add_u32_e32 v175, s56, v173
	s_add_i32 m0, s60, 0xc000
	ds_read_b128 v[192:195], v174
	ds_read_b128 v[196:199], v174 offset:1024
	ds_read_b128 v[200:203], v174 offset:2048
	ds_read_b128 v[204:207], v174 offset:3072
	ds_read_b128 v[214:217], v174 offset:4096
	ds_read_b128 v[218:221], v174 offset:5120
	ds_read_b128 v[222:225], v174 offset:6144
	ds_read_b128 v[226:229], v174 offset:7168
	global_load_lds_dwordx4 v175, s[4:5]
	v_add_u32_e32 v175, s56, v172
	s_add_i32 m0, s60, 0xe000
	s_nop 0
	global_load_lds_dwordx4 v175, s[4:5]
	s_waitcnt vmcnt(8)
	s_waitcnt lgkmcnt(0)
	s_barrier
	s_setprio 1
	s_waitcnt lgkmcnt(0)
	v_mfma_f32_16x16x32_bf16 v[134:137], v[142:145], v[192:195], 0
	v_mfma_f32_16x16x32_bf16 v[130:133], v[94:97], v[192:195], 0
	v_mfma_f32_16x16x32_bf16 v[126:129], v[142:145], v[200:203], 0
	v_mfma_f32_16x16x32_bf16 v[122:125], v[94:97], v[200:203], 0
	v_mfma_f32_16x16x32_bf16 v[118:121], v[142:145], v[214:217], 0
	v_mfma_f32_16x16x32_bf16 v[114:117], v[94:97], v[214:217], 0
	v_mfma_f32_16x16x32_bf16 v[110:113], v[142:145], v[222:225], 0
	v_mfma_f32_16x16x32_bf16 v[106:109], v[94:97], v[222:225], 0
	v_mfma_f32_16x16x32_bf16 v[134:137], v[90:93], v[196:199], v[134:137]
	v_mfma_f32_16x16x32_bf16 v[130:133], v[176:179], v[196:199], v[130:133]
	v_mfma_f32_16x16x32_bf16 v[126:129], v[90:93], v[204:207], v[126:129]
	v_mfma_f32_16x16x32_bf16 v[122:125], v[176:179], v[204:207], v[122:125]
	v_mfma_f32_16x16x32_bf16 v[118:121], v[90:93], v[218:221], v[118:121]
	v_mfma_f32_16x16x32_bf16 v[114:117], v[176:179], v[218:221], v[114:117]
	v_mfma_f32_16x16x32_bf16 v[110:113], v[90:93], v[226:229], v[110:113]
	v_mfma_f32_16x16x32_bf16 v[106:109], v[176:179], v[226:229], v[106:109]
	v_mfma_f32_16x16x32_bf16 v[62:65], v[146:149], v[192:195], 0
	v_mfma_f32_16x16x32_bf16 v[58:61], v[184:187], v[192:195], 0
	v_mfma_f32_16x16x32_bf16 v[54:57], v[146:149], v[200:203], 0
	v_mfma_f32_16x16x32_bf16 v[50:53], v[184:187], v[200:203], 0
	v_mfma_f32_16x16x32_bf16 v[46:49], v[146:149], v[214:217], 0
	v_mfma_f32_16x16x32_bf16 v[42:45], v[184:187], v[214:217], 0
	v_mfma_f32_16x16x32_bf16 v[38:41], v[146:149], v[222:225], 0
	v_mfma_f32_16x16x32_bf16 v[34:37], v[184:187], v[222:225], 0
	v_mfma_f32_16x16x32_bf16 v[62:65], v[180:183], v[196:199], v[62:65]
	v_mfma_f32_16x16x32_bf16 v[58:61], v[188:191], v[196:199], v[58:61]
	v_mfma_f32_16x16x32_bf16 v[54:57], v[180:183], v[204:207], v[54:57]
	v_mfma_f32_16x16x32_bf16 v[50:53], v[188:191], v[204:207], v[50:53]
	v_mfma_f32_16x16x32_bf16 v[46:49], v[180:183], v[218:221], v[46:49]
	v_mfma_f32_16x16x32_bf16 v[42:45], v[188:191], v[218:221], v[42:45]
	v_mfma_f32_16x16x32_bf16 v[38:41], v[180:183], v[226:229], v[38:41]
	v_mfma_f32_16x16x32_bf16 v[34:37], v[188:191], v[226:229], v[34:37]
	s_setprio 0
	s_barrier
	s_mov_b32 m0, s61
	v_add_u32_e32 v175, vcc_lo, v150
	ds_read_b128 v[192:195], v174 offset:16384
	ds_read_b128 v[196:199], v174 offset:17408
	ds_read_b128 v[200:203], v174 offset:18432
	ds_read_b128 v[204:207], v174 offset:19456
	ds_read_b128 v[214:217], v174 offset:20480
	ds_read_b128 v[218:221], v174 offset:21504
	ds_read_b128 v[222:225], v174 offset:22528
	ds_read_b128 v[226:229], v174 offset:23552
	global_load_lds_dwordx4 v175, s[6:7]
	v_add_u32_e32 v175, s59, v175
	s_mov_b32 m0, s62
	s_nop 0
	global_load_lds_dwordx4 v175, s[6:7]
	v_add_u32_e32 v175, vcc_lo, v151
	s_mov_b32 m0, s63
	s_nop 0
	global_load_lds_dwordx4 v175, s[6:7]
	v_add_u32_e32 v175, s59, v175
	s_mov_b32 m0, s64
	s_nop 0
	global_load_lds_dwordx4 v175, s[6:7]
	v_add_u32_e32 v175, s96, v1
	s_mov_b32 m0, s60
	s_nop 0
	global_load_lds_dwordx4 v175, s[4:5]
	v_add_u32_e32 v175, s58, v175
	s_mov_b32 m0, s65
	s_nop 0
	global_load_lds_dwordx4 v175, s[4:5]
	s_waitcnt vmcnt(8)
	s_waitcnt lgkmcnt(0)
	s_barrier
	s_setprio 1
	s_waitcnt lgkmcnt(0)
	v_mfma_f32_16x16x32_bf16 v[102:105], v[142:145], v[192:195], 0
	v_mfma_f32_16x16x32_bf16 v[98:101], v[94:97], v[192:195], 0
	v_mfma_f32_16x16x32_bf16 v[86:89], v[142:145], v[200:203], 0
	v_mfma_f32_16x16x32_bf16 v[82:85], v[94:97], v[200:203], 0
	v_mfma_f32_16x16x32_bf16 v[78:81], v[142:145], v[214:217], 0
	v_mfma_f32_16x16x32_bf16 v[74:77], v[94:97], v[214:217], 0
	v_mfma_f32_16x16x32_bf16 v[70:73], v[142:145], v[222:225], 0
	v_mfma_f32_16x16x32_bf16 v[66:69], v[94:97], v[222:225], 0
	v_mfma_f32_16x16x32_bf16 v[102:105], v[90:93], v[196:199], v[102:105]
	v_mfma_f32_16x16x32_bf16 v[98:101], v[176:179], v[196:199], v[98:101]
	v_mfma_f32_16x16x32_bf16 v[86:89], v[90:93], v[204:207], v[86:89]
	v_mfma_f32_16x16x32_bf16 v[82:85], v[176:179], v[204:207], v[82:85]
	v_mfma_f32_16x16x32_bf16 v[78:81], v[90:93], v[218:221], v[78:81]
	v_mfma_f32_16x16x32_bf16 v[74:77], v[176:179], v[218:221], v[74:77]
	v_mfma_f32_16x16x32_bf16 v[70:73], v[90:93], v[226:229], v[70:73]
	v_mfma_f32_16x16x32_bf16 v[66:69], v[176:179], v[226:229], v[66:69]
	v_mfma_f32_16x16x32_bf16 v[30:33], v[146:149], v[192:195], 0
	v_mfma_f32_16x16x32_bf16 v[26:29], v[184:187], v[192:195], 0
	v_mfma_f32_16x16x32_bf16 v[22:25], v[146:149], v[200:203], 0
	v_mfma_f32_16x16x32_bf16 v[18:21], v[184:187], v[200:203], 0
	v_mfma_f32_16x16x32_bf16 v[14:17], v[146:149], v[214:217], 0
	v_mfma_f32_16x16x32_bf16 v[10:13], v[184:187], v[214:217], 0
	v_mfma_f32_16x16x32_bf16 v[6:9], v[146:149], v[222:225], 0
	v_mfma_f32_16x16x32_bf16 v[2:5], v[184:187], v[222:225], 0
	v_mfma_f32_16x16x32_bf16 v[30:33], v[180:183], v[196:199], v[30:33]
	v_mfma_f32_16x16x32_bf16 v[26:29], v[188:191], v[196:199], v[26:29]
	v_mfma_f32_16x16x32_bf16 v[22:25], v[180:183], v[204:207], v[22:25]
	v_mfma_f32_16x16x32_bf16 v[18:21], v[188:191], v[204:207], v[18:21]
	v_mfma_f32_16x16x32_bf16 v[14:17], v[180:183], v[218:221], v[14:17]
	v_mfma_f32_16x16x32_bf16 v[10:13], v[188:191], v[218:221], v[10:13]
	v_mfma_f32_16x16x32_bf16 v[6:9], v[180:183], v[226:229], v[6:9]
	v_mfma_f32_16x16x32_bf16 v[2:5], v[188:191], v[226:229], v[2:5]
	s_setprio 0
	s_barrier
	s_branch .Lmid_8
.LBB0_2521:
	ds_read_b128 v[90:93], v160
	ds_read_b128 v[94:97], v161
	ds_read_b128 v[142:145], v156
	ds_read_b128 v[146:149], v157
	ds_read_b128 v[176:179], v162
	ds_read_b128 v[180:183], v163
	ds_read_b128 v[184:187], v164
	ds_read_b128 v[188:191], v165
	s_add_i32 s96, s56, 0x80
	s_cmp_eq_u32 s81, s74
	s_cselect_b32 vcc_lo, s55, s57
	s_cselect_b32 s96, s45, s96
	v_add_u32_e32 v175, s56, v173
	s_add_i32 m0, s60, 0xc000
	ds_read_b128 v[192:195], v174
	ds_read_b128 v[196:199], v174 offset:1024
	ds_read_b128 v[200:203], v174 offset:2048
	ds_read_b128 v[204:207], v174 offset:3072
	ds_read_b128 v[214:217], v174 offset:4096
	ds_read_b128 v[218:221], v174 offset:5120
	ds_read_b128 v[222:225], v174 offset:6144
	ds_read_b128 v[226:229], v174 offset:7168
	global_load_lds_dwordx4 v175, s[4:5]
	v_add_u32_e32 v175, s56, v172
	s_add_i32 m0, s60, 0xe000
	s_nop 0
	global_load_lds_dwordx4 v175, s[4:5]
	s_waitcnt vmcnt(8)
	s_waitcnt lgkmcnt(0)
	s_barrier
	s_setprio 1
	s_waitcnt lgkmcnt(0)
	v_mfma_f32_16x16x32_bf16 v[134:137], v[142:145], v[192:195], v[134:137]
	v_mfma_f32_16x16x32_bf16 v[130:133], v[94:97], v[192:195], v[130:133]
	v_mfma_f32_16x16x32_bf16 v[126:129], v[142:145], v[200:203], v[126:129]
	v_mfma_f32_16x16x32_bf16 v[122:125], v[94:97], v[200:203], v[122:125]
	v_mfma_f32_16x16x32_bf16 v[118:121], v[142:145], v[214:217], v[118:121]
	v_mfma_f32_16x16x32_bf16 v[114:117], v[94:97], v[214:217], v[114:117]
	v_mfma_f32_16x16x32_bf16 v[110:113], v[142:145], v[222:225], v[110:113]
	v_mfma_f32_16x16x32_bf16 v[106:109], v[94:97], v[222:225], v[106:109]
	v_mfma_f32_16x16x32_bf16 v[134:137], v[90:93], v[196:199], v[134:137]
	v_mfma_f32_16x16x32_bf16 v[130:133], v[176:179], v[196:199], v[130:133]
	v_mfma_f32_16x16x32_bf16 v[126:129], v[90:93], v[204:207], v[126:129]
	v_mfma_f32_16x16x32_bf16 v[122:125], v[176:179], v[204:207], v[122:125]
	v_mfma_f32_16x16x32_bf16 v[118:121], v[90:93], v[218:221], v[118:121]
	v_mfma_f32_16x16x32_bf16 v[114:117], v[176:179], v[218:221], v[114:117]
	v_mfma_f32_16x16x32_bf16 v[110:113], v[90:93], v[226:229], v[110:113]
	v_mfma_f32_16x16x32_bf16 v[106:109], v[176:179], v[226:229], v[106:109]
	v_mfma_f32_16x16x32_bf16 v[62:65], v[146:149], v[192:195], v[62:65]
	v_mfma_f32_16x16x32_bf16 v[58:61], v[184:187], v[192:195], v[58:61]
	v_mfma_f32_16x16x32_bf16 v[54:57], v[146:149], v[200:203], v[54:57]
	v_mfma_f32_16x16x32_bf16 v[50:53], v[184:187], v[200:203], v[50:53]
	v_mfma_f32_16x16x32_bf16 v[46:49], v[146:149], v[214:217], v[46:49]
	v_mfma_f32_16x16x32_bf16 v[42:45], v[184:187], v[214:217], v[42:45]
	v_mfma_f32_16x16x32_bf16 v[38:41], v[146:149], v[222:225], v[38:41]
	v_mfma_f32_16x16x32_bf16 v[34:37], v[184:187], v[222:225], v[34:37]
	v_mfma_f32_16x16x32_bf16 v[62:65], v[180:183], v[196:199], v[62:65]
	v_mfma_f32_16x16x32_bf16 v[58:61], v[188:191], v[196:199], v[58:61]
	v_mfma_f32_16x16x32_bf16 v[54:57], v[180:183], v[204:207], v[54:57]
	v_mfma_f32_16x16x32_bf16 v[50:53], v[188:191], v[204:207], v[50:53]
	v_mfma_f32_16x16x32_bf16 v[46:49], v[180:183], v[218:221], v[46:49]
	v_mfma_f32_16x16x32_bf16 v[42:45], v[188:191], v[218:221], v[42:45]
	v_mfma_f32_16x16x32_bf16 v[38:41], v[180:183], v[226:229], v[38:41]
	v_mfma_f32_16x16x32_bf16 v[34:37], v[188:191], v[226:229], v[34:37]
	s_setprio 0
	s_barrier
	s_mov_b32 m0, s61
	v_add_u32_e32 v175, vcc_lo, v150
	ds_read_b128 v[192:195], v174 offset:16384
	ds_read_b128 v[196:199], v174 offset:17408
	ds_read_b128 v[200:203], v174 offset:18432
	ds_read_b128 v[204:207], v174 offset:19456
	ds_read_b128 v[214:217], v174 offset:20480
	ds_read_b128 v[218:221], v174 offset:21504
	ds_read_b128 v[222:225], v174 offset:22528
	ds_read_b128 v[226:229], v174 offset:23552
	global_load_lds_dwordx4 v175, s[6:7]
	v_add_u32_e32 v175, s59, v175
	s_mov_b32 m0, s62
	s_nop 0
	global_load_lds_dwordx4 v175, s[6:7]
	v_add_u32_e32 v175, vcc_lo, v151
	s_mov_b32 m0, s63
	s_nop 0
	global_load_lds_dwordx4 v175, s[6:7]
	v_add_u32_e32 v175, s59, v175
	s_mov_b32 m0, s64
	s_nop 0
	global_load_lds_dwordx4 v175, s[6:7]
	v_add_u32_e32 v175, s96, v1
	s_mov_b32 m0, s60
	s_nop 0
	global_load_lds_dwordx4 v175, s[4:5]
	v_add_u32_e32 v175, s58, v175
	s_mov_b32 m0, s65
	s_nop 0
	global_load_lds_dwordx4 v175, s[4:5]
	s_waitcnt vmcnt(8)
	s_waitcnt lgkmcnt(0)
	s_barrier
	s_setprio 1
	s_waitcnt lgkmcnt(0)
	v_mfma_f32_16x16x32_bf16 v[102:105], v[142:145], v[192:195], v[102:105]
	v_mfma_f32_16x16x32_bf16 v[98:101], v[94:97], v[192:195], v[98:101]
	v_mfma_f32_16x16x32_bf16 v[86:89], v[142:145], v[200:203], v[86:89]
	v_mfma_f32_16x16x32_bf16 v[82:85], v[94:97], v[200:203], v[82:85]
	v_mfma_f32_16x16x32_bf16 v[78:81], v[142:145], v[214:217], v[78:81]
	v_mfma_f32_16x16x32_bf16 v[74:77], v[94:97], v[214:217], v[74:77]
	v_mfma_f32_16x16x32_bf16 v[70:73], v[142:145], v[222:225], v[70:73]
	v_mfma_f32_16x16x32_bf16 v[66:69], v[94:97], v[222:225], v[66:69]
	v_mfma_f32_16x16x32_bf16 v[102:105], v[90:93], v[196:199], v[102:105]
	v_mfma_f32_16x16x32_bf16 v[98:101], v[176:179], v[196:199], v[98:101]
	v_mfma_f32_16x16x32_bf16 v[86:89], v[90:93], v[204:207], v[86:89]
	v_mfma_f32_16x16x32_bf16 v[82:85], v[176:179], v[204:207], v[82:85]
	v_mfma_f32_16x16x32_bf16 v[78:81], v[90:93], v[218:221], v[78:81]
	v_mfma_f32_16x16x32_bf16 v[74:77], v[176:179], v[218:221], v[74:77]
	v_mfma_f32_16x16x32_bf16 v[70:73], v[90:93], v[226:229], v[70:73]
	v_mfma_f32_16x16x32_bf16 v[66:69], v[176:179], v[226:229], v[66:69]
	v_mfma_f32_16x16x32_bf16 v[30:33], v[146:149], v[192:195], v[30:33]
	v_mfma_f32_16x16x32_bf16 v[26:29], v[184:187], v[192:195], v[26:29]
	v_mfma_f32_16x16x32_bf16 v[22:25], v[146:149], v[200:203], v[22:25]
	v_mfma_f32_16x16x32_bf16 v[18:21], v[184:187], v[200:203], v[18:21]
	v_mfma_f32_16x16x32_bf16 v[14:17], v[146:149], v[214:217], v[14:17]
	v_mfma_f32_16x16x32_bf16 v[10:13], v[184:187], v[214:217], v[10:13]
	v_mfma_f32_16x16x32_bf16 v[6:9], v[146:149], v[222:225], v[6:9]
	v_mfma_f32_16x16x32_bf16 v[2:5], v[184:187], v[222:225], v[2:5]
	v_mfma_f32_16x16x32_bf16 v[30:33], v[180:183], v[196:199], v[30:33]
	v_mfma_f32_16x16x32_bf16 v[26:29], v[188:191], v[196:199], v[26:29]
	v_mfma_f32_16x16x32_bf16 v[22:25], v[180:183], v[204:207], v[22:25]
	v_mfma_f32_16x16x32_bf16 v[18:21], v[188:191], v[204:207], v[18:21]
	v_mfma_f32_16x16x32_bf16 v[14:17], v[180:183], v[218:221], v[14:17]
	v_mfma_f32_16x16x32_bf16 v[10:13], v[188:191], v[218:221], v[10:13]
	v_mfma_f32_16x16x32_bf16 v[6:9], v[180:183], v[226:229], v[6:9]
	v_mfma_f32_16x16x32_bf16 v[2:5], v[188:191], v[226:229], v[2:5]
	s_setprio 0
	s_barrier
.Lmid_8:
	ds_read_b128 v[90:93], v166
	ds_read_b128 v[94:97], v167
	ds_read_b128 v[142:145], v158
	ds_read_b128 v[146:149], v159
	ds_read_b128 v[176:179], v168
	ds_read_b128 v[180:183], v169
	ds_read_b128 v[184:187], v170
	ds_read_b128 v[188:191], v171
	s_mov_b32 m0, s66
	v_add_u32_e32 v175, s96, v152
	ds_read_b128 v[192:195], v174 offset:32768
	ds_read_b128 v[196:199], v174 offset:33792
	ds_read_b128 v[200:203], v174 offset:34816
	ds_read_b128 v[204:207], v174 offset:35840
	ds_read_b128 v[214:217], v174 offset:36864
	ds_read_b128 v[218:221], v174 offset:37888
	ds_read_b128 v[222:225], v174 offset:38912
	ds_read_b128 v[226:229], v174 offset:39936
	global_load_lds_dwordx4 v175, s[4:5]
	v_add_u32_e32 v175, s58, v175
	s_mov_b32 m0, s67
	s_nop 0
	global_load_lds_dwordx4 v175, s[4:5]
	s_waitcnt vmcnt(8)
	s_waitcnt lgkmcnt(0)
	s_barrier
	s_setprio 1
	s_waitcnt lgkmcnt(0)
	v_mfma_f32_16x16x32_bf16 v[134:137], v[142:145], v[192:195], v[134:137]
	v_mfma_f32_16x16x32_bf16 v[130:133], v[94:97], v[192:195], v[130:133]
	v_mfma_f32_16x16x32_bf16 v[126:129], v[142:145], v[200:203], v[126:129]
	v_mfma_f32_16x16x32_bf16 v[122:125], v[94:97], v[200:203], v[122:125]
	v_mfma_f32_16x16x32_bf16 v[118:121], v[142:145], v[214:217], v[118:121]
	v_mfma_f32_16x16x32_bf16 v[114:117], v[94:97], v[214:217], v[114:117]
	v_mfma_f32_16x16x32_bf16 v[110:113], v[142:145], v[222:225], v[110:113]
	v_mfma_f32_16x16x32_bf16 v[106:109], v[94:97], v[222:225], v[106:109]
	v_mfma_f32_16x16x32_bf16 v[134:137], v[90:93], v[196:199], v[134:137]
	v_mfma_f32_16x16x32_bf16 v[130:133], v[176:179], v[196:199], v[130:133]
	v_mfma_f32_16x16x32_bf16 v[126:129], v[90:93], v[204:207], v[126:129]
	v_mfma_f32_16x16x32_bf16 v[122:125], v[176:179], v[204:207], v[122:125]
	v_mfma_f32_16x16x32_bf16 v[118:121], v[90:93], v[218:221], v[118:121]
	v_mfma_f32_16x16x32_bf16 v[114:117], v[176:179], v[218:221], v[114:117]
	v_mfma_f32_16x16x32_bf16 v[110:113], v[90:93], v[226:229], v[110:113]
	v_mfma_f32_16x16x32_bf16 v[106:109], v[176:179], v[226:229], v[106:109]
	v_mfma_f32_16x16x32_bf16 v[62:65], v[146:149], v[192:195], v[62:65]
	v_mfma_f32_16x16x32_bf16 v[58:61], v[184:187], v[192:195], v[58:61]
	v_mfma_f32_16x16x32_bf16 v[54:57], v[146:149], v[200:203], v[54:57]
	v_mfma_f32_16x16x32_bf16 v[50:53], v[184:187], v[200:203], v[50:53]
	v_mfma_f32_16x16x32_bf16 v[46:49], v[146:149], v[214:217], v[46:49]
	v_mfma_f32_16x16x32_bf16 v[42:45], v[184:187], v[214:217], v[42:45]
	v_mfma_f32_16x16x32_bf16 v[38:41], v[146:149], v[222:225], v[38:41]
	v_mfma_f32_16x16x32_bf16 v[34:37], v[184:187], v[222:225], v[34:37]
	v_mfma_f32_16x16x32_bf16 v[62:65], v[180:183], v[196:199], v[62:65]
	v_mfma_f32_16x16x32_bf16 v[58:61], v[188:191], v[196:199], v[58:61]
	v_mfma_f32_16x16x32_bf16 v[54:57], v[180:183], v[204:207], v[54:57]
	v_mfma_f32_16x16x32_bf16 v[50:53], v[188:191], v[204:207], v[50:53]
	v_mfma_f32_16x16x32_bf16 v[46:49], v[180:183], v[218:221], v[46:49]
	v_mfma_f32_16x16x32_bf16 v[42:45], v[188:191], v[218:221], v[42:45]
	v_mfma_f32_16x16x32_bf16 v[38:41], v[180:183], v[226:229], v[38:41]
	v_mfma_f32_16x16x32_bf16 v[34:37], v[188:191], v[226:229], v[34:37]
	s_setprio 0
	s_barrier
	s_addk_i32 vcc_lo, 0x80
	s_mov_b32 m0, s71
	v_add_u32_e32 v175, vcc_lo, v150
	ds_read_b128 v[192:195], v174 offset:49152
	ds_read_b128 v[196:199], v174 offset:50176
	ds_read_b128 v[200:203], v174 offset:51200
	ds_read_b128 v[204:207], v174 offset:52224
	ds_read_b128 v[214:217], v174 offset:53248
	ds_read_b128 v[218:221], v174 offset:54272
	ds_read_b128 v[222:225], v174 offset:55296
	ds_read_b128 v[226:229], v174 offset:56320
	global_load_lds_dwordx4 v175, s[6:7]
	v_add_u32_e32 v175, s59, v175
	s_mov_b32 m0, s72
	s_nop 0
	global_load_lds_dwordx4 v175, s[6:7]
	v_add_u32_e32 v175, vcc_lo, v151
	s_mov_b32 m0, s77
	s_nop 0
	global_load_lds_dwordx4 v175, s[6:7]
	v_add_u32_e32 v175, s59, v175
	s_mov_b32 m0, s78
	s_nop 0
	global_load_lds_dwordx4 v175, s[6:7]
	v_add_u32_e32 v175, s96, v155
	s_mov_b32 m0, s73
	s_nop 0
	global_load_lds_dwordx4 v175, s[4:5]
	v_add_u32_e32 v175, s58, v175
	s_mov_b32 m0, s76
	s_nop 0
	global_load_lds_dwordx4 v175, s[4:5]
	s_waitcnt vmcnt(8)
	s_waitcnt lgkmcnt(0)
	s_barrier
	s_setprio 1
	s_waitcnt lgkmcnt(0)
	v_mfma_f32_16x16x32_bf16 v[102:105], v[142:145], v[192:195], v[102:105]
	v_mfma_f32_16x16x32_bf16 v[98:101], v[94:97], v[192:195], v[98:101]
	v_mfma_f32_16x16x32_bf16 v[86:89], v[142:145], v[200:203], v[86:89]
	v_mfma_f32_16x16x32_bf16 v[82:85], v[94:97], v[200:203], v[82:85]
	v_mfma_f32_16x16x32_bf16 v[78:81], v[142:145], v[214:217], v[78:81]
	v_mfma_f32_16x16x32_bf16 v[74:77], v[94:97], v[214:217], v[74:77]
	v_mfma_f32_16x16x32_bf16 v[70:73], v[142:145], v[222:225], v[70:73]
	v_mfma_f32_16x16x32_bf16 v[66:69], v[94:97], v[222:225], v[66:69]
	v_mfma_f32_16x16x32_bf16 v[102:105], v[90:93], v[196:199], v[102:105]
	v_mfma_f32_16x16x32_bf16 v[98:101], v[176:179], v[196:199], v[98:101]
	v_mfma_f32_16x16x32_bf16 v[86:89], v[90:93], v[204:207], v[86:89]
	v_mfma_f32_16x16x32_bf16 v[82:85], v[176:179], v[204:207], v[82:85]
	v_mfma_f32_16x16x32_bf16 v[78:81], v[90:93], v[218:221], v[78:81]
	v_mfma_f32_16x16x32_bf16 v[74:77], v[176:179], v[218:221], v[74:77]
	v_mfma_f32_16x16x32_bf16 v[70:73], v[90:93], v[226:229], v[70:73]
	v_mfma_f32_16x16x32_bf16 v[66:69], v[176:179], v[226:229], v[66:69]
	v_mfma_f32_16x16x32_bf16 v[30:33], v[146:149], v[192:195], v[30:33]
	v_mfma_f32_16x16x32_bf16 v[26:29], v[184:187], v[192:195], v[26:29]
	v_mfma_f32_16x16x32_bf16 v[22:25], v[146:149], v[200:203], v[22:25]
	v_mfma_f32_16x16x32_bf16 v[18:21], v[184:187], v[200:203], v[18:21]
	v_mfma_f32_16x16x32_bf16 v[14:17], v[146:149], v[214:217], v[14:17]
	v_mfma_f32_16x16x32_bf16 v[10:13], v[184:187], v[214:217], v[10:13]
	v_mfma_f32_16x16x32_bf16 v[6:9], v[146:149], v[222:225], v[6:9]
	v_mfma_f32_16x16x32_bf16 v[2:5], v[184:187], v[222:225], v[2:5]
	v_mfma_f32_16x16x32_bf16 v[30:33], v[180:183], v[196:199], v[30:33]
	v_mfma_f32_16x16x32_bf16 v[26:29], v[188:191], v[196:199], v[26:29]
	v_mfma_f32_16x16x32_bf16 v[22:25], v[180:183], v[204:207], v[22:25]
	v_mfma_f32_16x16x32_bf16 v[18:21], v[188:191], v[204:207], v[18:21]
	v_mfma_f32_16x16x32_bf16 v[14:17], v[180:183], v[218:221], v[14:17]
	v_mfma_f32_16x16x32_bf16 v[10:13], v[188:191], v[218:221], v[10:13]
	v_mfma_f32_16x16x32_bf16 v[6:9], v[180:183], v[226:229], v[6:9]
	v_mfma_f32_16x16x32_bf16 v[2:5], v[188:191], v[226:229], v[2:5]
	s_setprio 0
	s_barrier
	s_add_i32 s74, s74, 2
	s_addk_i32 s56, 0x100
	s_addk_i32 s57, 0x100
	s_cmp_ge_i32 s74, s69
	s_cbranch_scc0 .LBB0_2521

.LBB0_2595:
	s_andn2_b64 vcc, exec, s[12:13]
	s_cbranch_vccnz .Lzs_11
	s_add_i32 s60, s64, 0x80
	s_addk_i32 s63, 0x100
	s_mov_b32 s64, 0
	ds_read_b128 v[130:133], v206
	ds_read_b128 v[134:137], v207
	ds_read_b128 v[138:141], v202
	ds_read_b128 v[142:145], v203
	ds_read_b128 v[146:149], v208
	ds_read_b128 v[150:153], v209
	ds_read_b128 v[154:157], v211
	ds_read_b128 v[158:161], v213
	s_add_i32 s65, s60, 0x80
	s_cmp_eq_u32 s84, s64
	s_cselect_b32 s75, s61, s63
	s_cselect_b32 s65, s5, s65
	v_add_u32_e32 v194, s60, v221
	s_add_i32 m0, s45, 0xc000
	ds_read_b128 v[162:165], v222
	ds_read_b128 v[166:169], v222 offset:1024
	ds_read_b128 v[170:173], v222 offset:2048
	ds_read_b128 v[174:177], v222 offset:3072
	ds_read_b128 v[182:185], v222 offset:4096
	ds_read_b128 v[186:189], v222 offset:5120
	ds_read_b128 v[190:193], v222 offset:6144
	ds_read_b128 v[224:227], v222 offset:7168
	global_load_lds_dwordx4 v194, s[6:7]
	v_add_u32_e32 v194, s60, v220
	s_add_i32 m0, s45, 0xe000
	s_nop 0
	global_load_lds_dwordx4 v194, s[6:7]
	s_waitcnt vmcnt(8)
	s_waitcnt lgkmcnt(0)
	s_barrier
	s_setprio 1
	s_waitcnt lgkmcnt(0)
	v_mfma_f32_16x16x32_bf16 v[126:129], v[138:141], v[162:165], 0
	v_mfma_f32_16x16x32_bf16 v[122:125], v[134:137], v[162:165], 0
	v_mfma_f32_16x16x32_bf16 v[110:113], v[138:141], v[170:173], 0
	v_mfma_f32_16x16x32_bf16 v[106:109], v[134:137], v[170:173], 0
	v_mfma_f32_16x16x32_bf16 v[94:97], v[138:141], v[182:185], 0
	v_mfma_f32_16x16x32_bf16 v[90:93], v[134:137], v[182:185], 0
	v_mfma_f32_16x16x32_bf16 v[78:81], v[138:141], v[190:193], 0
	v_mfma_f32_16x16x32_bf16 v[74:77], v[134:137], v[190:193], 0
	v_mfma_f32_16x16x32_bf16 v[126:129], v[130:133], v[166:169], v[126:129]
	v_mfma_f32_16x16x32_bf16 v[122:125], v[146:149], v[166:169], v[122:125]
	v_mfma_f32_16x16x32_bf16 v[110:113], v[130:133], v[174:177], v[110:113]
	v_mfma_f32_16x16x32_bf16 v[106:109], v[146:149], v[174:177], v[106:109]
	v_mfma_f32_16x16x32_bf16 v[94:97], v[130:133], v[186:189], v[94:97]
	v_mfma_f32_16x16x32_bf16 v[90:93], v[146:149], v[186:189], v[90:93]
	v_mfma_f32_16x16x32_bf16 v[78:81], v[130:133], v[224:227], v[78:81]
	v_mfma_f32_16x16x32_bf16 v[74:77], v[146:149], v[224:227], v[74:77]
	v_mfma_f32_16x16x32_bf16 v[118:121], v[142:145], v[162:165], 0
	v_mfma_f32_16x16x32_bf16 v[114:117], v[154:157], v[162:165], 0
	v_mfma_f32_16x16x32_bf16 v[102:105], v[142:145], v[170:173], 0
	v_mfma_f32_16x16x32_bf16 v[98:101], v[154:157], v[170:173], 0
	v_mfma_f32_16x16x32_bf16 v[86:89], v[142:145], v[182:185], 0
	v_mfma_f32_16x16x32_bf16 v[82:85], v[154:157], v[182:185], 0
	v_mfma_f32_16x16x32_bf16 v[70:73], v[142:145], v[190:193], 0
	v_mfma_f32_16x16x32_bf16 v[66:69], v[154:157], v[190:193], 0
	v_mfma_f32_16x16x32_bf16 v[118:121], v[150:153], v[166:169], v[118:121]
	v_mfma_f32_16x16x32_bf16 v[114:117], v[158:161], v[166:169], v[114:117]
	v_mfma_f32_16x16x32_bf16 v[102:105], v[150:153], v[174:177], v[102:105]
	v_mfma_f32_16x16x32_bf16 v[98:101], v[158:161], v[174:177], v[98:101]
	v_mfma_f32_16x16x32_bf16 v[86:89], v[150:153], v[186:189], v[86:89]
	v_mfma_f32_16x16x32_bf16 v[82:85], v[158:161], v[186:189], v[82:85]
	v_mfma_f32_16x16x32_bf16 v[70:73], v[150:153], v[224:227], v[70:73]
	v_mfma_f32_16x16x32_bf16 v[66:69], v[158:161], v[224:227], v[66:69]
	s_setprio 0
	s_barrier
	s_mov_b32 m0, s66
	v_add_u32_e32 v194, s75, v196
	ds_read_b128 v[162:165], v222 offset:16384
	ds_read_b128 v[166:169], v222 offset:17408
	ds_read_b128 v[170:173], v222 offset:18432
	ds_read_b128 v[174:177], v222 offset:19456
	ds_read_b128 v[182:185], v222 offset:20480
	ds_read_b128 v[186:189], v222 offset:21504
	ds_read_b128 v[190:193], v222 offset:22528
	ds_read_b128 v[224:227], v222 offset:23552
	global_load_lds_dwordx4 v194, s[8:9]
	v_add_u32_e32 v194, s44, v194
	s_mov_b32 m0, s67
	s_nop 0
	global_load_lds_dwordx4 v194, s[8:9]
	v_add_u32_e32 v194, s75, v197
	s_mov_b32 m0, s68
	s_nop 0
	global_load_lds_dwordx4 v194, s[8:9]
	v_add_u32_e32 v194, s44, v194
	s_mov_b32 m0, s69
	s_nop 0
	global_load_lds_dwordx4 v194, s[8:9]
	v_add_u32_e32 v194, s65, v1
	s_mov_b32 m0, s45
	s_nop 0
	global_load_lds_dwordx4 v194, s[6:7]
	v_add_u32_e32 v194, s35, v194
	s_mov_b32 m0, s70
	s_nop 0
	global_load_lds_dwordx4 v194, s[6:7]
	s_waitcnt vmcnt(8)
	s_waitcnt lgkmcnt(0)
	s_barrier
	s_setprio 1
	s_waitcnt lgkmcnt(0)
	v_mfma_f32_16x16x32_bf16 v[62:65], v[138:141], v[162:165], 0
	v_mfma_f32_16x16x32_bf16 v[58:61], v[134:137], v[162:165], 0
	v_mfma_f32_16x16x32_bf16 v[46:49], v[138:141], v[170:173], 0
	v_mfma_f32_16x16x32_bf16 v[42:45], v[134:137], v[170:173], 0
	v_mfma_f32_16x16x32_bf16 v[30:33], v[138:141], v[182:185], 0
	v_mfma_f32_16x16x32_bf16 v[26:29], v[134:137], v[182:185], 0
	v_mfma_f32_16x16x32_bf16 v[14:17], v[138:141], v[190:193], 0
	v_mfma_f32_16x16x32_bf16 v[10:13], v[134:137], v[190:193], 0
	v_mfma_f32_16x16x32_bf16 v[62:65], v[130:133], v[166:169], v[62:65]
	v_mfma_f32_16x16x32_bf16 v[58:61], v[146:149], v[166:169], v[58:61]
	v_mfma_f32_16x16x32_bf16 v[46:49], v[130:133], v[174:177], v[46:49]
	v_mfma_f32_16x16x32_bf16 v[42:45], v[146:149], v[174:177], v[42:45]
	v_mfma_f32_16x16x32_bf16 v[30:33], v[130:133], v[186:189], v[30:33]
	v_mfma_f32_16x16x32_bf16 v[26:29], v[146:149], v[186:189], v[26:29]
	v_mfma_f32_16x16x32_bf16 v[14:17], v[130:133], v[224:227], v[14:17]
	v_mfma_f32_16x16x32_bf16 v[10:13], v[146:149], v[224:227], v[10:13]
	v_mfma_f32_16x16x32_bf16 v[54:57], v[142:145], v[162:165], 0
	v_mfma_f32_16x16x32_bf16 v[50:53], v[154:157], v[162:165], 0
	v_mfma_f32_16x16x32_bf16 v[38:41], v[142:145], v[170:173], 0
	v_mfma_f32_16x16x32_bf16 v[34:37], v[154:157], v[170:173], 0
	v_mfma_f32_16x16x32_bf16 v[22:25], v[142:145], v[182:185], 0
	v_mfma_f32_16x16x32_bf16 v[18:21], v[154:157], v[182:185], 0
	v_mfma_f32_16x16x32_bf16 v[6:9], v[142:145], v[190:193], 0
	v_mfma_f32_16x16x32_bf16 v[2:5], v[154:157], v[190:193], 0
	v_mfma_f32_16x16x32_bf16 v[54:57], v[150:153], v[166:169], v[54:57]
	v_mfma_f32_16x16x32_bf16 v[50:53], v[158:161], v[166:169], v[50:53]
	v_mfma_f32_16x16x32_bf16 v[38:41], v[150:153], v[174:177], v[38:41]
	v_mfma_f32_16x16x32_bf16 v[34:37], v[158:161], v[174:177], v[34:37]
	v_mfma_f32_16x16x32_bf16 v[22:25], v[150:153], v[186:189], v[22:25]
	v_mfma_f32_16x16x32_bf16 v[18:21], v[158:161], v[186:189], v[18:21]
	v_mfma_f32_16x16x32_bf16 v[6:9], v[150:153], v[224:227], v[6:9]
	v_mfma_f32_16x16x32_bf16 v[2:5], v[158:161], v[224:227], v[2:5]
	s_setprio 0
	s_barrier
	s_branch .Lmid_9
.LBB0_2597:
	ds_read_b128 v[130:133], v206
	ds_read_b128 v[134:137], v207
	ds_read_b128 v[138:141], v202
	ds_read_b128 v[142:145], v203
	ds_read_b128 v[146:149], v208
	ds_read_b128 v[150:153], v209
	ds_read_b128 v[154:157], v211
	ds_read_b128 v[158:161], v213
	s_add_i32 s65, s60, 0x80
	s_cmp_eq_u32 s84, s64
	s_cselect_b32 s75, s61, s63
	s_cselect_b32 s65, s5, s65
	v_add_u32_e32 v194, s60, v221
	s_add_i32 m0, s45, 0xc000
	ds_read_b128 v[162:165], v222
	ds_read_b128 v[166:169], v222 offset:1024
	ds_read_b128 v[170:173], v222 offset:2048
	ds_read_b128 v[174:177], v222 offset:3072
	ds_read_b128 v[182:185], v222 offset:4096
	ds_read_b128 v[186:189], v222 offset:5120
	ds_read_b128 v[190:193], v222 offset:6144
	ds_read_b128 v[224:227], v222 offset:7168
	global_load_lds_dwordx4 v194, s[6:7]
	v_add_u32_e32 v194, s60, v220
	s_add_i32 m0, s45, 0xe000
	s_nop 0
	global_load_lds_dwordx4 v194, s[6:7]
	s_waitcnt vmcnt(8)
	s_waitcnt lgkmcnt(0)
	s_barrier
	s_setprio 1
	s_waitcnt lgkmcnt(0)
	v_mfma_f32_16x16x32_bf16 v[126:129], v[138:141], v[162:165], v[126:129]
	v_mfma_f32_16x16x32_bf16 v[122:125], v[134:137], v[162:165], v[122:125]
	v_mfma_f32_16x16x32_bf16 v[110:113], v[138:141], v[170:173], v[110:113]
	v_mfma_f32_16x16x32_bf16 v[106:109], v[134:137], v[170:173], v[106:109]
	v_mfma_f32_16x16x32_bf16 v[94:97], v[138:141], v[182:185], v[94:97]
	v_mfma_f32_16x16x32_bf16 v[90:93], v[134:137], v[182:185], v[90:93]
	v_mfma_f32_16x16x32_bf16 v[78:81], v[138:141], v[190:193], v[78:81]
	v_mfma_f32_16x16x32_bf16 v[74:77], v[134:137], v[190:193], v[74:77]
	v_mfma_f32_16x16x32_bf16 v[126:129], v[130:133], v[166:169], v[126:129]
	v_mfma_f32_16x16x32_bf16 v[122:125], v[146:149], v[166:169], v[122:125]
	v_mfma_f32_16x16x32_bf16 v[110:113], v[130:133], v[174:177], v[110:113]
	v_mfma_f32_16x16x32_bf16 v[106:109], v[146:149], v[174:177], v[106:109]
	v_mfma_f32_16x16x32_bf16 v[94:97], v[130:133], v[186:189], v[94:97]
	v_mfma_f32_16x16x32_bf16 v[90:93], v[146:149], v[186:189], v[90:93]
	v_mfma_f32_16x16x32_bf16 v[78:81], v[130:133], v[224:227], v[78:81]
	v_mfma_f32_16x16x32_bf16 v[74:77], v[146:149], v[224:227], v[74:77]
	v_mfma_f32_16x16x32_bf16 v[118:121], v[142:145], v[162:165], v[118:121]
	v_mfma_f32_16x16x32_bf16 v[114:117], v[154:157], v[162:165], v[114:117]
	v_mfma_f32_16x16x32_bf16 v[102:105], v[142:145], v[170:173], v[102:105]
	v_mfma_f32_16x16x32_bf16 v[98:101], v[154:157], v[170:173], v[98:101]
	v_mfma_f32_16x16x32_bf16 v[86:89], v[142:145], v[182:185], v[86:89]
	v_mfma_f32_16x16x32_bf16 v[82:85], v[154:157], v[182:185], v[82:85]
	v_mfma_f32_16x16x32_bf16 v[70:73], v[142:145], v[190:193], v[70:73]
	v_mfma_f32_16x16x32_bf16 v[66:69], v[154:157], v[190:193], v[66:69]
	v_mfma_f32_16x16x32_bf16 v[118:121], v[150:153], v[166:169], v[118:121]
	v_mfma_f32_16x16x32_bf16 v[114:117], v[158:161], v[166:169], v[114:117]
	v_mfma_f32_16x16x32_bf16 v[102:105], v[150:153], v[174:177], v[102:105]
	v_mfma_f32_16x16x32_bf16 v[98:101], v[158:161], v[174:177], v[98:101]
	v_mfma_f32_16x16x32_bf16 v[86:89], v[150:153], v[186:189], v[86:89]
	v_mfma_f32_16x16x32_bf16 v[82:85], v[158:161], v[186:189], v[82:85]
	v_mfma_f32_16x16x32_bf16 v[70:73], v[150:153], v[224:227], v[70:73]
	v_mfma_f32_16x16x32_bf16 v[66:69], v[158:161], v[224:227], v[66:69]
	s_setprio 0
	s_barrier
	s_mov_b32 m0, s66
	v_add_u32_e32 v194, s75, v196
	ds_read_b128 v[162:165], v222 offset:16384
	ds_read_b128 v[166:169], v222 offset:17408
	ds_read_b128 v[170:173], v222 offset:18432
	ds_read_b128 v[174:177], v222 offset:19456
	ds_read_b128 v[182:185], v222 offset:20480
	ds_read_b128 v[186:189], v222 offset:21504
	ds_read_b128 v[190:193], v222 offset:22528
	ds_read_b128 v[224:227], v222 offset:23552
	global_load_lds_dwordx4 v194, s[8:9]
	v_add_u32_e32 v194, s44, v194
	s_mov_b32 m0, s67
	s_nop 0
	global_load_lds_dwordx4 v194, s[8:9]
	v_add_u32_e32 v194, s75, v197
	s_mov_b32 m0, s68
	s_nop 0
	global_load_lds_dwordx4 v194, s[8:9]
	v_add_u32_e32 v194, s44, v194
	s_mov_b32 m0, s69
	s_nop 0
	global_load_lds_dwordx4 v194, s[8:9]
	v_add_u32_e32 v194, s65, v1
	s_mov_b32 m0, s45
	s_nop 0
	global_load_lds_dwordx4 v194, s[6:7]
	v_add_u32_e32 v194, s35, v194
	s_mov_b32 m0, s70
	s_nop 0
	global_load_lds_dwordx4 v194, s[6:7]
	s_waitcnt vmcnt(8)
	s_waitcnt lgkmcnt(0)
	s_barrier
	s_setprio 1
	s_waitcnt lgkmcnt(0)
	v_mfma_f32_16x16x32_bf16 v[62:65], v[138:141], v[162:165], v[62:65]
	v_mfma_f32_16x16x32_bf16 v[58:61], v[134:137], v[162:165], v[58:61]
	v_mfma_f32_16x16x32_bf16 v[46:49], v[138:141], v[170:173], v[46:49]
	v_mfma_f32_16x16x32_bf16 v[42:45], v[134:137], v[170:173], v[42:45]
	v_mfma_f32_16x16x32_bf16 v[30:33], v[138:141], v[182:185], v[30:33]
	v_mfma_f32_16x16x32_bf16 v[26:29], v[134:137], v[182:185], v[26:29]
	v_mfma_f32_16x16x32_bf16 v[14:17], v[138:141], v[190:193], v[14:17]
	v_mfma_f32_16x16x32_bf16 v[10:13], v[134:137], v[190:193], v[10:13]
	v_mfma_f32_16x16x32_bf16 v[62:65], v[130:133], v[166:169], v[62:65]
	v_mfma_f32_16x16x32_bf16 v[58:61], v[146:149], v[166:169], v[58:61]
	v_mfma_f32_16x16x32_bf16 v[46:49], v[130:133], v[174:177], v[46:49]
	v_mfma_f32_16x16x32_bf16 v[42:45], v[146:149], v[174:177], v[42:45]
	v_mfma_f32_16x16x32_bf16 v[30:33], v[130:133], v[186:189], v[30:33]
	v_mfma_f32_16x16x32_bf16 v[26:29], v[146:149], v[186:189], v[26:29]
	v_mfma_f32_16x16x32_bf16 v[14:17], v[130:133], v[224:227], v[14:17]
	v_mfma_f32_16x16x32_bf16 v[10:13], v[146:149], v[224:227], v[10:13]
	v_mfma_f32_16x16x32_bf16 v[54:57], v[142:145], v[162:165], v[54:57]
	v_mfma_f32_16x16x32_bf16 v[50:53], v[154:157], v[162:165], v[50:53]
	v_mfma_f32_16x16x32_bf16 v[38:41], v[142:145], v[170:173], v[38:41]
	v_mfma_f32_16x16x32_bf16 v[34:37], v[154:157], v[170:173], v[34:37]
	v_mfma_f32_16x16x32_bf16 v[22:25], v[142:145], v[182:185], v[22:25]
	v_mfma_f32_16x16x32_bf16 v[18:21], v[154:157], v[182:185], v[18:21]
	v_mfma_f32_16x16x32_bf16 v[6:9], v[142:145], v[190:193], v[6:9]
	v_mfma_f32_16x16x32_bf16 v[2:5], v[154:157], v[190:193], v[2:5]
	v_mfma_f32_16x16x32_bf16 v[54:57], v[150:153], v[166:169], v[54:57]
	v_mfma_f32_16x16x32_bf16 v[50:53], v[158:161], v[166:169], v[50:53]
	v_mfma_f32_16x16x32_bf16 v[38:41], v[150:153], v[174:177], v[38:41]
	v_mfma_f32_16x16x32_bf16 v[34:37], v[158:161], v[174:177], v[34:37]
	v_mfma_f32_16x16x32_bf16 v[22:25], v[150:153], v[186:189], v[22:25]
	v_mfma_f32_16x16x32_bf16 v[18:21], v[158:161], v[186:189], v[18:21]
	v_mfma_f32_16x16x32_bf16 v[6:9], v[150:153], v[224:227], v[6:9]
	v_mfma_f32_16x16x32_bf16 v[2:5], v[158:161], v[224:227], v[2:5]
	s_setprio 0
	s_barrier
.Lmid_9:
	ds_read_b128 v[130:133], v214
	ds_read_b128 v[134:137], v215
	ds_read_b128 v[138:141], v204
	ds_read_b128 v[142:145], v205
	ds_read_b128 v[146:149], v216
	ds_read_b128 v[150:153], v217
	ds_read_b128 v[154:157], v218
	ds_read_b128 v[158:161], v219
	s_mov_b32 m0, s71
	v_add_u32_e32 v194, s65, v198
	ds_read_b128 v[162:165], v222 offset:32768
	ds_read_b128 v[166:169], v222 offset:33792
	ds_read_b128 v[170:173], v222 offset:34816
	ds_read_b128 v[174:177], v222 offset:35840
	ds_read_b128 v[182:185], v222 offset:36864
	ds_read_b128 v[186:189], v222 offset:37888
	ds_read_b128 v[190:193], v222 offset:38912
	ds_read_b128 v[224:227], v222 offset:39936
	global_load_lds_dwordx4 v194, s[6:7]
	v_add_u32_e32 v194, s35, v194
	s_mov_b32 m0, s72
	s_nop 0
	global_load_lds_dwordx4 v194, s[6:7]
	s_waitcnt vmcnt(8)
	s_waitcnt lgkmcnt(0)
	s_barrier
	s_setprio 1
	s_waitcnt lgkmcnt(0)
	v_mfma_f32_16x16x32_bf16 v[126:129], v[138:141], v[162:165], v[126:129]
	v_mfma_f32_16x16x32_bf16 v[122:125], v[134:137], v[162:165], v[122:125]
	v_mfma_f32_16x16x32_bf16 v[110:113], v[138:141], v[170:173], v[110:113]
	v_mfma_f32_16x16x32_bf16 v[106:109], v[134:137], v[170:173], v[106:109]
	v_mfma_f32_16x16x32_bf16 v[94:97], v[138:141], v[182:185], v[94:97]
	v_mfma_f32_16x16x32_bf16 v[90:93], v[134:137], v[182:185], v[90:93]
	v_mfma_f32_16x16x32_bf16 v[78:81], v[138:141], v[190:193], v[78:81]
	v_mfma_f32_16x16x32_bf16 v[74:77], v[134:137], v[190:193], v[74:77]
	v_mfma_f32_16x16x32_bf16 v[126:129], v[130:133], v[166:169], v[126:129]
	v_mfma_f32_16x16x32_bf16 v[122:125], v[146:149], v[166:169], v[122:125]
	v_mfma_f32_16x16x32_bf16 v[110:113], v[130:133], v[174:177], v[110:113]
	v_mfma_f32_16x16x32_bf16 v[106:109], v[146:149], v[174:177], v[106:109]
	v_mfma_f32_16x16x32_bf16 v[94:97], v[130:133], v[186:189], v[94:97]
	v_mfma_f32_16x16x32_bf16 v[90:93], v[146:149], v[186:189], v[90:93]
	v_mfma_f32_16x16x32_bf16 v[78:81], v[130:133], v[224:227], v[78:81]
	v_mfma_f32_16x16x32_bf16 v[74:77], v[146:149], v[224:227], v[74:77]
	v_mfma_f32_16x16x32_bf16 v[118:121], v[142:145], v[162:165], v[118:121]
	v_mfma_f32_16x16x32_bf16 v[114:117], v[154:157], v[162:165], v[114:117]
	v_mfma_f32_16x16x32_bf16 v[102:105], v[142:145], v[170:173], v[102:105]
	v_mfma_f32_16x16x32_bf16 v[98:101], v[154:157], v[170:173], v[98:101]
	v_mfma_f32_16x16x32_bf16 v[86:89], v[142:145], v[182:185], v[86:89]
	v_mfma_f32_16x16x32_bf16 v[82:85], v[154:157], v[182:185], v[82:85]
	v_mfma_f32_16x16x32_bf16 v[70:73], v[142:145], v[190:193], v[70:73]
	v_mfma_f32_16x16x32_bf16 v[66:69], v[154:157], v[190:193], v[66:69]
	v_mfma_f32_16x16x32_bf16 v[118:121], v[150:153], v[166:169], v[118:121]
	v_mfma_f32_16x16x32_bf16 v[114:117], v[158:161], v[166:169], v[114:117]
	v_mfma_f32_16x16x32_bf16 v[102:105], v[150:153], v[174:177], v[102:105]
	v_mfma_f32_16x16x32_bf16 v[98:101], v[158:161], v[174:177], v[98:101]
	v_mfma_f32_16x16x32_bf16 v[86:89], v[150:153], v[186:189], v[86:89]
	v_mfma_f32_16x16x32_bf16 v[82:85], v[158:161], v[186:189], v[82:85]
	v_mfma_f32_16x16x32_bf16 v[70:73], v[150:153], v[224:227], v[70:73]
	v_mfma_f32_16x16x32_bf16 v[66:69], v[158:161], v[224:227], v[66:69]
	s_setprio 0
	s_barrier
	s_addk_i32 s75, 0x80
	s_mov_b32 m0, s77
	v_add_u32_e32 v194, s75, v196
	ds_read_b128 v[162:165], v222 offset:49152
	ds_read_b128 v[166:169], v222 offset:50176
	ds_read_b128 v[170:173], v222 offset:51200
	ds_read_b128 v[174:177], v222 offset:52224
	ds_read_b128 v[182:185], v222 offset:53248
	ds_read_b128 v[186:189], v222 offset:54272
	ds_read_b128 v[190:193], v222 offset:55296
	ds_read_b128 v[224:227], v222 offset:56320
	global_load_lds_dwordx4 v194, s[8:9]
	v_add_u32_e32 v194, s44, v194
	s_mov_b32 m0, s78
	s_nop 0
	global_load_lds_dwordx4 v194, s[8:9]
	v_add_u32_e32 v194, s75, v197
	s_mov_b32 m0, s81
	s_nop 0
	global_load_lds_dwordx4 v194, s[8:9]
	v_add_u32_e32 v194, s44, v194
	s_mov_b32 m0, s82
	s_nop 0
	global_load_lds_dwordx4 v194, s[8:9]
	v_add_u32_e32 v194, s65, v201
	s_mov_b32 m0, s79
	s_nop 0
	global_load_lds_dwordx4 v194, s[6:7]
	v_add_u32_e32 v194, s35, v194
	s_mov_b32 m0, s80
	s_nop 0
	global_load_lds_dwordx4 v194, s[6:7]
	s_waitcnt vmcnt(8)
	s_waitcnt lgkmcnt(0)
	s_barrier
	s_setprio 1
	s_waitcnt lgkmcnt(0)
	v_mfma_f32_16x16x32_bf16 v[62:65], v[138:141], v[162:165], v[62:65]
	v_mfma_f32_16x16x32_bf16 v[58:61], v[134:137], v[162:165], v[58:61]
	v_mfma_f32_16x16x32_bf16 v[46:49], v[138:141], v[170:173], v[46:49]
	v_mfma_f32_16x16x32_bf16 v[42:45], v[134:137], v[170:173], v[42:45]
	v_mfma_f32_16x16x32_bf16 v[30:33], v[138:141], v[182:185], v[30:33]
	v_mfma_f32_16x16x32_bf16 v[26:29], v[134:137], v[182:185], v[26:29]
	v_mfma_f32_16x16x32_bf16 v[14:17], v[138:141], v[190:193], v[14:17]
	v_mfma_f32_16x16x32_bf16 v[10:13], v[134:137], v[190:193], v[10:13]
	v_mfma_f32_16x16x32_bf16 v[62:65], v[130:133], v[166:169], v[62:65]
	v_mfma_f32_16x16x32_bf16 v[58:61], v[146:149], v[166:169], v[58:61]
	v_mfma_f32_16x16x32_bf16 v[46:49], v[130:133], v[174:177], v[46:49]
	v_mfma_f32_16x16x32_bf16 v[42:45], v[146:149], v[174:177], v[42:45]
	v_mfma_f32_16x16x32_bf16 v[30:33], v[130:133], v[186:189], v[30:33]
	v_mfma_f32_16x16x32_bf16 v[26:29], v[146:149], v[186:189], v[26:29]
	v_mfma_f32_16x16x32_bf16 v[14:17], v[130:133], v[224:227], v[14:17]
	v_mfma_f32_16x16x32_bf16 v[10:13], v[146:149], v[224:227], v[10:13]
	v_mfma_f32_16x16x32_bf16 v[54:57], v[142:145], v[162:165], v[54:57]
	v_mfma_f32_16x16x32_bf16 v[50:53], v[154:157], v[162:165], v[50:53]
	v_mfma_f32_16x16x32_bf16 v[38:41], v[142:145], v[170:173], v[38:41]
	v_mfma_f32_16x16x32_bf16 v[34:37], v[154:157], v[170:173], v[34:37]
	v_mfma_f32_16x16x32_bf16 v[22:25], v[142:145], v[182:185], v[22:25]
	v_mfma_f32_16x16x32_bf16 v[18:21], v[154:157], v[182:185], v[18:21]
	v_mfma_f32_16x16x32_bf16 v[6:9], v[142:145], v[190:193], v[6:9]
	v_mfma_f32_16x16x32_bf16 v[2:5], v[154:157], v[190:193], v[2:5]
	v_mfma_f32_16x16x32_bf16 v[54:57], v[150:153], v[166:169], v[54:57]
	v_mfma_f32_16x16x32_bf16 v[50:53], v[158:161], v[166:169], v[50:53]
	v_mfma_f32_16x16x32_bf16 v[38:41], v[150:153], v[174:177], v[38:41]
	v_mfma_f32_16x16x32_bf16 v[34:37], v[158:161], v[174:177], v[34:37]
	v_mfma_f32_16x16x32_bf16 v[22:25], v[150:153], v[186:189], v[22:25]
	v_mfma_f32_16x16x32_bf16 v[18:21], v[158:161], v[186:189], v[18:21]
	v_mfma_f32_16x16x32_bf16 v[6:9], v[150:153], v[224:227], v[6:9]
	v_mfma_f32_16x16x32_bf16 v[2:5], v[158:161], v[224:227], v[2:5]
	s_setprio 0
	s_barrier
	s_add_i32 s64, s64, 2
	s_addk_i32 s60, 0x100
	s_addk_i32 s63, 0x100
	s_cmp_ge_i32 s64, s74
	s_cbranch_scc0 .LBB0_2597

.LBB0_2935:
	s_andn2_b64 vcc, exec, s[14:15]
	s_cbranch_vccnz .Lzs_12
	s_add_i32 s28, s82, 0x80
	s_add_i32 s82, s83, 0x100
	s_mov_b32 s83, 0
	ds_read_b128 v[18:21], v180
	ds_read_b128 v[22:25], v181
	ds_read_b128 v[26:29], v188
	ds_read_b128 v[30:33], v189
	ds_read_b128 v[2:5], v182
	ds_read_b128 v[6:9], v183
	ds_read_b128 v[10:13], v190
	ds_read_b128 v[14:17], v191
	s_add_i32 s84, s28, 0x80
	s_cmp_eq_u32 s67, s83
	s_cselect_b32 s86, s25, s84
	s_cselect_b32 s87, s29, s82
	s_add_i32 s84, s86, 0x80
	s_add_i32 s85, s87, 0x80
	v_mov_b32_e32 v172, v176
	ds_read_b128 v[164:167], v196
	ds_read_b128 v[168:171], v196 offset:1024
	ds_read_b128 v[198:201], v196 offset:2048
	ds_read_b128 v[202:205], v196 offset:3072
	ds_read_b128 v[214:217], v196 offset:4096
	ds_read_b128 v[218:221], v196 offset:5120
	ds_read_b128 v[222:225], v196 offset:6144
	ds_read_b128 v[226:229], v196 offset:7168
	s_add_i32 s88, s28, s65
	v_add_u32_e32 v172, s88, v172
	s_add_i32 m0, s49, 0xc000
	s_add_i32 s88, s28, s70
	global_load_lds_dwordx4 v172, s[4:5]
	v_mov_b32_e32 v172, v176
	s_add_i32 m0, s49, 0xe000
	v_add_u32_e32 v172, s88, v172
	global_load_lds_dwordx4 v172, s[4:5]
	s_waitcnt vmcnt(8)
	s_waitcnt lgkmcnt(0)
	s_barrier
	s_setprio 1
	s_waitcnt lgkmcnt(0)
	v_mfma_f32_16x16x128_f8f6f4 v[158:161], v[18:25], v[164:171], 0
	v_mfma_f32_16x16x128_f8f6f4 v[154:157], v[26:33], v[164:171], 0
	v_mfma_f32_16x16x128_f8f6f4 v[150:153], v[18:25], v[198:205], 0
	v_mfma_f32_16x16x128_f8f6f4 v[146:149], v[26:33], v[198:205], 0
	v_mfma_f32_16x16x128_f8f6f4 v[138:141], v[18:25], v[214:221], 0
	v_mfma_f32_16x16x128_f8f6f4 v[130:133], v[26:33], v[214:221], 0
	v_mfma_f32_16x16x128_f8f6f4 v[122:125], v[18:25], v[222:229], 0
	v_mfma_f32_16x16x128_f8f6f4 v[114:117], v[26:33], v[222:229], 0
	v_mfma_f32_16x16x128_f8f6f4 v[142:145], v[2:9], v[164:171], 0
	v_mfma_f32_16x16x128_f8f6f4 v[134:137], v[10:17], v[164:171], 0
	v_mfma_f32_16x16x128_f8f6f4 v[126:129], v[2:9], v[198:205], 0
	v_mfma_f32_16x16x128_f8f6f4 v[118:121], v[10:17], v[198:205], 0
	v_mfma_f32_16x16x128_f8f6f4 v[110:113], v[2:9], v[214:221], 0
	v_mfma_f32_16x16x128_f8f6f4 v[106:109], v[10:17], v[214:221], 0
	v_mfma_f32_16x16x128_f8f6f4 v[102:105], v[2:9], v[222:229], 0
	v_mfma_f32_16x16x128_f8f6f4 v[98:101], v[10:17], v[222:229], 0
	s_setprio 0
	s_barrier
	v_mov_b32_e32 v172, v177
	ds_read_b128 v[164:167], v196 offset:16384
	ds_read_b128 v[168:171], v196 offset:17408
	ds_read_b128 v[198:201], v196 offset:18432
	ds_read_b128 v[202:205], v196 offset:19456
	ds_read_b128 v[214:217], v196 offset:20480
	ds_read_b128 v[218:221], v196 offset:21504
	ds_read_b128 v[222:225], v196 offset:22528
	ds_read_b128 v[226:229], v196 offset:23552
	s_mov_b32 m0, s50
	v_add_u32_e32 v172, s87, v172
	global_load_lds_dwordx4 v172, s[6:7]
	v_mov_b32_e32 v172, v177
	s_add_i32 s87, s87, s48
	v_add_u32_e32 v172, s87, v172
	s_mov_b32 m0, s51
	s_add_i32 s87, s87, s48
	global_load_lds_dwordx4 v172, s[6:7]
	v_mov_b32_e32 v172, v177
	s_mov_b32 m0, s52
	v_add_u32_e32 v172, s87, v172
	global_load_lds_dwordx4 v172, s[6:7]
	v_mov_b32_e32 v172, v177
	s_add_i32 s87, s87, s48
	v_add_u32_e32 v172, s87, v172
	s_mov_b32 m0, s53
	s_nop 0
	global_load_lds_dwordx4 v172, s[6:7]
	v_mov_b32_e32 v172, v176
	s_mov_b32 m0, s49
	v_add_u32_e32 v172, s86, v172
	global_load_lds_dwordx4 v172, s[4:5]
	v_mov_b32_e32 v172, v176
	s_add_i32 s86, s86, s47
	v_add_u32_e32 v172, s86, v172
	s_mov_b32 m0, s54
	s_nop 0
	global_load_lds_dwordx4 v172, s[4:5]
	s_waitcnt vmcnt(8)
	s_waitcnt lgkmcnt(0)
	s_barrier
	s_setprio 1
	s_waitcnt lgkmcnt(0)
	v_mfma_f32_16x16x128_f8f6f4 v[94:97], v[18:25], v[164:171], 0
	v_mfma_f32_16x16x128_f8f6f4 v[90:93], v[26:33], v[164:171], 0
	v_mfma_f32_16x16x128_f8f6f4 v[86:89], v[18:25], v[198:205], 0
	v_mfma_f32_16x16x128_f8f6f4 v[82:85], v[26:33], v[198:205], 0
	v_mfma_f32_16x16x128_f8f6f4 v[74:77], v[18:25], v[214:221], 0
	v_mfma_f32_16x16x128_f8f6f4 v[66:69], v[26:33], v[214:221], 0
	v_mfma_f32_16x16x128_f8f6f4 v[58:61], v[18:25], v[222:229], 0
	v_mfma_f32_16x16x128_f8f6f4 v[50:53], v[26:33], v[222:229], 0
	v_mfma_f32_16x16x128_f8f6f4 v[78:81], v[2:9], v[164:171], 0
	v_mfma_f32_16x16x128_f8f6f4 v[70:73], v[10:17], v[164:171], 0
	v_mfma_f32_16x16x128_f8f6f4 v[62:65], v[2:9], v[198:205], 0
	v_mfma_f32_16x16x128_f8f6f4 v[54:57], v[10:17], v[198:205], 0
	v_mfma_f32_16x16x128_f8f6f4 v[46:49], v[2:9], v[214:221], 0
	v_mfma_f32_16x16x128_f8f6f4 v[42:45], v[10:17], v[214:221], 0
	v_mfma_f32_16x16x128_f8f6f4 v[38:41], v[2:9], v[222:229], 0
	v_mfma_f32_16x16x128_f8f6f4 v[34:37], v[10:17], v[222:229], 0
	s_setprio 0
	s_barrier
	s_branch .Lmid_10
.LBB0_2937:
	ds_read_b128 v[18:21], v180
	ds_read_b128 v[22:25], v181
	ds_read_b128 v[26:29], v188
	ds_read_b128 v[30:33], v189
	ds_read_b128 v[2:5], v182
	ds_read_b128 v[6:9], v183
	ds_read_b128 v[10:13], v190
	ds_read_b128 v[14:17], v191
	s_add_i32 s84, s28, 0x80
	s_cmp_eq_u32 s67, s83
	s_cselect_b32 s86, s25, s84
	s_cselect_b32 s87, s29, s82
	s_add_i32 s84, s86, 0x80
	s_add_i32 s85, s87, 0x80
	v_mov_b32_e32 v172, v176
	ds_read_b128 v[164:167], v196
	ds_read_b128 v[168:171], v196 offset:1024
	ds_read_b128 v[198:201], v196 offset:2048
	ds_read_b128 v[202:205], v196 offset:3072
	ds_read_b128 v[214:217], v196 offset:4096
	ds_read_b128 v[218:221], v196 offset:5120
	ds_read_b128 v[222:225], v196 offset:6144
	ds_read_b128 v[226:229], v196 offset:7168
	s_add_i32 s88, s28, s65
	v_add_u32_e32 v172, s88, v172
	s_add_i32 m0, s49, 0xc000
	s_add_i32 s88, s28, s70
	global_load_lds_dwordx4 v172, s[4:5]
	v_mov_b32_e32 v172, v176
	s_add_i32 m0, s49, 0xe000
	v_add_u32_e32 v172, s88, v172
	global_load_lds_dwordx4 v172, s[4:5]
	s_waitcnt vmcnt(8)
	s_waitcnt lgkmcnt(0)
	s_barrier
	s_setprio 1
	s_waitcnt lgkmcnt(0)
	v_mfma_f32_16x16x128_f8f6f4 v[158:161], v[18:25], v[164:171], v[158:161]
	v_mfma_f32_16x16x128_f8f6f4 v[154:157], v[26:33], v[164:171], v[154:157]
	v_mfma_f32_16x16x128_f8f6f4 v[150:153], v[18:25], v[198:205], v[150:153]
	v_mfma_f32_16x16x128_f8f6f4 v[146:149], v[26:33], v[198:205], v[146:149]
	v_mfma_f32_16x16x128_f8f6f4 v[138:141], v[18:25], v[214:221], v[138:141]
	v_mfma_f32_16x16x128_f8f6f4 v[130:133], v[26:33], v[214:221], v[130:133]
	v_mfma_f32_16x16x128_f8f6f4 v[122:125], v[18:25], v[222:229], v[122:125]
	v_mfma_f32_16x16x128_f8f6f4 v[114:117], v[26:33], v[222:229], v[114:117]
	v_mfma_f32_16x16x128_f8f6f4 v[142:145], v[2:9], v[164:171], v[142:145]
	v_mfma_f32_16x16x128_f8f6f4 v[134:137], v[10:17], v[164:171], v[134:137]
	v_mfma_f32_16x16x128_f8f6f4 v[126:129], v[2:9], v[198:205], v[126:129]
	v_mfma_f32_16x16x128_f8f6f4 v[118:121], v[10:17], v[198:205], v[118:121]
	v_mfma_f32_16x16x128_f8f6f4 v[110:113], v[2:9], v[214:221], v[110:113]
	v_mfma_f32_16x16x128_f8f6f4 v[106:109], v[10:17], v[214:221], v[106:109]
	v_mfma_f32_16x16x128_f8f6f4 v[102:105], v[2:9], v[222:229], v[102:105]
	v_mfma_f32_16x16x128_f8f6f4 v[98:101], v[10:17], v[222:229], v[98:101]
	s_setprio 0
	s_barrier
	v_mov_b32_e32 v172, v177
	ds_read_b128 v[164:167], v196 offset:16384
	ds_read_b128 v[168:171], v196 offset:17408
	ds_read_b128 v[198:201], v196 offset:18432
	ds_read_b128 v[202:205], v196 offset:19456
	ds_read_b128 v[214:217], v196 offset:20480
	ds_read_b128 v[218:221], v196 offset:21504
	ds_read_b128 v[222:225], v196 offset:22528
	ds_read_b128 v[226:229], v196 offset:23552
	s_mov_b32 m0, s50
	v_add_u32_e32 v172, s87, v172
	global_load_lds_dwordx4 v172, s[6:7]
	v_mov_b32_e32 v172, v177
	s_add_i32 s87, s87, s48
	v_add_u32_e32 v172, s87, v172
	s_mov_b32 m0, s51
	s_add_i32 s87, s87, s48
	global_load_lds_dwordx4 v172, s[6:7]
	v_mov_b32_e32 v172, v177
	s_mov_b32 m0, s52
	v_add_u32_e32 v172, s87, v172
	global_load_lds_dwordx4 v172, s[6:7]
	v_mov_b32_e32 v172, v177
	s_add_i32 s87, s87, s48
	v_add_u32_e32 v172, s87, v172
	s_mov_b32 m0, s53
	s_nop 0
	global_load_lds_dwordx4 v172, s[6:7]
	v_mov_b32_e32 v172, v176
	s_mov_b32 m0, s49
	v_add_u32_e32 v172, s86, v172
	global_load_lds_dwordx4 v172, s[4:5]
	v_mov_b32_e32 v172, v176
	s_add_i32 s86, s86, s47
	v_add_u32_e32 v172, s86, v172
	s_mov_b32 m0, s54
	s_nop 0
	global_load_lds_dwordx4 v172, s[4:5]
	s_waitcnt vmcnt(8)
	s_waitcnt lgkmcnt(0)
	s_barrier
	s_setprio 1
	s_waitcnt lgkmcnt(0)
	v_mfma_f32_16x16x128_f8f6f4 v[94:97], v[18:25], v[164:171], v[94:97]
	v_mfma_f32_16x16x128_f8f6f4 v[90:93], v[26:33], v[164:171], v[90:93]
	v_mfma_f32_16x16x128_f8f6f4 v[86:89], v[18:25], v[198:205], v[86:89]
	v_mfma_f32_16x16x128_f8f6f4 v[82:85], v[26:33], v[198:205], v[82:85]
	v_mfma_f32_16x16x128_f8f6f4 v[74:77], v[18:25], v[214:221], v[74:77]
	v_mfma_f32_16x16x128_f8f6f4 v[66:69], v[26:33], v[214:221], v[66:69]
	v_mfma_f32_16x16x128_f8f6f4 v[58:61], v[18:25], v[222:229], v[58:61]
	v_mfma_f32_16x16x128_f8f6f4 v[50:53], v[26:33], v[222:229], v[50:53]
	v_mfma_f32_16x16x128_f8f6f4 v[78:81], v[2:9], v[164:171], v[78:81]
	v_mfma_f32_16x16x128_f8f6f4 v[70:73], v[10:17], v[164:171], v[70:73]
	v_mfma_f32_16x16x128_f8f6f4 v[62:65], v[2:9], v[198:205], v[62:65]
	v_mfma_f32_16x16x128_f8f6f4 v[54:57], v[10:17], v[198:205], v[54:57]
	v_mfma_f32_16x16x128_f8f6f4 v[46:49], v[2:9], v[214:221], v[46:49]
	v_mfma_f32_16x16x128_f8f6f4 v[42:45], v[10:17], v[214:221], v[42:45]
	v_mfma_f32_16x16x128_f8f6f4 v[38:41], v[2:9], v[222:229], v[38:41]
	v_mfma_f32_16x16x128_f8f6f4 v[34:37], v[10:17], v[222:229], v[34:37]
	s_setprio 0
	s_barrier

.Ltx23_skip:
	ds_read_b128 v[2:5], v184
	ds_read_b128 v[6:9], v185
	ds_read_b128 v[10:13], v192
	ds_read_b128 v[14:17], v193
	ds_read_b128 v[18:21], v186
	ds_read_b128 v[22:25], v187
	ds_read_b128 v[26:29], v194
	ds_read_b128 v[30:33], v195
	v_mov_b32_e32 v172, v176
	ds_read_b128 v[164:167], v196 offset:32768
	ds_read_b128 v[168:171], v196 offset:33792
	ds_read_b128 v[198:201], v196 offset:34816
	ds_read_b128 v[202:205], v196 offset:35840
	ds_read_b128 v[214:217], v196 offset:36864
	ds_read_b128 v[218:221], v196 offset:37888
	ds_read_b128 v[222:225], v196 offset:38912
	ds_read_b128 v[226:229], v196 offset:39936
	s_add_i32 s86, s86, s47
	s_mov_b32 m0, s55
	v_add_u32_e32 v172, s86, v172
	global_load_lds_dwordx4 v172, s[4:5]
	v_mov_b32_e32 v172, v176
	s_add_i32 s86, s86, s47
	v_add_u32_e32 v172, s86, v172
	s_mov_b32 m0, s56
	s_nop 0
	global_load_lds_dwordx4 v172, s[4:5]
	s_waitcnt vmcnt(8)
	s_waitcnt lgkmcnt(0)
	s_barrier
	s_setprio 1
	s_waitcnt lgkmcnt(0)
	v_mfma_f32_16x16x128_f8f6f4 v[158:161], v[2:9], v[164:171], v[158:161]
	v_mfma_f32_16x16x128_f8f6f4 v[154:157], v[10:17], v[164:171], v[154:157]
	v_mfma_f32_16x16x128_f8f6f4 v[150:153], v[2:9], v[198:205], v[150:153]
	v_mfma_f32_16x16x128_f8f6f4 v[146:149], v[10:17], v[198:205], v[146:149]
	v_mfma_f32_16x16x128_f8f6f4 v[138:141], v[2:9], v[214:221], v[138:141]
	v_mfma_f32_16x16x128_f8f6f4 v[130:133], v[10:17], v[214:221], v[130:133]
	v_mfma_f32_16x16x128_f8f6f4 v[122:125], v[2:9], v[222:229], v[122:125]
	v_mfma_f32_16x16x128_f8f6f4 v[114:117], v[10:17], v[222:229], v[114:117]
	v_mfma_f32_16x16x128_f8f6f4 v[142:145], v[18:25], v[164:171], v[142:145]
	v_mfma_f32_16x16x128_f8f6f4 v[134:137], v[26:33], v[164:171], v[134:137]
	v_mfma_f32_16x16x128_f8f6f4 v[126:129], v[18:25], v[198:205], v[126:129]
	v_mfma_f32_16x16x128_f8f6f4 v[118:121], v[26:33], v[198:205], v[118:121]
	v_mfma_f32_16x16x128_f8f6f4 v[110:113], v[18:25], v[214:221], v[110:113]
	v_mfma_f32_16x16x128_f8f6f4 v[106:109], v[26:33], v[214:221], v[106:109]
	v_mfma_f32_16x16x128_f8f6f4 v[102:105], v[18:25], v[222:229], v[102:105]
	v_mfma_f32_16x16x128_f8f6f4 v[98:101], v[26:33], v[222:229], v[98:101]
	s_setprio 0
	s_barrier
	s_cmp_eq_u32 s67, s83
	s_cbranch_scc1 .Lh23_last
	v_mov_b32_e32 v172, v177
	ds_read_b128 v[164:167], v196 offset:49152
	ds_read_b128 v[168:171], v196 offset:50176
	ds_read_b128 v[198:201], v196 offset:51200
	ds_read_b128 v[202:205], v196 offset:52224
	ds_read_b128 v[214:217], v196 offset:53248
	ds_read_b128 v[218:221], v196 offset:54272
	ds_read_b128 v[222:225], v196 offset:55296
	ds_read_b128 v[226:229], v196 offset:56320
	s_mov_b32 m0, s58
	v_add_u32_e32 v172, s85, v172
	global_load_lds_dwordx4 v172, s[6:7]
	v_mov_b32_e32 v172, v177
	s_add_i32 s85, s85, s48
	v_add_u32_e32 v172, s85, v172
	s_mov_b32 m0, s59
	s_add_i32 s85, s85, s48
	global_load_lds_dwordx4 v172, s[6:7]
	v_mov_b32_e32 v172, v177
	s_mov_b32 m0, s62
	v_add_u32_e32 v172, s85, v172
	global_load_lds_dwordx4 v172, s[6:7]
	v_mov_b32_e32 v172, v177
	s_add_i32 s85, s85, s48
	v_add_u32_e32 v172, s85, v172
	s_mov_b32 m0, s63
	s_nop 0
	global_load_lds_dwordx4 v172, s[6:7]
	v_mov_b32_e32 v172, v176
	s_mov_b32 m0, s60
	v_add_u32_e32 v172, s84, v172
	global_load_lds_dwordx4 v172, s[4:5]
	v_mov_b32_e32 v172, v176
	s_add_i32 s84, s84, s47
	v_add_u32_e32 v172, s84, v172
	s_mov_b32 m0, s61
	s_nop 0
	global_load_lds_dwordx4 v172, s[4:5]
	s_waitcnt vmcnt(8)
	s_waitcnt lgkmcnt(0)
	s_barrier
	s_setprio 1
	s_waitcnt lgkmcnt(0)
	v_mfma_f32_16x16x128_f8f6f4 v[94:97], v[2:9], v[164:171], v[94:97]
	v_mfma_f32_16x16x128_f8f6f4 v[90:93], v[10:17], v[164:171], v[90:93]
	v_mfma_f32_16x16x128_f8f6f4 v[86:89], v[2:9], v[198:205], v[86:89]
	v_mfma_f32_16x16x128_f8f6f4 v[82:85], v[10:17], v[198:205], v[82:85]
	v_mfma_f32_16x16x128_f8f6f4 v[74:77], v[2:9], v[214:221], v[74:77]
	v_mfma_f32_16x16x128_f8f6f4 v[66:69], v[10:17], v[214:221], v[66:69]
	v_mfma_f32_16x16x128_f8f6f4 v[58:61], v[2:9], v[222:229], v[58:61]
	v_mfma_f32_16x16x128_f8f6f4 v[50:53], v[10:17], v[222:229], v[50:53]
	v_mfma_f32_16x16x128_f8f6f4 v[78:81], v[18:25], v[164:171], v[78:81]
	v_mfma_f32_16x16x128_f8f6f4 v[70:73], v[26:33], v[164:171], v[70:73]
	v_mfma_f32_16x16x128_f8f6f4 v[62:65], v[18:25], v[198:205], v[62:65]
	v_mfma_f32_16x16x128_f8f6f4 v[54:57], v[26:33], v[198:205], v[54:57]
	v_mfma_f32_16x16x128_f8f6f4 v[46:49], v[18:25], v[214:221], v[46:49]
	v_mfma_f32_16x16x128_f8f6f4 v[42:45], v[26:33], v[214:221], v[42:45]
	v_mfma_f32_16x16x128_f8f6f4 v[38:41], v[18:25], v[222:229], v[38:41]
	v_mfma_f32_16x16x128_f8f6f4 v[34:37], v[26:33], v[222:229], v[34:37]
	s_setprio 0
	s_barrier
	s_add_i32 s83, s83, 2
	s_addk_i32 s28, 0x100
	s_addk_i32 s82, 0x100
	s_cmp_ge_i32 s83, s64
	s_cbranch_scc0 .LBB0_2937
	s_branch .LBB0_2939
.Lh23_last:
	v_mov_b32_e32 v172, v177
	ds_read_b128 v[164:167], v196 offset:49152
	ds_read_b128 v[168:171], v196 offset:50176
	ds_read_b128 v[198:201], v196 offset:51200
	ds_read_b128 v[202:205], v196 offset:52224
	ds_read_b128 v[214:217], v196 offset:53248
	ds_read_b128 v[218:221], v196 offset:54272
	ds_read_b128 v[222:225], v196 offset:55296
	ds_read_b128 v[226:229], v196 offset:56320
	s_mov_b32 m0, s58
	v_add_u32_e32 v172, s85, v172
	global_load_lds_dwordx4 v172, s[6:7]
	v_mov_b32_e32 v172, v177
	s_add_i32 s85, s85, s48
	v_add_u32_e32 v172, s85, v172
	s_mov_b32 m0, s59
	s_add_i32 s85, s85, s48
	global_load_lds_dwordx4 v172, s[6:7]
	v_mov_b32_e32 v172, v177
	s_mov_b32 m0, s62
	v_add_u32_e32 v172, s85, v172
	global_load_lds_dwordx4 v172, s[6:7]
	v_mov_b32_e32 v172, v177
	s_add_i32 s85, s85, s48
	v_add_u32_e32 v172, s85, v172
	s_mov_b32 m0, s63
	s_nop 0
	global_load_lds_dwordx4 v172, s[6:7]
	v_mov_b32_e32 v172, v176
	s_mov_b32 m0, s60
	v_add_u32_e32 v172, s84, v172
	global_load_lds_dwordx4 v172, s[4:5]
	v_mov_b32_e32 v172, v176
	s_add_i32 s84, s84, s47
	v_add_u32_e32 v172, s84, v172
	s_mov_b32 m0, s61
	s_nop 0
	global_load_lds_dwordx4 v172, s[4:5]
	s_mul_hi_i32 s25, s81, 0x2e8ba2e9
	s_lshr_b32 s28, s25, 31
	s_lshr_b32 s25, s25, 3
	s_add_i32 s25, s25, s28
	s_mul_i32 s25, s25, 44
	s_sub_i32 s25, s81, s25
	s_lshl_b32 s28, s25, 7
	s_lshl_b32 s24, s24, 8
	s_add_i32 s24, s24, s66
	s_mul_i32 s24, s24, s71
	s_add_i32 s24, s24, s28
	s_add_i32 s24, s24, s8
	s_add_u32 s100, s12, s24
	s_addc_u32 s101, s13, 0
	s_mov_b32 s98, 0xbfb8aa3b
	v_mul_u32_u24_e32 v206, s71, v178
	v_lshl_add_u32 v206, v179, 3, v206
	v_pk_fma_f32 v[158:159], v[158:159], s[18:19], 0 op_sel_hi:[1,0,0]
	v_pk_fma_f32 v[160:161], v[160:161], s[18:19], 0 op_sel_hi:[1,0,0]
	v_pk_fma_f32 v[154:155], v[154:155], s[18:19], 0 op_sel_hi:[1,0,0]
	v_pk_fma_f32 v[156:157], v[156:157], s[18:19], 0 op_sel_hi:[1,0,0]
	v_pk_fma_f32 v[142:143], v[142:143], s[20:21], 0 op_sel_hi:[1,0,0]
	v_pk_fma_f32 v[144:145], v[144:145], s[20:21], 0 op_sel_hi:[1,0,0]
	v_pk_fma_f32 v[134:135], v[134:135], s[20:21], 0 op_sel_hi:[1,0,0]
	v_pk_fma_f32 v[136:137], v[136:137], s[20:21], 0 op_sel_hi:[1,0,0]
	v_pk_fma_f32 v[150:151], v[150:151], s[18:19], 0 op_sel_hi:[1,0,0]
	v_pk_fma_f32 v[152:153], v[152:153], s[18:19], 0 op_sel_hi:[1,0,0]
	v_pk_fma_f32 v[146:147], v[146:147], s[18:19], 0 op_sel_hi:[1,0,0]
	v_pk_fma_f32 v[148:149], v[148:149], s[18:19], 0 op_sel_hi:[1,0,0]
	v_pk_fma_f32 v[126:127], v[126:127], s[20:21], 0 op_sel_hi:[1,0,0]
	v_pk_fma_f32 v[128:129], v[128:129], s[20:21], 0 op_sel_hi:[1,0,0]
	v_pk_fma_f32 v[118:119], v[118:119], s[20:21], 0 op_sel_hi:[1,0,0]
	v_pk_fma_f32 v[120:121], v[120:121], s[20:21], 0 op_sel_hi:[1,0,0]
	v_pk_mul_f32 v[230:231], v[158:159], s[98:99] op_sel_hi:[1,0]
	v_pk_mul_f32 v[232:233], v[160:161], s[98:99] op_sel_hi:[1,0]
	v_pk_mul_f32 v[234:235], v[154:155], s[98:99] op_sel_hi:[1,0]
	v_pk_mul_f32 v[236:237], v[156:157], s[98:99] op_sel_hi:[1,0]
	v_pk_mul_f32 v[238:239], v[150:151], s[98:99] op_sel_hi:[1,0]
	v_pk_mul_f32 v[240:241], v[152:153], s[98:99] op_sel_hi:[1,0]
	v_pk_mul_f32 v[242:243], v[146:147], s[98:99] op_sel_hi:[1,0]
	v_pk_mul_f32 v[244:245], v[148:149], s[98:99] op_sel_hi:[1,0]
	v_exp_f32_e32 v230, v230
	v_exp_f32_e32 v231, v231
	v_exp_f32_e32 v232, v232
	v_exp_f32_e32 v233, v233
	v_exp_f32_e32 v234, v234
	v_exp_f32_e32 v235, v235
	v_exp_f32_e32 v236, v236
	v_exp_f32_e32 v237, v237
	v_exp_f32_e32 v238, v238
	v_exp_f32_e32 v239, v239
	v_exp_f32_e32 v240, v240
	v_exp_f32_e32 v241, v241
	v_exp_f32_e32 v242, v242
	v_exp_f32_e32 v243, v243
	v_exp_f32_e32 v244, v244
	v_exp_f32_e32 v245, v245
	v_pk_add_f32 v[230:231], v[230:231], 1.0 op_sel_hi:[1,0]
	v_pk_add_f32 v[232:233], v[232:233], 1.0 op_sel_hi:[1,0]
	v_pk_add_f32 v[234:235], v[234:235], 1.0 op_sel_hi:[1,0]
	v_pk_add_f32 v[236:237], v[236:237], 1.0 op_sel_hi:[1,0]
	v_pk_add_f32 v[238:239], v[238:239], 1.0 op_sel_hi:[1,0]
	v_pk_add_f32 v[240:241], v[240:241], 1.0 op_sel_hi:[1,0]
	v_pk_add_f32 v[242:243], v[242:243], 1.0 op_sel_hi:[1,0]
	v_pk_add_f32 v[244:245], v[244:245], 1.0 op_sel_hi:[1,0]
	v_rcp_f32_e32 v230, v230
	v_rcp_f32_e32 v231, v231
	v_rcp_f32_e32 v232, v232
	v_rcp_f32_e32 v233, v233
	v_rcp_f32_e32 v234, v234
	v_rcp_f32_e32 v235, v235
	v_rcp_f32_e32 v236, v236
	v_rcp_f32_e32 v237, v237
	v_rcp_f32_e32 v238, v238
	v_rcp_f32_e32 v239, v239
	v_rcp_f32_e32 v240, v240
	v_rcp_f32_e32 v241, v241
	v_rcp_f32_e32 v242, v242
	v_rcp_f32_e32 v243, v243
	v_rcp_f32_e32 v244, v244
	v_rcp_f32_e32 v245, v245
	v_pk_mul_f32 v[230:231], v[158:159], v[230:231]
	v_pk_mul_f32 v[232:233], v[160:161], v[232:233]
	v_pk_mul_f32 v[234:235], v[154:155], v[234:235]
	v_pk_mul_f32 v[236:237], v[156:157], v[236:237]
	v_pk_mul_f32 v[238:239], v[150:151], v[238:239]
	v_pk_mul_f32 v[240:241], v[152:153], v[240:241]
	v_pk_mul_f32 v[242:243], v[146:147], v[242:243]
	v_pk_mul_f32 v[244:245], v[148:149], v[244:245]
	v_pk_mul_f32 v[142:143], v[142:143], v[230:231]
	v_pk_mul_f32 v[144:145], v[144:145], v[232:233]
	v_pk_mul_f32 v[134:135], v[134:135], v[234:235]
	v_pk_mul_f32 v[136:137], v[136:137], v[236:237]
	v_pk_mul_f32 v[126:127], v[126:127], v[238:239]
	v_pk_mul_f32 v[128:129], v[128:129], v[240:241]
	v_pk_mul_f32 v[118:119], v[118:119], v[242:243]
	v_pk_mul_f32 v[120:121], v[120:121], v[244:245]
	v_med3_f32 v142, v142, s72, v197
	v_med3_f32 v143, v143, s72, v197
	v_med3_f32 v144, v144, s72, v197
	v_med3_f32 v145, v145, s72, v197
	v_med3_f32 v134, v134, s72, v197
	v_med3_f32 v135, v135, s72, v197
	v_med3_f32 v136, v136, s72, v197
	v_med3_f32 v137, v137, s72, v197
	v_med3_f32 v126, v126, s72, v197
	v_med3_f32 v127, v127, s72, v197
	v_med3_f32 v128, v128, s72, v197
	v_med3_f32 v129, v129, s72, v197
	v_med3_f32 v118, v118, s72, v197
	v_med3_f32 v119, v119, s72, v197
	v_med3_f32 v120, v120, s72, v197
	v_med3_f32 v121, v121, s72, v197
	v_cvt_pk_fp8_f32 v246, v142, v143
	v_cvt_pk_fp8_f32 v247, v134, v135
	v_cvt_pk_fp8_f32 v248, v126, v127
	v_cvt_pk_fp8_f32 v249, v118, v119
	v_add_u32_e32 v208, s57, v206
	v_cvt_pk_fp8_f32 v246, v144, v145 op_sel:[0,0,1]
	v_cvt_pk_fp8_f32 v247, v136, v137 op_sel:[0,0,1]
	v_cvt_pk_fp8_f32 v248, v128, v129 op_sel:[0,0,1]
	v_cvt_pk_fp8_f32 v249, v120, v121 op_sel:[0,0,1]
	s_nop 1
	global_store_dwordx2 v206, v[246:247], s[100:101]
	global_store_dwordx2 v208, v[248:249], s[100:101]
	s_waitcnt vmcnt(10)
	s_waitcnt lgkmcnt(0)
	s_barrier
	s_setprio 1
	s_waitcnt lgkmcnt(0)
	v_mfma_f32_16x16x128_f8f6f4 v[94:97], v[2:9], v[164:171], v[94:97]
	v_pk_fma_f32 v[138:139], v[138:139], s[18:19], 0 op_sel_hi:[1,0,0]
	v_pk_fma_f32 v[140:141], v[140:141], s[18:19], 0 op_sel_hi:[1,0,0]
	v_pk_fma_f32 v[130:131], v[130:131], s[18:19], 0 op_sel_hi:[1,0,0]
	v_pk_fma_f32 v[132:133], v[132:133], s[18:19], 0 op_sel_hi:[1,0,0]
	v_pk_fma_f32 v[110:111], v[110:111], s[20:21], 0 op_sel_hi:[1,0,0]
	v_pk_fma_f32 v[112:113], v[112:113], s[20:21], 0 op_sel_hi:[1,0,0]
	v_pk_fma_f32 v[106:107], v[106:107], s[20:21], 0 op_sel_hi:[1,0,0]
	v_mfma_f32_16x16x128_f8f6f4 v[90:93], v[10:17], v[164:171], v[90:93]
	v_pk_fma_f32 v[108:109], v[108:109], s[20:21], 0 op_sel_hi:[1,0,0]
	v_pk_fma_f32 v[122:123], v[122:123], s[18:19], 0 op_sel_hi:[1,0,0]
	v_pk_fma_f32 v[124:125], v[124:125], s[18:19], 0 op_sel_hi:[1,0,0]
	v_pk_fma_f32 v[114:115], v[114:115], s[18:19], 0 op_sel_hi:[1,0,0]
	v_pk_fma_f32 v[116:117], v[116:117], s[18:19], 0 op_sel_hi:[1,0,0]
	v_pk_fma_f32 v[102:103], v[102:103], s[20:21], 0 op_sel_hi:[1,0,0]
	v_pk_fma_f32 v[104:105], v[104:105], s[20:21], 0 op_sel_hi:[1,0,0]
	v_mfma_f32_16x16x128_f8f6f4 v[86:89], v[2:9], v[198:205], v[86:89]
	v_pk_fma_f32 v[98:99], v[98:99], s[20:21], 0 op_sel_hi:[1,0,0]
	v_pk_fma_f32 v[100:101], v[100:101], s[20:21], 0 op_sel_hi:[1,0,0]
	v_pk_mul_f32 v[230:231], v[138:139], s[98:99] op_sel_hi:[1,0]
	v_pk_mul_f32 v[232:233], v[140:141], s[98:99] op_sel_hi:[1,0]
	v_pk_mul_f32 v[234:235], v[130:131], s[98:99] op_sel_hi:[1,0]
	v_pk_mul_f32 v[236:237], v[132:133], s[98:99] op_sel_hi:[1,0]
	v_pk_mul_f32 v[238:239], v[122:123], s[98:99] op_sel_hi:[1,0]
	v_mfma_f32_16x16x128_f8f6f4 v[82:85], v[10:17], v[198:205], v[82:85]
	v_pk_mul_f32 v[240:241], v[124:125], s[98:99] op_sel_hi:[1,0]
	v_pk_mul_f32 v[242:243], v[114:115], s[98:99] op_sel_hi:[1,0]
	v_pk_mul_f32 v[244:245], v[116:117], s[98:99] op_sel_hi:[1,0]
	v_exp_f32_e32 v230, v230
	v_exp_f32_e32 v231, v231
	v_exp_f32_e32 v232, v232
	v_exp_f32_e32 v233, v233
	v_mfma_f32_16x16x128_f8f6f4 v[74:77], v[2:9], v[214:221], v[74:77]
	v_exp_f32_e32 v234, v234
	v_exp_f32_e32 v235, v235
	v_exp_f32_e32 v236, v236
	v_exp_f32_e32 v237, v237
	v_exp_f32_e32 v238, v238
	v_exp_f32_e32 v239, v239
	v_exp_f32_e32 v240, v240
	v_mfma_f32_16x16x128_f8f6f4 v[66:69], v[10:17], v[214:221], v[66:69]
	v_exp_f32_e32 v241, v241
	v_exp_f32_e32 v242, v242
	v_exp_f32_e32 v243, v243
	v_exp_f32_e32 v244, v244
	v_exp_f32_e32 v245, v245
	v_pk_add_f32 v[230:231], v[230:231], 1.0 op_sel_hi:[1,0]
	v_pk_add_f32 v[232:233], v[232:233], 1.0 op_sel_hi:[1,0]
	v_mfma_f32_16x16x128_f8f6f4 v[58:61], v[2:9], v[222:229], v[58:61]
	v_pk_add_f32 v[234:235], v[234:235], 1.0 op_sel_hi:[1,0]
	v_pk_add_f32 v[236:237], v[236:237], 1.0 op_sel_hi:[1,0]
	v_pk_add_f32 v[238:239], v[238:239], 1.0 op_sel_hi:[1,0]
	v_pk_add_f32 v[240:241], v[240:241], 1.0 op_sel_hi:[1,0]
	v_pk_add_f32 v[242:243], v[242:243], 1.0 op_sel_hi:[1,0]
	v_pk_add_f32 v[244:245], v[244:245], 1.0 op_sel_hi:[1,0]
	v_rcp_f32_e32 v230, v230
	v_mfma_f32_16x16x128_f8f6f4 v[50:53], v[10:17], v[222:229], v[50:53]
	v_rcp_f32_e32 v231, v231
	v_rcp_f32_e32 v232, v232
	v_rcp_f32_e32 v233, v233
	v_rcp_f32_e32 v234, v234
	v_rcp_f32_e32 v235, v235
	v_rcp_f32_e32 v236, v236
	v_rcp_f32_e32 v237, v237
	v_mfma_f32_16x16x128_f8f6f4 v[78:81], v[18:25], v[164:171], v[78:81]
	v_rcp_f32_e32 v238, v238
	v_rcp_f32_e32 v239, v239
	v_rcp_f32_e32 v240, v240
	v_rcp_f32_e32 v241, v241
	v_rcp_f32_e32 v242, v242
	v_rcp_f32_e32 v243, v243
	v_rcp_f32_e32 v244, v244
	v_mfma_f32_16x16x128_f8f6f4 v[70:73], v[26:33], v[164:171], v[70:73]
	v_rcp_f32_e32 v245, v245
	v_pk_mul_f32 v[230:231], v[138:139], v[230:231]
	v_pk_mul_f32 v[232:233], v[140:141], v[232:233]
	v_pk_mul_f32 v[234:235], v[130:131], v[234:235]
	v_pk_mul_f32 v[236:237], v[132:133], v[236:237]
	v_pk_mul_f32 v[238:239], v[122:123], v[238:239]
	v_pk_mul_f32 v[240:241], v[124:125], v[240:241]
	v_mfma_f32_16x16x128_f8f6f4 v[62:65], v[18:25], v[198:205], v[62:65]
	v_pk_mul_f32 v[242:243], v[114:115], v[242:243]
	v_pk_mul_f32 v[244:245], v[116:117], v[244:245]
	v_pk_mul_f32 v[110:111], v[110:111], v[230:231]
	v_pk_mul_f32 v[112:113], v[112:113], v[232:233]
	v_pk_mul_f32 v[106:107], v[106:107], v[234:235]
	v_pk_mul_f32 v[108:109], v[108:109], v[236:237]
	v_pk_mul_f32 v[102:103], v[102:103], v[238:239]
	v_mfma_f32_16x16x128_f8f6f4 v[54:57], v[26:33], v[198:205], v[54:57]
	v_pk_mul_f32 v[104:105], v[104:105], v[240:241]
	v_pk_mul_f32 v[98:99], v[98:99], v[242:243]
	v_pk_mul_f32 v[100:101], v[100:101], v[244:245]
	v_med3_f32 v110, v110, s72, v197
	v_med3_f32 v111, v111, s72, v197
	v_med3_f32 v112, v112, s72, v197
	v_med3_f32 v113, v113, s72, v197
	v_mfma_f32_16x16x128_f8f6f4 v[46:49], v[18:25], v[214:221], v[46:49]
	v_med3_f32 v106, v106, s72, v197
	v_med3_f32 v107, v107, s72, v197
	v_med3_f32 v108, v108, s72, v197
	v_med3_f32 v109, v109, s72, v197
	v_med3_f32 v102, v102, s72, v197
	v_med3_f32 v103, v103, s72, v197
	v_med3_f32 v104, v104, s72, v197
	v_mfma_f32_16x16x128_f8f6f4 v[42:45], v[26:33], v[214:221], v[42:45]
	v_med3_f32 v105, v105, s72, v197
	v_med3_f32 v98, v98, s72, v197
	v_med3_f32 v99, v99, s72, v197
	v_med3_f32 v100, v100, s72, v197
	v_med3_f32 v101, v101, s72, v197
	v_cvt_pk_fp8_f32 v246, v110, v111
	v_cvt_pk_fp8_f32 v247, v106, v107
	v_mfma_f32_16x16x128_f8f6f4 v[38:41], v[18:25], v[222:229], v[38:41]
	v_cvt_pk_fp8_f32 v248, v102, v103
	v_cvt_pk_fp8_f32 v249, v98, v99
	v_add_u32_e32 v207, s73, v206
	v_add_u32_e32 v208, s74, v206
	v_cvt_pk_fp8_f32 v246, v112, v113 op_sel:[0,0,1]
	v_cvt_pk_fp8_f32 v247, v108, v109 op_sel:[0,0,1]
	v_cvt_pk_fp8_f32 v248, v104, v105 op_sel:[0,0,1]
	v_mfma_f32_16x16x128_f8f6f4 v[34:37], v[26:33], v[222:229], v[34:37]
	v_cvt_pk_fp8_f32 v249, v100, v101 op_sel:[0,0,1]
	s_nop 1
	global_store_dwordx2 v207, v[246:247], s[100:101]
	global_store_dwordx2 v208, v[248:249], s[100:101]
	s_setprio 0
	s_barrier
	s_and_b64 vcc, exec, s[16:17]
	s_cbranch_vccz .Lh23_nb
	s_barrier

.LBB0_3005:
	s_andn2_b64 vcc, exec, s[12:13]
	v_mov_b64_e32 v[2:3], 0
	v_mov_b64_e32 v[4:5], 0
	v_mov_b64_e32 v[6:7], 0
	v_mov_b64_e32 v[8:9], 0
	v_mov_b64_e32 v[10:11], 0
	v_mov_b64_e32 v[12:13], 0
	v_mov_b64_e32 v[14:15], 0
	v_mov_b64_e32 v[16:17], 0
	v_mov_b64_e32 v[18:19], 0
	v_mov_b64_e32 v[20:21], 0
	v_mov_b64_e32 v[22:23], 0
	v_mov_b64_e32 v[24:25], 0
	v_mov_b64_e32 v[26:27], 0
	v_mov_b64_e32 v[28:29], 0
	v_mov_b64_e32 v[30:31], 0
	v_mov_b64_e32 v[32:33], 0
	s_cbranch_vccnz .Lzs_13
	s_add_i32 s20, s74, 0x80
	s_add_i32 s74, s75, 0x100
	s_mov_b32 s75, 0
	ds_read_b128 v[18:21], v168
	ds_read_b128 v[22:25], v169
	ds_read_b128 v[26:29], v176
	ds_read_b128 v[30:33], v177
	ds_read_b128 v[2:5], v170
	ds_read_b128 v[6:9], v171
	ds_read_b128 v[10:13], v178
	ds_read_b128 v[14:17], v179
	s_add_i32 s76, s20, 0x80
	s_cmp_eq_u32 s61, s75
	s_cselect_b32 s78, s11, s76
	s_cselect_b32 s77, s21, s74
	s_add_i32 s76, s78, 0x80
	v_mov_b32_e32 v185, v164
	ds_read_b128 v[186:189], v184
	ds_read_b128 v[190:193], v184 offset:1024
	ds_read_b128 v[194:197], v184 offset:2048
	ds_read_b128 v[198:201], v184 offset:3072
	ds_read_b128 v[202:205], v184 offset:4096
	ds_read_b128 v[206:209], v184 offset:5120
	ds_read_b128 v[214:217], v184 offset:6144
	ds_read_b128 v[218:221], v184 offset:7168
	s_add_i32 s79, s20, s59
	v_add_u32_e32 v185, s79, v185
	s_add_i32 m0, s30, 0xc000
	s_add_i32 s79, s20, s66
	global_load_lds_dwordx4 v185, s[4:5]
	v_mov_b32_e32 v185, v164
	s_add_i32 m0, s30, 0xe000
	v_add_u32_e32 v185, s79, v185
	global_load_lds_dwordx4 v185, s[4:5]
	s_waitcnt vmcnt(8)
	s_waitcnt lgkmcnt(0)
	s_barrier
	s_setprio 1
	s_waitcnt lgkmcnt(0)
	v_mfma_f32_16x16x128_f8f6f4 v[158:161], v[18:25], v[186:193], 0
	v_mfma_f32_16x16x128_f8f6f4 v[154:157], v[26:33], v[186:193], 0
	v_mfma_f32_16x16x128_f8f6f4 v[150:153], v[18:25], v[194:201], 0
	v_mfma_f32_16x16x128_f8f6f4 v[146:149], v[26:33], v[194:201], 0
	v_mfma_f32_16x16x128_f8f6f4 v[138:141], v[18:25], v[202:209], 0
	v_mfma_f32_16x16x128_f8f6f4 v[130:133], v[26:33], v[202:209], 0
	v_mfma_f32_16x16x128_f8f6f4 v[122:125], v[18:25], v[214:221], 0
	v_mfma_f32_16x16x128_f8f6f4 v[114:117], v[26:33], v[214:221], 0
	v_mfma_f32_16x16x128_f8f6f4 v[142:145], v[2:9], v[186:193], 0
	v_mfma_f32_16x16x128_f8f6f4 v[134:137], v[10:17], v[186:193], 0
	v_mfma_f32_16x16x128_f8f6f4 v[126:129], v[2:9], v[194:201], 0
	v_mfma_f32_16x16x128_f8f6f4 v[118:121], v[10:17], v[194:201], 0
	v_mfma_f32_16x16x128_f8f6f4 v[110:113], v[2:9], v[202:209], 0
	v_mfma_f32_16x16x128_f8f6f4 v[106:109], v[10:17], v[202:209], 0
	v_mfma_f32_16x16x128_f8f6f4 v[102:105], v[2:9], v[214:221], 0
	v_mfma_f32_16x16x128_f8f6f4 v[98:101], v[10:17], v[214:221], 0
	s_setprio 0
	s_barrier
	v_mov_b32_e32 v185, v165
	ds_read_b128 v[186:189], v184 offset:16384
	ds_read_b128 v[190:193], v184 offset:17408
	ds_read_b128 v[194:197], v184 offset:18432
	ds_read_b128 v[198:201], v184 offset:19456
	ds_read_b128 v[202:205], v184 offset:20480
	ds_read_b128 v[206:209], v184 offset:21504
	ds_read_b128 v[214:217], v184 offset:22528
	ds_read_b128 v[218:221], v184 offset:23552
	s_mov_b32 m0, s31
	v_add_u32_e32 v185, s77, v185
	global_load_lds_dwordx4 v185, s[6:7]
	v_mov_b32_e32 v185, v165
	s_add_i32 s79, s77, s25
	v_add_u32_e32 v185, s79, v185
	s_mov_b32 m0, s35
	s_add_i32 s79, s79, s25
	global_load_lds_dwordx4 v185, s[6:7]
	v_mov_b32_e32 v185, v165
	s_mov_b32 m0, s44
	v_add_u32_e32 v185, s79, v185
	global_load_lds_dwordx4 v185, s[6:7]
	v_mov_b32_e32 v185, v165
	s_add_i32 s79, s79, s25
	v_add_u32_e32 v185, s79, v185
	s_mov_b32 m0, s45
	s_nop 0
	global_load_lds_dwordx4 v185, s[6:7]
	v_mov_b32_e32 v185, v164
	s_mov_b32 m0, s30
	v_add_u32_e32 v185, s78, v185
	global_load_lds_dwordx4 v185, s[4:5]
	v_mov_b32_e32 v185, v164
	s_add_i32 s78, s78, s24
	v_add_u32_e32 v185, s78, v185
	s_mov_b32 m0, s46
	s_nop 0
	global_load_lds_dwordx4 v185, s[4:5]
	s_waitcnt vmcnt(8)
	s_waitcnt lgkmcnt(0)
	s_barrier
	s_setprio 1
	s_waitcnt lgkmcnt(0)
	v_mfma_f32_16x16x128_f8f6f4 v[94:97], v[18:25], v[186:193], 0
	v_mfma_f32_16x16x128_f8f6f4 v[90:93], v[26:33], v[186:193], 0
	v_mfma_f32_16x16x128_f8f6f4 v[86:89], v[18:25], v[194:201], 0
	v_mfma_f32_16x16x128_f8f6f4 v[82:85], v[26:33], v[194:201], 0
	v_mfma_f32_16x16x128_f8f6f4 v[74:77], v[18:25], v[202:209], 0
	v_mfma_f32_16x16x128_f8f6f4 v[66:69], v[26:33], v[202:209], 0
	v_mfma_f32_16x16x128_f8f6f4 v[58:61], v[18:25], v[214:221], 0
	v_mfma_f32_16x16x128_f8f6f4 v[50:53], v[26:33], v[214:221], 0
	v_mfma_f32_16x16x128_f8f6f4 v[78:81], v[2:9], v[186:193], 0
	v_mfma_f32_16x16x128_f8f6f4 v[70:73], v[10:17], v[186:193], 0
	v_mfma_f32_16x16x128_f8f6f4 v[62:65], v[2:9], v[194:201], 0
	v_mfma_f32_16x16x128_f8f6f4 v[54:57], v[10:17], v[194:201], 0
	v_mfma_f32_16x16x128_f8f6f4 v[46:49], v[2:9], v[202:209], 0
	v_mfma_f32_16x16x128_f8f6f4 v[42:45], v[10:17], v[202:209], 0
	v_mfma_f32_16x16x128_f8f6f4 v[38:41], v[2:9], v[214:221], 0
	v_mfma_f32_16x16x128_f8f6f4 v[34:37], v[10:17], v[214:221], 0
	s_setprio 0
	s_barrier
	s_branch .Lmid_11
.LBB0_3007:
	ds_read_b128 v[18:21], v168
	ds_read_b128 v[22:25], v169
	ds_read_b128 v[26:29], v176
	ds_read_b128 v[30:33], v177
	ds_read_b128 v[2:5], v170
	ds_read_b128 v[6:9], v171
	ds_read_b128 v[10:13], v178
	ds_read_b128 v[14:17], v179
	s_add_i32 s76, s20, 0x80
	s_cmp_eq_u32 s61, s75
	s_cselect_b32 s78, s11, s76
	s_cselect_b32 s77, s21, s74
	s_add_i32 s76, s78, 0x80
	v_mov_b32_e32 v185, v164
	ds_read_b128 v[186:189], v184
	ds_read_b128 v[190:193], v184 offset:1024
	ds_read_b128 v[194:197], v184 offset:2048
	ds_read_b128 v[198:201], v184 offset:3072
	ds_read_b128 v[202:205], v184 offset:4096
	ds_read_b128 v[206:209], v184 offset:5120
	ds_read_b128 v[214:217], v184 offset:6144
	ds_read_b128 v[218:221], v184 offset:7168
	s_add_i32 s79, s20, s59
	v_add_u32_e32 v185, s79, v185
	s_add_i32 m0, s30, 0xc000
	s_add_i32 s79, s20, s66
	global_load_lds_dwordx4 v185, s[4:5]
	v_mov_b32_e32 v185, v164
	s_add_i32 m0, s30, 0xe000
	v_add_u32_e32 v185, s79, v185
	global_load_lds_dwordx4 v185, s[4:5]
	s_waitcnt vmcnt(8)
	s_waitcnt lgkmcnt(0)
	s_barrier
	s_setprio 1
	s_waitcnt lgkmcnt(0)
	v_mfma_f32_16x16x128_f8f6f4 v[158:161], v[18:25], v[186:193], v[158:161]
	v_mfma_f32_16x16x128_f8f6f4 v[154:157], v[26:33], v[186:193], v[154:157]
	v_mfma_f32_16x16x128_f8f6f4 v[150:153], v[18:25], v[194:201], v[150:153]
	v_mfma_f32_16x16x128_f8f6f4 v[146:149], v[26:33], v[194:201], v[146:149]
	v_mfma_f32_16x16x128_f8f6f4 v[138:141], v[18:25], v[202:209], v[138:141]
	v_mfma_f32_16x16x128_f8f6f4 v[130:133], v[26:33], v[202:209], v[130:133]
	v_mfma_f32_16x16x128_f8f6f4 v[122:125], v[18:25], v[214:221], v[122:125]
	v_mfma_f32_16x16x128_f8f6f4 v[114:117], v[26:33], v[214:221], v[114:117]
	v_mfma_f32_16x16x128_f8f6f4 v[142:145], v[2:9], v[186:193], v[142:145]
	v_mfma_f32_16x16x128_f8f6f4 v[134:137], v[10:17], v[186:193], v[134:137]
	v_mfma_f32_16x16x128_f8f6f4 v[126:129], v[2:9], v[194:201], v[126:129]
	v_mfma_f32_16x16x128_f8f6f4 v[118:121], v[10:17], v[194:201], v[118:121]
	v_mfma_f32_16x16x128_f8f6f4 v[110:113], v[2:9], v[202:209], v[110:113]
	v_mfma_f32_16x16x128_f8f6f4 v[106:109], v[10:17], v[202:209], v[106:109]
	v_mfma_f32_16x16x128_f8f6f4 v[102:105], v[2:9], v[214:221], v[102:105]
	v_mfma_f32_16x16x128_f8f6f4 v[98:101], v[10:17], v[214:221], v[98:101]
	s_setprio 0
	s_barrier
	v_mov_b32_e32 v185, v165
	ds_read_b128 v[186:189], v184 offset:16384
	ds_read_b128 v[190:193], v184 offset:17408
	ds_read_b128 v[194:197], v184 offset:18432
	ds_read_b128 v[198:201], v184 offset:19456
	ds_read_b128 v[202:205], v184 offset:20480
	ds_read_b128 v[206:209], v184 offset:21504
	ds_read_b128 v[214:217], v184 offset:22528
	ds_read_b128 v[218:221], v184 offset:23552
	s_mov_b32 m0, s31
	v_add_u32_e32 v185, s77, v185
	global_load_lds_dwordx4 v185, s[6:7]
	v_mov_b32_e32 v185, v165
	s_add_i32 s79, s77, s25
	v_add_u32_e32 v185, s79, v185
	s_mov_b32 m0, s35
	s_add_i32 s79, s79, s25
	global_load_lds_dwordx4 v185, s[6:7]
	v_mov_b32_e32 v185, v165
	s_mov_b32 m0, s44
	v_add_u32_e32 v185, s79, v185
	global_load_lds_dwordx4 v185, s[6:7]
	v_mov_b32_e32 v185, v165
	s_add_i32 s79, s79, s25
	v_add_u32_e32 v185, s79, v185
	s_mov_b32 m0, s45
	s_nop 0
	global_load_lds_dwordx4 v185, s[6:7]
	v_mov_b32_e32 v185, v164
	s_mov_b32 m0, s30
	v_add_u32_e32 v185, s78, v185
	global_load_lds_dwordx4 v185, s[4:5]
	v_mov_b32_e32 v185, v164
	s_add_i32 s78, s78, s24
	v_add_u32_e32 v185, s78, v185
	s_mov_b32 m0, s46
	s_nop 0
	global_load_lds_dwordx4 v185, s[4:5]
	s_waitcnt vmcnt(8)
	s_waitcnt lgkmcnt(0)
	s_barrier
	s_setprio 1
	s_waitcnt lgkmcnt(0)
	v_mfma_f32_16x16x128_f8f6f4 v[94:97], v[18:25], v[186:193], v[94:97]
	v_mfma_f32_16x16x128_f8f6f4 v[90:93], v[26:33], v[186:193], v[90:93]
	v_mfma_f32_16x16x128_f8f6f4 v[86:89], v[18:25], v[194:201], v[86:89]
	v_mfma_f32_16x16x128_f8f6f4 v[82:85], v[26:33], v[194:201], v[82:85]
	v_mfma_f32_16x16x128_f8f6f4 v[74:77], v[18:25], v[202:209], v[74:77]
	v_mfma_f32_16x16x128_f8f6f4 v[66:69], v[26:33], v[202:209], v[66:69]
	v_mfma_f32_16x16x128_f8f6f4 v[58:61], v[18:25], v[214:221], v[58:61]
	v_mfma_f32_16x16x128_f8f6f4 v[50:53], v[26:33], v[214:221], v[50:53]
	v_mfma_f32_16x16x128_f8f6f4 v[78:81], v[2:9], v[186:193], v[78:81]
	v_mfma_f32_16x16x128_f8f6f4 v[70:73], v[10:17], v[186:193], v[70:73]
	v_mfma_f32_16x16x128_f8f6f4 v[62:65], v[2:9], v[194:201], v[62:65]
	v_mfma_f32_16x16x128_f8f6f4 v[54:57], v[10:17], v[194:201], v[54:57]
	v_mfma_f32_16x16x128_f8f6f4 v[46:49], v[2:9], v[202:209], v[46:49]
	v_mfma_f32_16x16x128_f8f6f4 v[42:45], v[10:17], v[202:209], v[42:45]
	v_mfma_f32_16x16x128_f8f6f4 v[38:41], v[2:9], v[214:221], v[38:41]
	v_mfma_f32_16x16x128_f8f6f4 v[34:37], v[10:17], v[214:221], v[34:37]
	s_setprio 0
	s_barrier

.Ltx24_skip:
	ds_read_b128 v[2:5], v172
	ds_read_b128 v[6:9], v173
	ds_read_b128 v[10:13], v180
	ds_read_b128 v[14:17], v181
	ds_read_b128 v[18:21], v174
	ds_read_b128 v[22:25], v175
	ds_read_b128 v[26:29], v182
	ds_read_b128 v[30:33], v183
	v_mov_b32_e32 v185, v164
	ds_read_b128 v[186:189], v184 offset:32768
	ds_read_b128 v[190:193], v184 offset:33792
	ds_read_b128 v[194:197], v184 offset:34816
	ds_read_b128 v[198:201], v184 offset:35840
	ds_read_b128 v[202:205], v184 offset:36864
	ds_read_b128 v[206:209], v184 offset:37888
	ds_read_b128 v[214:217], v184 offset:38912
	ds_read_b128 v[218:221], v184 offset:39936
	s_add_i32 s78, s78, s24
	s_mov_b32 m0, s47
	v_add_u32_e32 v185, s78, v185
	global_load_lds_dwordx4 v185, s[4:5]
	v_mov_b32_e32 v185, v164
	s_add_i32 s78, s78, s24
	v_add_u32_e32 v185, s78, v185
	s_mov_b32 m0, s48
	s_nop 0
	global_load_lds_dwordx4 v185, s[4:5]
	s_waitcnt vmcnt(8)
	s_waitcnt lgkmcnt(0)
	s_barrier
	s_setprio 1
	s_waitcnt lgkmcnt(0)
	v_mfma_f32_16x16x128_f8f6f4 v[158:161], v[2:9], v[186:193], v[158:161]
	v_mfma_f32_16x16x128_f8f6f4 v[154:157], v[10:17], v[186:193], v[154:157]
	v_mfma_f32_16x16x128_f8f6f4 v[150:153], v[2:9], v[194:201], v[150:153]
	v_mfma_f32_16x16x128_f8f6f4 v[146:149], v[10:17], v[194:201], v[146:149]
	v_mfma_f32_16x16x128_f8f6f4 v[138:141], v[2:9], v[202:209], v[138:141]
	v_mfma_f32_16x16x128_f8f6f4 v[130:133], v[10:17], v[202:209], v[130:133]
	v_mfma_f32_16x16x128_f8f6f4 v[122:125], v[2:9], v[214:221], v[122:125]
	v_mfma_f32_16x16x128_f8f6f4 v[114:117], v[10:17], v[214:221], v[114:117]
	v_mfma_f32_16x16x128_f8f6f4 v[142:145], v[18:25], v[186:193], v[142:145]
	v_mfma_f32_16x16x128_f8f6f4 v[134:137], v[26:33], v[186:193], v[134:137]
	v_mfma_f32_16x16x128_f8f6f4 v[126:129], v[18:25], v[194:201], v[126:129]
	v_mfma_f32_16x16x128_f8f6f4 v[118:121], v[26:33], v[194:201], v[118:121]
	v_mfma_f32_16x16x128_f8f6f4 v[110:113], v[18:25], v[202:209], v[110:113]
	v_mfma_f32_16x16x128_f8f6f4 v[106:109], v[26:33], v[202:209], v[106:109]
	v_mfma_f32_16x16x128_f8f6f4 v[102:105], v[18:25], v[214:221], v[102:105]
	v_mfma_f32_16x16x128_f8f6f4 v[98:101], v[26:33], v[214:221], v[98:101]
	s_setprio 0
	s_barrier
	v_mov_b32_e32 v185, v165
	ds_read_b128 v[186:189], v184 offset:49152
	ds_read_b128 v[190:193], v184 offset:50176
	ds_read_b128 v[194:197], v184 offset:51200
	ds_read_b128 v[198:201], v184 offset:52224
	ds_read_b128 v[202:205], v184 offset:53248
	ds_read_b128 v[206:209], v184 offset:54272
	ds_read_b128 v[214:217], v184 offset:55296
	ds_read_b128 v[218:221], v184 offset:56320
	s_addk_i32 s77, 0x80
	s_mov_b32 m0, s51
	v_add_u32_e32 v185, s77, v185
	global_load_lds_dwordx4 v185, s[6:7]
	v_mov_b32_e32 v185, v165
	s_add_i32 s77, s77, s25
	v_add_u32_e32 v185, s77, v185
	s_mov_b32 m0, s52
	s_add_i32 s77, s77, s25
	global_load_lds_dwordx4 v185, s[6:7]
	v_mov_b32_e32 v185, v165
	s_mov_b32 m0, s55
	v_add_u32_e32 v185, s77, v185
	global_load_lds_dwordx4 v185, s[6:7]
	v_mov_b32_e32 v185, v165
	s_add_i32 s77, s77, s25
	v_add_u32_e32 v185, s77, v185
	s_mov_b32 m0, s57
	s_nop 0
	global_load_lds_dwordx4 v185, s[6:7]
	v_mov_b32_e32 v185, v164
	s_mov_b32 m0, s53
	v_add_u32_e32 v185, s76, v185
	global_load_lds_dwordx4 v185, s[4:5]
	v_mov_b32_e32 v185, v164
	s_add_i32 s76, s76, s24
	v_add_u32_e32 v185, s76, v185
	s_mov_b32 m0, s54
	s_nop 0
	global_load_lds_dwordx4 v185, s[4:5]
	s_waitcnt vmcnt(8)
	s_waitcnt lgkmcnt(0)
	s_barrier
	s_setprio 1
	s_waitcnt lgkmcnt(0)
	v_mfma_f32_16x16x128_f8f6f4 v[94:97], v[2:9], v[186:193], v[94:97]
	v_mfma_f32_16x16x128_f8f6f4 v[90:93], v[10:17], v[186:193], v[90:93]
	v_mfma_f32_16x16x128_f8f6f4 v[86:89], v[2:9], v[194:201], v[86:89]
	v_mfma_f32_16x16x128_f8f6f4 v[82:85], v[10:17], v[194:201], v[82:85]
	v_mfma_f32_16x16x128_f8f6f4 v[74:77], v[2:9], v[202:209], v[74:77]
	v_mfma_f32_16x16x128_f8f6f4 v[66:69], v[10:17], v[202:209], v[66:69]
	v_mfma_f32_16x16x128_f8f6f4 v[58:61], v[2:9], v[214:221], v[58:61]
	v_mfma_f32_16x16x128_f8f6f4 v[50:53], v[10:17], v[214:221], v[50:53]
	v_mfma_f32_16x16x128_f8f6f4 v[78:81], v[18:25], v[186:193], v[78:81]
	v_mfma_f32_16x16x128_f8f6f4 v[70:73], v[26:33], v[186:193], v[70:73]
	v_mfma_f32_16x16x128_f8f6f4 v[62:65], v[18:25], v[194:201], v[62:65]
	v_mfma_f32_16x16x128_f8f6f4 v[54:57], v[26:33], v[194:201], v[54:57]
	v_mfma_f32_16x16x128_f8f6f4 v[46:49], v[18:25], v[202:209], v[46:49]
	v_mfma_f32_16x16x128_f8f6f4 v[42:45], v[26:33], v[202:209], v[42:45]
	v_mfma_f32_16x16x128_f8f6f4 v[38:41], v[18:25], v[214:221], v[38:41]
	v_mfma_f32_16x16x128_f8f6f4 v[34:37], v[26:33], v[214:221], v[34:37]
	s_setprio 0
	s_barrier
	s_add_i32 s75, s75, 2
	s_addk_i32 s20, 0x100
	s_addk_i32 s74, 0x100
	s_cmp_ge_i32 s75, s58
	s_cbranch_scc0 .LBB0_3007
	v_pk_mul_f32 v[2:3], v[160:161], s[16:17] op_sel_hi:[1,0]
	v_pk_mul_f32 v[4:5], v[158:159], s[16:17] op_sel_hi:[1,0]
	v_pk_mul_f32 v[6:7], v[156:157], s[16:17] op_sel_hi:[1,0]
	v_pk_mul_f32 v[12:13], v[154:155], s[16:17] op_sel_hi:[1,0]
	v_pk_mul_f32 v[144:145], v[144:145], s[16:17] op_sel_hi:[1,0]
	v_pk_mul_f32 v[142:143], v[142:143], s[16:17] op_sel_hi:[1,0]
	v_pk_mul_f32 v[136:137], v[136:137], s[16:17] op_sel_hi:[1,0]
	v_pk_mul_f32 v[134:135], v[134:135], s[16:17] op_sel_hi:[1,0]
	v_pk_mul_f32 v[8:9], v[152:153], s[16:17] op_sel_hi:[1,0]
	v_pk_mul_f32 v[14:15], v[150:151], s[16:17] op_sel_hi:[1,0]
	v_pk_mul_f32 v[18:19], v[148:149], s[16:17] op_sel_hi:[1,0]
	v_pk_mul_f32 v[26:27], v[146:147], s[16:17] op_sel_hi:[1,0]
	v_pk_mul_f32 v[128:129], v[128:129], s[16:17] op_sel_hi:[1,0]
	v_pk_mul_f32 v[126:127], v[126:127], s[16:17] op_sel_hi:[1,0]
	v_pk_mul_f32 v[120:121], v[120:121], s[16:17] op_sel_hi:[1,0]
	v_pk_mul_f32 v[118:119], v[118:119], s[16:17] op_sel_hi:[1,0]
	v_pk_mul_f32 v[10:11], v[140:141], s[16:17] op_sel_hi:[1,0]
	v_pk_mul_f32 v[20:21], v[138:139], s[16:17] op_sel_hi:[1,0]
	v_pk_mul_f32 v[22:23], v[132:133], s[16:17] op_sel_hi:[1,0]
	v_pk_mul_f32 v[30:31], v[130:131], s[16:17] op_sel_hi:[1,0]
	v_pk_mul_f32 v[112:113], v[112:113], s[16:17] op_sel_hi:[1,0]
	v_pk_mul_f32 v[110:111], v[110:111], s[16:17] op_sel_hi:[1,0]
	v_pk_mul_f32 v[108:109], v[108:109], s[16:17] op_sel_hi:[1,0]
	v_pk_mul_f32 v[106:107], v[106:107], s[16:17] op_sel_hi:[1,0]
	v_pk_mul_f32 v[16:17], v[124:125], s[16:17] op_sel_hi:[1,0]
	v_pk_mul_f32 v[24:25], v[122:123], s[16:17] op_sel_hi:[1,0]
	v_pk_mul_f32 v[28:29], v[116:117], s[16:17] op_sel_hi:[1,0]
	v_pk_mul_f32 v[32:33], v[114:115], s[16:17] op_sel_hi:[1,0]
	v_pk_mul_f32 v[104:105], v[104:105], s[16:17] op_sel_hi:[1,0]
	v_pk_mul_f32 v[102:103], v[102:103], s[16:17] op_sel_hi:[1,0]
	v_pk_mul_f32 v[100:101], v[100:101], s[16:17] op_sel_hi:[1,0]
	v_pk_mul_f32 v[98:99], v[98:99], s[16:17] op_sel_hi:[1,0]
	v_pk_mul_f32 v[96:97], v[96:97], s[16:17] op_sel_hi:[1,0]
	v_pk_mul_f32 v[94:95], v[94:95], s[16:17] op_sel_hi:[1,0]
	v_pk_mul_f32 v[92:93], v[92:93], s[16:17] op_sel_hi:[1,0]
	v_pk_mul_f32 v[90:91], v[90:91], s[16:17] op_sel_hi:[1,0]
	v_pk_mul_f32 v[114:115], v[80:81], s[16:17] op_sel_hi:[1,0]
	v_pk_mul_f32 v[116:117], v[78:79], s[16:17] op_sel_hi:[1,0]
	v_pk_mul_f32 v[122:123], v[72:73], s[16:17] op_sel_hi:[1,0]
	v_pk_mul_f32 v[124:125], v[70:71], s[16:17] op_sel_hi:[1,0]
	v_pk_mul_f32 v[70:71], v[88:89], s[16:17] op_sel_hi:[1,0]
	v_pk_mul_f32 v[72:73], v[86:87], s[16:17] op_sel_hi:[1,0]
	v_pk_mul_f32 v[78:79], v[84:85], s[16:17] op_sel_hi:[1,0]
	v_pk_mul_f32 v[80:81], v[82:83], s[16:17] op_sel_hi:[1,0]
	v_pk_mul_f32 v[82:83], v[64:65], s[16:17] op_sel_hi:[1,0]
	v_pk_mul_f32 v[84:85], v[62:63], s[16:17] op_sel_hi:[1,0]
	v_pk_mul_f32 v[86:87], v[56:57], s[16:17] op_sel_hi:[1,0]
	v_pk_mul_f32 v[88:89], v[54:55], s[16:17] op_sel_hi:[1,0]
	v_pk_mul_f32 v[54:55], v[76:77], s[16:17] op_sel_hi:[1,0]
	v_pk_mul_f32 v[56:57], v[74:75], s[16:17] op_sel_hi:[1,0]
	v_pk_mul_f32 v[62:63], v[68:69], s[16:17] op_sel_hi:[1,0]
	v_pk_mul_f32 v[64:65], v[66:67], s[16:17] op_sel_hi:[1,0]
	v_pk_mul_f32 v[66:67], v[48:49], s[16:17] op_sel_hi:[1,0]
	v_pk_mul_f32 v[68:69], v[46:47], s[16:17] op_sel_hi:[1,0]
	v_pk_mul_f32 v[74:75], v[44:45], s[16:17] op_sel_hi:[1,0]
	v_pk_mul_f32 v[76:77], v[42:43], s[16:17] op_sel_hi:[1,0]
	v_pk_mul_f32 v[42:43], v[60:61], s[16:17] op_sel_hi:[1,0]
	v_pk_mul_f32 v[44:45], v[58:59], s[16:17] op_sel_hi:[1,0]
	v_pk_mul_f32 v[46:47], v[52:53], s[16:17] op_sel_hi:[1,0]
	v_pk_mul_f32 v[48:49], v[50:51], s[16:17] op_sel_hi:[1,0]
	v_pk_mul_f32 v[40:41], v[40:41], s[16:17] op_sel_hi:[1,0]
	v_pk_mul_f32 v[38:39], v[38:39], s[16:17] op_sel_hi:[1,0]
	v_pk_mul_f32 v[36:37], v[36:37], s[16:17] op_sel_hi:[1,0]
	v_pk_mul_f32 v[34:35], v[34:35], s[16:17] op_sel_hi:[1,0]
